# s_setprio 1 moved above the barrier that opens every MFMA block of the GEMM K-loops (released wave wins issue arbitration at once)
# baseline (speedup 1.0000x reference)
.LBB0_296:
	ds_read_b128 v[160:163], v144
	ds_read_b128 v[164:167], v145
	ds_read_b128 v[168:171], v140
	ds_read_b128 v[172:175], v141
	ds_read_b128 v[176:179], v146
	ds_read_b128 v[180:183], v147
	ds_read_b128 v[184:187], v148
	ds_read_b128 v[188:191], v149
	s_add_i32 s72, s14, 0x80
	s_cmp_eq_u32 s54, s71
	s_cselect_b32 s73, s13, s70
	s_cselect_b32 s72, s15, s72
	v_add_u32_e32 v159, s14, v157
	s_add_i32 m0, s22, 0xc000
	ds_read_b128 v[192:195], v158
	ds_read_b128 v[196:199], v158 offset:1024
	ds_read_b128 v[200:203], v158 offset:2048
	ds_read_b128 v[204:207], v158 offset:3072
	ds_read_b128 v[214:217], v158 offset:4096
	ds_read_b128 v[218:221], v158 offset:5120
	ds_read_b128 v[222:225], v158 offset:6144
	ds_read_b128 v[226:229], v158 offset:7168
	global_load_lds_dwordx4 v159, s[4:5]
	v_add_u32_e32 v159, s14, v156
	s_add_i32 m0, s22, 0xe000
	s_nop 0
	global_load_lds_dwordx4 v159, s[4:5]
	s_waitcnt vmcnt(8)
	s_waitcnt lgkmcnt(0)
	s_setprio 1
	s_barrier
	s_waitcnt lgkmcnt(0)
	v_mfma_f32_16x16x32_bf16 v[122:125], v[168:171], v[192:195], v[122:125]
	v_mfma_f32_16x16x32_bf16 v[126:129], v[164:167], v[192:195], v[126:129]
	v_mfma_f32_16x16x32_bf16 v[110:113], v[168:171], v[200:203], v[110:113]
	v_mfma_f32_16x16x32_bf16 v[106:109], v[164:167], v[200:203], v[106:109]
	v_mfma_f32_16x16x32_bf16 v[94:97], v[168:171], v[214:217], v[94:97]
	v_mfma_f32_16x16x32_bf16 v[90:93], v[164:167], v[214:217], v[90:93]
	v_mfma_f32_16x16x32_bf16 v[78:81], v[168:171], v[222:225], v[78:81]
	v_mfma_f32_16x16x32_bf16 v[74:77], v[164:167], v[222:225], v[74:77]
	v_mfma_f32_16x16x32_bf16 v[122:125], v[160:163], v[196:199], v[122:125]
	v_mfma_f32_16x16x32_bf16 v[126:129], v[176:179], v[196:199], v[126:129]
	v_mfma_f32_16x16x32_bf16 v[110:113], v[160:163], v[204:207], v[110:113]
	v_mfma_f32_16x16x32_bf16 v[106:109], v[176:179], v[204:207], v[106:109]
	v_mfma_f32_16x16x32_bf16 v[94:97], v[160:163], v[218:221], v[94:97]
	v_mfma_f32_16x16x32_bf16 v[90:93], v[176:179], v[218:221], v[90:93]
	v_mfma_f32_16x16x32_bf16 v[78:81], v[160:163], v[226:229], v[78:81]
	v_mfma_f32_16x16x32_bf16 v[74:77], v[176:179], v[226:229], v[74:77]
	s_setprio 0
	s_setprio 1
	v_mfma_f32_16x16x32_bf16 v[118:121], v[172:175], v[192:195], v[118:121]
	v_mfma_f32_16x16x32_bf16 v[114:117], v[184:187], v[192:195], v[114:117]
	v_mfma_f32_16x16x32_bf16 v[102:105], v[172:175], v[200:203], v[102:105]
	v_mfma_f32_16x16x32_bf16 v[98:101], v[184:187], v[200:203], v[98:101]
	v_mfma_f32_16x16x32_bf16 v[86:89], v[172:175], v[214:217], v[86:89]
	v_mfma_f32_16x16x32_bf16 v[82:85], v[184:187], v[214:217], v[82:85]
	v_mfma_f32_16x16x32_bf16 v[70:73], v[172:175], v[222:225], v[70:73]
	v_mfma_f32_16x16x32_bf16 v[66:69], v[184:187], v[222:225], v[66:69]
	v_mfma_f32_16x16x32_bf16 v[118:121], v[180:183], v[196:199], v[118:121]
	v_mfma_f32_16x16x32_bf16 v[114:117], v[188:191], v[196:199], v[114:117]
	v_mfma_f32_16x16x32_bf16 v[102:105], v[180:183], v[204:207], v[102:105]
	v_mfma_f32_16x16x32_bf16 v[98:101], v[188:191], v[204:207], v[98:101]
	v_mfma_f32_16x16x32_bf16 v[86:89], v[180:183], v[218:221], v[86:89]
	v_mfma_f32_16x16x32_bf16 v[82:85], v[188:191], v[218:221], v[82:85]
	v_mfma_f32_16x16x32_bf16 v[70:73], v[180:183], v[226:229], v[70:73]
	v_mfma_f32_16x16x32_bf16 v[66:69], v[188:191], v[226:229], v[66:69]
	s_setprio 0
	s_barrier
	s_mov_b32 m0, s23
	v_add_u32_e32 v159, s73, v134
	ds_read_b128 v[192:195], v158 offset:16384
	ds_read_b128 v[196:199], v158 offset:17408
	ds_read_b128 v[200:203], v158 offset:18432
	ds_read_b128 v[204:207], v158 offset:19456
	ds_read_b128 v[214:217], v158 offset:20480
	ds_read_b128 v[218:221], v158 offset:21504
	ds_read_b128 v[222:225], v158 offset:22528
	ds_read_b128 v[226:229], v158 offset:23552
	global_load_lds_dwordx4 v159, s[20:21]
	v_add_u32_e32 v159, s17, v159
	s_mov_b32 m0, s28
	s_nop 0
	global_load_lds_dwordx4 v159, s[20:21]
	v_add_u32_e32 v159, s73, v135
	s_mov_b32 m0, s29
	s_nop 0
	global_load_lds_dwordx4 v159, s[20:21]
	v_add_u32_e32 v159, s17, v159
	s_mov_b32 m0, s30
	s_nop 0
	global_load_lds_dwordx4 v159, s[20:21]
	v_add_u32_e32 v159, s72, v1
	s_mov_b32 m0, s22
	s_nop 0
	global_load_lds_dwordx4 v159, s[4:5]
	v_add_u32_e32 v159, s16, v159
	s_mov_b32 m0, s31
	s_nop 0
	global_load_lds_dwordx4 v159, s[4:5]
	s_waitcnt vmcnt(8)
	s_waitcnt lgkmcnt(0)
	s_setprio 1
	s_barrier
	s_waitcnt lgkmcnt(0)
	v_mfma_f32_16x16x32_bf16 v[62:65], v[168:171], v[192:195], v[62:65]
	v_mfma_f32_16x16x32_bf16 v[58:61], v[164:167], v[192:195], v[58:61]
	v_mfma_f32_16x16x32_bf16 v[46:49], v[168:171], v[200:203], v[46:49]
	v_mfma_f32_16x16x32_bf16 v[42:45], v[164:167], v[200:203], v[42:45]
	v_mfma_f32_16x16x32_bf16 v[30:33], v[168:171], v[214:217], v[30:33]
	v_mfma_f32_16x16x32_bf16 v[26:29], v[164:167], v[214:217], v[26:29]
	v_mfma_f32_16x16x32_bf16 v[14:17], v[168:171], v[222:225], v[14:17]
	v_mfma_f32_16x16x32_bf16 v[10:13], v[164:167], v[222:225], v[10:13]
	v_mfma_f32_16x16x32_bf16 v[62:65], v[160:163], v[196:199], v[62:65]
	v_mfma_f32_16x16x32_bf16 v[58:61], v[176:179], v[196:199], v[58:61]
	v_mfma_f32_16x16x32_bf16 v[46:49], v[160:163], v[204:207], v[46:49]
	v_mfma_f32_16x16x32_bf16 v[42:45], v[176:179], v[204:207], v[42:45]
	v_mfma_f32_16x16x32_bf16 v[30:33], v[160:163], v[218:221], v[30:33]
	v_mfma_f32_16x16x32_bf16 v[26:29], v[176:179], v[218:221], v[26:29]
	v_mfma_f32_16x16x32_bf16 v[14:17], v[160:163], v[226:229], v[14:17]
	v_mfma_f32_16x16x32_bf16 v[10:13], v[176:179], v[226:229], v[10:13]
	s_setprio 0
	s_setprio 1
	v_mfma_f32_16x16x32_bf16 v[54:57], v[172:175], v[192:195], v[54:57]
	v_mfma_f32_16x16x32_bf16 v[50:53], v[184:187], v[192:195], v[50:53]
	v_mfma_f32_16x16x32_bf16 v[38:41], v[172:175], v[200:203], v[38:41]
	v_mfma_f32_16x16x32_bf16 v[34:37], v[184:187], v[200:203], v[34:37]
	v_mfma_f32_16x16x32_bf16 v[22:25], v[172:175], v[214:217], v[22:25]
	v_mfma_f32_16x16x32_bf16 v[18:21], v[184:187], v[214:217], v[18:21]
	v_mfma_f32_16x16x32_bf16 v[6:9], v[172:175], v[222:225], v[6:9]
	v_mfma_f32_16x16x32_bf16 v[2:5], v[184:187], v[222:225], v[2:5]
	v_mfma_f32_16x16x32_bf16 v[54:57], v[180:183], v[196:199], v[54:57]
	v_mfma_f32_16x16x32_bf16 v[50:53], v[188:191], v[196:199], v[50:53]
	v_mfma_f32_16x16x32_bf16 v[38:41], v[180:183], v[204:207], v[38:41]
	v_mfma_f32_16x16x32_bf16 v[34:37], v[188:191], v[204:207], v[34:37]
	v_mfma_f32_16x16x32_bf16 v[22:25], v[180:183], v[218:221], v[22:25]
	v_mfma_f32_16x16x32_bf16 v[18:21], v[188:191], v[218:221], v[18:21]
	v_mfma_f32_16x16x32_bf16 v[6:9], v[180:183], v[226:229], v[6:9]
	v_mfma_f32_16x16x32_bf16 v[2:5], v[188:191], v[226:229], v[2:5]
	s_setprio 0
	s_barrier
	ds_read_b128 v[160:163], v150
	ds_read_b128 v[164:167], v151
	ds_read_b128 v[168:171], v142
	ds_read_b128 v[172:175], v143
	ds_read_b128 v[176:179], v152
	ds_read_b128 v[180:183], v153
	ds_read_b128 v[184:187], v154
	ds_read_b128 v[188:191], v155
	s_mov_b32 m0, s35
	v_add_u32_e32 v159, s72, v136
	ds_read_b128 v[192:195], v158 offset:32768
	ds_read_b128 v[196:199], v158 offset:33792
	ds_read_b128 v[200:203], v158 offset:34816
	ds_read_b128 v[204:207], v158 offset:35840
	ds_read_b128 v[214:217], v158 offset:36864
	ds_read_b128 v[218:221], v158 offset:37888
	ds_read_b128 v[222:225], v158 offset:38912
	ds_read_b128 v[226:229], v158 offset:39936
	global_load_lds_dwordx4 v159, s[4:5]
	v_add_u32_e32 v159, s16, v159
	s_mov_b32 m0, s44
	s_nop 0
	global_load_lds_dwordx4 v159, s[4:5]
	s_waitcnt vmcnt(8)
	s_waitcnt lgkmcnt(0)
	s_setprio 1
	s_barrier
	s_waitcnt lgkmcnt(0)
	v_mfma_f32_16x16x32_bf16 v[122:125], v[168:171], v[192:195], v[122:125]
	v_mfma_f32_16x16x32_bf16 v[126:129], v[164:167], v[192:195], v[126:129]
	v_mfma_f32_16x16x32_bf16 v[110:113], v[168:171], v[200:203], v[110:113]
	v_mfma_f32_16x16x32_bf16 v[106:109], v[164:167], v[200:203], v[106:109]
	v_mfma_f32_16x16x32_bf16 v[94:97], v[168:171], v[214:217], v[94:97]
	v_mfma_f32_16x16x32_bf16 v[90:93], v[164:167], v[214:217], v[90:93]
	v_mfma_f32_16x16x32_bf16 v[78:81], v[168:171], v[222:225], v[78:81]
	v_mfma_f32_16x16x32_bf16 v[74:77], v[164:167], v[222:225], v[74:77]
	v_mfma_f32_16x16x32_bf16 v[122:125], v[160:163], v[196:199], v[122:125]
	v_mfma_f32_16x16x32_bf16 v[126:129], v[176:179], v[196:199], v[126:129]
	v_mfma_f32_16x16x32_bf16 v[110:113], v[160:163], v[204:207], v[110:113]
	v_mfma_f32_16x16x32_bf16 v[106:109], v[176:179], v[204:207], v[106:109]
	v_mfma_f32_16x16x32_bf16 v[94:97], v[160:163], v[218:221], v[94:97]
	v_mfma_f32_16x16x32_bf16 v[90:93], v[176:179], v[218:221], v[90:93]
	v_mfma_f32_16x16x32_bf16 v[78:81], v[160:163], v[226:229], v[78:81]
	v_mfma_f32_16x16x32_bf16 v[74:77], v[176:179], v[226:229], v[74:77]
	s_setprio 0
	s_setprio 1
	v_mfma_f32_16x16x32_bf16 v[118:121], v[172:175], v[192:195], v[118:121]
	v_mfma_f32_16x16x32_bf16 v[114:117], v[184:187], v[192:195], v[114:117]
	v_mfma_f32_16x16x32_bf16 v[102:105], v[172:175], v[200:203], v[102:105]
	v_mfma_f32_16x16x32_bf16 v[98:101], v[184:187], v[200:203], v[98:101]
	v_mfma_f32_16x16x32_bf16 v[86:89], v[172:175], v[214:217], v[86:89]
	v_mfma_f32_16x16x32_bf16 v[82:85], v[184:187], v[214:217], v[82:85]
	v_mfma_f32_16x16x32_bf16 v[70:73], v[172:175], v[222:225], v[70:73]
	v_mfma_f32_16x16x32_bf16 v[66:69], v[184:187], v[222:225], v[66:69]
	v_mfma_f32_16x16x32_bf16 v[118:121], v[180:183], v[196:199], v[118:121]
	v_mfma_f32_16x16x32_bf16 v[114:117], v[188:191], v[196:199], v[114:117]
	v_mfma_f32_16x16x32_bf16 v[102:105], v[180:183], v[204:207], v[102:105]
	v_mfma_f32_16x16x32_bf16 v[98:101], v[188:191], v[204:207], v[98:101]
	v_mfma_f32_16x16x32_bf16 v[86:89], v[180:183], v[218:221], v[86:89]
	v_mfma_f32_16x16x32_bf16 v[82:85], v[188:191], v[218:221], v[82:85]
	v_mfma_f32_16x16x32_bf16 v[70:73], v[180:183], v[226:229], v[70:73]
	v_mfma_f32_16x16x32_bf16 v[66:69], v[188:191], v[226:229], v[66:69]
	s_setprio 0
	s_barrier
	s_addk_i32 s73, 0x80
	s_mov_b32 m0, s46
	v_add_u32_e32 v159, s73, v134
	ds_read_b128 v[192:195], v158 offset:49152
	ds_read_b128 v[196:199], v158 offset:50176
	ds_read_b128 v[200:203], v158 offset:51200
	ds_read_b128 v[204:207], v158 offset:52224
	ds_read_b128 v[214:217], v158 offset:53248
	ds_read_b128 v[218:221], v158 offset:54272
	ds_read_b128 v[222:225], v158 offset:55296
	ds_read_b128 v[226:229], v158 offset:56320
	global_load_lds_dwordx4 v159, s[20:21]
	v_add_u32_e32 v159, s17, v159
	s_mov_b32 m0, s47
	s_nop 0
	global_load_lds_dwordx4 v159, s[20:21]
	v_add_u32_e32 v159, s73, v135
	s_mov_b32 m0, s50
	s_nop 0
	global_load_lds_dwordx4 v159, s[20:21]
	v_add_u32_e32 v159, s17, v159
	s_mov_b32 m0, s51
	s_nop 0
	global_load_lds_dwordx4 v159, s[20:21]
	v_add_u32_e32 v159, s72, v137
	s_mov_b32 m0, s48
	s_nop 0
	global_load_lds_dwordx4 v159, s[4:5]
	v_add_u32_e32 v159, s16, v159
	s_mov_b32 m0, s49
	s_nop 0
	global_load_lds_dwordx4 v159, s[4:5]
	s_waitcnt vmcnt(8)
	s_waitcnt lgkmcnt(0)
	s_setprio 1
	s_barrier
	s_waitcnt lgkmcnt(0)
	v_mfma_f32_16x16x32_bf16 v[62:65], v[168:171], v[192:195], v[62:65]
	v_mfma_f32_16x16x32_bf16 v[58:61], v[164:167], v[192:195], v[58:61]
	v_mfma_f32_16x16x32_bf16 v[46:49], v[168:171], v[200:203], v[46:49]
	v_mfma_f32_16x16x32_bf16 v[42:45], v[164:167], v[200:203], v[42:45]
	v_mfma_f32_16x16x32_bf16 v[30:33], v[168:171], v[214:217], v[30:33]
	v_mfma_f32_16x16x32_bf16 v[26:29], v[164:167], v[214:217], v[26:29]
	v_mfma_f32_16x16x32_bf16 v[14:17], v[168:171], v[222:225], v[14:17]
	v_mfma_f32_16x16x32_bf16 v[10:13], v[164:167], v[222:225], v[10:13]
	v_mfma_f32_16x16x32_bf16 v[62:65], v[160:163], v[196:199], v[62:65]
	v_mfma_f32_16x16x32_bf16 v[58:61], v[176:179], v[196:199], v[58:61]
	v_mfma_f32_16x16x32_bf16 v[46:49], v[160:163], v[204:207], v[46:49]
	v_mfma_f32_16x16x32_bf16 v[42:45], v[176:179], v[204:207], v[42:45]
	v_mfma_f32_16x16x32_bf16 v[30:33], v[160:163], v[218:221], v[30:33]
	v_mfma_f32_16x16x32_bf16 v[26:29], v[176:179], v[218:221], v[26:29]
	v_mfma_f32_16x16x32_bf16 v[14:17], v[160:163], v[226:229], v[14:17]
	v_mfma_f32_16x16x32_bf16 v[10:13], v[176:179], v[226:229], v[10:13]
	s_setprio 0
	s_setprio 1
	v_mfma_f32_16x16x32_bf16 v[54:57], v[172:175], v[192:195], v[54:57]
	v_mfma_f32_16x16x32_bf16 v[50:53], v[184:187], v[192:195], v[50:53]
	v_mfma_f32_16x16x32_bf16 v[38:41], v[172:175], v[200:203], v[38:41]
	v_mfma_f32_16x16x32_bf16 v[34:37], v[184:187], v[200:203], v[34:37]
	v_mfma_f32_16x16x32_bf16 v[22:25], v[172:175], v[214:217], v[22:25]
	v_mfma_f32_16x16x32_bf16 v[18:21], v[184:187], v[214:217], v[18:21]
	v_mfma_f32_16x16x32_bf16 v[6:9], v[172:175], v[222:225], v[6:9]
	v_mfma_f32_16x16x32_bf16 v[2:5], v[184:187], v[222:225], v[2:5]
	v_mfma_f32_16x16x32_bf16 v[54:57], v[180:183], v[196:199], v[54:57]
	v_mfma_f32_16x16x32_bf16 v[50:53], v[188:191], v[196:199], v[50:53]
	v_mfma_f32_16x16x32_bf16 v[38:41], v[180:183], v[204:207], v[38:41]
	v_mfma_f32_16x16x32_bf16 v[34:37], v[188:191], v[204:207], v[34:37]
	v_mfma_f32_16x16x32_bf16 v[22:25], v[180:183], v[218:221], v[22:25]
	v_mfma_f32_16x16x32_bf16 v[18:21], v[188:191], v[218:221], v[18:21]
	v_mfma_f32_16x16x32_bf16 v[6:9], v[180:183], v[226:229], v[6:9]
	v_mfma_f32_16x16x32_bf16 v[2:5], v[188:191], v[226:229], v[2:5]
	s_setprio 0
	s_barrier
	s_add_i32 s71, s71, 2
	s_addk_i32 s14, 0x100
	s_addk_i32 s70, 0x100
	s_cmp_ge_i32 s71, s52
	s_cbranch_scc0 .LBB0_296

.LBB0_584:
	ds_read_b128 v[54:57], v46
	ds_read_b128 v[58:61], v48
	s_add_i32 s67, s22, 0x80
	s_cmp_eq_u32 s58, s66
	s_cselect_b32 s68, s23, s65
	s_cselect_b32 s67, s21, s67
	v_add_u32_e32 v38, s22, v51
	s_add_i32 m0, s29, 0xc000
	ds_read_b128 v[62:65], v52
	ds_read_b128 v[66:69], v52 offset:1024
	ds_read_b128 v[70:73], v52 offset:2048
	ds_read_b128 v[74:77], v52 offset:3072
	ds_read_b128 v[78:81], v52 offset:4096
	ds_read_b128 v[82:85], v52 offset:5120
	ds_read_b128 v[86:89], v52 offset:6144
	ds_read_b128 v[90:93], v52 offset:7168
	global_load_lds_dwordx4 v38, s[4:5]
	v_add_u32_e32 v38, s22, v50
	s_add_i32 m0, s29, 0xe000
	s_nop 0
	global_load_lds_dwordx4 v38, s[4:5]
	s_waitcnt vmcnt(8)
	s_waitcnt lgkmcnt(0)
	s_setprio 1
	s_barrier
	s_waitcnt lgkmcnt(0)
	v_mfma_f32_16x16x32_bf16 v[26:29], v[54:57], v[62:65], v[26:29]
	v_mfma_f32_16x16x32_bf16 v[30:33], v[54:57], v[70:73], v[30:33]
	v_mfma_f32_16x16x32_bf16 v[22:25], v[54:57], v[78:81], v[22:25]
	v_mfma_f32_16x16x32_bf16 v[18:21], v[54:57], v[86:89], v[18:21]
	v_mfma_f32_16x16x32_bf16 v[26:29], v[58:61], v[66:69], v[26:29]
	v_mfma_f32_16x16x32_bf16 v[30:33], v[58:61], v[74:77], v[30:33]
	v_mfma_f32_16x16x32_bf16 v[22:25], v[58:61], v[82:85], v[22:25]
	v_mfma_f32_16x16x32_bf16 v[18:21], v[58:61], v[90:93], v[18:21]
	s_setprio 0
	s_setprio 1
	s_setprio 0
	s_barrier
	s_mov_b32 m0, s30
	v_add_u32_e32 v38, s68, v40
	ds_read_b128 v[62:65], v52 offset:16384
	ds_read_b128 v[66:69], v52 offset:17408
	ds_read_b128 v[70:73], v52 offset:18432
	ds_read_b128 v[74:77], v52 offset:19456
	ds_read_b128 v[78:81], v52 offset:20480
	ds_read_b128 v[82:85], v52 offset:21504
	ds_read_b128 v[86:89], v52 offset:22528
	ds_read_b128 v[90:93], v52 offset:23552
	global_load_lds_dwordx4 v38, s[6:7]
	v_add_u32_e32 v38, s28, v38
	s_mov_b32 m0, s31
	s_nop 0
	global_load_lds_dwordx4 v38, s[6:7]
	v_add_u32_e32 v38, s68, v41
	s_mov_b32 m0, s35
	s_nop 0
	global_load_lds_dwordx4 v38, s[6:7]
	v_add_u32_e32 v38, s28, v38
	s_mov_b32 m0, s44
	s_nop 0
	global_load_lds_dwordx4 v38, s[6:7]
	v_add_u32_e32 v38, s67, v1
	s_mov_b32 m0, s29
	s_nop 0
	global_load_lds_dwordx4 v38, s[4:5]
	v_add_u32_e32 v38, s25, v38
	s_mov_b32 m0, s45
	s_nop 0
	global_load_lds_dwordx4 v38, s[4:5]
	s_waitcnt vmcnt(8)
	s_waitcnt lgkmcnt(0)
	s_setprio 1
	s_barrier
	s_waitcnt lgkmcnt(0)
	v_mfma_f32_16x16x32_bf16 v[14:17], v[54:57], v[62:65], v[14:17]
	v_mfma_f32_16x16x32_bf16 v[10:13], v[54:57], v[70:73], v[10:13]
	v_mfma_f32_16x16x32_bf16 v[6:9], v[54:57], v[78:81], v[6:9]
	v_mfma_f32_16x16x32_bf16 v[2:5], v[54:57], v[86:89], v[2:5]
	v_mfma_f32_16x16x32_bf16 v[14:17], v[58:61], v[66:69], v[14:17]
	v_mfma_f32_16x16x32_bf16 v[10:13], v[58:61], v[74:77], v[10:13]
	v_mfma_f32_16x16x32_bf16 v[6:9], v[58:61], v[82:85], v[6:9]
	v_mfma_f32_16x16x32_bf16 v[2:5], v[58:61], v[90:93], v[2:5]
	s_setprio 0
	s_setprio 1
	s_setprio 0
	s_barrier
	ds_read_b128 v[54:57], v47
	ds_read_b128 v[58:61], v49
	s_mov_b32 m0, s46
	v_add_u32_e32 v38, s67, v42
	ds_read_b128 v[62:65], v52 offset:32768
	ds_read_b128 v[66:69], v52 offset:33792
	ds_read_b128 v[70:73], v52 offset:34816
	ds_read_b128 v[74:77], v52 offset:35840
	ds_read_b128 v[78:81], v52 offset:36864
	ds_read_b128 v[82:85], v52 offset:37888
	ds_read_b128 v[86:89], v52 offset:38912
	ds_read_b128 v[90:93], v52 offset:39936
	global_load_lds_dwordx4 v38, s[4:5]
	v_add_u32_e32 v38, s25, v38
	s_mov_b32 m0, s47
	s_nop 0
	global_load_lds_dwordx4 v38, s[4:5]
	s_waitcnt vmcnt(8)
	s_waitcnt lgkmcnt(0)
	s_setprio 1
	s_barrier
	s_waitcnt lgkmcnt(0)
	v_mfma_f32_16x16x32_bf16 v[26:29], v[54:57], v[62:65], v[26:29]
	v_mfma_f32_16x16x32_bf16 v[30:33], v[54:57], v[70:73], v[30:33]
	v_mfma_f32_16x16x32_bf16 v[22:25], v[54:57], v[78:81], v[22:25]
	v_mfma_f32_16x16x32_bf16 v[18:21], v[54:57], v[86:89], v[18:21]
	v_mfma_f32_16x16x32_bf16 v[26:29], v[58:61], v[66:69], v[26:29]
	v_mfma_f32_16x16x32_bf16 v[30:33], v[58:61], v[74:77], v[30:33]
	v_mfma_f32_16x16x32_bf16 v[22:25], v[58:61], v[82:85], v[22:25]
	v_mfma_f32_16x16x32_bf16 v[18:21], v[58:61], v[90:93], v[18:21]
	s_setprio 0
	s_setprio 1
	s_setprio 0
	s_barrier
	s_addk_i32 s68, 0x80
	s_mov_b32 m0, s50
	v_add_u32_e32 v38, s68, v40
	ds_read_b128 v[62:65], v52 offset:49152
	ds_read_b128 v[66:69], v52 offset:50176
	ds_read_b128 v[70:73], v52 offset:51200
	ds_read_b128 v[74:77], v52 offset:52224
	ds_read_b128 v[78:81], v52 offset:53248
	ds_read_b128 v[82:85], v52 offset:54272
	ds_read_b128 v[86:89], v52 offset:55296
	ds_read_b128 v[90:93], v52 offset:56320
	global_load_lds_dwordx4 v38, s[6:7]
	v_add_u32_e32 v38, s28, v38
	s_mov_b32 m0, s51
	s_nop 0
	global_load_lds_dwordx4 v38, s[6:7]
	v_add_u32_e32 v38, s68, v41
	s_mov_b32 m0, s54
	s_nop 0
	global_load_lds_dwordx4 v38, s[6:7]
	v_add_u32_e32 v38, s28, v38
	s_mov_b32 m0, s55
	s_nop 0
	global_load_lds_dwordx4 v38, s[6:7]
	v_add_u32_e32 v38, s67, v43
	s_mov_b32 m0, s52
	s_nop 0
	global_load_lds_dwordx4 v38, s[4:5]
	v_add_u32_e32 v38, s25, v38
	s_mov_b32 m0, s53
	s_nop 0
	global_load_lds_dwordx4 v38, s[4:5]
	s_waitcnt vmcnt(8)
	s_waitcnt lgkmcnt(0)
	s_setprio 1
	s_barrier
	s_waitcnt lgkmcnt(0)
	v_mfma_f32_16x16x32_bf16 v[14:17], v[54:57], v[62:65], v[14:17]
	v_mfma_f32_16x16x32_bf16 v[10:13], v[54:57], v[70:73], v[10:13]
	v_mfma_f32_16x16x32_bf16 v[6:9], v[54:57], v[78:81], v[6:9]
	v_mfma_f32_16x16x32_bf16 v[2:5], v[54:57], v[86:89], v[2:5]
	v_mfma_f32_16x16x32_bf16 v[14:17], v[58:61], v[66:69], v[14:17]
	v_mfma_f32_16x16x32_bf16 v[10:13], v[58:61], v[74:77], v[10:13]
	v_mfma_f32_16x16x32_bf16 v[6:9], v[58:61], v[82:85], v[6:9]
	v_mfma_f32_16x16x32_bf16 v[2:5], v[58:61], v[90:93], v[2:5]
	s_setprio 0
	s_setprio 1
	s_setprio 0
	s_barrier
	s_add_i32 s66, s66, 2
	s_addk_i32 s22, 0x100
	s_addk_i32 s65, 0x100
	s_cmp_ge_i32 s66, s56
	s_cbranch_scc0 .LBB0_584

.LBB0_603:
	ds_read_b128 v[164:167], v147
	ds_read_b128 v[168:171], v148
	ds_read_b128 v[172:175], v143
	ds_read_b128 v[176:179], v144
	ds_read_b128 v[180:183], v149
	ds_read_b128 v[184:187], v150
	ds_read_b128 v[188:191], v151
	ds_read_b128 v[192:195], v152
	s_add_i32 s75, s16, 0x80
	s_cmp_eq_u32 s59, s74
	s_cselect_b32 s76, s17, s73
	s_cselect_b32 s75, s72, s75
	v_add_u32_e32 v134, s16, v160
	s_add_i32 m0, s28, 0xc000
	ds_read_b128 v[196:199], v161
	ds_read_b128 v[200:203], v161 offset:1024
	ds_read_b128 v[204:207], v161 offset:2048
	ds_read_b128 v[214:217], v161 offset:3072
	ds_read_b128 v[218:221], v161 offset:4096
	ds_read_b128 v[222:225], v161 offset:5120
	ds_read_b128 v[226:229], v161 offset:6144
	ds_read_b128 v[230:233], v161 offset:7168
	global_load_lds_dwordx4 v134, s[4:5]
	v_add_u32_e32 v134, s16, v159
	s_add_i32 m0, s28, 0xe000
	s_nop 0
	global_load_lds_dwordx4 v134, s[4:5]
	s_waitcnt vmcnt(8)
	s_waitcnt lgkmcnt(0)
	s_setprio 1
	s_barrier
	s_waitcnt lgkmcnt(0)
	v_mfma_f32_16x16x32_bf16 v[126:129], v[172:175], v[196:199], v[126:129]
	v_mfma_f32_16x16x32_bf16 v[122:125], v[168:171], v[196:199], v[122:125]
	v_mfma_f32_16x16x32_bf16 v[110:113], v[172:175], v[204:207], v[110:113]
	v_mfma_f32_16x16x32_bf16 v[106:109], v[168:171], v[204:207], v[106:109]
	v_mfma_f32_16x16x32_bf16 v[94:97], v[172:175], v[218:221], v[94:97]
	v_mfma_f32_16x16x32_bf16 v[90:93], v[168:171], v[218:221], v[90:93]
	v_mfma_f32_16x16x32_bf16 v[78:81], v[172:175], v[226:229], v[78:81]
	v_mfma_f32_16x16x32_bf16 v[74:77], v[168:171], v[226:229], v[74:77]
	v_mfma_f32_16x16x32_bf16 v[126:129], v[164:167], v[200:203], v[126:129]
	v_mfma_f32_16x16x32_bf16 v[122:125], v[180:183], v[200:203], v[122:125]
	v_mfma_f32_16x16x32_bf16 v[110:113], v[164:167], v[214:217], v[110:113]
	v_mfma_f32_16x16x32_bf16 v[106:109], v[180:183], v[214:217], v[106:109]
	v_mfma_f32_16x16x32_bf16 v[94:97], v[164:167], v[222:225], v[94:97]
	v_mfma_f32_16x16x32_bf16 v[90:93], v[180:183], v[222:225], v[90:93]
	v_mfma_f32_16x16x32_bf16 v[78:81], v[164:167], v[230:233], v[78:81]
	v_mfma_f32_16x16x32_bf16 v[74:77], v[180:183], v[230:233], v[74:77]
	s_setprio 0
	s_setprio 1
	v_mfma_f32_16x16x32_bf16 v[118:121], v[176:179], v[196:199], v[118:121]
	v_mfma_f32_16x16x32_bf16 v[114:117], v[188:191], v[196:199], v[114:117]
	v_mfma_f32_16x16x32_bf16 v[102:105], v[176:179], v[204:207], v[102:105]
	v_mfma_f32_16x16x32_bf16 v[98:101], v[188:191], v[204:207], v[98:101]
	v_mfma_f32_16x16x32_bf16 v[86:89], v[176:179], v[218:221], v[86:89]
	v_mfma_f32_16x16x32_bf16 v[82:85], v[188:191], v[218:221], v[82:85]
	v_mfma_f32_16x16x32_bf16 v[70:73], v[176:179], v[226:229], v[70:73]
	v_mfma_f32_16x16x32_bf16 v[66:69], v[188:191], v[226:229], v[66:69]
	v_mfma_f32_16x16x32_bf16 v[118:121], v[184:187], v[200:203], v[118:121]
	v_mfma_f32_16x16x32_bf16 v[114:117], v[192:195], v[200:203], v[114:117]
	v_mfma_f32_16x16x32_bf16 v[102:105], v[184:187], v[214:217], v[102:105]
	v_mfma_f32_16x16x32_bf16 v[98:101], v[192:195], v[214:217], v[98:101]
	v_mfma_f32_16x16x32_bf16 v[86:89], v[184:187], v[222:225], v[86:89]
	v_mfma_f32_16x16x32_bf16 v[82:85], v[192:195], v[222:225], v[82:85]
	v_mfma_f32_16x16x32_bf16 v[70:73], v[184:187], v[230:233], v[70:73]
	v_mfma_f32_16x16x32_bf16 v[66:69], v[192:195], v[230:233], v[66:69]
	s_setprio 0
	s_barrier
	s_mov_b32 m0, s29
	v_add_u32_e32 v134, s76, v135
	ds_read_b128 v[196:199], v161 offset:16384
	ds_read_b128 v[200:203], v161 offset:17408
	ds_read_b128 v[204:207], v161 offset:18432
	ds_read_b128 v[214:217], v161 offset:19456
	ds_read_b128 v[218:221], v161 offset:20480
	ds_read_b128 v[222:225], v161 offset:21504
	ds_read_b128 v[226:229], v161 offset:22528
	ds_read_b128 v[230:233], v161 offset:23552
	global_load_lds_dwordx4 v134, s[6:7]
	v_add_u32_e32 v134, s23, v134
	s_mov_b32 m0, s30
	s_nop 0
	global_load_lds_dwordx4 v134, s[6:7]
	v_add_u32_e32 v134, s76, v138
	s_mov_b32 m0, s31
	s_nop 0
	global_load_lds_dwordx4 v134, s[6:7]
	v_add_u32_e32 v134, s23, v134
	s_mov_b32 m0, s35
	s_nop 0
	global_load_lds_dwordx4 v134, s[6:7]
	v_add_u32_e32 v134, s75, v1
	s_mov_b32 m0, s28
	s_nop 0
	global_load_lds_dwordx4 v134, s[4:5]
	v_add_u32_e32 v134, s22, v134
	s_mov_b32 m0, s44
	s_nop 0
	global_load_lds_dwordx4 v134, s[4:5]
	s_waitcnt vmcnt(8)
	s_waitcnt lgkmcnt(0)
	s_setprio 1
	s_barrier
	s_waitcnt lgkmcnt(0)
	v_mfma_f32_16x16x32_bf16 v[62:65], v[172:175], v[196:199], v[62:65]
	v_mfma_f32_16x16x32_bf16 v[58:61], v[168:171], v[196:199], v[58:61]
	v_mfma_f32_16x16x32_bf16 v[46:49], v[172:175], v[204:207], v[46:49]
	v_mfma_f32_16x16x32_bf16 v[42:45], v[168:171], v[204:207], v[42:45]
	v_mfma_f32_16x16x32_bf16 v[30:33], v[172:175], v[218:221], v[30:33]
	v_mfma_f32_16x16x32_bf16 v[26:29], v[168:171], v[218:221], v[26:29]
	v_mfma_f32_16x16x32_bf16 v[14:17], v[172:175], v[226:229], v[14:17]
	v_mfma_f32_16x16x32_bf16 v[10:13], v[168:171], v[226:229], v[10:13]
	v_mfma_f32_16x16x32_bf16 v[62:65], v[164:167], v[200:203], v[62:65]
	v_mfma_f32_16x16x32_bf16 v[58:61], v[180:183], v[200:203], v[58:61]
	v_mfma_f32_16x16x32_bf16 v[46:49], v[164:167], v[214:217], v[46:49]
	v_mfma_f32_16x16x32_bf16 v[42:45], v[180:183], v[214:217], v[42:45]
	v_mfma_f32_16x16x32_bf16 v[30:33], v[164:167], v[222:225], v[30:33]
	v_mfma_f32_16x16x32_bf16 v[26:29], v[180:183], v[222:225], v[26:29]
	v_mfma_f32_16x16x32_bf16 v[14:17], v[164:167], v[230:233], v[14:17]
	v_mfma_f32_16x16x32_bf16 v[10:13], v[180:183], v[230:233], v[10:13]
	s_setprio 0
	s_setprio 1
	v_mfma_f32_16x16x32_bf16 v[54:57], v[176:179], v[196:199], v[54:57]
	v_mfma_f32_16x16x32_bf16 v[50:53], v[188:191], v[196:199], v[50:53]
	v_mfma_f32_16x16x32_bf16 v[38:41], v[176:179], v[204:207], v[38:41]
	v_mfma_f32_16x16x32_bf16 v[34:37], v[188:191], v[204:207], v[34:37]
	v_mfma_f32_16x16x32_bf16 v[22:25], v[176:179], v[218:221], v[22:25]
	v_mfma_f32_16x16x32_bf16 v[18:21], v[188:191], v[218:221], v[18:21]
	v_mfma_f32_16x16x32_bf16 v[6:9], v[176:179], v[226:229], v[6:9]
	v_mfma_f32_16x16x32_bf16 v[2:5], v[188:191], v[226:229], v[2:5]
	v_mfma_f32_16x16x32_bf16 v[54:57], v[184:187], v[200:203], v[54:57]
	v_mfma_f32_16x16x32_bf16 v[50:53], v[192:195], v[200:203], v[50:53]
	v_mfma_f32_16x16x32_bf16 v[38:41], v[184:187], v[214:217], v[38:41]
	v_mfma_f32_16x16x32_bf16 v[34:37], v[192:195], v[214:217], v[34:37]
	v_mfma_f32_16x16x32_bf16 v[22:25], v[184:187], v[222:225], v[22:25]
	v_mfma_f32_16x16x32_bf16 v[18:21], v[192:195], v[222:225], v[18:21]
	v_mfma_f32_16x16x32_bf16 v[6:9], v[184:187], v[230:233], v[6:9]
	v_mfma_f32_16x16x32_bf16 v[2:5], v[192:195], v[230:233], v[2:5]
	s_setprio 0
	s_barrier
	ds_read_b128 v[164:167], v153
	ds_read_b128 v[168:171], v154
	ds_read_b128 v[172:175], v145
	ds_read_b128 v[176:179], v146
	ds_read_b128 v[180:183], v155
	ds_read_b128 v[184:187], v156
	ds_read_b128 v[188:191], v157
	ds_read_b128 v[192:195], v158
	s_mov_b32 m0, s45
	v_add_u32_e32 v134, s75, v139
	ds_read_b128 v[196:199], v161 offset:32768
	ds_read_b128 v[200:203], v161 offset:33792
	ds_read_b128 v[204:207], v161 offset:34816
	ds_read_b128 v[214:217], v161 offset:35840
	ds_read_b128 v[218:221], v161 offset:36864
	ds_read_b128 v[222:225], v161 offset:37888
	ds_read_b128 v[226:229], v161 offset:38912
	ds_read_b128 v[230:233], v161 offset:39936
	global_load_lds_dwordx4 v134, s[4:5]
	v_add_u32_e32 v134, s22, v134
	s_mov_b32 m0, s46
	s_nop 0
	global_load_lds_dwordx4 v134, s[4:5]
	s_waitcnt vmcnt(8)
	s_waitcnt lgkmcnt(0)
	s_setprio 1
	s_barrier
	s_waitcnt lgkmcnt(0)
	v_mfma_f32_16x16x32_bf16 v[126:129], v[172:175], v[196:199], v[126:129]
	v_mfma_f32_16x16x32_bf16 v[122:125], v[168:171], v[196:199], v[122:125]
	v_mfma_f32_16x16x32_bf16 v[110:113], v[172:175], v[204:207], v[110:113]
	v_mfma_f32_16x16x32_bf16 v[106:109], v[168:171], v[204:207], v[106:109]
	v_mfma_f32_16x16x32_bf16 v[94:97], v[172:175], v[218:221], v[94:97]
	v_mfma_f32_16x16x32_bf16 v[90:93], v[168:171], v[218:221], v[90:93]
	v_mfma_f32_16x16x32_bf16 v[78:81], v[172:175], v[226:229], v[78:81]
	v_mfma_f32_16x16x32_bf16 v[74:77], v[168:171], v[226:229], v[74:77]
	v_mfma_f32_16x16x32_bf16 v[126:129], v[164:167], v[200:203], v[126:129]
	v_mfma_f32_16x16x32_bf16 v[122:125], v[180:183], v[200:203], v[122:125]
	v_mfma_f32_16x16x32_bf16 v[110:113], v[164:167], v[214:217], v[110:113]
	v_mfma_f32_16x16x32_bf16 v[106:109], v[180:183], v[214:217], v[106:109]
	v_mfma_f32_16x16x32_bf16 v[94:97], v[164:167], v[222:225], v[94:97]
	v_mfma_f32_16x16x32_bf16 v[90:93], v[180:183], v[222:225], v[90:93]
	v_mfma_f32_16x16x32_bf16 v[78:81], v[164:167], v[230:233], v[78:81]
	v_mfma_f32_16x16x32_bf16 v[74:77], v[180:183], v[230:233], v[74:77]
	s_setprio 0
	s_setprio 1
	v_mfma_f32_16x16x32_bf16 v[118:121], v[176:179], v[196:199], v[118:121]
	v_mfma_f32_16x16x32_bf16 v[114:117], v[188:191], v[196:199], v[114:117]
	v_mfma_f32_16x16x32_bf16 v[102:105], v[176:179], v[204:207], v[102:105]
	v_mfma_f32_16x16x32_bf16 v[98:101], v[188:191], v[204:207], v[98:101]
	v_mfma_f32_16x16x32_bf16 v[86:89], v[176:179], v[218:221], v[86:89]
	v_mfma_f32_16x16x32_bf16 v[82:85], v[188:191], v[218:221], v[82:85]
	v_mfma_f32_16x16x32_bf16 v[70:73], v[176:179], v[226:229], v[70:73]
	v_mfma_f32_16x16x32_bf16 v[66:69], v[188:191], v[226:229], v[66:69]
	v_mfma_f32_16x16x32_bf16 v[118:121], v[184:187], v[200:203], v[118:121]
	v_mfma_f32_16x16x32_bf16 v[114:117], v[192:195], v[200:203], v[114:117]
	v_mfma_f32_16x16x32_bf16 v[102:105], v[184:187], v[214:217], v[102:105]
	v_mfma_f32_16x16x32_bf16 v[98:101], v[192:195], v[214:217], v[98:101]
	v_mfma_f32_16x16x32_bf16 v[86:89], v[184:187], v[222:225], v[86:89]
	v_mfma_f32_16x16x32_bf16 v[82:85], v[192:195], v[222:225], v[82:85]
	v_mfma_f32_16x16x32_bf16 v[70:73], v[184:187], v[230:233], v[70:73]
	v_mfma_f32_16x16x32_bf16 v[66:69], v[192:195], v[230:233], v[66:69]
	s_setprio 0
	s_barrier
	s_addk_i32 s76, 0x80
	s_mov_b32 m0, s48
	v_add_u32_e32 v134, s76, v135
	ds_read_b128 v[196:199], v161 offset:49152
	ds_read_b128 v[200:203], v161 offset:50176
	ds_read_b128 v[204:207], v161 offset:51200
	ds_read_b128 v[214:217], v161 offset:52224
	ds_read_b128 v[218:221], v161 offset:53248
	ds_read_b128 v[222:225], v161 offset:54272
	ds_read_b128 v[226:229], v161 offset:55296
	ds_read_b128 v[230:233], v161 offset:56320
	global_load_lds_dwordx4 v134, s[6:7]
	v_add_u32_e32 v134, s23, v134
	s_mov_b32 m0, s49
	s_nop 0
	global_load_lds_dwordx4 v134, s[6:7]
	v_add_u32_e32 v134, s76, v138
	s_mov_b32 m0, s52
	s_nop 0
	global_load_lds_dwordx4 v134, s[6:7]
	v_add_u32_e32 v134, s23, v134
	s_mov_b32 m0, s53
	s_nop 0
	global_load_lds_dwordx4 v134, s[6:7]
	v_add_u32_e32 v134, s75, v140
	s_mov_b32 m0, s50
	s_nop 0
	global_load_lds_dwordx4 v134, s[4:5]
	v_add_u32_e32 v134, s22, v134
	s_mov_b32 m0, s51
	s_nop 0
	global_load_lds_dwordx4 v134, s[4:5]
	s_waitcnt vmcnt(8)
	s_waitcnt lgkmcnt(0)
	s_setprio 1
	s_barrier
	s_waitcnt lgkmcnt(0)
	v_mfma_f32_16x16x32_bf16 v[62:65], v[172:175], v[196:199], v[62:65]
	v_mfma_f32_16x16x32_bf16 v[58:61], v[168:171], v[196:199], v[58:61]
	v_mfma_f32_16x16x32_bf16 v[46:49], v[172:175], v[204:207], v[46:49]
	v_mfma_f32_16x16x32_bf16 v[42:45], v[168:171], v[204:207], v[42:45]
	v_mfma_f32_16x16x32_bf16 v[30:33], v[172:175], v[218:221], v[30:33]
	v_mfma_f32_16x16x32_bf16 v[26:29], v[168:171], v[218:221], v[26:29]
	v_mfma_f32_16x16x32_bf16 v[14:17], v[172:175], v[226:229], v[14:17]
	v_mfma_f32_16x16x32_bf16 v[10:13], v[168:171], v[226:229], v[10:13]
	v_mfma_f32_16x16x32_bf16 v[62:65], v[164:167], v[200:203], v[62:65]
	v_mfma_f32_16x16x32_bf16 v[58:61], v[180:183], v[200:203], v[58:61]
	v_mfma_f32_16x16x32_bf16 v[46:49], v[164:167], v[214:217], v[46:49]
	v_mfma_f32_16x16x32_bf16 v[42:45], v[180:183], v[214:217], v[42:45]
	v_mfma_f32_16x16x32_bf16 v[30:33], v[164:167], v[222:225], v[30:33]
	v_mfma_f32_16x16x32_bf16 v[26:29], v[180:183], v[222:225], v[26:29]
	v_mfma_f32_16x16x32_bf16 v[14:17], v[164:167], v[230:233], v[14:17]
	v_mfma_f32_16x16x32_bf16 v[10:13], v[180:183], v[230:233], v[10:13]
	s_setprio 0
	s_setprio 1
	v_mfma_f32_16x16x32_bf16 v[54:57], v[176:179], v[196:199], v[54:57]
	v_mfma_f32_16x16x32_bf16 v[50:53], v[188:191], v[196:199], v[50:53]
	v_mfma_f32_16x16x32_bf16 v[38:41], v[176:179], v[204:207], v[38:41]
	v_mfma_f32_16x16x32_bf16 v[34:37], v[188:191], v[204:207], v[34:37]
	v_mfma_f32_16x16x32_bf16 v[22:25], v[176:179], v[218:221], v[22:25]
	v_mfma_f32_16x16x32_bf16 v[18:21], v[188:191], v[218:221], v[18:21]
	v_mfma_f32_16x16x32_bf16 v[6:9], v[176:179], v[226:229], v[6:9]
	v_mfma_f32_16x16x32_bf16 v[2:5], v[188:191], v[226:229], v[2:5]
	v_mfma_f32_16x16x32_bf16 v[54:57], v[184:187], v[200:203], v[54:57]
	v_mfma_f32_16x16x32_bf16 v[50:53], v[192:195], v[200:203], v[50:53]
	v_mfma_f32_16x16x32_bf16 v[38:41], v[184:187], v[214:217], v[38:41]
	v_mfma_f32_16x16x32_bf16 v[34:37], v[192:195], v[214:217], v[34:37]
	v_mfma_f32_16x16x32_bf16 v[22:25], v[184:187], v[222:225], v[22:25]
	v_mfma_f32_16x16x32_bf16 v[18:21], v[192:195], v[222:225], v[18:21]
	v_mfma_f32_16x16x32_bf16 v[6:9], v[184:187], v[230:233], v[6:9]
	v_mfma_f32_16x16x32_bf16 v[2:5], v[192:195], v[230:233], v[2:5]
	s_setprio 0
	s_barrier
	s_add_i32 s74, s74, 2
	s_addk_i32 s16, 0x100
	s_addk_i32 s73, 0x100
	s_cmp_ge_i32 s74, s54
	s_cbranch_scc0 .LBB0_603

.LBB0_620:
	ds_read_b128 v[160:163], v144
	ds_read_b128 v[164:167], v145
	ds_read_b128 v[168:171], v140
	ds_read_b128 v[172:175], v141
	ds_read_b128 v[176:179], v146
	ds_read_b128 v[180:183], v147
	ds_read_b128 v[184:187], v148
	ds_read_b128 v[188:191], v149
	s_add_i32 s73, s16, 0x80
	s_cmp_eq_u32 s20, s72
	s_cselect_b32 s74, s15, s71
	s_cselect_b32 s73, s17, s73
	v_add_u32_e32 v159, s16, v157
	s_add_i32 m0, s28, 0xc000
	ds_read_b128 v[192:195], v158
	ds_read_b128 v[196:199], v158 offset:1024
	ds_read_b128 v[200:203], v158 offset:2048
	ds_read_b128 v[204:207], v158 offset:3072
	ds_read_b128 v[214:217], v158 offset:4096
	ds_read_b128 v[218:221], v158 offset:5120
	ds_read_b128 v[222:225], v158 offset:6144
	ds_read_b128 v[226:229], v158 offset:7168
	global_load_lds_dwordx4 v159, s[4:5]
	v_add_u32_e32 v159, s16, v156
	s_add_i32 m0, s28, 0xe000
	s_nop 0
	global_load_lds_dwordx4 v159, s[4:5]
	s_waitcnt vmcnt(8)
	s_waitcnt lgkmcnt(0)
	s_setprio 1
	s_barrier
	s_waitcnt lgkmcnt(0)
	v_mfma_f32_16x16x32_bf16 v[122:125], v[168:171], v[192:195], v[122:125]
	v_mfma_f32_16x16x32_bf16 v[126:129], v[164:167], v[192:195], v[126:129]
	v_mfma_f32_16x16x32_bf16 v[110:113], v[168:171], v[200:203], v[110:113]
	v_mfma_f32_16x16x32_bf16 v[106:109], v[164:167], v[200:203], v[106:109]
	v_mfma_f32_16x16x32_bf16 v[94:97], v[168:171], v[214:217], v[94:97]
	v_mfma_f32_16x16x32_bf16 v[90:93], v[164:167], v[214:217], v[90:93]
	v_mfma_f32_16x16x32_bf16 v[78:81], v[168:171], v[222:225], v[78:81]
	v_mfma_f32_16x16x32_bf16 v[74:77], v[164:167], v[222:225], v[74:77]
	v_mfma_f32_16x16x32_bf16 v[122:125], v[160:163], v[196:199], v[122:125]
	v_mfma_f32_16x16x32_bf16 v[126:129], v[176:179], v[196:199], v[126:129]
	v_mfma_f32_16x16x32_bf16 v[110:113], v[160:163], v[204:207], v[110:113]
	v_mfma_f32_16x16x32_bf16 v[106:109], v[176:179], v[204:207], v[106:109]
	v_mfma_f32_16x16x32_bf16 v[94:97], v[160:163], v[218:221], v[94:97]
	v_mfma_f32_16x16x32_bf16 v[90:93], v[176:179], v[218:221], v[90:93]
	v_mfma_f32_16x16x32_bf16 v[78:81], v[160:163], v[226:229], v[78:81]
	v_mfma_f32_16x16x32_bf16 v[74:77], v[176:179], v[226:229], v[74:77]
	s_setprio 0
	s_setprio 1
	v_mfma_f32_16x16x32_bf16 v[118:121], v[172:175], v[192:195], v[118:121]
	v_mfma_f32_16x16x32_bf16 v[114:117], v[184:187], v[192:195], v[114:117]
	v_mfma_f32_16x16x32_bf16 v[102:105], v[172:175], v[200:203], v[102:105]
	v_mfma_f32_16x16x32_bf16 v[98:101], v[184:187], v[200:203], v[98:101]
	v_mfma_f32_16x16x32_bf16 v[86:89], v[172:175], v[214:217], v[86:89]
	v_mfma_f32_16x16x32_bf16 v[82:85], v[184:187], v[214:217], v[82:85]
	v_mfma_f32_16x16x32_bf16 v[70:73], v[172:175], v[222:225], v[70:73]
	v_mfma_f32_16x16x32_bf16 v[66:69], v[184:187], v[222:225], v[66:69]
	v_mfma_f32_16x16x32_bf16 v[118:121], v[180:183], v[196:199], v[118:121]
	v_mfma_f32_16x16x32_bf16 v[114:117], v[188:191], v[196:199], v[114:117]
	v_mfma_f32_16x16x32_bf16 v[102:105], v[180:183], v[204:207], v[102:105]
	v_mfma_f32_16x16x32_bf16 v[98:101], v[188:191], v[204:207], v[98:101]
	v_mfma_f32_16x16x32_bf16 v[86:89], v[180:183], v[218:221], v[86:89]
	v_mfma_f32_16x16x32_bf16 v[82:85], v[188:191], v[218:221], v[82:85]
	v_mfma_f32_16x16x32_bf16 v[70:73], v[180:183], v[226:229], v[70:73]
	v_mfma_f32_16x16x32_bf16 v[66:69], v[188:191], v[226:229], v[66:69]
	s_setprio 0
	s_barrier
	s_mov_b32 m0, s29
	v_add_u32_e32 v159, s74, v134
	ds_read_b128 v[192:195], v158 offset:16384
	ds_read_b128 v[196:199], v158 offset:17408
	ds_read_b128 v[200:203], v158 offset:18432
	ds_read_b128 v[204:207], v158 offset:19456
	ds_read_b128 v[214:217], v158 offset:20480
	ds_read_b128 v[218:221], v158 offset:21504
	ds_read_b128 v[222:225], v158 offset:22528
	ds_read_b128 v[226:229], v158 offset:23552
	global_load_lds_dwordx4 v159, s[6:7]
	v_add_u32_e32 v159, s23, v159
	s_mov_b32 m0, s30
	s_nop 0
	global_load_lds_dwordx4 v159, s[6:7]
	v_add_u32_e32 v159, s74, v135
	s_mov_b32 m0, s31
	s_nop 0
	global_load_lds_dwordx4 v159, s[6:7]
	v_add_u32_e32 v159, s23, v159
	s_mov_b32 m0, s35
	s_nop 0
	global_load_lds_dwordx4 v159, s[6:7]
	v_add_u32_e32 v159, s73, v1
	s_mov_b32 m0, s28
	s_nop 0
	global_load_lds_dwordx4 v159, s[4:5]
	v_add_u32_e32 v159, s22, v159
	s_mov_b32 m0, s44
	s_nop 0
	global_load_lds_dwordx4 v159, s[4:5]
	s_waitcnt vmcnt(8)
	s_waitcnt lgkmcnt(0)
	s_setprio 1
	s_barrier
	s_waitcnt lgkmcnt(0)
	v_mfma_f32_16x16x32_bf16 v[62:65], v[168:171], v[192:195], v[62:65]
	v_mfma_f32_16x16x32_bf16 v[58:61], v[164:167], v[192:195], v[58:61]
	v_mfma_f32_16x16x32_bf16 v[46:49], v[168:171], v[200:203], v[46:49]
	v_mfma_f32_16x16x32_bf16 v[42:45], v[164:167], v[200:203], v[42:45]
	v_mfma_f32_16x16x32_bf16 v[30:33], v[168:171], v[214:217], v[30:33]
	v_mfma_f32_16x16x32_bf16 v[26:29], v[164:167], v[214:217], v[26:29]
	v_mfma_f32_16x16x32_bf16 v[14:17], v[168:171], v[222:225], v[14:17]
	v_mfma_f32_16x16x32_bf16 v[10:13], v[164:167], v[222:225], v[10:13]
	v_mfma_f32_16x16x32_bf16 v[62:65], v[160:163], v[196:199], v[62:65]
	v_mfma_f32_16x16x32_bf16 v[58:61], v[176:179], v[196:199], v[58:61]
	v_mfma_f32_16x16x32_bf16 v[46:49], v[160:163], v[204:207], v[46:49]
	v_mfma_f32_16x16x32_bf16 v[42:45], v[176:179], v[204:207], v[42:45]
	v_mfma_f32_16x16x32_bf16 v[30:33], v[160:163], v[218:221], v[30:33]
	v_mfma_f32_16x16x32_bf16 v[26:29], v[176:179], v[218:221], v[26:29]
	v_mfma_f32_16x16x32_bf16 v[14:17], v[160:163], v[226:229], v[14:17]
	v_mfma_f32_16x16x32_bf16 v[10:13], v[176:179], v[226:229], v[10:13]
	s_setprio 0
	s_setprio 1
	v_mfma_f32_16x16x32_bf16 v[54:57], v[172:175], v[192:195], v[54:57]
	v_mfma_f32_16x16x32_bf16 v[50:53], v[184:187], v[192:195], v[50:53]
	v_mfma_f32_16x16x32_bf16 v[38:41], v[172:175], v[200:203], v[38:41]
	v_mfma_f32_16x16x32_bf16 v[34:37], v[184:187], v[200:203], v[34:37]
	v_mfma_f32_16x16x32_bf16 v[22:25], v[172:175], v[214:217], v[22:25]
	v_mfma_f32_16x16x32_bf16 v[18:21], v[184:187], v[214:217], v[18:21]
	v_mfma_f32_16x16x32_bf16 v[6:9], v[172:175], v[222:225], v[6:9]
	v_mfma_f32_16x16x32_bf16 v[2:5], v[184:187], v[222:225], v[2:5]
	v_mfma_f32_16x16x32_bf16 v[54:57], v[180:183], v[196:199], v[54:57]
	v_mfma_f32_16x16x32_bf16 v[50:53], v[188:191], v[196:199], v[50:53]
	v_mfma_f32_16x16x32_bf16 v[38:41], v[180:183], v[204:207], v[38:41]
	v_mfma_f32_16x16x32_bf16 v[34:37], v[188:191], v[204:207], v[34:37]
	v_mfma_f32_16x16x32_bf16 v[22:25], v[180:183], v[218:221], v[22:25]
	v_mfma_f32_16x16x32_bf16 v[18:21], v[188:191], v[218:221], v[18:21]
	v_mfma_f32_16x16x32_bf16 v[6:9], v[180:183], v[226:229], v[6:9]
	v_mfma_f32_16x16x32_bf16 v[2:5], v[188:191], v[226:229], v[2:5]
	s_setprio 0
	s_barrier
	ds_read_b128 v[160:163], v150
	ds_read_b128 v[164:167], v151
	ds_read_b128 v[168:171], v142
	ds_read_b128 v[172:175], v143
	ds_read_b128 v[176:179], v152
	ds_read_b128 v[180:183], v153
	ds_read_b128 v[184:187], v154
	ds_read_b128 v[188:191], v155
	s_mov_b32 m0, s45
	v_add_u32_e32 v159, s73, v136
	ds_read_b128 v[192:195], v158 offset:32768
	ds_read_b128 v[196:199], v158 offset:33792
	ds_read_b128 v[200:203], v158 offset:34816
	ds_read_b128 v[204:207], v158 offset:35840
	ds_read_b128 v[214:217], v158 offset:36864
	ds_read_b128 v[218:221], v158 offset:37888
	ds_read_b128 v[222:225], v158 offset:38912
	ds_read_b128 v[226:229], v158 offset:39936
	global_load_lds_dwordx4 v159, s[4:5]
	v_add_u32_e32 v159, s22, v159
	s_mov_b32 m0, s46
	s_nop 0
	global_load_lds_dwordx4 v159, s[4:5]
	s_waitcnt vmcnt(8)
	s_waitcnt lgkmcnt(0)
	s_setprio 1
	s_barrier
	s_waitcnt lgkmcnt(0)
	v_mfma_f32_16x16x32_bf16 v[122:125], v[168:171], v[192:195], v[122:125]
	v_mfma_f32_16x16x32_bf16 v[126:129], v[164:167], v[192:195], v[126:129]
	v_mfma_f32_16x16x32_bf16 v[110:113], v[168:171], v[200:203], v[110:113]
	v_mfma_f32_16x16x32_bf16 v[106:109], v[164:167], v[200:203], v[106:109]
	v_mfma_f32_16x16x32_bf16 v[94:97], v[168:171], v[214:217], v[94:97]
	v_mfma_f32_16x16x32_bf16 v[90:93], v[164:167], v[214:217], v[90:93]
	v_mfma_f32_16x16x32_bf16 v[78:81], v[168:171], v[222:225], v[78:81]
	v_mfma_f32_16x16x32_bf16 v[74:77], v[164:167], v[222:225], v[74:77]
	v_mfma_f32_16x16x32_bf16 v[122:125], v[160:163], v[196:199], v[122:125]
	v_mfma_f32_16x16x32_bf16 v[126:129], v[176:179], v[196:199], v[126:129]
	v_mfma_f32_16x16x32_bf16 v[110:113], v[160:163], v[204:207], v[110:113]
	v_mfma_f32_16x16x32_bf16 v[106:109], v[176:179], v[204:207], v[106:109]
	v_mfma_f32_16x16x32_bf16 v[94:97], v[160:163], v[218:221], v[94:97]
	v_mfma_f32_16x16x32_bf16 v[90:93], v[176:179], v[218:221], v[90:93]
	v_mfma_f32_16x16x32_bf16 v[78:81], v[160:163], v[226:229], v[78:81]
	v_mfma_f32_16x16x32_bf16 v[74:77], v[176:179], v[226:229], v[74:77]
	s_setprio 0
	s_setprio 1
	v_mfma_f32_16x16x32_bf16 v[118:121], v[172:175], v[192:195], v[118:121]
	v_mfma_f32_16x16x32_bf16 v[114:117], v[184:187], v[192:195], v[114:117]
	v_mfma_f32_16x16x32_bf16 v[102:105], v[172:175], v[200:203], v[102:105]
	v_mfma_f32_16x16x32_bf16 v[98:101], v[184:187], v[200:203], v[98:101]
	v_mfma_f32_16x16x32_bf16 v[86:89], v[172:175], v[214:217], v[86:89]
	v_mfma_f32_16x16x32_bf16 v[82:85], v[184:187], v[214:217], v[82:85]
	v_mfma_f32_16x16x32_bf16 v[70:73], v[172:175], v[222:225], v[70:73]
	v_mfma_f32_16x16x32_bf16 v[66:69], v[184:187], v[222:225], v[66:69]
	v_mfma_f32_16x16x32_bf16 v[118:121], v[180:183], v[196:199], v[118:121]
	v_mfma_f32_16x16x32_bf16 v[114:117], v[188:191], v[196:199], v[114:117]
	v_mfma_f32_16x16x32_bf16 v[102:105], v[180:183], v[204:207], v[102:105]
	v_mfma_f32_16x16x32_bf16 v[98:101], v[188:191], v[204:207], v[98:101]
	v_mfma_f32_16x16x32_bf16 v[86:89], v[180:183], v[218:221], v[86:89]
	v_mfma_f32_16x16x32_bf16 v[82:85], v[188:191], v[218:221], v[82:85]
	v_mfma_f32_16x16x32_bf16 v[70:73], v[180:183], v[226:229], v[70:73]
	v_mfma_f32_16x16x32_bf16 v[66:69], v[188:191], v[226:229], v[66:69]
	s_setprio 0
	s_barrier
	s_addk_i32 s74, 0x80
	s_mov_b32 m0, s49
	v_add_u32_e32 v159, s74, v134
	ds_read_b128 v[192:195], v158 offset:49152
	ds_read_b128 v[196:199], v158 offset:50176
	ds_read_b128 v[200:203], v158 offset:51200
	ds_read_b128 v[204:207], v158 offset:52224
	ds_read_b128 v[214:217], v158 offset:53248
	ds_read_b128 v[218:221], v158 offset:54272
	ds_read_b128 v[222:225], v158 offset:55296
	ds_read_b128 v[226:229], v158 offset:56320
	global_load_lds_dwordx4 v159, s[6:7]
	v_add_u32_e32 v159, s23, v159
	s_mov_b32 m0, s50
	s_nop 0
	global_load_lds_dwordx4 v159, s[6:7]
	v_add_u32_e32 v159, s74, v135
	s_mov_b32 m0, s53
	s_nop 0
	global_load_lds_dwordx4 v159, s[6:7]
	v_add_u32_e32 v159, s23, v159
	s_mov_b32 m0, s54
	s_nop 0
	global_load_lds_dwordx4 v159, s[6:7]
	v_add_u32_e32 v159, s73, v137
	s_mov_b32 m0, s51
	s_nop 0
	global_load_lds_dwordx4 v159, s[4:5]
	v_add_u32_e32 v159, s22, v159
	s_mov_b32 m0, s52
	s_nop 0
	global_load_lds_dwordx4 v159, s[4:5]
	s_waitcnt vmcnt(8)
	s_waitcnt lgkmcnt(0)
	s_setprio 1
	s_barrier
	s_waitcnt lgkmcnt(0)
	v_mfma_f32_16x16x32_bf16 v[62:65], v[168:171], v[192:195], v[62:65]
	v_mfma_f32_16x16x32_bf16 v[58:61], v[164:167], v[192:195], v[58:61]
	v_mfma_f32_16x16x32_bf16 v[46:49], v[168:171], v[200:203], v[46:49]
	v_mfma_f32_16x16x32_bf16 v[42:45], v[164:167], v[200:203], v[42:45]
	v_mfma_f32_16x16x32_bf16 v[30:33], v[168:171], v[214:217], v[30:33]
	v_mfma_f32_16x16x32_bf16 v[26:29], v[164:167], v[214:217], v[26:29]
	v_mfma_f32_16x16x32_bf16 v[14:17], v[168:171], v[222:225], v[14:17]
	v_mfma_f32_16x16x32_bf16 v[10:13], v[164:167], v[222:225], v[10:13]
	v_mfma_f32_16x16x32_bf16 v[62:65], v[160:163], v[196:199], v[62:65]
	v_mfma_f32_16x16x32_bf16 v[58:61], v[176:179], v[196:199], v[58:61]
	v_mfma_f32_16x16x32_bf16 v[46:49], v[160:163], v[204:207], v[46:49]
	v_mfma_f32_16x16x32_bf16 v[42:45], v[176:179], v[204:207], v[42:45]
	v_mfma_f32_16x16x32_bf16 v[30:33], v[160:163], v[218:221], v[30:33]
	v_mfma_f32_16x16x32_bf16 v[26:29], v[176:179], v[218:221], v[26:29]
	v_mfma_f32_16x16x32_bf16 v[14:17], v[160:163], v[226:229], v[14:17]
	v_mfma_f32_16x16x32_bf16 v[10:13], v[176:179], v[226:229], v[10:13]
	s_setprio 0
	s_setprio 1
	v_mfma_f32_16x16x32_bf16 v[54:57], v[172:175], v[192:195], v[54:57]
	v_mfma_f32_16x16x32_bf16 v[50:53], v[184:187], v[192:195], v[50:53]
	v_mfma_f32_16x16x32_bf16 v[38:41], v[172:175], v[200:203], v[38:41]
	v_mfma_f32_16x16x32_bf16 v[34:37], v[184:187], v[200:203], v[34:37]
	v_mfma_f32_16x16x32_bf16 v[22:25], v[172:175], v[214:217], v[22:25]
	v_mfma_f32_16x16x32_bf16 v[18:21], v[184:187], v[214:217], v[18:21]
	v_mfma_f32_16x16x32_bf16 v[6:9], v[172:175], v[222:225], v[6:9]
	v_mfma_f32_16x16x32_bf16 v[2:5], v[184:187], v[222:225], v[2:5]
	v_mfma_f32_16x16x32_bf16 v[54:57], v[180:183], v[196:199], v[54:57]
	v_mfma_f32_16x16x32_bf16 v[50:53], v[188:191], v[196:199], v[50:53]
	v_mfma_f32_16x16x32_bf16 v[38:41], v[180:183], v[204:207], v[38:41]
	v_mfma_f32_16x16x32_bf16 v[34:37], v[188:191], v[204:207], v[34:37]
	v_mfma_f32_16x16x32_bf16 v[22:25], v[180:183], v[218:221], v[22:25]
	v_mfma_f32_16x16x32_bf16 v[18:21], v[188:191], v[218:221], v[18:21]
	v_mfma_f32_16x16x32_bf16 v[6:9], v[180:183], v[226:229], v[6:9]
	v_mfma_f32_16x16x32_bf16 v[2:5], v[188:191], v[226:229], v[2:5]
	s_setprio 0
	s_barrier
	s_add_i32 s72, s72, 2
	s_addk_i32 s16, 0x100
	s_addk_i32 s71, 0x100
	s_cmp_ge_i32 s72, s55
	s_cbranch_scc0 .LBB0_620

.LBB0_637:
	ds_read_b128 v[130:133], v188
	ds_read_b128 v[134:137], v189
	ds_read_b128 v[138:141], v184
	ds_read_b128 v[142:145], v185
	ds_read_b128 v[146:149], v190
	ds_read_b128 v[150:153], v191
	ds_read_b128 v[154:157], v192
	ds_read_b128 v[158:161], v193
	s_add_i32 s75, s28, 0x80
	s_cmp_eq_u32 s66, s80
	s_cselect_b32 s81, s25, s79
	s_cselect_b32 s75, s29, s75
	v_add_u32_e32 v203, s28, v201
	s_add_i32 m0, s46, 0xc000
	ds_read_b128 v[162:165], v202
	ds_read_b128 v[166:169], v202 offset:1024
	ds_read_b128 v[170:173], v202 offset:2048
	ds_read_b128 v[204:207], v202 offset:3072
	ds_read_b128 v[214:217], v202 offset:4096
	ds_read_b128 v[218:221], v202 offset:5120
	ds_read_b128 v[222:225], v202 offset:6144
	ds_read_b128 v[226:229], v202 offset:7168
	global_load_lds_dwordx4 v203, s[4:5]
	v_add_u32_e32 v203, s28, v200
	s_add_i32 m0, s46, 0xe000
	s_nop 0
	global_load_lds_dwordx4 v203, s[4:5]
	s_waitcnt vmcnt(8)
	s_waitcnt lgkmcnt(0)
	s_setprio 1
	s_barrier
	s_waitcnt lgkmcnt(0)
	v_mfma_f32_16x16x32_bf16 v[126:129], v[138:141], v[162:165], v[126:129]
	v_mfma_f32_16x16x32_bf16 v[118:121], v[134:137], v[162:165], v[118:121]
	v_mfma_f32_16x16x32_bf16 v[110:113], v[138:141], v[170:173], v[110:113]
	v_mfma_f32_16x16x32_bf16 v[102:105], v[134:137], v[170:173], v[102:105]
	v_mfma_f32_16x16x32_bf16 v[94:97], v[138:141], v[214:217], v[94:97]
	v_mfma_f32_16x16x32_bf16 v[86:89], v[134:137], v[214:217], v[86:89]
	v_mfma_f32_16x16x32_bf16 v[78:81], v[138:141], v[222:225], v[78:81]
	v_mfma_f32_16x16x32_bf16 v[70:73], v[134:137], v[222:225], v[70:73]
	v_mfma_f32_16x16x32_bf16 v[126:129], v[130:133], v[166:169], v[126:129]
	v_mfma_f32_16x16x32_bf16 v[118:121], v[146:149], v[166:169], v[118:121]
	v_mfma_f32_16x16x32_bf16 v[110:113], v[130:133], v[204:207], v[110:113]
	v_mfma_f32_16x16x32_bf16 v[102:105], v[146:149], v[204:207], v[102:105]
	v_mfma_f32_16x16x32_bf16 v[94:97], v[130:133], v[218:221], v[94:97]
	v_mfma_f32_16x16x32_bf16 v[86:89], v[146:149], v[218:221], v[86:89]
	v_mfma_f32_16x16x32_bf16 v[78:81], v[130:133], v[226:229], v[78:81]
	v_mfma_f32_16x16x32_bf16 v[70:73], v[146:149], v[226:229], v[70:73]
	s_setprio 0
	s_setprio 1
	v_mfma_f32_16x16x32_bf16 v[122:125], v[142:145], v[162:165], v[122:125]
	v_mfma_f32_16x16x32_bf16 v[114:117], v[154:157], v[162:165], v[114:117]
	v_mfma_f32_16x16x32_bf16 v[106:109], v[142:145], v[170:173], v[106:109]
	v_mfma_f32_16x16x32_bf16 v[98:101], v[154:157], v[170:173], v[98:101]
	v_mfma_f32_16x16x32_bf16 v[90:93], v[142:145], v[214:217], v[90:93]
	v_mfma_f32_16x16x32_bf16 v[82:85], v[154:157], v[214:217], v[82:85]
	v_mfma_f32_16x16x32_bf16 v[74:77], v[142:145], v[222:225], v[74:77]
	v_mfma_f32_16x16x32_bf16 v[66:69], v[154:157], v[222:225], v[66:69]
	v_mfma_f32_16x16x32_bf16 v[122:125], v[150:153], v[166:169], v[122:125]
	v_mfma_f32_16x16x32_bf16 v[114:117], v[158:161], v[166:169], v[114:117]
	v_mfma_f32_16x16x32_bf16 v[106:109], v[150:153], v[204:207], v[106:109]
	v_mfma_f32_16x16x32_bf16 v[98:101], v[158:161], v[204:207], v[98:101]
	v_mfma_f32_16x16x32_bf16 v[90:93], v[150:153], v[218:221], v[90:93]
	v_mfma_f32_16x16x32_bf16 v[82:85], v[158:161], v[218:221], v[82:85]
	v_mfma_f32_16x16x32_bf16 v[74:77], v[150:153], v[226:229], v[74:77]
	v_mfma_f32_16x16x32_bf16 v[66:69], v[158:161], v[226:229], v[66:69]
	s_setprio 0
	s_barrier
	s_mov_b32 m0, s47
	v_add_u32_e32 v203, s81, v178
	ds_read_b128 v[162:165], v202 offset:16384
	ds_read_b128 v[166:169], v202 offset:17408
	ds_read_b128 v[170:173], v202 offset:18432
	ds_read_b128 v[204:207], v202 offset:19456
	ds_read_b128 v[214:217], v202 offset:20480
	ds_read_b128 v[218:221], v202 offset:21504
	ds_read_b128 v[222:225], v202 offset:22528
	ds_read_b128 v[226:229], v202 offset:23552
	global_load_lds_dwordx4 v203, s[6:7]
	v_add_u32_e32 v203, s35, v203
	s_mov_b32 m0, s48
	s_nop 0
	global_load_lds_dwordx4 v203, s[6:7]
	v_add_u32_e32 v203, s81, v179
	s_mov_b32 m0, s49
	s_nop 0
	global_load_lds_dwordx4 v203, s[6:7]
	v_add_u32_e32 v203, s35, v203
	s_mov_b32 m0, s50
	s_nop 0
	global_load_lds_dwordx4 v203, s[6:7]
	v_add_u32_e32 v203, s75, v1
	s_mov_b32 m0, s46
	s_nop 0
	global_load_lds_dwordx4 v203, s[4:5]
	v_add_u32_e32 v203, s31, v203
	s_mov_b32 m0, s51
	s_nop 0
	global_load_lds_dwordx4 v203, s[4:5]
	s_waitcnt vmcnt(8)
	s_waitcnt lgkmcnt(0)
	s_setprio 1
	s_barrier
	s_waitcnt lgkmcnt(0)
	v_mfma_f32_16x16x32_bf16 v[62:65], v[138:141], v[162:165], v[62:65]
	v_mfma_f32_16x16x32_bf16 v[54:57], v[134:137], v[162:165], v[54:57]
	v_mfma_f32_16x16x32_bf16 v[46:49], v[138:141], v[170:173], v[46:49]
	v_mfma_f32_16x16x32_bf16 v[38:41], v[134:137], v[170:173], v[38:41]
	v_mfma_f32_16x16x32_bf16 v[30:33], v[138:141], v[214:217], v[30:33]
	v_mfma_f32_16x16x32_bf16 v[22:25], v[134:137], v[214:217], v[22:25]
	v_mfma_f32_16x16x32_bf16 v[14:17], v[138:141], v[222:225], v[14:17]
	v_mfma_f32_16x16x32_bf16 v[6:9], v[134:137], v[222:225], v[6:9]
	v_mfma_f32_16x16x32_bf16 v[62:65], v[130:133], v[166:169], v[62:65]
	v_mfma_f32_16x16x32_bf16 v[54:57], v[146:149], v[166:169], v[54:57]
	v_mfma_f32_16x16x32_bf16 v[46:49], v[130:133], v[204:207], v[46:49]
	v_mfma_f32_16x16x32_bf16 v[38:41], v[146:149], v[204:207], v[38:41]
	v_mfma_f32_16x16x32_bf16 v[30:33], v[130:133], v[218:221], v[30:33]
	v_mfma_f32_16x16x32_bf16 v[22:25], v[146:149], v[218:221], v[22:25]
	v_mfma_f32_16x16x32_bf16 v[14:17], v[130:133], v[226:229], v[14:17]
	v_mfma_f32_16x16x32_bf16 v[6:9], v[146:149], v[226:229], v[6:9]
	s_setprio 0
	s_setprio 1
	v_mfma_f32_16x16x32_bf16 v[58:61], v[142:145], v[162:165], v[58:61]
	v_mfma_f32_16x16x32_bf16 v[50:53], v[154:157], v[162:165], v[50:53]
	v_mfma_f32_16x16x32_bf16 v[42:45], v[142:145], v[170:173], v[42:45]
	v_mfma_f32_16x16x32_bf16 v[34:37], v[154:157], v[170:173], v[34:37]
	v_mfma_f32_16x16x32_bf16 v[26:29], v[142:145], v[214:217], v[26:29]
	v_mfma_f32_16x16x32_bf16 v[18:21], v[154:157], v[214:217], v[18:21]
	v_mfma_f32_16x16x32_bf16 v[10:13], v[142:145], v[222:225], v[10:13]
	v_mfma_f32_16x16x32_bf16 v[2:5], v[154:157], v[222:225], v[2:5]
	v_mfma_f32_16x16x32_bf16 v[58:61], v[150:153], v[166:169], v[58:61]
	v_mfma_f32_16x16x32_bf16 v[50:53], v[158:161], v[166:169], v[50:53]
	v_mfma_f32_16x16x32_bf16 v[42:45], v[150:153], v[204:207], v[42:45]
	v_mfma_f32_16x16x32_bf16 v[34:37], v[158:161], v[204:207], v[34:37]
	v_mfma_f32_16x16x32_bf16 v[26:29], v[150:153], v[218:221], v[26:29]
	v_mfma_f32_16x16x32_bf16 v[18:21], v[158:161], v[218:221], v[18:21]
	v_mfma_f32_16x16x32_bf16 v[10:13], v[150:153], v[226:229], v[10:13]
	v_mfma_f32_16x16x32_bf16 v[2:5], v[158:161], v[226:229], v[2:5]
	s_setprio 0
	s_barrier
	ds_read_b128 v[130:133], v194
	ds_read_b128 v[134:137], v195
	ds_read_b128 v[138:141], v186
	ds_read_b128 v[142:145], v187
	ds_read_b128 v[146:149], v196
	ds_read_b128 v[150:153], v197
	ds_read_b128 v[154:157], v198
	ds_read_b128 v[158:161], v199
	s_mov_b32 m0, s52
	v_add_u32_e32 v203, s75, v180
	ds_read_b128 v[162:165], v202 offset:32768
	ds_read_b128 v[166:169], v202 offset:33792
	ds_read_b128 v[170:173], v202 offset:34816
	ds_read_b128 v[204:207], v202 offset:35840
	ds_read_b128 v[214:217], v202 offset:36864
	ds_read_b128 v[218:221], v202 offset:37888
	ds_read_b128 v[222:225], v202 offset:38912
	ds_read_b128 v[226:229], v202 offset:39936
	global_load_lds_dwordx4 v203, s[4:5]
	v_add_u32_e32 v203, s31, v203
	s_mov_b32 m0, s53
	s_nop 0
	global_load_lds_dwordx4 v203, s[4:5]
	s_waitcnt vmcnt(8)
	s_waitcnt lgkmcnt(0)
	s_setprio 1
	s_barrier
	s_waitcnt lgkmcnt(0)
	v_mfma_f32_16x16x32_bf16 v[126:129], v[138:141], v[162:165], v[126:129]
	v_mfma_f32_16x16x32_bf16 v[118:121], v[134:137], v[162:165], v[118:121]
	v_mfma_f32_16x16x32_bf16 v[110:113], v[138:141], v[170:173], v[110:113]
	v_mfma_f32_16x16x32_bf16 v[102:105], v[134:137], v[170:173], v[102:105]
	v_mfma_f32_16x16x32_bf16 v[94:97], v[138:141], v[214:217], v[94:97]
	v_mfma_f32_16x16x32_bf16 v[86:89], v[134:137], v[214:217], v[86:89]
	v_mfma_f32_16x16x32_bf16 v[78:81], v[138:141], v[222:225], v[78:81]
	v_mfma_f32_16x16x32_bf16 v[70:73], v[134:137], v[222:225], v[70:73]
	v_mfma_f32_16x16x32_bf16 v[126:129], v[130:133], v[166:169], v[126:129]
	v_mfma_f32_16x16x32_bf16 v[118:121], v[146:149], v[166:169], v[118:121]
	v_mfma_f32_16x16x32_bf16 v[110:113], v[130:133], v[204:207], v[110:113]
	v_mfma_f32_16x16x32_bf16 v[102:105], v[146:149], v[204:207], v[102:105]
	v_mfma_f32_16x16x32_bf16 v[94:97], v[130:133], v[218:221], v[94:97]
	v_mfma_f32_16x16x32_bf16 v[86:89], v[146:149], v[218:221], v[86:89]
	v_mfma_f32_16x16x32_bf16 v[78:81], v[130:133], v[226:229], v[78:81]
	v_mfma_f32_16x16x32_bf16 v[70:73], v[146:149], v[226:229], v[70:73]
	s_setprio 0
	s_setprio 1
	v_mfma_f32_16x16x32_bf16 v[122:125], v[142:145], v[162:165], v[122:125]
	v_mfma_f32_16x16x32_bf16 v[114:117], v[154:157], v[162:165], v[114:117]
	v_mfma_f32_16x16x32_bf16 v[106:109], v[142:145], v[170:173], v[106:109]
	v_mfma_f32_16x16x32_bf16 v[98:101], v[154:157], v[170:173], v[98:101]
	v_mfma_f32_16x16x32_bf16 v[90:93], v[142:145], v[214:217], v[90:93]
	v_mfma_f32_16x16x32_bf16 v[82:85], v[154:157], v[214:217], v[82:85]
	v_mfma_f32_16x16x32_bf16 v[74:77], v[142:145], v[222:225], v[74:77]
	v_mfma_f32_16x16x32_bf16 v[66:69], v[154:157], v[222:225], v[66:69]
	v_mfma_f32_16x16x32_bf16 v[122:125], v[150:153], v[166:169], v[122:125]
	v_mfma_f32_16x16x32_bf16 v[114:117], v[158:161], v[166:169], v[114:117]
	v_mfma_f32_16x16x32_bf16 v[106:109], v[150:153], v[204:207], v[106:109]
	v_mfma_f32_16x16x32_bf16 v[98:101], v[158:161], v[204:207], v[98:101]
	v_mfma_f32_16x16x32_bf16 v[90:93], v[150:153], v[218:221], v[90:93]
	v_mfma_f32_16x16x32_bf16 v[82:85], v[158:161], v[218:221], v[82:85]
	v_mfma_f32_16x16x32_bf16 v[74:77], v[150:153], v[226:229], v[74:77]
	v_mfma_f32_16x16x32_bf16 v[66:69], v[158:161], v[226:229], v[66:69]
	s_setprio 0
	s_barrier
	s_addk_i32 s81, 0x80
	s_mov_b32 m0, s55
	v_add_u32_e32 v203, s81, v178
	ds_read_b128 v[162:165], v202 offset:49152
	ds_read_b128 v[166:169], v202 offset:50176
	ds_read_b128 v[170:173], v202 offset:51200
	ds_read_b128 v[204:207], v202 offset:52224
	ds_read_b128 v[214:217], v202 offset:53248
	ds_read_b128 v[218:221], v202 offset:54272
	ds_read_b128 v[222:225], v202 offset:55296
	ds_read_b128 v[226:229], v202 offset:56320
	global_load_lds_dwordx4 v203, s[6:7]
	v_add_u32_e32 v203, s35, v203
	s_mov_b32 m0, s56
	s_nop 0
	global_load_lds_dwordx4 v203, s[6:7]
	v_add_u32_e32 v203, s81, v179
	s_mov_b32 m0, s59
	s_nop 0
	global_load_lds_dwordx4 v203, s[6:7]
	v_add_u32_e32 v203, s35, v203
	s_mov_b32 m0, s60
	s_nop 0
	global_load_lds_dwordx4 v203, s[6:7]
	v_add_u32_e32 v203, s75, v181
	s_mov_b32 m0, s57
	s_nop 0
	global_load_lds_dwordx4 v203, s[4:5]
	v_add_u32_e32 v203, s31, v203
	s_mov_b32 m0, s58
	s_nop 0
	global_load_lds_dwordx4 v203, s[4:5]
	s_waitcnt vmcnt(8)
	s_waitcnt lgkmcnt(0)
	s_setprio 1
	s_barrier
	s_waitcnt lgkmcnt(0)
	v_mfma_f32_16x16x32_bf16 v[62:65], v[138:141], v[162:165], v[62:65]
	v_mfma_f32_16x16x32_bf16 v[54:57], v[134:137], v[162:165], v[54:57]
	v_mfma_f32_16x16x32_bf16 v[46:49], v[138:141], v[170:173], v[46:49]
	v_mfma_f32_16x16x32_bf16 v[38:41], v[134:137], v[170:173], v[38:41]
	v_mfma_f32_16x16x32_bf16 v[30:33], v[138:141], v[214:217], v[30:33]
	v_mfma_f32_16x16x32_bf16 v[22:25], v[134:137], v[214:217], v[22:25]
	v_mfma_f32_16x16x32_bf16 v[14:17], v[138:141], v[222:225], v[14:17]
	v_mfma_f32_16x16x32_bf16 v[6:9], v[134:137], v[222:225], v[6:9]
	v_mfma_f32_16x16x32_bf16 v[62:65], v[130:133], v[166:169], v[62:65]
	v_mfma_f32_16x16x32_bf16 v[54:57], v[146:149], v[166:169], v[54:57]
	v_mfma_f32_16x16x32_bf16 v[46:49], v[130:133], v[204:207], v[46:49]
	v_mfma_f32_16x16x32_bf16 v[38:41], v[146:149], v[204:207], v[38:41]
	v_mfma_f32_16x16x32_bf16 v[30:33], v[130:133], v[218:221], v[30:33]
	v_mfma_f32_16x16x32_bf16 v[22:25], v[146:149], v[218:221], v[22:25]
	v_mfma_f32_16x16x32_bf16 v[14:17], v[130:133], v[226:229], v[14:17]
	v_mfma_f32_16x16x32_bf16 v[6:9], v[146:149], v[226:229], v[6:9]
	s_setprio 0
	s_setprio 1
	v_mfma_f32_16x16x32_bf16 v[58:61], v[142:145], v[162:165], v[58:61]
	v_mfma_f32_16x16x32_bf16 v[50:53], v[154:157], v[162:165], v[50:53]
	v_mfma_f32_16x16x32_bf16 v[42:45], v[142:145], v[170:173], v[42:45]
	v_mfma_f32_16x16x32_bf16 v[34:37], v[154:157], v[170:173], v[34:37]
	v_mfma_f32_16x16x32_bf16 v[26:29], v[142:145], v[214:217], v[26:29]
	v_mfma_f32_16x16x32_bf16 v[18:21], v[154:157], v[214:217], v[18:21]
	v_mfma_f32_16x16x32_bf16 v[10:13], v[142:145], v[222:225], v[10:13]
	v_mfma_f32_16x16x32_bf16 v[2:5], v[154:157], v[222:225], v[2:5]
	v_mfma_f32_16x16x32_bf16 v[58:61], v[150:153], v[166:169], v[58:61]
	v_mfma_f32_16x16x32_bf16 v[50:53], v[158:161], v[166:169], v[50:53]
	v_mfma_f32_16x16x32_bf16 v[42:45], v[150:153], v[204:207], v[42:45]
	v_mfma_f32_16x16x32_bf16 v[34:37], v[158:161], v[204:207], v[34:37]
	v_mfma_f32_16x16x32_bf16 v[26:29], v[150:153], v[218:221], v[26:29]
	v_mfma_f32_16x16x32_bf16 v[18:21], v[158:161], v[218:221], v[18:21]
	v_mfma_f32_16x16x32_bf16 v[10:13], v[150:153], v[226:229], v[10:13]
	v_mfma_f32_16x16x32_bf16 v[2:5], v[158:161], v[226:229], v[2:5]
	s_setprio 0
	s_barrier
	s_add_i32 s80, s80, 2
	s_addk_i32 s28, 0x100
	s_addk_i32 s79, 0x100
	s_cmp_ge_i32 s80, s61
	s_cbranch_scc0 .LBB0_637

.LBB0_1183:
	ds_read_b128 v[114:117], v206
	ds_read_b128 v[118:121], v207
	ds_read_b128 v[122:125], v202
	ds_read_b128 v[126:129], v203
	ds_read_b128 v[146:149], v208
	ds_read_b128 v[150:153], v209
	ds_read_b128 v[154:157], v211
	ds_read_b128 v[158:161], v213
	s_add_i32 s60, s6, 0x80
	s_cmp_eq_u32 s90, s59
	s_cselect_b32 s61, s5, s58
	s_cselect_b32 s60, s7, s60
	v_add_u32_e32 v194, s6, v221
	s_add_i32 m0, s70, 0xc000
	ds_read_b128 v[162:165], v222
	ds_read_b128 v[170:173], v222 offset:1024
	ds_read_b128 v[174:177], v222 offset:2048
	ds_read_b128 v[178:181], v222 offset:3072
	ds_read_b128 v[182:185], v222 offset:4096
	ds_read_b128 v[186:189], v222 offset:5120
	ds_read_b128 v[190:193], v222 offset:6144
	ds_read_b128 v[226:229], v222 offset:7168
	global_load_lds_dwordx4 v194, s[8:9]
	v_add_u32_e32 v194, s6, v220
	s_add_i32 m0, s70, 0xe000
	s_nop 0
	global_load_lds_dwordx4 v194, s[8:9]
	s_waitcnt vmcnt(8)
	s_waitcnt lgkmcnt(0)
	s_setprio 1
	s_barrier
	s_waitcnt lgkmcnt(0)
	v_mfma_f32_16x16x32_bf16 v[142:145], v[122:125], v[162:165], v[142:145]
	v_mfma_f32_16x16x32_bf16 v[138:141], v[118:121], v[162:165], v[138:141]
	v_mfma_f32_16x16x32_bf16 v[110:113], v[122:125], v[174:177], v[110:113]
	v_mfma_f32_16x16x32_bf16 v[106:109], v[118:121], v[174:177], v[106:109]
	v_mfma_f32_16x16x32_bf16 v[94:97], v[122:125], v[182:185], v[94:97]
	v_mfma_f32_16x16x32_bf16 v[90:93], v[118:121], v[182:185], v[90:93]
	v_mfma_f32_16x16x32_bf16 v[78:81], v[122:125], v[190:193], v[78:81]
	v_mfma_f32_16x16x32_bf16 v[74:77], v[118:121], v[190:193], v[74:77]
	v_mfma_f32_16x16x32_bf16 v[142:145], v[114:117], v[170:173], v[142:145]
	v_mfma_f32_16x16x32_bf16 v[138:141], v[146:149], v[170:173], v[138:141]
	v_mfma_f32_16x16x32_bf16 v[110:113], v[114:117], v[178:181], v[110:113]
	v_mfma_f32_16x16x32_bf16 v[106:109], v[146:149], v[178:181], v[106:109]
	v_mfma_f32_16x16x32_bf16 v[94:97], v[114:117], v[186:189], v[94:97]
	v_mfma_f32_16x16x32_bf16 v[90:93], v[146:149], v[186:189], v[90:93]
	v_mfma_f32_16x16x32_bf16 v[78:81], v[114:117], v[226:229], v[78:81]
	v_mfma_f32_16x16x32_bf16 v[74:77], v[146:149], v[226:229], v[74:77]
	s_setprio 0
	s_setprio 1
	v_mfma_f32_16x16x32_bf16 v[134:137], v[126:129], v[162:165], v[134:137]
	v_mfma_f32_16x16x32_bf16 v[130:133], v[154:157], v[162:165], v[130:133]
	v_mfma_f32_16x16x32_bf16 v[102:105], v[126:129], v[174:177], v[102:105]
	v_mfma_f32_16x16x32_bf16 v[98:101], v[154:157], v[174:177], v[98:101]
	v_mfma_f32_16x16x32_bf16 v[86:89], v[126:129], v[182:185], v[86:89]
	v_mfma_f32_16x16x32_bf16 v[82:85], v[154:157], v[182:185], v[82:85]
	v_mfma_f32_16x16x32_bf16 v[70:73], v[126:129], v[190:193], v[70:73]
	v_mfma_f32_16x16x32_bf16 v[66:69], v[154:157], v[190:193], v[66:69]
	v_mfma_f32_16x16x32_bf16 v[134:137], v[150:153], v[170:173], v[134:137]
	v_mfma_f32_16x16x32_bf16 v[130:133], v[158:161], v[170:173], v[130:133]
	v_mfma_f32_16x16x32_bf16 v[102:105], v[150:153], v[178:181], v[102:105]
	v_mfma_f32_16x16x32_bf16 v[98:101], v[158:161], v[178:181], v[98:101]
	v_mfma_f32_16x16x32_bf16 v[86:89], v[150:153], v[186:189], v[86:89]
	v_mfma_f32_16x16x32_bf16 v[82:85], v[158:161], v[186:189], v[82:85]
	v_mfma_f32_16x16x32_bf16 v[70:73], v[150:153], v[226:229], v[70:73]
	v_mfma_f32_16x16x32_bf16 v[66:69], v[158:161], v[226:229], v[66:69]
	s_setprio 0
	s_barrier
	s_mov_b32 m0, s71
	v_add_u32_e32 v194, s61, v196
	ds_read_b128 v[162:165], v222 offset:16384
	ds_read_b128 v[170:173], v222 offset:17408
	ds_read_b128 v[174:177], v222 offset:18432
	ds_read_b128 v[178:181], v222 offset:19456
	ds_read_b128 v[182:185], v222 offset:20480
	ds_read_b128 v[186:189], v222 offset:21504
	ds_read_b128 v[190:193], v222 offset:22528
	ds_read_b128 v[226:229], v222 offset:23552
	global_load_lds_dwordx4 v194, s[20:21]
	v_add_u32_e32 v194, s35, v194
	s_mov_b32 m0, s72
	s_nop 0
	global_load_lds_dwordx4 v194, s[20:21]
	v_add_u32_e32 v194, s61, v197
	s_mov_b32 m0, s73
	s_nop 0
	global_load_lds_dwordx4 v194, s[20:21]
	v_add_u32_e32 v194, s35, v194
	s_mov_b32 m0, s76
	s_nop 0
	global_load_lds_dwordx4 v194, s[20:21]
	v_add_u32_e32 v194, s60, v1
	s_mov_b32 m0, s70
	s_nop 0
	global_load_lds_dwordx4 v194, s[8:9]
	v_add_u32_e32 v194, s29, v194
	s_mov_b32 m0, s77
	s_nop 0
	global_load_lds_dwordx4 v194, s[8:9]
	s_waitcnt vmcnt(8)
	s_waitcnt lgkmcnt(0)
	s_setprio 1
	s_barrier
	s_waitcnt lgkmcnt(0)
	v_mfma_f32_16x16x32_bf16 v[62:65], v[122:125], v[162:165], v[62:65]
	v_mfma_f32_16x16x32_bf16 v[58:61], v[118:121], v[162:165], v[58:61]
	v_mfma_f32_16x16x32_bf16 v[46:49], v[122:125], v[174:177], v[46:49]
	v_mfma_f32_16x16x32_bf16 v[42:45], v[118:121], v[174:177], v[42:45]
	v_mfma_f32_16x16x32_bf16 v[30:33], v[122:125], v[182:185], v[30:33]
	v_mfma_f32_16x16x32_bf16 v[26:29], v[118:121], v[182:185], v[26:29]
	v_mfma_f32_16x16x32_bf16 v[14:17], v[122:125], v[190:193], v[14:17]
	v_mfma_f32_16x16x32_bf16 v[10:13], v[118:121], v[190:193], v[10:13]
	v_mfma_f32_16x16x32_bf16 v[62:65], v[114:117], v[170:173], v[62:65]
	v_mfma_f32_16x16x32_bf16 v[58:61], v[146:149], v[170:173], v[58:61]
	v_mfma_f32_16x16x32_bf16 v[46:49], v[114:117], v[178:181], v[46:49]
	v_mfma_f32_16x16x32_bf16 v[42:45], v[146:149], v[178:181], v[42:45]
	v_mfma_f32_16x16x32_bf16 v[30:33], v[114:117], v[186:189], v[30:33]
	v_mfma_f32_16x16x32_bf16 v[26:29], v[146:149], v[186:189], v[26:29]
	v_mfma_f32_16x16x32_bf16 v[14:17], v[114:117], v[226:229], v[14:17]
	v_mfma_f32_16x16x32_bf16 v[10:13], v[146:149], v[226:229], v[10:13]
	s_setprio 0
	s_setprio 1
	v_mfma_f32_16x16x32_bf16 v[54:57], v[126:129], v[162:165], v[54:57]
	v_mfma_f32_16x16x32_bf16 v[50:53], v[154:157], v[162:165], v[50:53]
	v_mfma_f32_16x16x32_bf16 v[38:41], v[126:129], v[174:177], v[38:41]
	v_mfma_f32_16x16x32_bf16 v[34:37], v[154:157], v[174:177], v[34:37]
	v_mfma_f32_16x16x32_bf16 v[22:25], v[126:129], v[182:185], v[22:25]
	v_mfma_f32_16x16x32_bf16 v[18:21], v[154:157], v[182:185], v[18:21]
	v_mfma_f32_16x16x32_bf16 v[6:9], v[126:129], v[190:193], v[6:9]
	v_mfma_f32_16x16x32_bf16 v[2:5], v[154:157], v[190:193], v[2:5]
	v_mfma_f32_16x16x32_bf16 v[54:57], v[150:153], v[170:173], v[54:57]
	v_mfma_f32_16x16x32_bf16 v[50:53], v[158:161], v[170:173], v[50:53]
	v_mfma_f32_16x16x32_bf16 v[38:41], v[150:153], v[178:181], v[38:41]
	v_mfma_f32_16x16x32_bf16 v[34:37], v[158:161], v[178:181], v[34:37]
	v_mfma_f32_16x16x32_bf16 v[22:25], v[150:153], v[186:189], v[22:25]
	v_mfma_f32_16x16x32_bf16 v[18:21], v[158:161], v[186:189], v[18:21]
	v_mfma_f32_16x16x32_bf16 v[6:9], v[150:153], v[226:229], v[6:9]
	v_mfma_f32_16x16x32_bf16 v[2:5], v[158:161], v[226:229], v[2:5]
	s_setprio 0
	s_barrier
	ds_read_b128 v[114:117], v214
	ds_read_b128 v[118:121], v215
	ds_read_b128 v[122:125], v204
	ds_read_b128 v[126:129], v205
	ds_read_b128 v[146:149], v216
	ds_read_b128 v[150:153], v217
	ds_read_b128 v[154:157], v218
	ds_read_b128 v[158:161], v219
	s_mov_b32 m0, s78
	v_add_u32_e32 v194, s60, v198
	ds_read_b128 v[162:165], v222 offset:32768
	ds_read_b128 v[170:173], v222 offset:33792
	ds_read_b128 v[174:177], v222 offset:34816
	ds_read_b128 v[178:181], v222 offset:35840
	ds_read_b128 v[182:185], v222 offset:36864
	ds_read_b128 v[186:189], v222 offset:37888
	ds_read_b128 v[190:193], v222 offset:38912
	ds_read_b128 v[226:229], v222 offset:39936
	global_load_lds_dwordx4 v194, s[8:9]
	v_add_u32_e32 v194, s29, v194
	s_mov_b32 m0, s79
	s_nop 0
	global_load_lds_dwordx4 v194, s[8:9]
	s_waitcnt vmcnt(8)
	s_waitcnt lgkmcnt(0)
	s_setprio 1
	s_barrier
	s_waitcnt lgkmcnt(0)
	v_mfma_f32_16x16x32_bf16 v[142:145], v[122:125], v[162:165], v[142:145]
	v_mfma_f32_16x16x32_bf16 v[138:141], v[118:121], v[162:165], v[138:141]
	v_mfma_f32_16x16x32_bf16 v[110:113], v[122:125], v[174:177], v[110:113]
	v_mfma_f32_16x16x32_bf16 v[106:109], v[118:121], v[174:177], v[106:109]
	v_mfma_f32_16x16x32_bf16 v[94:97], v[122:125], v[182:185], v[94:97]
	v_mfma_f32_16x16x32_bf16 v[90:93], v[118:121], v[182:185], v[90:93]
	v_mfma_f32_16x16x32_bf16 v[78:81], v[122:125], v[190:193], v[78:81]
	v_mfma_f32_16x16x32_bf16 v[74:77], v[118:121], v[190:193], v[74:77]
	v_mfma_f32_16x16x32_bf16 v[142:145], v[114:117], v[170:173], v[142:145]
	v_mfma_f32_16x16x32_bf16 v[138:141], v[146:149], v[170:173], v[138:141]
	v_mfma_f32_16x16x32_bf16 v[110:113], v[114:117], v[178:181], v[110:113]
	v_mfma_f32_16x16x32_bf16 v[106:109], v[146:149], v[178:181], v[106:109]
	v_mfma_f32_16x16x32_bf16 v[94:97], v[114:117], v[186:189], v[94:97]
	v_mfma_f32_16x16x32_bf16 v[90:93], v[146:149], v[186:189], v[90:93]
	v_mfma_f32_16x16x32_bf16 v[78:81], v[114:117], v[226:229], v[78:81]
	v_mfma_f32_16x16x32_bf16 v[74:77], v[146:149], v[226:229], v[74:77]
	s_setprio 0
	s_setprio 1
	v_mfma_f32_16x16x32_bf16 v[134:137], v[126:129], v[162:165], v[134:137]
	v_mfma_f32_16x16x32_bf16 v[130:133], v[154:157], v[162:165], v[130:133]
	v_mfma_f32_16x16x32_bf16 v[102:105], v[126:129], v[174:177], v[102:105]
	v_mfma_f32_16x16x32_bf16 v[98:101], v[154:157], v[174:177], v[98:101]
	v_mfma_f32_16x16x32_bf16 v[86:89], v[126:129], v[182:185], v[86:89]
	v_mfma_f32_16x16x32_bf16 v[82:85], v[154:157], v[182:185], v[82:85]
	v_mfma_f32_16x16x32_bf16 v[70:73], v[126:129], v[190:193], v[70:73]
	v_mfma_f32_16x16x32_bf16 v[66:69], v[154:157], v[190:193], v[66:69]
	v_mfma_f32_16x16x32_bf16 v[134:137], v[150:153], v[170:173], v[134:137]
	v_mfma_f32_16x16x32_bf16 v[130:133], v[158:161], v[170:173], v[130:133]
	v_mfma_f32_16x16x32_bf16 v[102:105], v[150:153], v[178:181], v[102:105]
	v_mfma_f32_16x16x32_bf16 v[98:101], v[158:161], v[178:181], v[98:101]
	v_mfma_f32_16x16x32_bf16 v[86:89], v[150:153], v[186:189], v[86:89]
	v_mfma_f32_16x16x32_bf16 v[82:85], v[158:161], v[186:189], v[82:85]
	v_mfma_f32_16x16x32_bf16 v[70:73], v[150:153], v[226:229], v[70:73]
	v_mfma_f32_16x16x32_bf16 v[66:69], v[158:161], v[226:229], v[66:69]
	s_setprio 0
	s_barrier
	s_addk_i32 s61, 0x80
	s_mov_b32 m0, s81
	v_add_u32_e32 v194, s61, v196
	ds_read_b128 v[162:165], v222 offset:49152
	ds_read_b128 v[170:173], v222 offset:50176
	ds_read_b128 v[174:177], v222 offset:51200
	ds_read_b128 v[178:181], v222 offset:52224
	ds_read_b128 v[182:185], v222 offset:53248
	ds_read_b128 v[186:189], v222 offset:54272
	ds_read_b128 v[190:193], v222 offset:55296
	ds_read_b128 v[226:229], v222 offset:56320
	global_load_lds_dwordx4 v194, s[20:21]
	v_add_u32_e32 v194, s35, v194
	s_mov_b32 m0, s82
	s_nop 0
	global_load_lds_dwordx4 v194, s[20:21]
	v_add_u32_e32 v194, s61, v197
	s_mov_b32 m0, s85
	s_nop 0
	global_load_lds_dwordx4 v194, s[20:21]
	v_add_u32_e32 v194, s35, v194
	s_mov_b32 m0, s86
	s_nop 0
	global_load_lds_dwordx4 v194, s[20:21]
	v_add_u32_e32 v194, s60, v201
	s_mov_b32 m0, s83
	s_nop 0
	global_load_lds_dwordx4 v194, s[8:9]
	v_add_u32_e32 v194, s29, v194
	s_mov_b32 m0, s84
	s_nop 0
	global_load_lds_dwordx4 v194, s[8:9]
	s_waitcnt vmcnt(8)
	s_waitcnt lgkmcnt(0)
	s_setprio 1
	s_barrier
	s_waitcnt lgkmcnt(0)
	v_mfma_f32_16x16x32_bf16 v[62:65], v[122:125], v[162:165], v[62:65]
	v_mfma_f32_16x16x32_bf16 v[58:61], v[118:121], v[162:165], v[58:61]
	v_mfma_f32_16x16x32_bf16 v[46:49], v[122:125], v[174:177], v[46:49]
	v_mfma_f32_16x16x32_bf16 v[42:45], v[118:121], v[174:177], v[42:45]
	v_mfma_f32_16x16x32_bf16 v[30:33], v[122:125], v[182:185], v[30:33]
	v_mfma_f32_16x16x32_bf16 v[26:29], v[118:121], v[182:185], v[26:29]
	v_mfma_f32_16x16x32_bf16 v[14:17], v[122:125], v[190:193], v[14:17]
	v_mfma_f32_16x16x32_bf16 v[10:13], v[118:121], v[190:193], v[10:13]
	v_mfma_f32_16x16x32_bf16 v[62:65], v[114:117], v[170:173], v[62:65]
	v_mfma_f32_16x16x32_bf16 v[58:61], v[146:149], v[170:173], v[58:61]
	v_mfma_f32_16x16x32_bf16 v[46:49], v[114:117], v[178:181], v[46:49]
	v_mfma_f32_16x16x32_bf16 v[42:45], v[146:149], v[178:181], v[42:45]
	v_mfma_f32_16x16x32_bf16 v[30:33], v[114:117], v[186:189], v[30:33]
	v_mfma_f32_16x16x32_bf16 v[26:29], v[146:149], v[186:189], v[26:29]
	v_mfma_f32_16x16x32_bf16 v[14:17], v[114:117], v[226:229], v[14:17]
	v_mfma_f32_16x16x32_bf16 v[10:13], v[146:149], v[226:229], v[10:13]
	s_setprio 0
	s_setprio 1
	v_mfma_f32_16x16x32_bf16 v[54:57], v[126:129], v[162:165], v[54:57]
	v_mfma_f32_16x16x32_bf16 v[50:53], v[154:157], v[162:165], v[50:53]
	v_mfma_f32_16x16x32_bf16 v[38:41], v[126:129], v[174:177], v[38:41]
	v_mfma_f32_16x16x32_bf16 v[34:37], v[154:157], v[174:177], v[34:37]
	v_mfma_f32_16x16x32_bf16 v[22:25], v[126:129], v[182:185], v[22:25]
	v_mfma_f32_16x16x32_bf16 v[18:21], v[154:157], v[182:185], v[18:21]
	v_mfma_f32_16x16x32_bf16 v[6:9], v[126:129], v[190:193], v[6:9]
	v_mfma_f32_16x16x32_bf16 v[2:5], v[154:157], v[190:193], v[2:5]
	v_mfma_f32_16x16x32_bf16 v[54:57], v[150:153], v[170:173], v[54:57]
	v_mfma_f32_16x16x32_bf16 v[50:53], v[158:161], v[170:173], v[50:53]
	v_mfma_f32_16x16x32_bf16 v[38:41], v[150:153], v[178:181], v[38:41]
	v_mfma_f32_16x16x32_bf16 v[34:37], v[158:161], v[178:181], v[34:37]
	v_mfma_f32_16x16x32_bf16 v[22:25], v[150:153], v[186:189], v[22:25]
	v_mfma_f32_16x16x32_bf16 v[18:21], v[158:161], v[186:189], v[18:21]
	v_mfma_f32_16x16x32_bf16 v[6:9], v[150:153], v[226:229], v[6:9]
	v_mfma_f32_16x16x32_bf16 v[2:5], v[158:161], v[226:229], v[2:5]
	s_setprio 0
	s_barrier
	s_add_i32 s59, s59, 2
	s_addk_i32 s6, 0x100
	s_addk_i32 s58, 0x100
	s_cmp_ge_i32 s59, s87
	s_cbranch_scc0 .LBB0_1183

.LBB0_1186:
	v_mov_b32_e32 v146, v199
	v_mov_b32_e32 v160, v200
	s_mov_b32 s6, s39
	s_mov_b32 s61, s37
	s_mov_b32 s7, s38
	s_mov_b32 s60, s36
	s_add_u32 s58, s7, 0x2a400000
	s_addc_u32 s59, s6, 0
	s_min_i32 s63, s4, 0x80
	s_lshr_b32 s63, s63, 5
	s_mul_i32 s64, s63, 0x3000
	s_ashr_i32 s65, s64, 31
	s_ashr_i32 s5, s4, 31
	s_lshl_b64 s[64:65], s[64:65], 2
	s_add_u32 s64, s7, s64
	s_addc_u32 s65, s6, s65
	s_lshl_b32 s63, s62, 8
	s_or_b32 s63, s63, s89
	v_lshl_add_u32 v170, v160, 3, s63
	v_ashrrev_i32_e32 v171, 31, v170
	v_lshlrev_b64 v[188:189], 2, v[170:171]
	v_lshl_add_u64 v[126:127], s[64:65], 0, v[188:189]
	s_mov_b64 s[64:65], 0x104000
	v_lshl_add_u64 v[156:157], v[126:127], 0, s[64:65]
	s_load_dwordx2 s[64:65], s[0:1], 0x38
	s_mov_b32 s63, 0x104000
	v_add_co_u32_e32 v114, vcc, s63, v126
	s_mov_b32 s63, 0x108000
	s_waitcnt lgkmcnt(0)
	v_lshl_add_u64 v[152:153], s[64:65], 0, v[188:189]
	s_mov_b64 s[64:65], 0x108000
	v_addc_co_u32_e32 v115, vcc, 0, v127, vcc
	v_lshl_add_u64 v[158:159], v[126:127], 0, s[64:65]
	v_add_co_u32_e32 v126, vcc, s63, v126
	flat_load_dwordx4 v[114:117], v[114:115]
	s_nop 0
	global_load_dwordx4 v[122:125], v[152:153], off offset:16
	global_load_dwordx4 v[118:121], v[152:153], off
	v_addc_co_u32_e32 v127, vcc, 0, v127, vcc
	flat_load_dwordx4 v[126:129], v[126:127]
	s_add_u32 s64, s7, 0x800000
	s_addc_u32 s65, s6, 0
	s_and_b64 s[66:67], s[22:23], exec
	s_cselect_b32 s67, s61, s11
	s_cselect_b32 s66, s60, s10
	s_and_b64 s[68:69], s[24:25], exec
	s_cselect_b32 s69, s65, s13
	s_cselect_b32 s68, s64, s12
	s_lshl_b64 s[4:5], s[4:5], 8
	s_add_u32 s4, s4, s88
	v_ashrrev_i32_e32 v147, 31, v146
	s_addc_u32 s5, s5, s91
	v_lshl_add_u64 v[190:191], s[4:5], 0, v[146:147]
	s_lshl_b32 s4, s62, 2
	s_ashr_i32 s5, s4, 31
	s_lshl_b64 s[4:5], s[4:5], 2
	s_add_u32 s4, s7, s4
	s_addc_u32 s5, s6, s5
	s_add_u32 s4, s4, s94
	s_addc_u32 s5, s5, 0
	s_add_u32 s62, s4, 0xa4500000
	v_lshlrev_b64 v[238:239], 13, v[190:191]
	s_addc_u32 s63, s5, 0
	s_mov_b64 s[4:5], 0x8000
	v_cmp_gt_i64_e64 s[6:7], s[4:5], v[190:191]
	v_lshl_add_u64 v[146:147], s[66:67], 0, v[238:239]
	v_lshl_add_u64 v[192:193], v[190:191], 0, 16
	v_lshlrev_b64 v[194:195], 13, v[192:193]
	s_mov_b64 s[4:5], 0x7ff0
	v_cmp_gt_i64_e64 s[4:5], s[4:5], v[190:191]
	v_cmp_eq_u32_e32 vcc, 0, v160
	v_lshl_add_u64 v[240:241], s[64:65], 0, v[238:239]
	v_lshl_add_u64 v[240:241], v[240:241], 0, s[30:31]
	s_waitcnt vmcnt(0) lgkmcnt(0)
	v_pk_add_f32 v[128:129], v[128:129], 1.0 op_sel_hi:[1,0]
	v_pk_add_f32 v[126:127], v[126:127], 1.0 op_sel_hi:[1,0]
	v_pk_mul_f32 v[120:121], v[120:121], v[128:129]
	v_pk_mul_f32 v[118:119], v[118:119], v[126:127]
	v_pk_mul_f32 v[172:173], v[120:121], s[28:29] op_sel_hi:[1,0]
	v_pk_mul_f32 v[174:175], v[118:119], s[28:29] op_sel_hi:[1,0]
	flat_load_dwordx4 v[118:121], v[156:157] offset:16
	flat_load_dwordx4 v[126:129], v[158:159] offset:16
	s_waitcnt vmcnt(0) lgkmcnt(0)
	v_pk_add_f32 v[128:129], v[128:129], 1.0 op_sel_hi:[1,0]
	v_pk_add_f32 v[126:127], v[126:127], 1.0 op_sel_hi:[1,0]
	v_pk_mul_f32 v[124:125], v[124:125], v[128:129]
	v_pk_mul_f32 v[122:123], v[122:123], v[126:127]
	v_pk_mul_f32 v[180:181], v[124:125], s[28:29] op_sel_hi:[1,0]
	v_pk_mul_f32 v[182:183], v[122:123], s[28:29] op_sel_hi:[1,0]
	flat_load_dwordx4 v[122:125], v[156:157] offset:512
	global_load_dwordx4 v[148:151], v[152:153], off offset:528
	global_load_dwordx4 v[126:129], v[152:153], off offset:512
	s_nop 0
	flat_load_dwordx4 v[152:155], v[158:159] offset:512
	s_waitcnt vmcnt(0) lgkmcnt(0)
	v_pk_add_f32 v[154:155], v[154:155], 1.0 op_sel_hi:[1,0]
	v_pk_add_f32 v[152:153], v[152:153], 1.0 op_sel_hi:[1,0]
	v_pk_mul_f32 v[128:129], v[128:129], v[154:155]
	v_pk_mul_f32 v[126:127], v[126:127], v[152:153]
	v_pk_mul_f32 v[176:177], v[128:129], s[28:29] op_sel_hi:[1,0]
	v_pk_mul_f32 v[178:179], v[126:127], s[28:29] op_sel_hi:[1,0]
	flat_load_dwordx4 v[126:129], v[156:157] offset:528
	flat_load_dwordx4 v[152:155], v[158:159] offset:528
	s_waitcnt vmcnt(0) lgkmcnt(0)
	v_pk_add_f32 v[152:153], v[152:153], 1.0 op_sel_hi:[1,0]
	s_nop 0
	v_pk_mul_f32 v[148:149], v[148:149], v[152:153]
	v_pk_add_f32 v[154:155], v[154:155], 1.0 op_sel_hi:[1,0]
	v_pk_mul_f32 v[186:187], v[148:149], s[28:29] op_sel_hi:[1,0]
	v_lshl_add_u64 v[148:149], s[68:69], 0, v[238:239]
	v_lshl_add_u64 v[148:149], v[148:149], 0, s[30:31]
	v_cndmask_b32_e64 v147, v149, v147, s[6:7]
	v_cndmask_b32_e64 v146, v148, v146, s[6:7]
	v_lshl_add_u64 v[146:147], v[146:147], 0, v[188:189]
	flat_load_dwordx4 v[226:229], v[146:147] nt
	flat_load_dwordx4 v[230:233], v[146:147] offset:16 nt
	flat_load_dwordx4 v[234:237], v[146:147] offset:512 nt
	flat_load_dwordx4 v[162:165], v[146:147] offset:528 nt
	v_lshl_add_u64 v[148:149], s[68:69], 0, v[194:195]
	v_lshl_add_u64 v[146:147], s[66:67], 0, v[194:195]
	v_lshl_add_u64 v[148:149], v[148:149], 0, s[30:31]
	v_cndmask_b32_e64 v147, v149, v147, s[4:5]
	v_cndmask_b32_e64 v146, v148, v146, s[4:5]
	v_pk_mul_f32 v[150:151], v[150:151], v[154:155]
	v_lshl_add_u64 v[146:147], v[146:147], 0, v[188:189]
	v_pk_mul_f32 v[184:185], v[150:151], s[28:29] op_sel_hi:[1,0]
	flat_load_dwordx4 v[158:161], v[146:147] nt
	flat_load_dwordx4 v[154:157], v[146:147] offset:16 nt
	flat_load_dwordx4 v[150:153], v[146:147] offset:512 nt
	s_nop 0
	flat_load_dwordx4 v[146:149], v[146:147] offset:528 nt
	v_lshl_add_u64 v[238:239], s[60:61], 0, v[238:239]
	v_cndmask_b32_e64 v239, v241, v239, s[6:7]
	v_cndmask_b32_e64 v238, v240, v238, s[6:7]
	v_lshlrev_b64 v[240:241], 11, v[190:191]
	v_lshl_add_u64 v[240:241], s[58:59], 0, v[240:241]
	s_waitcnt vmcnt(0) lgkmcnt(0)
	v_pk_fma_f32 v[144:145], v[144:145], v[116:117], v[228:229]
	v_pk_fma_f32 v[142:143], v[142:143], v[114:115], v[226:227]
	v_mul_f32_e32 v228, v145, v145
	v_mul_f32_e32 v225, v143, v143
	v_pk_fma_f32 v[140:141], v[140:141], v[120:121], v[232:233]
	v_pk_fma_f32 v[138:139], v[138:139], v[118:119], v[230:231]
	v_fmac_f32_e32 v225, v142, v142
	v_fmac_f32_e32 v228, v144, v144
	v_add_f32_e32 v225, v225, v228
	v_mul_f32_e32 v228, v139, v139
	v_mul_f32_e32 v229, v141, v141
	v_lshl_add_u64 v[226:227], v[238:239], 0, v[188:189]
	v_fmac_f32_e32 v228, v138, v138
	v_fmac_f32_e32 v229, v140, v140
	flat_store_dwordx4 v[226:227], v[142:145] nt
	flat_store_dwordx4 v[226:227], v[138:141] offset:16 nt
	v_add_f32_e32 v228, v228, v229
	v_pk_mul_f32 v[142:143], v[174:175], v[142:143]
	v_add_f32_e32 v225, v225, v228
	v_med3_f32 v228, v142, s95, v223
	v_med3_f32 v143, v143, s95, v223
	v_mov_b32_e32 v142, 0
	v_cvt_pk_fp8_f32 v142, v228, v143
	v_pk_mul_f32 v[144:145], v[172:173], v[144:145]
	v_pk_mul_f32 v[138:139], v[182:183], v[138:139]
	v_med3_f32 v143, v144, s95, v223
	v_med3_f32 v144, v145, s95, v223
	v_cvt_pk_fp8_f32 v142, v143, v144 op_sel:[0,0,1]
	v_med3_f32 v138, v138, s95, v223
	v_med3_f32 v139, v139, s95, v223
	v_mov_b32_e32 v143, 0
	v_cvt_pk_fp8_f32 v143, v138, v139
	v_pk_mul_f32 v[140:141], v[180:181], v[140:141]
	v_pk_fma_f32 v[136:137], v[136:137], v[124:125], v[236:237]
	v_med3_f32 v138, v140, s95, v223
	v_med3_f32 v139, v141, s95, v223
	v_cvt_pk_fp8_f32 v143, v138, v139 op_sel:[0,0,1]
	v_pk_fma_f32 v[134:135], v[134:135], v[122:123], v[234:235]
	v_mul_f32_e32 v141, v137, v137
	v_mul_f32_e32 v140, v135, v135
	v_lshl_add_u64 v[138:139], v[240:241], 0, v[170:171]
	v_pk_fma_f32 v[132:133], v[132:133], v[128:129], v[164:165]
	v_pk_fma_f32 v[130:131], v[130:131], v[126:127], v[162:163]
	v_fmac_f32_e32 v140, v134, v134
	v_fmac_f32_e32 v141, v136, v136
	flat_store_dwordx2 v[138:139], v[142:143]
	v_add_f32_e32 v140, v140, v141
	v_mul_f32_e32 v141, v131, v131
	v_mul_f32_e32 v142, v133, v133
	v_fmac_f32_e32 v141, v130, v130
	v_fmac_f32_e32 v142, v132, v132
	flat_store_dwordx4 v[226:227], v[134:137] offset:512 nt
	flat_store_dwordx4 v[226:227], v[130:133] offset:528 nt
	v_add_f32_e32 v141, v141, v142
	v_pk_mul_f32 v[134:135], v[178:179], v[134:135]
	v_add_f32_e32 v140, v140, v141
	v_med3_f32 v141, v134, s95, v223
	v_med3_f32 v135, v135, s95, v223
	v_mov_b32_e32 v134, 0
	v_cvt_pk_fp8_f32 v134, v141, v135
	v_pk_mul_f32 v[136:137], v[176:177], v[136:137]
	v_pk_mul_f32 v[130:131], v[186:187], v[130:131]
	v_med3_f32 v135, v136, s95, v223
	v_med3_f32 v136, v137, s95, v223
	v_cvt_pk_fp8_f32 v134, v135, v136 op_sel:[0,0,1]
	v_med3_f32 v130, v130, s95, v223
	v_med3_f32 v131, v131, s95, v223
	v_mov_b32_e32 v135, 0
	v_cvt_pk_fp8_f32 v135, v130, v131
	v_pk_mul_f32 v[132:133], v[184:185], v[132:133]
	v_add_f32_e32 v140, v225, v140
	v_med3_f32 v130, v132, s95, v223
	v_med3_f32 v131, v133, s95, v223
	v_cvt_pk_fp8_f32 v135, v130, v131 op_sel:[0,0,1]
	v_and_b32_e32 v131, 64, v224
	v_xor_b32_e32 v130, 16, v224
	v_add_u32_e32 v131, 64, v131
	v_cmp_lt_i32_e64 s[6:7], v130, v131
	v_xor_b32_e32 v132, 32, v224
	flat_store_dwordx2 v[138:139], v[134:135] offset:128
	v_cndmask_b32_e64 v130, v224, v130, s[6:7]
	v_lshlrev_b32_e32 v225, 2, v130
	ds_bpermute_b32 v130, v225, v140
	v_cmp_lt_i32_e64 s[6:7], v132, v131
	s_waitcnt lgkmcnt(0)
	v_add_f32_e32 v130, v140, v130
	v_cndmask_b32_e64 v131, v224, v132, s[6:7]
	v_lshlrev_b32_e32 v226, 2, v131
	ds_bpermute_b32 v131, v226, v130
	s_and_saveexec_b64 s[6:7], vcc
	s_cbranch_execz .LBB0_1188
	v_lshlrev_b64 v[132:133], 7, v[190:191]
	v_lshl_add_u64 v[132:133], s[62:63], 0, v[132:133]
	s_waitcnt lgkmcnt(0)
	v_add_f32_e32 v130, v130, v131
	flat_store_dword v[132:133], v130
.LBB0_1188:
	s_or_b64 exec, exec, s[6:7]
	v_lshl_add_u64 v[162:163], v[190:191], 0, 32
	v_lshlrev_b64 v[164:165], 13, v[162:163]
	v_lshl_add_u64 v[132:133], s[68:69], 0, v[164:165]
	s_mov_b64 s[6:7], 0x7fe0
	s_waitcnt lgkmcnt(0)
	v_lshl_add_u64 v[130:131], s[66:67], 0, v[164:165]
	v_lshl_add_u64 v[132:133], v[132:133], 0, s[30:31]
	v_cmp_gt_i64_e64 s[6:7], s[6:7], v[190:191]
	v_pk_fma_f32 v[112:113], v[112:113], v[116:117], v[160:161]
	v_pk_fma_f32 v[110:111], v[110:111], v[114:115], v[158:159]
	v_cndmask_b32_e64 v131, v133, v131, s[6:7]
	v_cndmask_b32_e64 v130, v132, v130, s[6:7]
	v_lshl_add_u64 v[130:131], v[130:131], 0, v[188:189]
	flat_load_dwordx4 v[142:145], v[130:131] nt
	flat_load_dwordx4 v[138:141], v[130:131] offset:16 nt
	flat_load_dwordx4 v[134:137], v[130:131] offset:512 nt
	s_nop 0
	flat_load_dwordx4 v[130:133], v[130:131] offset:528 nt
	v_lshl_add_u64 v[228:229], s[64:65], 0, v[194:195]
	v_pk_fma_f32 v[108:109], v[108:109], v[120:121], v[156:157]
	v_mul_f32_e32 v156, v111, v111
	v_mul_f32_e32 v157, v113, v113
	v_lshl_add_u64 v[228:229], v[228:229], 0, s[30:31]
	v_lshl_add_u64 v[194:195], s[60:61], 0, v[194:195]
	v_pk_fma_f32 v[106:107], v[106:107], v[118:119], v[154:155]
	v_fmac_f32_e32 v156, v110, v110
	v_fmac_f32_e32 v157, v112, v112
	v_cndmask_b32_e64 v195, v229, v195, s[4:5]
	v_cndmask_b32_e64 v194, v228, v194, s[4:5]
	v_add_f32_e32 v156, v156, v157
	v_mul_f32_e32 v157, v107, v107
	v_mul_f32_e32 v158, v109, v109
	v_lshl_add_u64 v[154:155], v[194:195], 0, v[188:189]
	v_fmac_f32_e32 v157, v106, v106
	v_fmac_f32_e32 v158, v108, v108
	flat_store_dwordx4 v[154:155], v[110:113] nt
	flat_store_dwordx4 v[154:155], v[106:109] offset:16 nt
	v_add_f32_e32 v157, v157, v158
	v_pk_mul_f32 v[110:111], v[174:175], v[110:111]
	v_add_f32_e32 v156, v156, v157
	v_pk_mul_f32 v[106:107], v[182:183], v[106:107]
	v_med3_f32 v157, v110, s95, v223
	v_med3_f32 v111, v111, s95, v223
	v_mov_b32_e32 v110, 0
	v_cvt_pk_fp8_f32 v110, v157, v111
	v_med3_f32 v106, v106, s95, v223
	v_med3_f32 v107, v107, s95, v223
	v_mov_b32_e32 v111, 0
	v_cvt_pk_fp8_f32 v111, v106, v107
	v_pk_mul_f32 v[108:109], v[180:181], v[108:109]
	v_pk_fma_f32 v[104:105], v[104:105], v[124:125], v[152:153]
	v_med3_f32 v106, v108, s95, v223
	v_med3_f32 v107, v109, s95, v223
	v_pk_fma_f32 v[102:103], v[102:103], v[122:123], v[150:151]
	v_cvt_pk_fp8_f32 v111, v106, v107 op_sel:[0,0,1]
	v_pk_fma_f32 v[106:107], v[98:99], v[126:127], v[146:147]
	v_mul_f32_e32 v98, v103, v103
	v_mul_f32_e32 v99, v105, v105
	v_pk_fma_f32 v[108:109], v[100:101], v[128:129], v[148:149]
	v_fmac_f32_e32 v98, v102, v102
	v_fmac_f32_e32 v99, v104, v104
	v_add_f32_e32 v98, v98, v99
	v_mul_f32_e32 v99, v107, v107
	v_mul_f32_e32 v100, v109, v109
	v_fmac_f32_e32 v99, v106, v106
	v_fmac_f32_e32 v100, v108, v108
	v_add_f32_e32 v99, v99, v100
	v_pk_mul_f32 v[100:101], v[178:179], v[102:103]
	v_add_f32_e32 v98, v98, v99
	v_pk_mul_f32 v[148:149], v[186:187], v[106:107]
	v_med3_f32 v151, v100, s95, v223
	v_med3_f32 v101, v101, s95, v223
	v_mov_b32_e32 v100, 0
	v_add_f32_e32 v150, v156, v98
	v_cvt_pk_fp8_f32 v100, v151, v101
	v_med3_f32 v148, v148, s95, v223
	v_med3_f32 v149, v149, s95, v223
	v_mov_b32_e32 v101, 0
	v_cvt_pk_fp8_f32 v101, v148, v149
	ds_bpermute_b32 v148, v225, v150
	v_pk_mul_f32 v[98:99], v[176:177], v[104:105]
	v_pk_mul_f32 v[146:147], v[184:185], v[108:109]
	v_med3_f32 v98, v98, s95, v223
	v_med3_f32 v99, v99, s95, v223
	v_cvt_pk_fp8_f32 v100, v98, v99 op_sel:[0,0,1]
	v_med3_f32 v98, v146, s95, v223
	v_med3_f32 v99, v147, s95, v223
	v_pk_mul_f32 v[112:113], v[172:173], v[112:113]
	v_cvt_pk_fp8_f32 v101, v98, v99 op_sel:[0,0,1]
	s_waitcnt lgkmcnt(0)
	v_add_f32_e32 v98, v150, v148
	v_med3_f32 v112, v112, s95, v223
	v_med3_f32 v113, v113, s95, v223
	ds_bpermute_b32 v99, v226, v98
	v_cvt_pk_fp8_f32 v110, v112, v113 op_sel:[0,0,1]
	v_lshlrev_b64 v[228:229], 11, v[192:193]
	v_lshl_add_u64 v[228:229], s[58:59], 0, v[228:229]
	v_lshl_add_u64 v[112:113], v[228:229], 0, v[170:171]
	flat_store_dwordx2 v[112:113], v[110:111]
	flat_store_dwordx4 v[154:155], v[102:105] offset:512 nt
	flat_store_dwordx4 v[154:155], v[106:109] offset:528 nt
	flat_store_dwordx2 v[112:113], v[100:101] offset:128
	s_and_saveexec_b64 s[4:5], vcc
	s_cbranch_execz .LBB0_1190
	v_lshlrev_b64 v[100:101], 7, v[192:193]
	v_lshl_add_u64 v[100:101], s[62:63], 0, v[100:101]
	s_waitcnt lgkmcnt(0)
	v_add_f32_e32 v98, v98, v99
	flat_store_dword v[100:101], v98
.LBB0_1190:
	s_or_b64 exec, exec, s[4:5]
	v_lshl_add_u64 v[146:147], v[190:191], 0, 48
	v_lshlrev_b64 v[148:149], 13, v[146:147]
	v_lshl_add_u64 v[100:101], s[68:69], 0, v[148:149]
	s_mov_b64 s[4:5], 0x7fd0
	s_waitcnt lgkmcnt(0)
	v_lshl_add_u64 v[98:99], s[66:67], 0, v[148:149]
	v_lshl_add_u64 v[100:101], v[100:101], 0, s[30:31]
	v_cmp_gt_i64_e64 s[4:5], s[4:5], v[190:191]
	s_waitcnt vmcnt(0)
	v_pk_fma_f32 v[96:97], v[96:97], v[116:117], v[144:145]
	v_pk_fma_f32 v[94:95], v[94:95], v[114:115], v[142:143]
	v_cndmask_b32_e64 v99, v101, v99, s[4:5]
	v_cndmask_b32_e64 v98, v100, v98, s[4:5]
	v_lshl_add_u64 v[98:99], v[98:99], 0, v[188:189]
	flat_load_dwordx4 v[110:113], v[98:99] nt
	flat_load_dwordx4 v[106:109], v[98:99] offset:16 nt
	flat_load_dwordx4 v[102:105], v[98:99] offset:512 nt
	s_nop 0
	flat_load_dwordx4 v[98:101], v[98:99] offset:528 nt
	v_lshl_add_u64 v[150:151], s[64:65], 0, v[164:165]
	v_pk_fma_f32 v[92:93], v[92:93], v[120:121], v[140:141]
	v_mul_f32_e32 v140, v95, v95
	v_mul_f32_e32 v141, v97, v97
	v_lshl_add_u64 v[150:151], v[150:151], 0, s[30:31]
	v_lshl_add_u64 v[152:153], s[60:61], 0, v[164:165]
	v_pk_fma_f32 v[90:91], v[90:91], v[118:119], v[138:139]
	v_fmac_f32_e32 v140, v94, v94
	v_fmac_f32_e32 v141, v96, v96
	v_cndmask_b32_e64 v151, v151, v153, s[6:7]
	v_cndmask_b32_e64 v150, v150, v152, s[6:7]
	v_add_f32_e32 v140, v140, v141
	v_mul_f32_e32 v141, v91, v91
	v_mul_f32_e32 v142, v93, v93
	v_lshl_add_u64 v[138:139], v[150:151], 0, v[188:189]
	v_fmac_f32_e32 v141, v90, v90
	v_fmac_f32_e32 v142, v92, v92
	flat_store_dwordx4 v[138:139], v[94:97] nt
	flat_store_dwordx4 v[138:139], v[90:93] offset:16 nt
	v_add_f32_e32 v141, v141, v142
	v_pk_mul_f32 v[94:95], v[174:175], v[94:95]
	v_add_f32_e32 v140, v140, v141
	v_pk_mul_f32 v[90:91], v[182:183], v[90:91]
	v_med3_f32 v141, v94, s95, v223
	v_med3_f32 v95, v95, s95, v223
	v_mov_b32_e32 v94, 0
	v_cvt_pk_fp8_f32 v94, v141, v95
	v_med3_f32 v90, v90, s95, v223
	v_med3_f32 v91, v91, s95, v223
	v_mov_b32_e32 v95, 0
	v_cvt_pk_fp8_f32 v95, v90, v91
	v_pk_mul_f32 v[92:93], v[180:181], v[92:93]
	v_pk_fma_f32 v[88:89], v[88:89], v[124:125], v[136:137]
	v_med3_f32 v90, v92, s95, v223
	v_med3_f32 v91, v93, s95, v223
	v_pk_fma_f32 v[86:87], v[86:87], v[122:123], v[134:135]
	v_cvt_pk_fp8_f32 v95, v90, v91 op_sel:[0,0,1]
	v_pk_fma_f32 v[90:91], v[82:83], v[126:127], v[130:131]
	v_mul_f32_e32 v82, v87, v87
	v_mul_f32_e32 v83, v89, v89
	v_pk_fma_f32 v[92:93], v[84:85], v[128:129], v[132:133]
	v_fmac_f32_e32 v82, v86, v86
	v_fmac_f32_e32 v83, v88, v88
	v_add_f32_e32 v82, v82, v83
	v_mul_f32_e32 v83, v91, v91
	v_mul_f32_e32 v84, v93, v93
	v_fmac_f32_e32 v83, v90, v90
	v_fmac_f32_e32 v84, v92, v92
	v_add_f32_e32 v83, v83, v84
	v_pk_mul_f32 v[84:85], v[178:179], v[86:87]
	v_add_f32_e32 v82, v82, v83
	v_pk_mul_f32 v[132:133], v[186:187], v[90:91]
	v_med3_f32 v135, v84, s95, v223
	v_med3_f32 v85, v85, s95, v223
	v_mov_b32_e32 v84, 0
	v_add_f32_e32 v134, v140, v82
	v_cvt_pk_fp8_f32 v84, v135, v85
	v_med3_f32 v132, v132, s95, v223
	v_med3_f32 v133, v133, s95, v223
	v_mov_b32_e32 v85, 0
	v_cvt_pk_fp8_f32 v85, v132, v133
	ds_bpermute_b32 v132, v225, v134
	v_pk_mul_f32 v[82:83], v[176:177], v[88:89]
	v_pk_mul_f32 v[130:131], v[184:185], v[92:93]
	v_med3_f32 v82, v82, s95, v223
	v_med3_f32 v83, v83, s95, v223
	v_cvt_pk_fp8_f32 v84, v82, v83 op_sel:[0,0,1]
	v_med3_f32 v82, v130, s95, v223
	v_med3_f32 v83, v131, s95, v223
	v_pk_mul_f32 v[96:97], v[172:173], v[96:97]
	v_cvt_pk_fp8_f32 v85, v82, v83 op_sel:[0,0,1]
	s_waitcnt lgkmcnt(0)
	v_add_f32_e32 v82, v134, v132
	v_med3_f32 v96, v96, s95, v223
	v_med3_f32 v97, v97, s95, v223
	ds_bpermute_b32 v83, v226, v82
	v_cvt_pk_fp8_f32 v94, v96, v97 op_sel:[0,0,1]
	v_lshlrev_b64 v[152:153], 11, v[162:163]
	v_lshl_add_u64 v[152:153], s[58:59], 0, v[152:153]
	v_lshl_add_u64 v[96:97], v[152:153], 0, v[170:171]
	flat_store_dwordx2 v[96:97], v[94:95]
	flat_store_dwordx4 v[138:139], v[86:89] offset:512 nt
	flat_store_dwordx4 v[138:139], v[90:93] offset:528 nt
	flat_store_dwordx2 v[96:97], v[84:85] offset:128
	s_and_saveexec_b64 s[6:7], vcc
	s_cbranch_execz .LBB0_1192
	v_lshlrev_b64 v[84:85], 7, v[162:163]
	v_lshl_add_u64 v[84:85], s[62:63], 0, v[84:85]
	s_waitcnt lgkmcnt(0)
	v_add_f32_e32 v82, v82, v83
	flat_store_dword v[84:85], v82
.LBB0_1192:
	s_or_b64 exec, exec, s[6:7]
	s_mov_b64 s[6:7], 0x80
	v_lshl_add_u64 v[130:131], v[190:191], 0, s[6:7]
	v_lshlrev_b64 v[132:133], 13, v[130:131]
	v_lshl_add_u64 v[84:85], s[68:69], 0, v[132:133]
	s_mov_b64 s[6:7], 0x7f80
	s_waitcnt lgkmcnt(0)
	v_lshl_add_u64 v[82:83], s[66:67], 0, v[132:133]
	v_lshl_add_u64 v[84:85], v[84:85], 0, s[30:31]
	v_cmp_gt_i64_e64 s[6:7], s[6:7], v[190:191]
	s_waitcnt vmcnt(0)
	v_pk_fma_f32 v[80:81], v[80:81], v[116:117], v[112:113]
	v_pk_fma_f32 v[78:79], v[78:79], v[114:115], v[110:111]
	v_cndmask_b32_e64 v83, v85, v83, s[6:7]
	v_cndmask_b32_e64 v82, v84, v82, s[6:7]
	v_lshl_add_u64 v[82:83], v[82:83], 0, v[188:189]
	flat_load_dwordx4 v[94:97], v[82:83] nt
	flat_load_dwordx4 v[90:93], v[82:83] offset:16 nt
	flat_load_dwordx4 v[86:89], v[82:83] offset:512 nt
	s_nop 0
	flat_load_dwordx4 v[82:85], v[82:83] offset:528 nt
	v_lshl_add_u64 v[134:135], s[64:65], 0, v[148:149]
	v_pk_fma_f32 v[76:77], v[76:77], v[120:121], v[108:109]
	v_mul_f32_e32 v108, v79, v79
	v_mul_f32_e32 v109, v81, v81
	v_lshl_add_u64 v[134:135], v[134:135], 0, s[30:31]
	v_lshl_add_u64 v[136:137], s[60:61], 0, v[148:149]
	v_pk_fma_f32 v[74:75], v[74:75], v[118:119], v[106:107]
	v_fmac_f32_e32 v108, v78, v78
	v_fmac_f32_e32 v109, v80, v80
	v_cndmask_b32_e64 v135, v135, v137, s[4:5]
	v_cndmask_b32_e64 v134, v134, v136, s[4:5]
	v_add_f32_e32 v108, v108, v109
	v_mul_f32_e32 v109, v75, v75
	v_mul_f32_e32 v110, v77, v77
	v_lshl_add_u64 v[106:107], v[134:135], 0, v[188:189]
	v_fmac_f32_e32 v109, v74, v74
	v_fmac_f32_e32 v110, v76, v76
	flat_store_dwordx4 v[106:107], v[78:81] nt
	flat_store_dwordx4 v[106:107], v[74:77] offset:16 nt
	v_add_f32_e32 v109, v109, v110
	v_pk_mul_f32 v[78:79], v[174:175], v[78:79]
	v_add_f32_e32 v108, v108, v109
	v_pk_mul_f32 v[74:75], v[182:183], v[74:75]
	v_med3_f32 v109, v78, s95, v223
	v_med3_f32 v79, v79, s95, v223
	v_mov_b32_e32 v78, 0
	v_cvt_pk_fp8_f32 v78, v109, v79
	v_med3_f32 v74, v74, s95, v223
	v_med3_f32 v75, v75, s95, v223
	v_mov_b32_e32 v79, 0
	v_cvt_pk_fp8_f32 v79, v74, v75
	v_pk_mul_f32 v[76:77], v[180:181], v[76:77]
	v_pk_fma_f32 v[72:73], v[72:73], v[124:125], v[104:105]
	v_med3_f32 v74, v76, s95, v223
	v_med3_f32 v75, v77, s95, v223
	v_pk_fma_f32 v[70:71], v[70:71], v[122:123], v[102:103]
	v_cvt_pk_fp8_f32 v79, v74, v75 op_sel:[0,0,1]
	v_pk_fma_f32 v[74:75], v[66:67], v[126:127], v[98:99]
	v_mul_f32_e32 v66, v71, v71
	v_mul_f32_e32 v67, v73, v73
	v_pk_fma_f32 v[76:77], v[68:69], v[128:129], v[100:101]
	v_fmac_f32_e32 v66, v70, v70
	v_fmac_f32_e32 v67, v72, v72
	v_add_f32_e32 v66, v66, v67
	v_mul_f32_e32 v67, v75, v75
	v_mul_f32_e32 v68, v77, v77
	v_fmac_f32_e32 v67, v74, v74
	v_fmac_f32_e32 v68, v76, v76
	v_add_f32_e32 v67, v67, v68
	v_pk_mul_f32 v[68:69], v[178:179], v[70:71]
	v_add_f32_e32 v66, v66, v67
	v_pk_mul_f32 v[100:101], v[186:187], v[74:75]
	v_med3_f32 v103, v68, s95, v223
	v_med3_f32 v69, v69, s95, v223
	v_mov_b32_e32 v68, 0
	v_add_f32_e32 v102, v108, v66
	v_cvt_pk_fp8_f32 v68, v103, v69
	v_med3_f32 v100, v100, s95, v223
	v_med3_f32 v101, v101, s95, v223
	v_mov_b32_e32 v69, 0
	v_cvt_pk_fp8_f32 v69, v100, v101
	ds_bpermute_b32 v100, v225, v102
	v_pk_mul_f32 v[66:67], v[176:177], v[72:73]
	v_pk_mul_f32 v[98:99], v[184:185], v[76:77]
	v_med3_f32 v66, v66, s95, v223
	v_med3_f32 v67, v67, s95, v223
	v_cvt_pk_fp8_f32 v68, v66, v67 op_sel:[0,0,1]
	v_med3_f32 v66, v98, s95, v223
	v_med3_f32 v67, v99, s95, v223
	v_pk_mul_f32 v[80:81], v[172:173], v[80:81]
	v_cvt_pk_fp8_f32 v69, v66, v67 op_sel:[0,0,1]
	s_waitcnt lgkmcnt(0)
	v_add_f32_e32 v66, v102, v100
	v_med3_f32 v80, v80, s95, v223
	v_med3_f32 v81, v81, s95, v223
	ds_bpermute_b32 v67, v226, v66
	v_cvt_pk_fp8_f32 v78, v80, v81 op_sel:[0,0,1]
	v_lshlrev_b64 v[136:137], 11, v[146:147]
	v_lshl_add_u64 v[136:137], s[58:59], 0, v[136:137]
	v_lshl_add_u64 v[80:81], v[136:137], 0, v[170:171]
	flat_store_dwordx2 v[80:81], v[78:79]
	flat_store_dwordx4 v[106:107], v[70:73] offset:512 nt
	flat_store_dwordx4 v[106:107], v[74:77] offset:528 nt
	flat_store_dwordx2 v[80:81], v[68:69] offset:128
	s_and_saveexec_b64 s[4:5], vcc
	s_cbranch_execz .LBB0_1194
	v_lshlrev_b64 v[68:69], 7, v[146:147]
	v_lshl_add_u64 v[68:69], s[62:63], 0, v[68:69]
	s_waitcnt lgkmcnt(0)
	v_add_f32_e32 v66, v66, v67
	flat_store_dword v[68:69], v66
.LBB0_1194:
	s_or_b64 exec, exec, s[4:5]
	v_lshl_add_u64 v[98:99], v[190:191], 0, s[46:47]
	v_lshlrev_b64 v[100:101], 13, v[98:99]
	v_lshl_add_u64 v[68:69], s[68:69], 0, v[100:101]
	s_waitcnt lgkmcnt(0)
	v_lshl_add_u64 v[66:67], s[66:67], 0, v[100:101]
	v_lshl_add_u64 v[68:69], v[68:69], 0, s[30:31]
	v_cmp_gt_i64_e64 s[4:5], s[48:49], v[190:191]
	s_waitcnt vmcnt(0)
	v_pk_fma_f32 v[64:65], v[64:65], v[116:117], v[96:97]
	v_pk_fma_f32 v[62:63], v[62:63], v[114:115], v[94:95]
	v_cndmask_b32_e64 v67, v69, v67, s[4:5]
	v_cndmask_b32_e64 v66, v68, v66, s[4:5]
	v_lshl_add_u64 v[66:67], v[66:67], 0, v[188:189]
	flat_load_dwordx4 v[78:81], v[66:67] nt
	flat_load_dwordx4 v[74:77], v[66:67] offset:16 nt
	flat_load_dwordx4 v[70:73], v[66:67] offset:512 nt
	s_nop 0
	flat_load_dwordx4 v[66:69], v[66:67] offset:528 nt
	v_lshl_add_u64 v[102:103], s[64:65], 0, v[132:133]
	v_pk_fma_f32 v[60:61], v[60:61], v[120:121], v[92:93]
	v_mul_f32_e32 v92, v63, v63
	v_mul_f32_e32 v93, v65, v65
	v_lshl_add_u64 v[102:103], v[102:103], 0, s[30:31]
	v_lshl_add_u64 v[104:105], s[60:61], 0, v[132:133]
	v_pk_fma_f32 v[58:59], v[58:59], v[118:119], v[90:91]
	v_fmac_f32_e32 v92, v62, v62
	v_fmac_f32_e32 v93, v64, v64
	v_cndmask_b32_e64 v103, v103, v105, s[6:7]
	v_cndmask_b32_e64 v102, v102, v104, s[6:7]
	v_add_f32_e32 v92, v92, v93
	v_mul_f32_e32 v93, v59, v59
	v_mul_f32_e32 v94, v61, v61
	v_lshl_add_u64 v[90:91], v[102:103], 0, v[188:189]
	v_fmac_f32_e32 v93, v58, v58
	v_fmac_f32_e32 v94, v60, v60
	flat_store_dwordx4 v[90:91], v[62:65] nt
	flat_store_dwordx4 v[90:91], v[58:61] offset:16 nt
	v_add_f32_e32 v93, v93, v94
	v_pk_mul_f32 v[62:63], v[174:175], v[62:63]
	v_add_f32_e32 v92, v92, v93
	v_pk_mul_f32 v[58:59], v[182:183], v[58:59]
	v_med3_f32 v93, v62, s95, v223
	v_med3_f32 v63, v63, s95, v223
	v_mov_b32_e32 v62, 0
	v_cvt_pk_fp8_f32 v62, v93, v63
	v_med3_f32 v58, v58, s95, v223
	v_med3_f32 v59, v59, s95, v223
	v_mov_b32_e32 v63, 0
	v_cvt_pk_fp8_f32 v63, v58, v59
	v_pk_mul_f32 v[60:61], v[180:181], v[60:61]
	v_pk_fma_f32 v[56:57], v[56:57], v[124:125], v[88:89]
	v_med3_f32 v58, v60, s95, v223
	v_med3_f32 v59, v61, s95, v223
	v_pk_fma_f32 v[54:55], v[54:55], v[122:123], v[86:87]
	v_cvt_pk_fp8_f32 v63, v58, v59 op_sel:[0,0,1]
	v_pk_fma_f32 v[58:59], v[50:51], v[126:127], v[82:83]
	v_mul_f32_e32 v50, v55, v55
	v_mul_f32_e32 v51, v57, v57
	v_pk_fma_f32 v[60:61], v[52:53], v[128:129], v[84:85]
	v_fmac_f32_e32 v50, v54, v54
	v_fmac_f32_e32 v51, v56, v56
	v_add_f32_e32 v50, v50, v51
	v_mul_f32_e32 v51, v59, v59
	v_mul_f32_e32 v52, v61, v61
	v_fmac_f32_e32 v51, v58, v58
	v_fmac_f32_e32 v52, v60, v60
	v_add_f32_e32 v51, v51, v52
	v_pk_mul_f32 v[52:53], v[178:179], v[54:55]
	v_add_f32_e32 v50, v50, v51
	v_pk_mul_f32 v[84:85], v[186:187], v[58:59]
	v_med3_f32 v87, v52, s95, v223
	v_med3_f32 v53, v53, s95, v223
	v_mov_b32_e32 v52, 0
	v_add_f32_e32 v86, v92, v50
	v_cvt_pk_fp8_f32 v52, v87, v53
	v_med3_f32 v84, v84, s95, v223
	v_med3_f32 v85, v85, s95, v223
	v_mov_b32_e32 v53, 0
	v_cvt_pk_fp8_f32 v53, v84, v85
	ds_bpermute_b32 v84, v225, v86
	v_pk_mul_f32 v[50:51], v[176:177], v[56:57]
	v_pk_mul_f32 v[82:83], v[184:185], v[60:61]
	v_med3_f32 v50, v50, s95, v223
	v_med3_f32 v51, v51, s95, v223
	v_cvt_pk_fp8_f32 v52, v50, v51 op_sel:[0,0,1]
	v_med3_f32 v50, v82, s95, v223
	v_med3_f32 v51, v83, s95, v223
	v_pk_mul_f32 v[64:65], v[172:173], v[64:65]
	v_cvt_pk_fp8_f32 v53, v50, v51 op_sel:[0,0,1]
	s_waitcnt lgkmcnt(0)
	v_add_f32_e32 v50, v86, v84
	v_med3_f32 v64, v64, s95, v223
	v_med3_f32 v65, v65, s95, v223
	ds_bpermute_b32 v51, v226, v50
	v_cvt_pk_fp8_f32 v62, v64, v65 op_sel:[0,0,1]
	v_lshlrev_b64 v[104:105], 11, v[130:131]
	v_lshl_add_u64 v[104:105], s[58:59], 0, v[104:105]
	v_lshl_add_u64 v[64:65], v[104:105], 0, v[170:171]
	flat_store_dwordx2 v[64:65], v[62:63]
	flat_store_dwordx4 v[90:91], v[54:57] offset:512 nt
	flat_store_dwordx4 v[90:91], v[58:61] offset:528 nt
	flat_store_dwordx2 v[64:65], v[52:53] offset:128
	s_and_saveexec_b64 s[6:7], vcc
	s_cbranch_execz .LBB0_1196
	v_lshlrev_b64 v[52:53], 7, v[130:131]
	v_lshl_add_u64 v[52:53], s[62:63], 0, v[52:53]
	s_waitcnt lgkmcnt(0)
	v_add_f32_e32 v50, v50, v51
	flat_store_dword v[52:53], v50
.LBB0_1196:
	s_or_b64 exec, exec, s[6:7]
	v_lshl_add_u64 v[82:83], v[190:191], 0, s[50:51]
	v_lshlrev_b64 v[84:85], 13, v[82:83]
	v_lshl_add_u64 v[52:53], s[68:69], 0, v[84:85]
	s_waitcnt lgkmcnt(0)
	v_lshl_add_u64 v[50:51], s[66:67], 0, v[84:85]
	v_lshl_add_u64 v[52:53], v[52:53], 0, s[30:31]
	v_cmp_gt_i64_e64 s[6:7], s[52:53], v[190:191]
	s_waitcnt vmcnt(0)
	v_pk_fma_f32 v[48:49], v[48:49], v[116:117], v[80:81]
	v_pk_fma_f32 v[46:47], v[46:47], v[114:115], v[78:79]
	v_cndmask_b32_e64 v51, v53, v51, s[6:7]
	v_cndmask_b32_e64 v50, v52, v50, s[6:7]
	v_lshl_add_u64 v[50:51], v[50:51], 0, v[188:189]
	flat_load_dwordx4 v[62:65], v[50:51] nt
	flat_load_dwordx4 v[58:61], v[50:51] offset:16 nt
	flat_load_dwordx4 v[54:57], v[50:51] offset:512 nt
	s_nop 0
	flat_load_dwordx4 v[50:53], v[50:51] offset:528 nt
	v_lshl_add_u64 v[86:87], s[64:65], 0, v[100:101]
	v_pk_fma_f32 v[44:45], v[44:45], v[120:121], v[76:77]
	v_mul_f32_e32 v76, v47, v47
	v_mul_f32_e32 v77, v49, v49
	v_lshl_add_u64 v[86:87], v[86:87], 0, s[30:31]
	v_lshl_add_u64 v[88:89], s[60:61], 0, v[100:101]
	v_pk_fma_f32 v[42:43], v[42:43], v[118:119], v[74:75]
	v_fmac_f32_e32 v76, v46, v46
	v_fmac_f32_e32 v77, v48, v48
	v_cndmask_b32_e64 v87, v87, v89, s[4:5]
	v_cndmask_b32_e64 v86, v86, v88, s[4:5]
	v_add_f32_e32 v76, v76, v77
	v_mul_f32_e32 v77, v43, v43
	v_mul_f32_e32 v78, v45, v45
	v_lshl_add_u64 v[74:75], v[86:87], 0, v[188:189]
	v_fmac_f32_e32 v77, v42, v42
	v_fmac_f32_e32 v78, v44, v44
	flat_store_dwordx4 v[74:75], v[46:49] nt
	flat_store_dwordx4 v[74:75], v[42:45] offset:16 nt
	v_add_f32_e32 v77, v77, v78
	v_pk_mul_f32 v[46:47], v[174:175], v[46:47]
	v_add_f32_e32 v76, v76, v77
	v_pk_mul_f32 v[42:43], v[182:183], v[42:43]
	v_med3_f32 v77, v46, s95, v223
	v_med3_f32 v47, v47, s95, v223
	v_mov_b32_e32 v46, 0
	v_cvt_pk_fp8_f32 v46, v77, v47
	v_med3_f32 v42, v42, s95, v223
	v_med3_f32 v43, v43, s95, v223
	v_mov_b32_e32 v47, 0
	v_cvt_pk_fp8_f32 v47, v42, v43
	v_pk_mul_f32 v[44:45], v[180:181], v[44:45]
	v_pk_fma_f32 v[40:41], v[40:41], v[124:125], v[72:73]
	v_med3_f32 v42, v44, s95, v223
	v_med3_f32 v43, v45, s95, v223
	v_pk_fma_f32 v[38:39], v[38:39], v[122:123], v[70:71]
	v_cvt_pk_fp8_f32 v47, v42, v43 op_sel:[0,0,1]
	v_pk_fma_f32 v[42:43], v[34:35], v[126:127], v[66:67]
	v_mul_f32_e32 v34, v39, v39
	v_mul_f32_e32 v35, v41, v41
	v_pk_fma_f32 v[44:45], v[36:37], v[128:129], v[68:69]
	v_fmac_f32_e32 v34, v38, v38
	v_fmac_f32_e32 v35, v40, v40
	v_add_f32_e32 v34, v34, v35
	v_mul_f32_e32 v35, v43, v43
	v_mul_f32_e32 v36, v45, v45
	v_fmac_f32_e32 v35, v42, v42
	v_fmac_f32_e32 v36, v44, v44
	v_add_f32_e32 v35, v35, v36
	v_pk_mul_f32 v[36:37], v[178:179], v[38:39]
	v_add_f32_e32 v34, v34, v35
	v_pk_mul_f32 v[68:69], v[186:187], v[42:43]
	v_med3_f32 v71, v36, s95, v223
	v_med3_f32 v37, v37, s95, v223
	v_mov_b32_e32 v36, 0
	v_add_f32_e32 v70, v76, v34
	v_cvt_pk_fp8_f32 v36, v71, v37
	v_med3_f32 v68, v68, s95, v223
	v_med3_f32 v69, v69, s95, v223
	v_mov_b32_e32 v37, 0
	v_cvt_pk_fp8_f32 v37, v68, v69
	ds_bpermute_b32 v68, v225, v70
	v_pk_mul_f32 v[34:35], v[176:177], v[40:41]
	v_pk_mul_f32 v[66:67], v[184:185], v[44:45]
	v_med3_f32 v34, v34, s95, v223
	v_med3_f32 v35, v35, s95, v223
	v_cvt_pk_fp8_f32 v36, v34, v35 op_sel:[0,0,1]
	v_med3_f32 v34, v66, s95, v223
	v_med3_f32 v35, v67, s95, v223
	v_pk_mul_f32 v[48:49], v[172:173], v[48:49]
	v_cvt_pk_fp8_f32 v37, v34, v35 op_sel:[0,0,1]
	s_waitcnt lgkmcnt(0)
	v_add_f32_e32 v34, v70, v68
	v_med3_f32 v48, v48, s95, v223
	v_med3_f32 v49, v49, s95, v223
	ds_bpermute_b32 v35, v226, v34
	v_cvt_pk_fp8_f32 v46, v48, v49 op_sel:[0,0,1]
	v_lshlrev_b64 v[88:89], 11, v[98:99]
	v_lshl_add_u64 v[88:89], s[58:59], 0, v[88:89]
	v_lshl_add_u64 v[48:49], v[88:89], 0, v[170:171]
	flat_store_dwordx2 v[48:49], v[46:47]
	flat_store_dwordx4 v[74:75], v[38:41] offset:512 nt
	flat_store_dwordx4 v[74:75], v[42:45] offset:528 nt
	flat_store_dwordx2 v[48:49], v[36:37] offset:128
	s_and_saveexec_b64 s[4:5], vcc
	s_cbranch_execz .LBB0_1198
	v_lshlrev_b64 v[36:37], 7, v[98:99]
	v_lshl_add_u64 v[36:37], s[62:63], 0, v[36:37]
	s_waitcnt lgkmcnt(0)
	v_add_f32_e32 v34, v34, v35
	flat_store_dword v[36:37], v34
.LBB0_1198:
	s_or_b64 exec, exec, s[4:5]
	v_lshl_add_u64 v[66:67], v[190:191], 0, s[54:55]
	v_lshlrev_b64 v[68:69], 13, v[66:67]
	v_lshl_add_u64 v[36:37], s[68:69], 0, v[68:69]
	s_waitcnt lgkmcnt(0)
	v_lshl_add_u64 v[34:35], s[66:67], 0, v[68:69]
	v_lshl_add_u64 v[36:37], v[36:37], 0, s[30:31]
	v_cmp_gt_i64_e64 s[4:5], s[56:57], v[190:191]
	s_waitcnt vmcnt(0)
	v_pk_fma_f32 v[32:33], v[32:33], v[116:117], v[64:65]
	v_pk_fma_f32 v[30:31], v[30:31], v[114:115], v[62:63]
	v_cndmask_b32_e64 v35, v37, v35, s[4:5]
	v_cndmask_b32_e64 v34, v36, v34, s[4:5]
	v_lshl_add_u64 v[34:35], v[34:35], 0, v[188:189]
	flat_load_dwordx4 v[46:49], v[34:35] nt
	flat_load_dwordx4 v[42:45], v[34:35] offset:16 nt
	flat_load_dwordx4 v[38:41], v[34:35] offset:512 nt
	s_nop 0
	flat_load_dwordx4 v[34:37], v[34:35] offset:528 nt
	v_lshl_add_u64 v[70:71], s[64:65], 0, v[84:85]
	v_pk_fma_f32 v[28:29], v[28:29], v[120:121], v[60:61]
	v_mul_f32_e32 v60, v31, v31
	v_mul_f32_e32 v61, v33, v33
	v_lshl_add_u64 v[70:71], v[70:71], 0, s[30:31]
	v_lshl_add_u64 v[72:73], s[60:61], 0, v[84:85]
	v_pk_fma_f32 v[26:27], v[26:27], v[118:119], v[58:59]
	v_fmac_f32_e32 v60, v30, v30
	v_fmac_f32_e32 v61, v32, v32
	v_cndmask_b32_e64 v71, v71, v73, s[6:7]
	v_cndmask_b32_e64 v70, v70, v72, s[6:7]
	v_add_f32_e32 v60, v60, v61
	v_mul_f32_e32 v61, v27, v27
	v_mul_f32_e32 v62, v29, v29
	v_lshl_add_u64 v[58:59], v[70:71], 0, v[188:189]
	v_fmac_f32_e32 v61, v26, v26
	v_fmac_f32_e32 v62, v28, v28
	flat_store_dwordx4 v[58:59], v[30:33] nt
	flat_store_dwordx4 v[58:59], v[26:29] offset:16 nt
	v_add_f32_e32 v61, v61, v62
	v_pk_mul_f32 v[30:31], v[174:175], v[30:31]
	v_add_f32_e32 v60, v60, v61
	v_pk_mul_f32 v[26:27], v[182:183], v[26:27]
	v_med3_f32 v61, v30, s95, v223
	v_med3_f32 v31, v31, s95, v223
	v_mov_b32_e32 v30, 0
	v_cvt_pk_fp8_f32 v30, v61, v31
	v_med3_f32 v26, v26, s95, v223
	v_med3_f32 v27, v27, s95, v223
	v_mov_b32_e32 v31, 0
	v_cvt_pk_fp8_f32 v31, v26, v27
	v_pk_mul_f32 v[28:29], v[180:181], v[28:29]
	v_pk_fma_f32 v[24:25], v[24:25], v[124:125], v[56:57]
	v_med3_f32 v26, v28, s95, v223
	v_med3_f32 v27, v29, s95, v223
	v_pk_fma_f32 v[22:23], v[22:23], v[122:123], v[54:55]
	v_cvt_pk_fp8_f32 v31, v26, v27 op_sel:[0,0,1]
	v_pk_fma_f32 v[26:27], v[18:19], v[126:127], v[50:51]
	v_mul_f32_e32 v18, v23, v23
	v_mul_f32_e32 v19, v25, v25
	v_pk_fma_f32 v[28:29], v[20:21], v[128:129], v[52:53]
	v_fmac_f32_e32 v18, v22, v22
	v_fmac_f32_e32 v19, v24, v24
	v_add_f32_e32 v18, v18, v19
	v_mul_f32_e32 v19, v27, v27
	v_mul_f32_e32 v20, v29, v29
	v_fmac_f32_e32 v19, v26, v26
	v_fmac_f32_e32 v20, v28, v28
	v_add_f32_e32 v19, v19, v20
	v_pk_mul_f32 v[20:21], v[178:179], v[22:23]
	v_add_f32_e32 v18, v18, v19
	v_pk_mul_f32 v[52:53], v[186:187], v[26:27]
	v_med3_f32 v55, v20, s95, v223
	v_med3_f32 v21, v21, s95, v223
	v_mov_b32_e32 v20, 0
	v_add_f32_e32 v54, v60, v18
	v_cvt_pk_fp8_f32 v20, v55, v21
	v_med3_f32 v52, v52, s95, v223
	v_med3_f32 v53, v53, s95, v223
	v_mov_b32_e32 v21, 0
	v_cvt_pk_fp8_f32 v21, v52, v53
	ds_bpermute_b32 v52, v225, v54
	v_pk_mul_f32 v[18:19], v[176:177], v[24:25]
	v_pk_mul_f32 v[50:51], v[184:185], v[28:29]
	v_med3_f32 v18, v18, s95, v223
	v_med3_f32 v19, v19, s95, v223
	v_cvt_pk_fp8_f32 v20, v18, v19 op_sel:[0,0,1]
	v_med3_f32 v18, v50, s95, v223
	v_med3_f32 v19, v51, s95, v223
	v_pk_mul_f32 v[32:33], v[172:173], v[32:33]
	v_cvt_pk_fp8_f32 v21, v18, v19 op_sel:[0,0,1]
	s_waitcnt lgkmcnt(0)
	v_add_f32_e32 v18, v54, v52
	v_med3_f32 v32, v32, s95, v223
	v_med3_f32 v33, v33, s95, v223
	ds_bpermute_b32 v19, v226, v18
	v_cvt_pk_fp8_f32 v30, v32, v33 op_sel:[0,0,1]
	v_lshlrev_b64 v[72:73], 11, v[82:83]
	v_lshl_add_u64 v[72:73], s[58:59], 0, v[72:73]
	v_lshl_add_u64 v[32:33], v[72:73], 0, v[170:171]
	flat_store_dwordx2 v[32:33], v[30:31]
	flat_store_dwordx4 v[58:59], v[22:25] offset:512 nt
	flat_store_dwordx4 v[58:59], v[26:29] offset:528 nt
	flat_store_dwordx2 v[32:33], v[20:21] offset:128
	s_and_saveexec_b64 s[6:7], vcc
	s_cbranch_execz .LBB0_1200
	v_lshlrev_b64 v[20:21], 7, v[82:83]
	v_lshl_add_u64 v[20:21], s[62:63], 0, v[20:21]
	s_waitcnt lgkmcnt(0)
	v_add_f32_e32 v18, v18, v19
	flat_store_dword v[20:21], v18
.LBB0_1200:
	s_or_b64 exec, exec, s[6:7]
	s_waitcnt vmcnt(0)
	v_pk_fma_f32 v[16:17], v[16:17], v[116:117], v[48:49]
	v_pk_fma_f32 v[14:15], v[14:15], v[114:115], v[46:47]
	s_waitcnt lgkmcnt(0)
	v_lshl_add_u64 v[18:19], s[64:65], 0, v[68:69]
	v_mul_f32_e32 v22, v15, v15
	v_mul_f32_e32 v23, v17, v17
	v_lshl_add_u64 v[18:19], v[18:19], 0, s[30:31]
	v_lshl_add_u64 v[20:21], s[60:61], 0, v[68:69]
	v_pk_fma_f32 v[12:13], v[12:13], v[120:121], v[44:45]
	v_pk_fma_f32 v[10:11], v[10:11], v[118:119], v[42:43]
	v_fmac_f32_e32 v22, v14, v14
	v_fmac_f32_e32 v23, v16, v16
	v_cndmask_b32_e64 v19, v19, v21, s[4:5]
	v_cndmask_b32_e64 v18, v18, v20, s[4:5]
	v_add_f32_e32 v22, v22, v23
	v_mul_f32_e32 v23, v11, v11
	v_mul_f32_e32 v24, v13, v13
	v_lshl_add_u64 v[18:19], v[170:171], 2, v[18:19]
	v_fmac_f32_e32 v23, v10, v10
	v_fmac_f32_e32 v24, v12, v12
	flat_store_dwordx4 v[18:19], v[14:17] nt
	flat_store_dwordx4 v[18:19], v[10:13] offset:16 nt
	v_add_f32_e32 v23, v23, v24
	v_pk_mul_f32 v[14:15], v[174:175], v[14:15]
	v_add_f32_e32 v22, v22, v23
	v_pk_mul_f32 v[10:11], v[182:183], v[10:11]
	v_med3_f32 v23, v14, s95, v223
	v_med3_f32 v15, v15, s95, v223
	v_mov_b32_e32 v14, 0
	v_cvt_pk_fp8_f32 v14, v23, v15
	v_med3_f32 v10, v10, s95, v223
	v_med3_f32 v11, v11, s95, v223
	v_mov_b32_e32 v15, 0
	v_cvt_pk_fp8_f32 v15, v10, v11
	v_pk_mul_f32 v[12:13], v[180:181], v[12:13]
	v_pk_fma_f32 v[8:9], v[8:9], v[124:125], v[40:41]
	v_med3_f32 v10, v12, s95, v223
	v_med3_f32 v11, v13, s95, v223
	v_pk_fma_f32 v[6:7], v[6:7], v[122:123], v[38:39]
	v_cvt_pk_fp8_f32 v15, v10, v11 op_sel:[0,0,1]
	v_pk_fma_f32 v[10:11], v[2:3], v[126:127], v[34:35]
	v_mul_f32_e32 v2, v7, v7
	v_mul_f32_e32 v3, v9, v9
	v_pk_fma_f32 v[12:13], v[4:5], v[128:129], v[36:37]
	v_fmac_f32_e32 v2, v6, v6
	v_fmac_f32_e32 v3, v8, v8
	v_add_f32_e32 v2, v2, v3
	v_mul_f32_e32 v3, v11, v11
	v_mul_f32_e32 v4, v13, v13
	v_fmac_f32_e32 v3, v10, v10
	v_fmac_f32_e32 v4, v12, v12
	v_add_f32_e32 v3, v3, v4
	v_add_f32_e32 v2, v2, v3
	v_pk_mul_f32 v[4:5], v[178:179], v[6:7]
	v_add_f32_e32 v24, v22, v2
	v_pk_mul_f32 v[22:23], v[186:187], v[10:11]
	v_med3_f32 v25, v4, s95, v223
	v_med3_f32 v5, v5, s95, v223
	v_mov_b32_e32 v4, 0
	v_cvt_pk_fp8_f32 v4, v25, v5
	v_med3_f32 v22, v22, s95, v223
	v_med3_f32 v23, v23, s95, v223
	v_mov_b32_e32 v5, 0
	v_cvt_pk_fp8_f32 v5, v22, v23
	ds_bpermute_b32 v22, v225, v24
	v_lshlrev_b64 v[20:21], 11, v[66:67]
	v_pk_mul_f32 v[16:17], v[172:173], v[16:17]
	v_lshl_add_u64 v[20:21], s[58:59], 0, v[20:21]
	v_med3_f32 v16, v16, s95, v223
	v_med3_f32 v17, v17, s95, v223
	v_pk_mul_f32 v[2:3], v[176:177], v[8:9]
	v_cvt_pk_fp8_f32 v14, v16, v17 op_sel:[0,0,1]
	v_lshl_add_u64 v[16:17], v[20:21], 0, v[170:171]
	v_pk_mul_f32 v[20:21], v[184:185], v[12:13]
	v_med3_f32 v2, v2, s95, v223
	v_med3_f32 v3, v3, s95, v223
	v_cvt_pk_fp8_f32 v4, v2, v3 op_sel:[0,0,1]
	v_med3_f32 v2, v20, s95, v223
	v_med3_f32 v3, v21, s95, v223
	v_cvt_pk_fp8_f32 v5, v2, v3 op_sel:[0,0,1]
	s_waitcnt lgkmcnt(0)
	v_add_f32_e32 v2, v24, v22
	ds_bpermute_b32 v3, v226, v2
	flat_store_dwordx2 v[16:17], v[14:15]
	flat_store_dwordx4 v[18:19], v[6:9] offset:512 nt
	flat_store_dwordx4 v[18:19], v[10:13] offset:528 nt
	flat_store_dwordx2 v[16:17], v[4:5] offset:128
	s_and_saveexec_b64 s[4:5], vcc
	s_cbranch_execz .LBB0_1202
	v_lshlrev_b64 v[4:5], 7, v[66:67]
	v_lshl_add_u64 v[4:5], s[62:63], 0, v[4:5]
	s_waitcnt lgkmcnt(0)
	v_add_f32_e32 v2, v2, v3
	flat_store_dword v[4:5], v2
.LBB0_1202:
	s_or_b64 exec, exec, s[4:5]
	s_andn2_b64 vcc, exec, s[2:3]
	s_mov_b64 s[2:3], -1
	s_cbranch_vccnz .LBB0_1178
	s_andn2_b64 vcc, exec, s[14:15]
	s_cbranch_vccnz .LBB0_1177
	s_barrier
	s_branch .LBB0_1177

.LBB0_1397:
	ds_read_b128 v[18:21], v177
	ds_read_b128 v[22:25], v178
	ds_read_b128 v[26:29], v185
	ds_read_b128 v[30:33], v186
	ds_read_b128 v[2:5], v179
	ds_read_b128 v[6:9], v180
	ds_read_b128 v[10:13], v187
	ds_read_b128 v[14:17], v188
	s_add_i32 s75, s92, 0x80
	s_and_b64 s[30:31], s[30:31], exec
	s_cselect_b32 s75, s75, s91
	s_cselect_b32 s96, s93, s29
	s_add_i32 s30, s75, 0x80
	s_add_i32 s31, s96, 0x80
	v_mov_b32_e32 v162, v1
	ds_read_b128 v[198:201], v193
	ds_read_b128 v[202:205], v193 offset:1024
	ds_read_b128 v[214:217], v193 offset:2048
	ds_read_b128 v[218:221], v193 offset:3072
	ds_read_b128 v[222:225], v193 offset:4096
	ds_read_b128 v[226:229], v193 offset:5120
	ds_read_b128 v[230:233], v193 offset:6144
	ds_read_b128 v[234:237], v193 offset:7168
	s_add_i32 s97, s92, s65
	v_add_u32_e32 v162, s97, v162
	s_add_i32 m0, s47, 0xc000
	s_add_i32 s97, s92, s74
	global_load_lds_dwordx4 v162, s[10:11]
	v_mov_b32_e32 v162, v1
	s_add_i32 m0, s47, 0xe000
	v_add_u32_e32 v162, s97, v162
	global_load_lds_dwordx4 v162, s[10:11]
	s_waitcnt vmcnt(8)
	s_waitcnt lgkmcnt(0)
	s_setprio 1
	s_barrier
	s_waitcnt lgkmcnt(0)
	v_mfma_f32_16x16x128_f8f6f4 v[158:161], v[18:25], v[198:205], v[158:161]
	v_mfma_f32_16x16x128_f8f6f4 v[150:153], v[26:33], v[198:205], v[150:153]
	v_mfma_f32_16x16x128_f8f6f4 v[142:145], v[18:25], v[214:221], v[142:145]
	v_mfma_f32_16x16x128_f8f6f4 v[134:137], v[26:33], v[214:221], v[134:137]
	v_mfma_f32_16x16x128_f8f6f4 v[126:129], v[18:25], v[222:229], v[126:129]
	v_mfma_f32_16x16x128_f8f6f4 v[118:121], v[26:33], v[222:229], v[118:121]
	v_mfma_f32_16x16x128_f8f6f4 v[110:113], v[18:25], v[230:237], v[110:113]
	v_mfma_f32_16x16x128_f8f6f4 v[102:105], v[26:33], v[230:237], v[102:105]
	s_setprio 0
	s_setprio 1
	v_mfma_f32_16x16x128_f8f6f4 v[154:157], v[2:9], v[198:205], v[154:157]
	v_mfma_f32_16x16x128_f8f6f4 v[146:149], v[10:17], v[198:205], v[146:149]
	v_mfma_f32_16x16x128_f8f6f4 v[138:141], v[2:9], v[214:221], v[138:141]
	v_mfma_f32_16x16x128_f8f6f4 v[130:133], v[10:17], v[214:221], v[130:133]
	v_mfma_f32_16x16x128_f8f6f4 v[122:125], v[2:9], v[222:229], v[122:125]
	v_mfma_f32_16x16x128_f8f6f4 v[114:117], v[10:17], v[222:229], v[114:117]
	v_mfma_f32_16x16x128_f8f6f4 v[106:109], v[2:9], v[230:237], v[106:109]
	v_mfma_f32_16x16x128_f8f6f4 v[98:101], v[10:17], v[230:237], v[98:101]
	s_setprio 0
	s_barrier
	v_mov_b32_e32 v162, v174
	ds_read_b128 v[198:201], v193 offset:16384
	ds_read_b128 v[202:205], v193 offset:17408
	ds_read_b128 v[214:217], v193 offset:18432
	ds_read_b128 v[218:221], v193 offset:19456
	ds_read_b128 v[222:225], v193 offset:20480
	ds_read_b128 v[226:229], v193 offset:21504
	ds_read_b128 v[230:233], v193 offset:22528
	ds_read_b128 v[234:237], v193 offset:23552
	s_mov_b32 m0, s48
	v_add_u32_e32 v162, s96, v162
	global_load_lds_dwordx4 v162, s[20:21]
	v_mov_b32_e32 v162, v174
	s_add_i32 s96, s96, s46
	v_add_u32_e32 v162, s96, v162
	s_mov_b32 m0, s49
	s_add_i32 s96, s96, s46
	global_load_lds_dwordx4 v162, s[20:21]
	v_mov_b32_e32 v162, v174
	s_mov_b32 m0, s50
	v_add_u32_e32 v162, s96, v162
	global_load_lds_dwordx4 v162, s[20:21]
	v_mov_b32_e32 v162, v174
	s_add_i32 s96, s96, s46
	v_add_u32_e32 v162, s96, v162
	s_mov_b32 m0, s51
	s_nop 0
	global_load_lds_dwordx4 v162, s[20:21]
	v_mov_b32_e32 v162, v1
	s_mov_b32 m0, s47
	v_add_u32_e32 v162, s75, v162
	global_load_lds_dwordx4 v162, s[10:11]
	v_mov_b32_e32 v162, v1
	s_add_i32 s75, s75, s45
	v_add_u32_e32 v162, s75, v162
	s_mov_b32 m0, s52
	s_nop 0
	global_load_lds_dwordx4 v162, s[10:11]
	s_waitcnt vmcnt(8)
	s_waitcnt lgkmcnt(0)
	s_setprio 1
	s_barrier
	s_waitcnt lgkmcnt(0)
	v_mfma_f32_16x16x128_f8f6f4 v[94:97], v[18:25], v[198:205], v[94:97]
	v_mfma_f32_16x16x128_f8f6f4 v[86:89], v[26:33], v[198:205], v[86:89]
	v_mfma_f32_16x16x128_f8f6f4 v[78:81], v[18:25], v[214:221], v[78:81]
	v_mfma_f32_16x16x128_f8f6f4 v[70:73], v[26:33], v[214:221], v[70:73]
	v_mfma_f32_16x16x128_f8f6f4 v[62:65], v[18:25], v[222:229], v[62:65]
	v_mfma_f32_16x16x128_f8f6f4 v[54:57], v[26:33], v[222:229], v[54:57]
	v_mfma_f32_16x16x128_f8f6f4 v[46:49], v[18:25], v[230:237], v[46:49]
	v_mfma_f32_16x16x128_f8f6f4 v[38:41], v[26:33], v[230:237], v[38:41]
	s_setprio 0
	s_setprio 1
	v_mfma_f32_16x16x128_f8f6f4 v[90:93], v[2:9], v[198:205], v[90:93]
	v_mfma_f32_16x16x128_f8f6f4 v[82:85], v[10:17], v[198:205], v[82:85]
	v_mfma_f32_16x16x128_f8f6f4 v[74:77], v[2:9], v[214:221], v[74:77]
	v_mfma_f32_16x16x128_f8f6f4 v[66:69], v[10:17], v[214:221], v[66:69]
	v_mfma_f32_16x16x128_f8f6f4 v[58:61], v[2:9], v[222:229], v[58:61]
	v_mfma_f32_16x16x128_f8f6f4 v[50:53], v[10:17], v[222:229], v[50:53]
	v_mfma_f32_16x16x128_f8f6f4 v[42:45], v[2:9], v[230:237], v[42:45]
	v_mfma_f32_16x16x128_f8f6f4 v[34:37], v[10:17], v[230:237], v[34:37]
	s_setprio 0
	s_barrier
	ds_read_b128 v[2:5], v181
	ds_read_b128 v[6:9], v182
	ds_read_b128 v[10:13], v189
	ds_read_b128 v[14:17], v190
	ds_read_b128 v[18:21], v183
	ds_read_b128 v[22:25], v184
	ds_read_b128 v[26:29], v191
	ds_read_b128 v[30:33], v192
	v_mov_b32_e32 v162, v1
	ds_read_b128 v[198:201], v193 offset:32768
	ds_read_b128 v[202:205], v193 offset:33792
	ds_read_b128 v[214:217], v193 offset:34816
	ds_read_b128 v[218:221], v193 offset:35840
	ds_read_b128 v[222:225], v193 offset:36864
	ds_read_b128 v[226:229], v193 offset:37888
	ds_read_b128 v[230:233], v193 offset:38912
	ds_read_b128 v[234:237], v193 offset:39936
	s_add_i32 s75, s75, s45
	s_mov_b32 m0, s53
	v_add_u32_e32 v162, s75, v162
	global_load_lds_dwordx4 v162, s[10:11]
	v_mov_b32_e32 v162, v1
	s_add_i32 s75, s75, s45
	v_add_u32_e32 v162, s75, v162
	s_mov_b32 m0, s54
	s_nop 0
	global_load_lds_dwordx4 v162, s[10:11]
	s_waitcnt vmcnt(8)
	s_waitcnt lgkmcnt(0)
	s_setprio 1
	s_barrier
	s_waitcnt lgkmcnt(0)
	v_mfma_f32_16x16x128_f8f6f4 v[158:161], v[2:9], v[198:205], v[158:161]
	v_mfma_f32_16x16x128_f8f6f4 v[150:153], v[10:17], v[198:205], v[150:153]
	v_mfma_f32_16x16x128_f8f6f4 v[142:145], v[2:9], v[214:221], v[142:145]
	v_mfma_f32_16x16x128_f8f6f4 v[134:137], v[10:17], v[214:221], v[134:137]
	v_mfma_f32_16x16x128_f8f6f4 v[126:129], v[2:9], v[222:229], v[126:129]
	v_mfma_f32_16x16x128_f8f6f4 v[118:121], v[10:17], v[222:229], v[118:121]
	v_mfma_f32_16x16x128_f8f6f4 v[110:113], v[2:9], v[230:237], v[110:113]
	v_mfma_f32_16x16x128_f8f6f4 v[102:105], v[10:17], v[230:237], v[102:105]
	s_setprio 0
	s_setprio 1
	v_mfma_f32_16x16x128_f8f6f4 v[154:157], v[18:25], v[198:205], v[154:157]
	v_mfma_f32_16x16x128_f8f6f4 v[146:149], v[26:33], v[198:205], v[146:149]
	v_mfma_f32_16x16x128_f8f6f4 v[138:141], v[18:25], v[214:221], v[138:141]
	v_mfma_f32_16x16x128_f8f6f4 v[130:133], v[26:33], v[214:221], v[130:133]
	v_mfma_f32_16x16x128_f8f6f4 v[122:125], v[18:25], v[222:229], v[122:125]
	v_mfma_f32_16x16x128_f8f6f4 v[114:117], v[26:33], v[222:229], v[114:117]
	v_mfma_f32_16x16x128_f8f6f4 v[106:109], v[18:25], v[230:237], v[106:109]
	v_mfma_f32_16x16x128_f8f6f4 v[98:101], v[26:33], v[230:237], v[98:101]
	s_setprio 0
	s_barrier
	v_mov_b32_e32 v162, v174
	ds_read_b128 v[198:201], v193 offset:49152
	ds_read_b128 v[202:205], v193 offset:50176
	ds_read_b128 v[214:217], v193 offset:51200
	ds_read_b128 v[218:221], v193 offset:52224
	ds_read_b128 v[222:225], v193 offset:53248
	ds_read_b128 v[226:229], v193 offset:54272
	ds_read_b128 v[230:233], v193 offset:55296
	ds_read_b128 v[234:237], v193 offset:56320
	s_mov_b32 m0, s58
	v_add_u32_e32 v162, s31, v162
	global_load_lds_dwordx4 v162, s[20:21]
	v_mov_b32_e32 v162, v174
	s_add_i32 s31, s31, s46
	v_add_u32_e32 v162, s31, v162
	s_mov_b32 m0, s59
	s_add_i32 s31, s31, s46
	global_load_lds_dwordx4 v162, s[20:21]
	v_mov_b32_e32 v162, v174
	s_mov_b32 m0, s62
	v_add_u32_e32 v162, s31, v162
	global_load_lds_dwordx4 v162, s[20:21]
	v_mov_b32_e32 v162, v174
	s_add_i32 s31, s31, s46
	v_add_u32_e32 v162, s31, v162
	s_mov_b32 m0, s63
	s_nop 0
	global_load_lds_dwordx4 v162, s[20:21]
	v_mov_b32_e32 v162, v1
	s_mov_b32 m0, s60
	v_add_u32_e32 v162, s30, v162
	global_load_lds_dwordx4 v162, s[10:11]
	v_mov_b32_e32 v162, v1
	s_add_i32 s30, s30, s45
	v_add_u32_e32 v162, s30, v162
	s_mov_b32 m0, s61
	s_nop 0
	global_load_lds_dwordx4 v162, s[10:11]
	s_waitcnt vmcnt(8)
	s_waitcnt lgkmcnt(0)
	s_setprio 1
	s_barrier
	s_waitcnt lgkmcnt(0)
	v_mfma_f32_16x16x128_f8f6f4 v[94:97], v[2:9], v[198:205], v[94:97]
	v_mfma_f32_16x16x128_f8f6f4 v[86:89], v[10:17], v[198:205], v[86:89]
	v_mfma_f32_16x16x128_f8f6f4 v[78:81], v[2:9], v[214:221], v[78:81]
	v_mfma_f32_16x16x128_f8f6f4 v[70:73], v[10:17], v[214:221], v[70:73]
	v_mfma_f32_16x16x128_f8f6f4 v[62:65], v[2:9], v[222:229], v[62:65]
	v_mfma_f32_16x16x128_f8f6f4 v[54:57], v[10:17], v[222:229], v[54:57]
	v_mfma_f32_16x16x128_f8f6f4 v[46:49], v[2:9], v[230:237], v[46:49]
	v_mfma_f32_16x16x128_f8f6f4 v[38:41], v[10:17], v[230:237], v[38:41]
	s_setprio 0
	s_setprio 1
	v_mfma_f32_16x16x128_f8f6f4 v[90:93], v[18:25], v[198:205], v[90:93]
	v_mfma_f32_16x16x128_f8f6f4 v[82:85], v[26:33], v[198:205], v[82:85]
	v_mfma_f32_16x16x128_f8f6f4 v[74:77], v[18:25], v[214:221], v[74:77]
	v_mfma_f32_16x16x128_f8f6f4 v[66:69], v[26:33], v[214:221], v[66:69]
	v_mfma_f32_16x16x128_f8f6f4 v[58:61], v[18:25], v[222:229], v[58:61]
	v_mfma_f32_16x16x128_f8f6f4 v[50:53], v[26:33], v[222:229], v[50:53]
	v_mfma_f32_16x16x128_f8f6f4 v[42:45], v[18:25], v[230:237], v[42:45]
	v_mfma_f32_16x16x128_f8f6f4 v[34:37], v[26:33], v[230:237], v[34:37]
	s_setprio 0
	s_barrier
	s_add_i32 s94, s94, 2
	s_addk_i32 s92, 0x100
	s_addk_i32 s93, 0x100
	s_cmp_ge_i32 s94, s64
	s_cbranch_scc1 .LBB0_1400

.LBB0_1603:
	ds_read_b128 v[18:21], v235
	ds_read_b128 v[22:25], v236
	ds_read_b128 v[26:29], v243
	ds_read_b128 v[30:33], v244
	s_waitcnt lgkmcnt(0)
	ds_read_b128 v[2:5], v237
	ds_read_b128 v[6:9], v238
	ds_read_b128 v[10:13], v245
	ds_read_b128 v[14:17], v246
	s_add_i32 s63, s6, 0x80
	s_cmp_eq_u32 s89, s62
	s_cselect_b32 s65, s7, s63
	s_cselect_b32 s64, s5, s61
	s_add_i32 s63, s65, 0x80
	v_mov_b32_e32 v194, v1
	ds_read_b128 v[162:165], v251
	ds_read_b128 v[166:169], v251 offset:1024
	ds_read_b128 v[170:173], v251 offset:2048
	ds_read_b128 v[174:177], v251 offset:3072
	ds_read_b128 v[178:181], v251 offset:4096
	ds_read_b128 v[182:185], v251 offset:5120
	ds_read_b128 v[186:189], v251 offset:6144
	ds_read_b128 v[190:193], v251 offset:7168
	s_add_i32 s66, s6, s86
	v_add_u32_e32 v194, s66, v194
	s_add_i32 m0, s70, 0xc000
	s_add_i32 s66, s6, s93
	global_load_lds_dwordx4 v194, s[8:9]
	v_mov_b32_e32 v194, v1
	s_add_i32 m0, s70, 0xe000
	v_add_u32_e32 v194, s66, v194
	global_load_lds_dwordx4 v194, s[8:9]
	s_waitcnt vmcnt(8)
	s_waitcnt lgkmcnt(0)
	s_setprio 1
	s_barrier
	s_waitcnt lgkmcnt(0)
	v_mfma_f32_16x16x128_f8f6f4 v[158:161], v[18:25], v[162:169], v[158:161]
	v_mfma_f32_16x16x128_f8f6f4 v[154:157], v[26:33], v[162:169], v[154:157]
	v_mfma_f32_16x16x128_f8f6f4 v[142:145], v[18:25], v[170:177], v[142:145]
	v_mfma_f32_16x16x128_f8f6f4 v[138:141], v[26:33], v[170:177], v[138:141]
	v_mfma_f32_16x16x128_f8f6f4 v[126:129], v[18:25], v[178:185], v[126:129]
	v_mfma_f32_16x16x128_f8f6f4 v[122:125], v[26:33], v[178:185], v[122:125]
	v_mfma_f32_16x16x128_f8f6f4 v[110:113], v[18:25], v[186:193], v[110:113]
	v_mfma_f32_16x16x128_f8f6f4 v[106:109], v[26:33], v[186:193], v[106:109]
	s_setprio 0
	s_setprio 1
	v_mfma_f32_16x16x128_f8f6f4 v[150:153], v[2:9], v[162:169], v[150:153]
	v_mfma_f32_16x16x128_f8f6f4 v[146:149], v[10:17], v[162:169], v[146:149]
	v_mfma_f32_16x16x128_f8f6f4 v[134:137], v[2:9], v[170:177], v[134:137]
	v_mfma_f32_16x16x128_f8f6f4 v[130:133], v[10:17], v[170:177], v[130:133]
	v_mfma_f32_16x16x128_f8f6f4 v[118:121], v[2:9], v[178:185], v[118:121]
	v_mfma_f32_16x16x128_f8f6f4 v[114:117], v[10:17], v[178:185], v[114:117]
	v_mfma_f32_16x16x128_f8f6f4 v[102:105], v[2:9], v[186:193], v[102:105]
	v_mfma_f32_16x16x128_f8f6f4 v[98:101], v[10:17], v[186:193], v[98:101]
	s_setprio 0
	s_barrier
	v_mov_b32_e32 v194, v211
	ds_read_b128 v[162:165], v251 offset:16384
	ds_read_b128 v[166:169], v251 offset:17408
	ds_read_b128 v[170:173], v251 offset:18432
	ds_read_b128 v[174:177], v251 offset:19456
	ds_read_b128 v[178:181], v251 offset:20480
	ds_read_b128 v[182:185], v251 offset:21504
	ds_read_b128 v[186:189], v251 offset:22528
	ds_read_b128 v[190:193], v251 offset:23552
	s_mov_b32 m0, s71
	v_add_u32_e32 v194, s64, v194
	global_load_lds_dwordx4 v194, s[20:21]
	v_mov_b32_e32 v194, v211
	s_add_i32 s66, s64, s35
	v_add_u32_e32 v194, s66, v194
	s_mov_b32 m0, s72
	s_add_i32 s66, s66, s35
	global_load_lds_dwordx4 v194, s[20:21]
	v_mov_b32_e32 v194, v211
	s_mov_b32 m0, s73
	v_add_u32_e32 v194, s66, v194
	global_load_lds_dwordx4 v194, s[20:21]
	v_mov_b32_e32 v194, v211
	s_add_i32 s66, s66, s35
	v_add_u32_e32 v194, s66, v194
	s_mov_b32 m0, s76
	s_nop 0
	global_load_lds_dwordx4 v194, s[20:21]
	v_mov_b32_e32 v194, v1
	s_mov_b32 m0, s70
	v_add_u32_e32 v194, s65, v194
	global_load_lds_dwordx4 v194, s[8:9]
	v_mov_b32_e32 v194, v1
	s_add_i32 s65, s65, s23
	v_add_u32_e32 v194, s65, v194
	s_mov_b32 m0, s77
	s_nop 0
	global_load_lds_dwordx4 v194, s[8:9]
	s_waitcnt vmcnt(8)
	s_waitcnt lgkmcnt(0)
	s_setprio 1
	s_barrier
	s_waitcnt lgkmcnt(0)
	v_mfma_f32_16x16x128_f8f6f4 v[94:97], v[18:25], v[162:169], v[94:97]
	v_mfma_f32_16x16x128_f8f6f4 v[90:93], v[26:33], v[162:169], v[90:93]
	v_mfma_f32_16x16x128_f8f6f4 v[78:81], v[18:25], v[170:177], v[78:81]
	v_mfma_f32_16x16x128_f8f6f4 v[74:77], v[26:33], v[170:177], v[74:77]
	v_mfma_f32_16x16x128_f8f6f4 v[62:65], v[18:25], v[178:185], v[62:65]
	v_mfma_f32_16x16x128_f8f6f4 v[58:61], v[26:33], v[178:185], v[58:61]
	v_mfma_f32_16x16x128_f8f6f4 v[46:49], v[18:25], v[186:193], v[46:49]
	v_mfma_f32_16x16x128_f8f6f4 v[42:45], v[26:33], v[186:193], v[42:45]
	s_setprio 0
	s_setprio 1
	v_mfma_f32_16x16x128_f8f6f4 v[86:89], v[2:9], v[162:169], v[86:89]
	v_mfma_f32_16x16x128_f8f6f4 v[82:85], v[10:17], v[162:169], v[82:85]
	v_mfma_f32_16x16x128_f8f6f4 v[70:73], v[2:9], v[170:177], v[70:73]
	v_mfma_f32_16x16x128_f8f6f4 v[66:69], v[10:17], v[170:177], v[66:69]
	v_mfma_f32_16x16x128_f8f6f4 v[54:57], v[2:9], v[178:185], v[54:57]
	v_mfma_f32_16x16x128_f8f6f4 v[50:53], v[10:17], v[178:185], v[50:53]
	v_mfma_f32_16x16x128_f8f6f4 v[38:41], v[2:9], v[186:193], v[38:41]
	v_mfma_f32_16x16x128_f8f6f4 v[34:37], v[10:17], v[186:193], v[34:37]
	s_setprio 0
	s_barrier
	ds_read_b128 v[2:5], v239
	ds_read_b128 v[6:9], v240
	ds_read_b128 v[10:13], v247
	ds_read_b128 v[14:17], v248
	ds_read_b128 v[18:21], v241
	ds_read_b128 v[22:25], v242
	ds_read_b128 v[26:29], v249
	ds_read_b128 v[30:33], v250
	v_mov_b32_e32 v194, v1
	ds_read_b128 v[162:165], v251 offset:32768
	ds_read_b128 v[166:169], v251 offset:33792
	ds_read_b128 v[170:173], v251 offset:34816
	ds_read_b128 v[174:177], v251 offset:35840
	ds_read_b128 v[178:181], v251 offset:36864
	ds_read_b128 v[182:185], v251 offset:37888
	ds_read_b128 v[186:189], v251 offset:38912
	ds_read_b128 v[190:193], v251 offset:39936
	s_add_i32 s65, s65, s23
	s_mov_b32 m0, s78
	v_add_u32_e32 v194, s65, v194
	global_load_lds_dwordx4 v194, s[8:9]
	v_mov_b32_e32 v194, v1
	s_add_i32 s65, s65, s23
	v_add_u32_e32 v194, s65, v194
	s_mov_b32 m0, s44
	s_nop 0
	global_load_lds_dwordx4 v194, s[8:9]
	s_waitcnt vmcnt(8)
	s_waitcnt lgkmcnt(0)
	s_setprio 1
	s_barrier
	s_waitcnt lgkmcnt(0)
	v_mfma_f32_16x16x128_f8f6f4 v[158:161], v[2:9], v[162:169], v[158:161]
	v_mfma_f32_16x16x128_f8f6f4 v[154:157], v[10:17], v[162:169], v[154:157]
	v_mfma_f32_16x16x128_f8f6f4 v[142:145], v[2:9], v[170:177], v[142:145]
	v_mfma_f32_16x16x128_f8f6f4 v[138:141], v[10:17], v[170:177], v[138:141]
	v_mfma_f32_16x16x128_f8f6f4 v[126:129], v[2:9], v[178:185], v[126:129]
	v_mfma_f32_16x16x128_f8f6f4 v[122:125], v[10:17], v[178:185], v[122:125]
	v_mfma_f32_16x16x128_f8f6f4 v[110:113], v[2:9], v[186:193], v[110:113]
	v_mfma_f32_16x16x128_f8f6f4 v[106:109], v[10:17], v[186:193], v[106:109]
	s_setprio 0
	s_setprio 1
	v_mfma_f32_16x16x128_f8f6f4 v[150:153], v[18:25], v[162:169], v[150:153]
	v_mfma_f32_16x16x128_f8f6f4 v[146:149], v[26:33], v[162:169], v[146:149]
	v_mfma_f32_16x16x128_f8f6f4 v[134:137], v[18:25], v[170:177], v[134:137]
	v_mfma_f32_16x16x128_f8f6f4 v[130:133], v[26:33], v[170:177], v[130:133]
	v_mfma_f32_16x16x128_f8f6f4 v[118:121], v[18:25], v[178:185], v[118:121]
	v_mfma_f32_16x16x128_f8f6f4 v[114:117], v[26:33], v[178:185], v[114:117]
	v_mfma_f32_16x16x128_f8f6f4 v[102:105], v[18:25], v[186:193], v[102:105]
	v_mfma_f32_16x16x128_f8f6f4 v[98:101], v[26:33], v[186:193], v[98:101]
	s_setprio 0
	s_barrier
	v_mov_b32_e32 v194, v211
	ds_read_b128 v[162:165], v251 offset:49152
	ds_read_b128 v[166:169], v251 offset:50176
	ds_read_b128 v[170:173], v251 offset:51200
	ds_read_b128 v[174:177], v251 offset:52224
	ds_read_b128 v[178:181], v251 offset:53248
	ds_read_b128 v[182:185], v251 offset:54272
	ds_read_b128 v[186:189], v251 offset:55296
	ds_read_b128 v[190:193], v251 offset:56320
	s_addk_i32 s64, 0x80
	s_mov_b32 m0, s79
	v_add_u32_e32 v194, s64, v194
	global_load_lds_dwordx4 v194, s[20:21]
	v_mov_b32_e32 v194, v211
	s_add_i32 s64, s64, s35
	v_add_u32_e32 v194, s64, v194
	s_mov_b32 m0, s80
	s_add_i32 s64, s64, s35
	global_load_lds_dwordx4 v194, s[20:21]
	v_mov_b32_e32 v194, v211
	s_mov_b32 m0, s83
	v_add_u32_e32 v194, s64, v194
	global_load_lds_dwordx4 v194, s[20:21]
	v_mov_b32_e32 v194, v211
	s_add_i32 s64, s64, s35
	v_add_u32_e32 v194, s64, v194
	s_mov_b32 m0, s84
	s_nop 0
	global_load_lds_dwordx4 v194, s[20:21]
	v_mov_b32_e32 v194, v1
	s_mov_b32 m0, s81
	v_add_u32_e32 v194, s63, v194
	global_load_lds_dwordx4 v194, s[8:9]
	v_mov_b32_e32 v194, v1
	s_add_i32 s63, s63, s23
	v_add_u32_e32 v194, s63, v194
	s_mov_b32 m0, s82
	s_nop 0
	global_load_lds_dwordx4 v194, s[8:9]
	s_waitcnt vmcnt(8)
	s_waitcnt lgkmcnt(0)
	s_setprio 1
	s_barrier
	s_waitcnt lgkmcnt(0)
	v_mfma_f32_16x16x128_f8f6f4 v[94:97], v[2:9], v[162:169], v[94:97]
	v_mfma_f32_16x16x128_f8f6f4 v[90:93], v[10:17], v[162:169], v[90:93]
	v_mfma_f32_16x16x128_f8f6f4 v[78:81], v[2:9], v[170:177], v[78:81]
	v_mfma_f32_16x16x128_f8f6f4 v[74:77], v[10:17], v[170:177], v[74:77]
	v_mfma_f32_16x16x128_f8f6f4 v[62:65], v[2:9], v[178:185], v[62:65]
	v_mfma_f32_16x16x128_f8f6f4 v[58:61], v[10:17], v[178:185], v[58:61]
	v_mfma_f32_16x16x128_f8f6f4 v[46:49], v[2:9], v[186:193], v[46:49]
	v_mfma_f32_16x16x128_f8f6f4 v[42:45], v[10:17], v[186:193], v[42:45]
	s_setprio 0
	s_setprio 1
	v_mfma_f32_16x16x128_f8f6f4 v[86:89], v[18:25], v[162:169], v[86:89]
	v_mfma_f32_16x16x128_f8f6f4 v[82:85], v[26:33], v[162:169], v[82:85]
	v_mfma_f32_16x16x128_f8f6f4 v[70:73], v[18:25], v[170:177], v[70:73]
	v_mfma_f32_16x16x128_f8f6f4 v[66:69], v[26:33], v[170:177], v[66:69]
	v_mfma_f32_16x16x128_f8f6f4 v[54:57], v[18:25], v[178:185], v[54:57]
	v_mfma_f32_16x16x128_f8f6f4 v[50:53], v[26:33], v[178:185], v[50:53]
	v_mfma_f32_16x16x128_f8f6f4 v[38:41], v[18:25], v[186:193], v[38:41]
	v_mfma_f32_16x16x128_f8f6f4 v[34:37], v[26:33], v[186:193], v[34:37]
	s_setprio 0
	s_barrier
	s_add_i32 s62, s62, 2
	s_addk_i32 s6, 0x100
	s_addk_i32 s61, 0x100
	s_cmp_ge_i32 s62, s85
	s_cbranch_scc0 .LBB0_1603

.LBB0_1606:
	s_min_i32 s6, s4, 0x80
	s_lshr_b32 s6, s6, 5
	s_mulk_i32 s6, 0x3000
	v_mov_b32_e32 v253, v234
	v_mov_b32_e32 v2, v213
	s_ashr_i32 s7, s6, 31
	s_nop 15
	s_nop 15
	s_mov_b32 s61, s39
	s_mov_b32 s65, s37
	s_mov_b32 s68, s38
	s_mov_b32 s64, s36
	s_ashr_i32 s5, s4, 31
	s_lshl_b64 s[6:7], s[6:7], 2
	s_add_u32 s6, s68, s6
	s_addc_u32 s7, s61, s7
	s_lshl_b32 s62, s60, 8
	s_or_b32 s62, s62, s88
	v_lshl_add_u32 v218, v253, 3, s62
	v_ashrrev_i32_e32 v219, 31, v218
	v_lshlrev_b64 v[4:5], 2, v[218:219]
	v_lshl_add_u64 v[6:7], s[6:7], 0, v[4:5]
	s_mov_b64 s[6:7], 0x10a000
	v_lshl_add_u64 v[8:9], v[6:7], 0, s[6:7]
	s_load_dwordx2 s[6:7], s[0:1], 0xf0
	s_add_u32 s66, s68, 0x800000
	s_addc_u32 s67, s61, 0
	s_lshl_b64 s[4:5], s[4:5], 8
	s_add_u32 s4, s4, s87
	s_waitcnt lgkmcnt(0)
	v_lshl_add_u64 v[10:11], s[6:7], 0, v[4:5]
	s_mov_b64 s[6:7], 0x13e000
	v_lshl_add_u64 v[12:13], v[6:7], 0, s[6:7]
	s_mov_b32 s6, 0x10a000
	v_add_co_u32_e32 v14, vcc, s6, v6
	v_ashrrev_i32_e32 v3, 31, v2
	s_addc_u32 s5, s5, s90
	v_addc_co_u32_e32 v15, vcc, 0, v7, vcc
	s_mov_b32 s6, 0x13e000
	v_lshl_add_u64 v[220:221], s[4:5], 0, v[2:3]
	v_add_co_u32_e32 v6, vcc, s6, v6
	v_lshlrev_b64 v[2:3], 13, v[220:221]
	s_nop 0
	v_addc_co_u32_e32 v7, vcc, 0, v7, vcc
	v_lshl_add_u64 v[232:233], s[64:65], 0, v[2:3]
	v_lshl_add_u64 v[2:3], s[66:67], 0, v[2:3]
	s_mov_b64 s[4:5], 0x8000
	v_lshl_add_u64 v[230:231], v[2:3], 0, s[16:17]
	v_cmp_gt_i64_e32 vcc, s[4:5], v[220:221]
	global_load_dwordx4 v[174:177], v[10:11], off offset:16
	global_load_dwordx4 v[190:193], v[10:11], off
	v_cndmask_b32_e32 v3, v231, v233, vcc
	v_cndmask_b32_e32 v2, v230, v232, vcc
	flat_load_dwordx4 v[202:205], v[6:7]
	flat_load_dwordx4 v[194:197], v[8:9] offset:16
	flat_load_dwordx4 v[182:185], v[8:9] offset:512
	global_load_dwordx4 v[26:29], v[10:11], off offset:528
	global_load_dwordx4 v[178:181], v[10:11], off offset:512
	flat_load_dwordx4 v[198:201], v[12:13] offset:16
	flat_load_dwordx4 v[186:189], v[12:13] offset:512
	flat_load_dwordx4 v[170:173], v[8:9] offset:528
	flat_load_dwordx4 v[206:209], v[14:15]
	flat_load_dwordx4 v[166:169], v[12:13] offset:528
	v_lshl_add_u64 v[2:3], v[2:3], 0, v[4:5]
	v_lshl_add_u64 v[222:223], v[220:221], 0, 16
	flat_load_dwordx4 v[162:165], v[2:3] nt
	flat_load_dwordx4 v[30:33], v[2:3] offset:16 nt
	flat_load_dwordx4 v[22:25], v[2:3] offset:512 nt
	flat_load_dwordx4 v[14:17], v[2:3] offset:528 nt
	v_lshlrev_b64 v[2:3], 13, v[222:223]
	v_lshl_add_u64 v[226:227], s[64:65], 0, v[2:3]
	v_lshl_add_u64 v[2:3], s[66:67], 0, v[2:3]
	v_lshl_add_u64 v[224:225], v[2:3], 0, s[16:17]
	v_cmp_gt_i64_e64 s[4:5], s[18:19], v[220:221]
	v_mov_b64_e32 v[228:229], v[220:221]
	s_nop 0
	v_cndmask_b32_e64 v3, v225, v227, s[4:5]
	v_cndmask_b32_e64 v2, v224, v226, s[4:5]
	v_lshl_add_u64 v[2:3], v[2:3], 0, v[4:5]
	flat_load_dwordx4 v[18:21], v[2:3] nt
	flat_load_dwordx4 v[10:13], v[2:3] offset:16 nt
	flat_load_dwordx4 v[6:9], v[2:3] offset:512 nt
	s_nop 0
	flat_load_dwordx4 v[2:5], v[2:3] offset:528 nt
	s_and_saveexec_b64 s[6:7], vcc
	v_lshlrev_b32_e32 v230, 7, v220
	v_bfe_u32 v228, v220, 6, 7
	v_and_b32_e32 v229, 0xffffe000, v220
	v_and_b32_e32 v230, 0x1f80, v230
	v_or3_b32 v228, v229, v230, v228
	v_mov_b32_e32 v229, v221
	v_mov_b64_e32 v[230:231], v[232:233]
	s_or_b64 exec, exec, s[6:7]
	s_waitcnt vmcnt(0) lgkmcnt(0)
	v_pk_add_f32 v[204:205], v[204:205], 1.0 op_sel_hi:[1,0]
	v_pk_add_f32 v[202:203], v[202:203], 1.0 op_sel_hi:[1,0]
	v_pk_mul_f32 v[192:193], v[192:193], v[204:205]
	v_pk_mul_f32 v[204:205], v[196:197], s[22:23] op_sel_hi:[1,0]
	v_pk_add_f32 v[196:197], v[198:199], 1.0 op_sel_hi:[1,0]
	v_pk_mul_f32 v[190:191], v[190:191], v[202:203]
	v_pk_mul_f32 v[202:203], v[194:195], s[22:23] op_sel_hi:[1,0]
	v_pk_add_f32 v[194:195], v[200:201], 1.0 op_sel_hi:[1,0]
	v_pk_mul_f32 v[196:197], v[174:175], v[196:197]
	v_pk_add_f32 v[174:175], v[188:189], 1.0 op_sel_hi:[1,0]
	v_pk_add_f32 v[186:187], v[186:187], 1.0 op_sel_hi:[1,0]
	s_add_u32 s62, s68, 0x2a400000
	v_pk_mul_f32 v[194:195], v[176:177], v[194:195]
	v_pk_mul_f32 v[176:177], v[180:181], v[174:175]
	v_pk_mul_f32 v[174:175], v[178:179], v[186:187]
	v_pk_add_f32 v[168:169], v[168:169], 1.0 op_sel_hi:[1,0]
	v_pk_add_f32 v[178:179], v[166:167], 1.0 op_sel_hi:[1,0]
	s_addc_u32 s63, s61, 0
	v_pk_mul_f32 v[208:209], v[208:209], s[22:23] op_sel_hi:[1,0]
	v_pk_mul_f32 v[206:207], v[206:207], s[22:23] op_sel_hi:[1,0]
	v_pk_mul_f32 v[166:167], v[28:29], v[168:169]
	v_pk_mul_f32 v[168:169], v[26:27], v[178:179]
	v_lshlrev_b64 v[26:27], 12, v[228:229]
	v_lshl_add_u64 v[178:179], s[62:63], 0, v[26:27]
	v_pk_fma_f32 v[28:29], v[160:161], v[208:209], v[164:165]
	v_pk_fma_f32 v[26:27], v[158:159], v[206:207], v[162:163]
	v_pk_fma_f32 v[32:33], v[156:157], v[204:205], v[32:33]
	v_mul_f32_e32 v156, v27, v27
	v_mul_f32_e32 v157, v29, v29
	v_pk_fma_f32 v[30:31], v[154:155], v[202:203], v[30:31]
	v_fmac_f32_e32 v156, v26, v26
	v_fmac_f32_e32 v157, v28, v28
	v_lshl_add_u64 v[154:155], v[218:219], 2, v[230:231]
	v_add_f32_e32 v156, v156, v157
	v_mul_f32_e32 v157, v31, v31
	v_mul_f32_e32 v158, v33, v33
	v_pk_mul_f32 v[184:185], v[184:185], s[22:23] op_sel_hi:[1,0]
	v_pk_mul_f32 v[182:183], v[182:183], s[22:23] op_sel_hi:[1,0]
	flat_store_dwordx4 v[154:155], v[26:29] nt
	flat_store_dwordx4 v[154:155], v[30:33] offset:16 nt
	v_fmac_f32_e32 v157, v30, v30
	v_fmac_f32_e32 v158, v32, v32
	v_pk_mul_f32 v[28:29], v[192:193], v[28:29]
	v_pk_mul_f32 v[26:27], v[190:191], v[26:27]
	v_pk_mul_f32 v[32:33], v[194:195], v[32:33]
	v_pk_mul_f32 v[30:31], v[196:197], v[30:31]
	s_lshl_b32 s6, s60, 2
	v_cvt_pk_bf16_f32 v26, v26, v27
	v_cvt_pk_bf16_f32 v27, v28, v29
	v_cvt_pk_bf16_f32 v28, v30, v31
	v_cvt_pk_bf16_f32 v29, v32, v33
	v_lshl_add_u64 v[30:31], v[218:219], 1, v[178:179]
	v_pk_fma_f32 v[24:25], v[152:153], v[184:185], v[24:25]
	v_pk_fma_f32 v[22:23], v[150:151], v[182:183], v[22:23]
	v_pk_mul_f32 v[172:173], v[172:173], s[22:23] op_sel_hi:[1,0]
	v_pk_mul_f32 v[170:171], v[170:171], s[22:23] op_sel_hi:[1,0]
	s_ashr_i32 s7, s6, 31
	flat_store_dwordx4 v[30:31], v[26:29]
	s_lshl_b64 s[6:7], s[6:7], 2
	v_pk_fma_f32 v[16:17], v[148:149], v[172:173], v[16:17]
	v_mul_f32_e32 v26, v23, v23
	v_mul_f32_e32 v27, v25, v25
	v_pk_fma_f32 v[14:15], v[146:147], v[170:171], v[14:15]
	v_fmac_f32_e32 v26, v22, v22
	v_fmac_f32_e32 v27, v24, v24
	s_add_u32 s6, s68, s6
	v_add_f32_e32 v26, v26, v27
	v_mul_f32_e32 v27, v15, v15
	v_mul_f32_e32 v28, v17, v17
	s_addc_u32 s7, s61, s7
	v_fmac_f32_e32 v27, v14, v14
	v_fmac_f32_e32 v28, v16, v16
	s_add_u32 s6, s6, s94
	v_add_f32_e32 v157, v157, v158
	v_add_f32_e32 v27, v27, v28
	s_addc_u32 s7, s7, 0
	v_add_f32_e32 v156, v156, v157
	v_add_f32_e32 v26, v26, v27
	v_and_b32_e32 v27, 64, v252
	s_add_u32 s60, s6, 0xa4500000
	v_add_f32_e32 v28, v156, v26
	v_xor_b32_e32 v26, 16, v252
	v_add_u32_e32 v29, 64, v27
	s_addc_u32 s61, s7, 0
	v_cmp_lt_i32_e64 s[6:7], v26, v29
	flat_store_dwordx4 v[154:155], v[22:25] offset:512 nt
	flat_store_dwordx4 v[154:155], v[14:17] offset:528 nt
	v_cndmask_b32_e64 v26, v252, v26, s[6:7]
	v_lshlrev_b32_e32 v152, 2, v26
	ds_bpermute_b32 v32, v152, v28
	v_pk_mul_f32 v[26:27], v[168:169], v[14:15]
	v_xor_b32_e32 v15, 32, v252
	v_cmp_lt_i32_e64 s[6:7], v15, v29
	v_pk_mul_f32 v[24:25], v[176:177], v[24:25]
	s_waitcnt lgkmcnt(0)
	v_add_f32_e32 v14, v28, v32
	v_cndmask_b32_e64 v15, v252, v15, s[6:7]
	v_lshlrev_b32_e32 v153, 2, v15
	ds_bpermute_b32 v15, v153, v14
	v_pk_mul_f32 v[22:23], v[174:175], v[22:23]
	v_pk_mul_f32 v[16:17], v[166:167], v[16:17]
	v_cmp_eq_u32_e32 vcc, 0, v253
	v_cvt_pk_bf16_f32 v22, v22, v23
	v_cvt_pk_bf16_f32 v23, v24, v25
	v_cvt_pk_bf16_f32 v24, v26, v27
	v_cvt_pk_bf16_f32 v25, v16, v17
	flat_store_dwordx4 v[30:31], v[22:25] offset:256
	s_and_saveexec_b64 s[6:7], vcc
	s_cbranch_execz .LBB0_1610
	v_lshlrev_b64 v[16:17], 7, v[228:229]
	v_lshl_add_u64 v[16:17], s[60:61], 0, v[16:17]
	s_waitcnt lgkmcnt(0)
	v_add_f32_e32 v14, v14, v15
	flat_store_dword v[16:17], v14
.LBB0_1610:
	s_or_b64 exec, exec, s[6:7]
	v_lshl_add_u64 v[146:147], v[220:221], 0, 32
	s_waitcnt lgkmcnt(0)
	v_lshlrev_b64 v[14:15], 13, v[146:147]
	v_lshl_add_u64 v[150:151], s[64:65], 0, v[14:15]
	v_lshl_add_u64 v[14:15], s[66:67], 0, v[14:15]
	v_lshl_add_u64 v[148:149], v[14:15], 0, s[16:17]
	v_cmp_gt_i64_e64 s[6:7], s[24:25], v[220:221]
	s_nop 1
	v_cndmask_b32_e64 v15, v149, v151, s[6:7]
	v_cndmask_b32_e64 v14, v148, v150, s[6:7]
	v_lshl_add_u64 v[14:15], v[218:219], 2, v[14:15]
	flat_load_dwordx4 v[30:33], v[14:15] nt
	flat_load_dwordx4 v[26:29], v[14:15] offset:16 nt
	flat_load_dwordx4 v[22:25], v[14:15] offset:512 nt
	s_nop 0
	flat_load_dwordx4 v[14:17], v[14:15] offset:528 nt
	s_and_saveexec_b64 s[68:69], s[4:5]
	v_lshlrev_b32_e32 v156, 7, v222
	v_bfe_u32 v154, v222, 6, 7
	v_and_b32_e32 v155, 0xffffe000, v222
	v_and_b32_e32 v156, 0x1f80, v156
	v_or3_b32 v222, v155, v156, v154
	v_mov_b64_e32 v[224:225], v[226:227]
	s_or_b64 exec, exec, s[68:69]
	v_pk_fma_f32 v[20:21], v[144:145], v[208:209], v[20:21]
	v_pk_fma_f32 v[18:19], v[142:143], v[206:207], v[18:19]
	v_pk_fma_f32 v[12:13], v[140:141], v[204:205], v[12:13]
	v_mul_f32_e32 v140, v19, v19
	v_mul_f32_e32 v141, v21, v21
	v_pk_fma_f32 v[10:11], v[138:139], v[202:203], v[10:11]
	v_fmac_f32_e32 v140, v18, v18
	v_fmac_f32_e32 v141, v20, v20
	v_add_f32_e32 v140, v140, v141
	v_mul_f32_e32 v141, v11, v11
	v_mul_f32_e32 v142, v13, v13
	v_fmac_f32_e32 v141, v10, v10
	v_fmac_f32_e32 v142, v12, v12
	v_lshlrev_b64 v[154:155], 12, v[222:223]
	v_lshl_add_u64 v[138:139], v[218:219], 2, v[224:225]
	v_add_f32_e32 v141, v141, v142
	v_lshl_add_u64 v[154:155], s[62:63], 0, v[154:155]
	flat_store_dwordx4 v[138:139], v[18:21] nt
	flat_store_dwordx4 v[138:139], v[10:13] offset:16 nt
	v_add_f32_e32 v142, v140, v141
	v_pk_mul_f32 v[20:21], v[192:193], v[20:21]
	v_pk_mul_f32 v[18:19], v[190:191], v[18:19]
	v_pk_mul_f32 v[140:141], v[194:195], v[12:13]
	v_pk_mul_f32 v[12:13], v[196:197], v[10:11]
	v_cvt_pk_bf16_f32 v10, v18, v19
	v_cvt_pk_bf16_f32 v11, v20, v21
	v_cvt_pk_bf16_f32 v12, v12, v13
	v_cvt_pk_bf16_f32 v13, v140, v141
	v_lshl_add_u64 v[18:19], v[218:219], 1, v[154:155]
	v_pk_fma_f32 v[8:9], v[136:137], v[184:185], v[8:9]
	v_pk_fma_f32 v[6:7], v[134:135], v[182:183], v[6:7]
	flat_store_dwordx4 v[18:19], v[10:13]
	v_pk_fma_f32 v[4:5], v[132:133], v[172:173], v[4:5]
	v_pk_fma_f32 v[2:3], v[130:131], v[170:171], v[2:3]
	v_mul_f32_e32 v10, v7, v7
	v_mul_f32_e32 v11, v9, v9
	v_fmac_f32_e32 v10, v6, v6
	v_fmac_f32_e32 v11, v8, v8
	v_add_f32_e32 v10, v10, v11
	v_mul_f32_e32 v11, v3, v3
	v_mul_f32_e32 v12, v5, v5
	v_fmac_f32_e32 v11, v2, v2
	v_fmac_f32_e32 v12, v4, v4
	v_add_f32_e32 v11, v11, v12
	v_add_f32_e32 v10, v10, v11
	v_add_f32_e32 v20, v142, v10
	ds_bpermute_b32 v21, v152, v20
	flat_store_dwordx4 v[138:139], v[6:9] offset:512 nt
	flat_store_dwordx4 v[138:139], v[2:5] offset:528 nt
	v_pk_mul_f32 v[12:13], v[168:169], v[2:3]
	v_pk_mul_f32 v[8:9], v[176:177], v[8:9]
	v_pk_mul_f32 v[6:7], v[174:175], v[6:7]
	s_waitcnt lgkmcnt(0)
	v_add_f32_e32 v2, v20, v21
	ds_bpermute_b32 v3, v153, v2
	v_pk_mul_f32 v[10:11], v[166:167], v[4:5]
	v_cvt_pk_bf16_f32 v4, v6, v7
	v_cvt_pk_bf16_f32 v5, v8, v9
	v_cvt_pk_bf16_f32 v6, v12, v13
	v_cvt_pk_bf16_f32 v7, v10, v11
	flat_store_dwordx4 v[18:19], v[4:7] offset:256
	s_and_saveexec_b64 s[4:5], vcc
	s_cbranch_execz .LBB0_1614
	v_lshlrev_b64 v[4:5], 7, v[222:223]
	v_lshl_add_u64 v[4:5], s[60:61], 0, v[4:5]
	s_waitcnt lgkmcnt(0)
	v_add_f32_e32 v2, v2, v3
	flat_store_dword v[4:5], v2
.LBB0_1614:
	s_or_b64 exec, exec, s[4:5]
	v_lshl_add_u64 v[134:135], v[220:221], 0, 48
	s_waitcnt lgkmcnt(0)
	v_lshlrev_b64 v[2:3], 13, v[134:135]
	v_lshl_add_u64 v[138:139], s[64:65], 0, v[2:3]
	v_lshl_add_u64 v[2:3], s[66:67], 0, v[2:3]
	v_lshl_add_u64 v[136:137], v[2:3], 0, s[16:17]
	v_cmp_gt_i64_e64 s[4:5], s[28:29], v[220:221]
	s_nop 1
	v_cndmask_b32_e64 v3, v137, v139, s[4:5]
	v_cndmask_b32_e64 v2, v136, v138, s[4:5]
	v_lshl_add_u64 v[2:3], v[218:219], 2, v[2:3]
	flat_load_dwordx4 v[130:133], v[2:3] nt
	flat_load_dwordx4 v[18:21], v[2:3] offset:16 nt
	flat_load_dwordx4 v[10:13], v[2:3] offset:512 nt
	s_nop 0
	flat_load_dwordx4 v[2:5], v[2:3] offset:528 nt
	s_and_saveexec_b64 s[68:69], s[6:7]
	v_lshlrev_b32_e32 v8, 7, v146
	v_bfe_u32 v6, v146, 6, 7
	v_and_b32_e32 v7, 0xffffe000, v146
	v_and_b32_e32 v8, 0x1f80, v8
	v_or3_b32 v146, v7, v8, v6
	v_mov_b64_e32 v[148:149], v[150:151]
	s_or_b64 exec, exec, s[68:69]
	v_lshlrev_b64 v[6:7], 12, v[146:147]
	v_lshl_add_u64 v[140:141], s[62:63], 0, v[6:7]
	s_waitcnt vmcnt(0)
	v_pk_fma_f32 v[8:9], v[128:129], v[208:209], v[32:33]
	v_pk_fma_f32 v[6:7], v[126:127], v[206:207], v[30:31]
	v_mul_f32_e32 v33, v9, v9
	v_mul_f32_e32 v32, v7, v7
	v_pk_fma_f32 v[28:29], v[124:125], v[204:205], v[28:29]
	v_pk_fma_f32 v[26:27], v[122:123], v[202:203], v[26:27]
	v_fmac_f32_e32 v32, v6, v6
	v_fmac_f32_e32 v33, v8, v8
	v_lshl_add_u64 v[30:31], v[218:219], 2, v[148:149]
	v_add_f32_e32 v32, v32, v33
	v_mul_f32_e32 v33, v27, v27
	v_mul_f32_e32 v122, v29, v29
	flat_store_dwordx4 v[30:31], v[6:9] nt
	flat_store_dwordx4 v[30:31], v[26:29] offset:16 nt
	v_fmac_f32_e32 v33, v26, v26
	v_fmac_f32_e32 v122, v28, v28
	v_pk_mul_f32 v[8:9], v[192:193], v[8:9]
	v_pk_mul_f32 v[6:7], v[190:191], v[6:7]
	v_pk_mul_f32 v[28:29], v[194:195], v[28:29]
	v_pk_mul_f32 v[26:27], v[196:197], v[26:27]
	v_cvt_pk_bf16_f32 v6, v6, v7
	v_cvt_pk_bf16_f32 v7, v8, v9
	v_cvt_pk_bf16_f32 v8, v26, v27
	v_cvt_pk_bf16_f32 v9, v28, v29
	v_lshl_add_u64 v[26:27], v[218:219], 1, v[140:141]
	flat_store_dwordx4 v[26:27], v[6:9]
	v_pk_fma_f32 v[16:17], v[116:117], v[172:173], v[16:17]
	v_pk_fma_f32 v[14:15], v[114:115], v[170:171], v[14:15]
	v_pk_fma_f32 v[8:9], v[120:121], v[184:185], v[24:25]
	v_pk_fma_f32 v[6:7], v[118:119], v[182:183], v[22:23]
	v_mul_f32_e32 v23, v9, v9
	v_mul_f32_e32 v22, v7, v7
	v_fmac_f32_e32 v22, v6, v6
	v_fmac_f32_e32 v23, v8, v8
	v_add_f32_e32 v22, v22, v23
	v_mul_f32_e32 v23, v15, v15
	v_mul_f32_e32 v24, v17, v17
	v_fmac_f32_e32 v23, v14, v14
	v_fmac_f32_e32 v24, v16, v16
	v_add_f32_e32 v33, v33, v122
	v_add_f32_e32 v23, v23, v24
	v_add_f32_e32 v32, v32, v33
	v_add_f32_e32 v22, v22, v23
	v_add_f32_e32 v24, v32, v22
	ds_bpermute_b32 v25, v152, v24
	flat_store_dwordx4 v[30:31], v[6:9] offset:512 nt
	flat_store_dwordx4 v[30:31], v[14:17] offset:528 nt
	v_pk_mul_f32 v[22:23], v[166:167], v[16:17]
	v_pk_mul_f32 v[6:7], v[174:175], v[6:7]
	v_pk_mul_f32 v[16:17], v[168:169], v[14:15]
	v_cvt_pk_bf16_f32 v14, v6, v7
	s_waitcnt lgkmcnt(0)
	v_add_f32_e32 v6, v24, v25
	ds_bpermute_b32 v7, v153, v6
	v_pk_mul_f32 v[8:9], v[176:177], v[8:9]
	v_cvt_pk_bf16_f32 v16, v16, v17
	v_cvt_pk_bf16_f32 v15, v8, v9
	v_cvt_pk_bf16_f32 v17, v22, v23
	flat_store_dwordx4 v[26:27], v[14:17] offset:256
	s_and_saveexec_b64 s[6:7], vcc
	s_cbranch_execz .LBB0_1618
	v_lshlrev_b64 v[8:9], 7, v[146:147]
	v_lshl_add_u64 v[8:9], s[60:61], 0, v[8:9]
	s_waitcnt lgkmcnt(0)
	v_add_f32_e32 v6, v6, v7
	flat_store_dword v[8:9], v6
.LBB0_1618:
	s_or_b64 exec, exec, s[6:7]
	v_lshl_add_u64 v[114:115], v[220:221], 0, s[30:31]
	s_waitcnt lgkmcnt(0)
	v_lshlrev_b64 v[6:7], 13, v[114:115]
	v_lshl_add_u64 v[118:119], s[64:65], 0, v[6:7]
	v_lshl_add_u64 v[6:7], s[66:67], 0, v[6:7]
	v_lshl_add_u64 v[116:117], v[6:7], 0, s[16:17]
	v_cmp_gt_i64_e64 s[6:7], s[46:47], v[220:221]
	s_nop 1
	v_cndmask_b32_e64 v7, v117, v119, s[6:7]
	v_cndmask_b32_e64 v6, v116, v118, s[6:7]
	v_lshl_add_u64 v[6:7], v[218:219], 2, v[6:7]
	flat_load_dwordx4 v[26:29], v[6:7] nt
	flat_load_dwordx4 v[22:25], v[6:7] offset:16 nt
	flat_load_dwordx4 v[14:17], v[6:7] offset:512 nt
	s_nop 0
	flat_load_dwordx4 v[6:9], v[6:7] offset:528 nt
	s_and_saveexec_b64 s[68:69], s[4:5]
	v_lshlrev_b32_e32 v32, 7, v134
	v_bfe_u32 v30, v134, 6, 7
	v_and_b32_e32 v31, 0xffffe000, v134
	v_and_b32_e32 v32, 0x1f80, v32
	v_or3_b32 v134, v31, v32, v30
	v_mov_b64_e32 v[136:137], v[138:139]
	s_or_b64 exec, exec, s[68:69]
	v_lshlrev_b64 v[30:31], 12, v[134:135]
	v_lshl_add_u64 v[120:121], s[62:63], 0, v[30:31]
	v_pk_fma_f32 v[32:33], v[112:113], v[208:209], v[132:133]
	v_pk_fma_f32 v[30:31], v[110:111], v[206:207], v[130:131]
	v_pk_fma_f32 v[20:21], v[108:109], v[204:205], v[20:21]
	v_mul_f32_e32 v108, v31, v31
	v_mul_f32_e32 v109, v33, v33
	v_pk_fma_f32 v[18:19], v[106:107], v[202:203], v[18:19]
	v_fmac_f32_e32 v108, v30, v30
	v_fmac_f32_e32 v109, v32, v32
	v_add_f32_e32 v108, v108, v109
	v_mul_f32_e32 v109, v19, v19
	v_mul_f32_e32 v110, v21, v21
	v_fmac_f32_e32 v109, v18, v18
	v_fmac_f32_e32 v110, v20, v20
	v_lshl_add_u64 v[106:107], v[218:219], 2, v[136:137]
	v_add_f32_e32 v109, v109, v110
	flat_store_dwordx4 v[106:107], v[30:33] nt
	flat_store_dwordx4 v[106:107], v[18:21] offset:16 nt
	v_add_f32_e32 v110, v108, v109
	v_pk_mul_f32 v[32:33], v[192:193], v[32:33]
	v_pk_mul_f32 v[30:31], v[190:191], v[30:31]
	v_pk_mul_f32 v[108:109], v[194:195], v[20:21]
	v_pk_mul_f32 v[20:21], v[196:197], v[18:19]
	v_cvt_pk_bf16_f32 v18, v30, v31
	v_cvt_pk_bf16_f32 v19, v32, v33
	v_cvt_pk_bf16_f32 v20, v20, v21
	v_cvt_pk_bf16_f32 v21, v108, v109
	v_lshl_add_u64 v[30:31], v[218:219], 1, v[120:121]
	v_pk_fma_f32 v[12:13], v[104:105], v[184:185], v[12:13]
	v_pk_fma_f32 v[10:11], v[102:103], v[182:183], v[10:11]
	flat_store_dwordx4 v[30:31], v[18:21]
	v_pk_fma_f32 v[4:5], v[100:101], v[172:173], v[4:5]
	v_pk_fma_f32 v[2:3], v[98:99], v[170:171], v[2:3]
	v_mul_f32_e32 v18, v11, v11
	v_mul_f32_e32 v19, v13, v13
	v_fmac_f32_e32 v18, v10, v10
	v_fmac_f32_e32 v19, v12, v12
	v_add_f32_e32 v18, v18, v19
	v_mul_f32_e32 v19, v3, v3
	v_mul_f32_e32 v20, v5, v5
	v_fmac_f32_e32 v19, v2, v2
	v_fmac_f32_e32 v20, v4, v4
	v_add_f32_e32 v19, v19, v20
	v_add_f32_e32 v18, v18, v19
	v_add_f32_e32 v20, v110, v18
	ds_bpermute_b32 v21, v152, v20
	flat_store_dwordx4 v[106:107], v[10:13] offset:512 nt
	flat_store_dwordx4 v[106:107], v[2:5] offset:528 nt
	v_pk_mul_f32 v[18:19], v[168:169], v[2:3]
	v_pk_mul_f32 v[12:13], v[176:177], v[12:13]
	v_pk_mul_f32 v[10:11], v[174:175], v[10:11]
	s_waitcnt lgkmcnt(0)
	v_add_f32_e32 v2, v20, v21
	ds_bpermute_b32 v3, v153, v2
	v_pk_mul_f32 v[4:5], v[166:167], v[4:5]
	v_cvt_pk_bf16_f32 v10, v10, v11
	v_cvt_pk_bf16_f32 v11, v12, v13
	v_cvt_pk_bf16_f32 v12, v18, v19
	v_cvt_pk_bf16_f32 v13, v4, v5
	flat_store_dwordx4 v[30:31], v[10:13] offset:256
	s_and_saveexec_b64 s[4:5], vcc
	s_cbranch_execz .LBB0_1622
	v_lshlrev_b64 v[4:5], 7, v[134:135]
	v_lshl_add_u64 v[4:5], s[60:61], 0, v[4:5]
	s_waitcnt lgkmcnt(0)
	v_add_f32_e32 v2, v2, v3
	flat_store_dword v[4:5], v2
.LBB0_1622:
	s_or_b64 exec, exec, s[4:5]
	v_lshl_add_u64 v[98:99], v[220:221], 0, s[48:49]
	s_waitcnt lgkmcnt(0)
	v_lshlrev_b64 v[2:3], 13, v[98:99]
	v_lshl_add_u64 v[102:103], s[64:65], 0, v[2:3]
	v_lshl_add_u64 v[2:3], s[66:67], 0, v[2:3]
	v_lshl_add_u64 v[100:101], v[2:3], 0, s[16:17]
	v_cmp_gt_i64_e64 s[4:5], s[50:51], v[220:221]
	s_nop 1
	v_cndmask_b32_e64 v3, v101, v103, s[4:5]
	v_cndmask_b32_e64 v2, v100, v102, s[4:5]
	v_lshl_add_u64 v[2:3], v[218:219], 2, v[2:3]
	flat_load_dwordx4 v[30:33], v[2:3] nt
	flat_load_dwordx4 v[18:21], v[2:3] offset:16 nt
	flat_load_dwordx4 v[10:13], v[2:3] offset:512 nt
	s_nop 0
	flat_load_dwordx4 v[2:5], v[2:3] offset:528 nt
	s_and_saveexec_b64 s[68:69], s[6:7]
	v_lshlrev_b32_e32 v106, 7, v114
	v_bfe_u32 v104, v114, 6, 7
	v_and_b32_e32 v105, 0xffffe000, v114
	v_and_b32_e32 v106, 0x1f80, v106
	v_or3_b32 v114, v105, v106, v104
	v_mov_b64_e32 v[116:117], v[118:119]
	s_or_b64 exec, exec, s[68:69]
	s_waitcnt vmcnt(0)
	v_pk_fma_f32 v[28:29], v[96:97], v[208:209], v[28:29]
	v_pk_fma_f32 v[26:27], v[94:95], v[206:207], v[26:27]
	v_pk_fma_f32 v[24:25], v[92:93], v[204:205], v[24:25]
	v_mul_f32_e32 v92, v27, v27
	v_mul_f32_e32 v93, v29, v29
	v_pk_fma_f32 v[22:23], v[90:91], v[202:203], v[22:23]
	v_fmac_f32_e32 v92, v26, v26
	v_fmac_f32_e32 v93, v28, v28
	v_add_f32_e32 v92, v92, v93
	v_mul_f32_e32 v93, v23, v23
	v_mul_f32_e32 v94, v25, v25
	v_fmac_f32_e32 v93, v22, v22
	v_fmac_f32_e32 v94, v24, v24
	v_lshlrev_b64 v[104:105], 12, v[114:115]
	v_lshl_add_u64 v[90:91], v[218:219], 2, v[116:117]
	v_add_f32_e32 v93, v93, v94
	v_lshl_add_u64 v[104:105], s[62:63], 0, v[104:105]
	flat_store_dwordx4 v[90:91], v[26:29] nt
	flat_store_dwordx4 v[90:91], v[22:25] offset:16 nt
	v_add_f32_e32 v94, v92, v93
	v_pk_mul_f32 v[28:29], v[192:193], v[28:29]
	v_pk_mul_f32 v[26:27], v[190:191], v[26:27]
	v_pk_mul_f32 v[92:93], v[194:195], v[24:25]
	v_pk_mul_f32 v[24:25], v[196:197], v[22:23]
	v_cvt_pk_bf16_f32 v22, v26, v27
	v_cvt_pk_bf16_f32 v23, v28, v29
	v_cvt_pk_bf16_f32 v24, v24, v25
	v_cvt_pk_bf16_f32 v25, v92, v93
	v_lshl_add_u64 v[26:27], v[218:219], 1, v[104:105]
	v_pk_fma_f32 v[16:17], v[88:89], v[184:185], v[16:17]
	v_pk_fma_f32 v[14:15], v[86:87], v[182:183], v[14:15]
	flat_store_dwordx4 v[26:27], v[22:25]
	v_pk_fma_f32 v[8:9], v[84:85], v[172:173], v[8:9]
	v_pk_fma_f32 v[6:7], v[82:83], v[170:171], v[6:7]
	v_mul_f32_e32 v22, v15, v15
	v_mul_f32_e32 v23, v17, v17
	v_fmac_f32_e32 v22, v14, v14
	v_fmac_f32_e32 v23, v16, v16
	v_add_f32_e32 v22, v22, v23
	v_mul_f32_e32 v23, v7, v7
	v_mul_f32_e32 v24, v9, v9
	v_fmac_f32_e32 v23, v6, v6
	v_fmac_f32_e32 v24, v8, v8
	v_add_f32_e32 v23, v23, v24
	v_add_f32_e32 v22, v22, v23
	v_add_f32_e32 v24, v94, v22
	ds_bpermute_b32 v25, v152, v24
	flat_store_dwordx4 v[90:91], v[14:17] offset:512 nt
	flat_store_dwordx4 v[90:91], v[6:9] offset:528 nt
	v_pk_mul_f32 v[22:23], v[168:169], v[6:7]
	v_pk_mul_f32 v[16:17], v[176:177], v[16:17]
	v_pk_mul_f32 v[14:15], v[174:175], v[14:15]
	s_waitcnt lgkmcnt(0)
	v_add_f32_e32 v6, v24, v25
	ds_bpermute_b32 v7, v153, v6
	v_pk_mul_f32 v[8:9], v[166:167], v[8:9]
	v_cvt_pk_bf16_f32 v14, v14, v15
	v_cvt_pk_bf16_f32 v15, v16, v17
	v_cvt_pk_bf16_f32 v16, v22, v23
	v_cvt_pk_bf16_f32 v17, v8, v9
	flat_store_dwordx4 v[26:27], v[14:17] offset:256
	s_and_saveexec_b64 s[6:7], vcc
	s_cbranch_execz .LBB0_1626
	v_lshlrev_b64 v[8:9], 7, v[114:115]
	v_lshl_add_u64 v[8:9], s[60:61], 0, v[8:9]
	s_waitcnt lgkmcnt(0)
	v_add_f32_e32 v6, v6, v7
	flat_store_dword v[8:9], v6
.LBB0_1626:
	s_or_b64 exec, exec, s[6:7]
	v_lshl_add_u64 v[82:83], v[220:221], 0, s[52:53]
	s_waitcnt lgkmcnt(0)
	v_lshlrev_b64 v[6:7], 13, v[82:83]
	v_lshl_add_u64 v[86:87], s[64:65], 0, v[6:7]
	v_lshl_add_u64 v[6:7], s[66:67], 0, v[6:7]
	v_lshl_add_u64 v[84:85], v[6:7], 0, s[16:17]
	v_cmp_gt_i64_e64 s[6:7], s[54:55], v[220:221]
	s_nop 1
	v_cndmask_b32_e64 v7, v85, v87, s[6:7]
	v_cndmask_b32_e64 v6, v84, v86, s[6:7]
	v_lshl_add_u64 v[6:7], v[218:219], 2, v[6:7]
	flat_load_dwordx4 v[26:29], v[6:7] nt
	flat_load_dwordx4 v[22:25], v[6:7] offset:16 nt
	flat_load_dwordx4 v[14:17], v[6:7] offset:512 nt
	s_nop 0
	flat_load_dwordx4 v[6:9], v[6:7] offset:528 nt
	s_and_saveexec_b64 s[68:69], s[4:5]
	v_lshlrev_b32_e32 v90, 7, v98
	v_bfe_u32 v88, v98, 6, 7
	v_and_b32_e32 v89, 0xffffe000, v98
	v_and_b32_e32 v90, 0x1f80, v90
	v_or3_b32 v98, v89, v90, v88
	v_mov_b64_e32 v[100:101], v[102:103]
	s_or_b64 exec, exec, s[68:69]
	v_pk_fma_f32 v[32:33], v[80:81], v[208:209], v[32:33]
	v_pk_fma_f32 v[30:31], v[78:79], v[206:207], v[30:31]
	v_pk_fma_f32 v[20:21], v[76:77], v[204:205], v[20:21]
	v_mul_f32_e32 v76, v31, v31
	v_mul_f32_e32 v77, v33, v33
	v_pk_fma_f32 v[18:19], v[74:75], v[202:203], v[18:19]
	v_fmac_f32_e32 v76, v30, v30
	v_fmac_f32_e32 v77, v32, v32
	v_add_f32_e32 v76, v76, v77
	v_mul_f32_e32 v77, v19, v19
	v_mul_f32_e32 v78, v21, v21
	v_fmac_f32_e32 v77, v18, v18
	v_fmac_f32_e32 v78, v20, v20
	v_lshlrev_b64 v[88:89], 12, v[98:99]
	v_lshl_add_u64 v[74:75], v[218:219], 2, v[100:101]
	v_add_f32_e32 v77, v77, v78
	v_lshl_add_u64 v[88:89], s[62:63], 0, v[88:89]
	flat_store_dwordx4 v[74:75], v[30:33] nt
	flat_store_dwordx4 v[74:75], v[18:21] offset:16 nt
	v_add_f32_e32 v78, v76, v77
	v_pk_mul_f32 v[32:33], v[192:193], v[32:33]
	v_pk_mul_f32 v[30:31], v[190:191], v[30:31]
	v_pk_mul_f32 v[76:77], v[194:195], v[20:21]
	v_pk_mul_f32 v[20:21], v[196:197], v[18:19]
	v_cvt_pk_bf16_f32 v18, v30, v31
	v_cvt_pk_bf16_f32 v19, v32, v33
	v_cvt_pk_bf16_f32 v20, v20, v21
	v_cvt_pk_bf16_f32 v21, v76, v77
	v_lshl_add_u64 v[30:31], v[218:219], 1, v[88:89]
	v_pk_fma_f32 v[12:13], v[72:73], v[184:185], v[12:13]
	v_pk_fma_f32 v[10:11], v[70:71], v[182:183], v[10:11]
	flat_store_dwordx4 v[30:31], v[18:21]
	v_pk_fma_f32 v[4:5], v[68:69], v[172:173], v[4:5]
	v_pk_fma_f32 v[2:3], v[66:67], v[170:171], v[2:3]
	v_mul_f32_e32 v18, v11, v11
	v_mul_f32_e32 v19, v13, v13
	v_fmac_f32_e32 v18, v10, v10
	v_fmac_f32_e32 v19, v12, v12
	v_add_f32_e32 v18, v18, v19
	v_mul_f32_e32 v19, v3, v3
	v_mul_f32_e32 v20, v5, v5
	v_fmac_f32_e32 v19, v2, v2
	v_fmac_f32_e32 v20, v4, v4
	v_add_f32_e32 v19, v19, v20
	v_add_f32_e32 v18, v18, v19
	v_add_f32_e32 v20, v78, v18
	ds_bpermute_b32 v21, v152, v20
	flat_store_dwordx4 v[74:75], v[10:13] offset:512 nt
	flat_store_dwordx4 v[74:75], v[2:5] offset:528 nt
	v_pk_mul_f32 v[18:19], v[168:169], v[2:3]
	v_pk_mul_f32 v[12:13], v[176:177], v[12:13]
	v_pk_mul_f32 v[10:11], v[174:175], v[10:11]
	s_waitcnt lgkmcnt(0)
	v_add_f32_e32 v2, v20, v21
	ds_bpermute_b32 v3, v153, v2
	v_pk_mul_f32 v[4:5], v[166:167], v[4:5]
	v_cvt_pk_bf16_f32 v10, v10, v11
	v_cvt_pk_bf16_f32 v11, v12, v13
	v_cvt_pk_bf16_f32 v12, v18, v19
	v_cvt_pk_bf16_f32 v13, v4, v5
	flat_store_dwordx4 v[30:31], v[10:13] offset:256
	s_and_saveexec_b64 s[4:5], vcc
	s_cbranch_execz .LBB0_1630
	v_lshlrev_b64 v[4:5], 7, v[98:99]
	v_lshl_add_u64 v[4:5], s[60:61], 0, v[4:5]
	s_waitcnt lgkmcnt(0)
	v_add_f32_e32 v2, v2, v3
	flat_store_dword v[4:5], v2
.LBB0_1630:
	s_or_b64 exec, exec, s[4:5]
	v_lshl_add_u64 v[66:67], v[220:221], 0, s[56:57]
	s_waitcnt lgkmcnt(0)
	v_lshlrev_b64 v[2:3], 13, v[66:67]
	v_lshl_add_u64 v[70:71], s[64:65], 0, v[2:3]
	v_lshl_add_u64 v[2:3], s[66:67], 0, v[2:3]
	v_lshl_add_u64 v[68:69], v[2:3], 0, s[16:17]
	v_cmp_gt_i64_e64 s[4:5], s[58:59], v[220:221]
	s_nop 1
	v_cndmask_b32_e64 v3, v69, v71, s[4:5]
	v_cndmask_b32_e64 v2, v68, v70, s[4:5]
	v_lshl_add_u64 v[2:3], v[218:219], 2, v[2:3]
	flat_load_dwordx4 v[30:33], v[2:3] nt
	flat_load_dwordx4 v[18:21], v[2:3] offset:16 nt
	flat_load_dwordx4 v[10:13], v[2:3] offset:512 nt
	s_nop 0
	flat_load_dwordx4 v[2:5], v[2:3] offset:528 nt
	s_and_saveexec_b64 s[64:65], s[6:7]
	v_lshlrev_b32_e32 v74, 7, v82
	v_bfe_u32 v72, v82, 6, 7
	v_and_b32_e32 v73, 0xffffe000, v82
	v_and_b32_e32 v74, 0x1f80, v74
	v_or3_b32 v82, v73, v74, v72
	v_mov_b64_e32 v[84:85], v[86:87]
	s_or_b64 exec, exec, s[64:65]
	s_waitcnt vmcnt(0)
	v_pk_fma_f32 v[28:29], v[64:65], v[208:209], v[28:29]
	v_pk_fma_f32 v[26:27], v[62:63], v[206:207], v[26:27]
	v_pk_fma_f32 v[24:25], v[60:61], v[204:205], v[24:25]
	v_mul_f32_e32 v60, v27, v27
	v_mul_f32_e32 v61, v29, v29
	v_pk_fma_f32 v[22:23], v[58:59], v[202:203], v[22:23]
	v_fmac_f32_e32 v60, v26, v26
	v_fmac_f32_e32 v61, v28, v28
	v_add_f32_e32 v60, v60, v61
	v_mul_f32_e32 v61, v23, v23
	v_mul_f32_e32 v62, v25, v25
	v_fmac_f32_e32 v61, v22, v22
	v_fmac_f32_e32 v62, v24, v24
	v_lshlrev_b64 v[72:73], 12, v[82:83]
	v_lshl_add_u64 v[58:59], v[218:219], 2, v[84:85]
	v_add_f32_e32 v61, v61, v62
	v_lshl_add_u64 v[72:73], s[62:63], 0, v[72:73]
	flat_store_dwordx4 v[58:59], v[26:29] nt
	flat_store_dwordx4 v[58:59], v[22:25] offset:16 nt
	v_add_f32_e32 v62, v60, v61
	v_pk_mul_f32 v[28:29], v[192:193], v[28:29]
	v_pk_mul_f32 v[26:27], v[190:191], v[26:27]
	v_pk_mul_f32 v[60:61], v[194:195], v[24:25]
	v_pk_mul_f32 v[24:25], v[196:197], v[22:23]
	v_cvt_pk_bf16_f32 v22, v26, v27
	v_cvt_pk_bf16_f32 v23, v28, v29
	v_cvt_pk_bf16_f32 v24, v24, v25
	v_cvt_pk_bf16_f32 v25, v60, v61
	v_lshl_add_u64 v[26:27], v[218:219], 1, v[72:73]
	v_pk_fma_f32 v[16:17], v[56:57], v[184:185], v[16:17]
	v_pk_fma_f32 v[14:15], v[54:55], v[182:183], v[14:15]
	flat_store_dwordx4 v[26:27], v[22:25]
	v_pk_fma_f32 v[8:9], v[52:53], v[172:173], v[8:9]
	v_pk_fma_f32 v[6:7], v[50:51], v[170:171], v[6:7]
	v_mul_f32_e32 v22, v15, v15
	v_mul_f32_e32 v23, v17, v17
	v_fmac_f32_e32 v22, v14, v14
	v_fmac_f32_e32 v23, v16, v16
	v_add_f32_e32 v22, v22, v23
	v_mul_f32_e32 v23, v7, v7
	v_mul_f32_e32 v24, v9, v9
	v_fmac_f32_e32 v23, v6, v6
	v_fmac_f32_e32 v24, v8, v8
	v_add_f32_e32 v23, v23, v24
	v_add_f32_e32 v22, v22, v23
	v_add_f32_e32 v24, v62, v22
	ds_bpermute_b32 v25, v152, v24
	flat_store_dwordx4 v[58:59], v[14:17] offset:512 nt
	flat_store_dwordx4 v[58:59], v[6:9] offset:528 nt
	v_pk_mul_f32 v[22:23], v[168:169], v[6:7]
	v_pk_mul_f32 v[16:17], v[176:177], v[16:17]
	v_pk_mul_f32 v[14:15], v[174:175], v[14:15]
	s_waitcnt lgkmcnt(0)
	v_add_f32_e32 v6, v24, v25
	ds_bpermute_b32 v7, v153, v6
	v_pk_mul_f32 v[8:9], v[166:167], v[8:9]
	v_cvt_pk_bf16_f32 v14, v14, v15
	v_cvt_pk_bf16_f32 v15, v16, v17
	v_cvt_pk_bf16_f32 v16, v22, v23
	v_cvt_pk_bf16_f32 v17, v8, v9
	flat_store_dwordx4 v[26:27], v[14:17] offset:256
	s_and_saveexec_b64 s[6:7], vcc
	s_cbranch_execz .LBB0_1634
	v_lshlrev_b64 v[8:9], 7, v[82:83]
	v_lshl_add_u64 v[8:9], s[60:61], 0, v[8:9]
	s_waitcnt lgkmcnt(0)
	v_add_f32_e32 v6, v6, v7
	flat_store_dword v[8:9], v6
.LBB0_1634:
	s_or_b64 exec, exec, s[6:7]
	s_and_saveexec_b64 s[6:7], s[4:5]
	s_cbranch_execz .LBB0_1636
	v_lshlrev_b32_e32 v8, 7, v66
	v_bfe_u32 v6, v66, 6, 7
	s_waitcnt lgkmcnt(0)
	v_and_b32_e32 v7, 0xffffe000, v66
	v_and_b32_e32 v8, 0x1f80, v8
	v_or3_b32 v66, v7, v8, v6
	v_mov_b64_e32 v[68:69], v[70:71]
.LBB0_1636:
	s_or_b64 exec, exec, s[6:7]
	s_waitcnt lgkmcnt(0)
	v_lshlrev_b64 v[6:7], 12, v[66:67]
	v_lshl_add_u64 v[22:23], s[62:63], 0, v[6:7]
	v_pk_fma_f32 v[8:9], v[48:49], v[208:209], v[32:33]
	v_pk_fma_f32 v[6:7], v[46:47], v[206:207], v[30:31]
	v_pk_fma_f32 v[16:17], v[44:45], v[204:205], v[20:21]
	v_mul_f32_e32 v20, v7, v7
	v_mul_f32_e32 v21, v9, v9
	v_pk_fma_f32 v[14:15], v[42:43], v[202:203], v[18:19]
	v_fmac_f32_e32 v20, v6, v6
	v_fmac_f32_e32 v21, v8, v8
	v_lshl_add_u64 v[18:19], v[218:219], 2, v[68:69]
	v_add_f32_e32 v20, v20, v21
	v_mul_f32_e32 v21, v15, v15
	v_mul_f32_e32 v24, v17, v17
	flat_store_dwordx4 v[18:19], v[6:9] nt
	flat_store_dwordx4 v[18:19], v[14:17] offset:16 nt
	v_fmac_f32_e32 v21, v14, v14
	v_fmac_f32_e32 v24, v16, v16
	v_pk_mul_f32 v[8:9], v[192:193], v[8:9]
	v_pk_mul_f32 v[6:7], v[190:191], v[6:7]
	v_pk_mul_f32 v[16:17], v[194:195], v[16:17]
	v_pk_mul_f32 v[14:15], v[196:197], v[14:15]
	v_cvt_pk_bf16_f32 v6, v6, v7
	v_cvt_pk_bf16_f32 v7, v8, v9
	v_cvt_pk_bf16_f32 v8, v14, v15
	v_cvt_pk_bf16_f32 v9, v16, v17
	v_lshl_add_u64 v[14:15], v[218:219], 1, v[22:23]
	flat_store_dwordx4 v[14:15], v[6:9]
	v_pk_fma_f32 v[4:5], v[36:37], v[172:173], v[4:5]
	v_pk_fma_f32 v[2:3], v[34:35], v[170:171], v[2:3]
	v_pk_fma_f32 v[8:9], v[40:41], v[184:185], v[12:13]
	v_pk_fma_f32 v[6:7], v[38:39], v[182:183], v[10:11]
	v_mul_f32_e32 v11, v9, v9
	v_mul_f32_e32 v10, v7, v7
	v_fmac_f32_e32 v10, v6, v6
	v_fmac_f32_e32 v11, v8, v8
	v_add_f32_e32 v10, v10, v11
	v_mul_f32_e32 v11, v3, v3
	v_mul_f32_e32 v12, v5, v5
	v_fmac_f32_e32 v11, v2, v2
	v_fmac_f32_e32 v12, v4, v4
	v_add_f32_e32 v21, v21, v24
	v_add_f32_e32 v11, v11, v12
	v_add_f32_e32 v20, v20, v21
	v_add_f32_e32 v10, v10, v11
	v_add_f32_e32 v16, v20, v10
	ds_bpermute_b32 v17, v152, v16
	flat_store_dwordx4 v[18:19], v[6:9] offset:512 nt
	flat_store_dwordx4 v[18:19], v[2:5] offset:528 nt
	v_pk_mul_f32 v[12:13], v[168:169], v[2:3]
	v_pk_mul_f32 v[8:9], v[176:177], v[8:9]
	v_pk_mul_f32 v[6:7], v[174:175], v[6:7]
	s_waitcnt lgkmcnt(0)
	v_add_f32_e32 v2, v16, v17
	ds_bpermute_b32 v3, v153, v2
	v_pk_mul_f32 v[10:11], v[166:167], v[4:5]
	v_cvt_pk_bf16_f32 v4, v6, v7
	v_cvt_pk_bf16_f32 v5, v8, v9
	v_cvt_pk_bf16_f32 v6, v12, v13
	v_cvt_pk_bf16_f32 v7, v10, v11
	flat_store_dwordx4 v[14:15], v[4:7] offset:256
	s_and_saveexec_b64 s[4:5], vcc
	s_cbranch_execz .LBB0_1638
	v_lshlrev_b64 v[4:5], 7, v[66:67]
	v_lshl_add_u64 v[4:5], s[60:61], 0, v[4:5]
	s_waitcnt lgkmcnt(0)
	v_add_f32_e32 v2, v2, v3
	flat_store_dword v[4:5], v2
.LBB0_1638:
	s_or_b64 exec, exec, s[4:5]
	s_andn2_b64 vcc, exec, s[2:3]
	s_mov_b64 s[2:3], -1
	s_cbranch_vccnz .LBB0_1598
	s_andn2_b64 vcc, exec, s[10:11]
	s_cbranch_vccnz .LBB0_1597
	s_barrier
	s_branch .LBB0_1597

.LBB0_1841:
	ds_read_b128 v[132:135], v170
	ds_read_b128 v[136:139], v171
	ds_read_b128 v[140:143], v166
	ds_read_b128 v[154:157], v167
	ds_read_b128 v[188:191], v172
	ds_read_b128 v[192:195], v173
	ds_read_b128 v[196:199], v174
	ds_read_b128 v[200:203], v175
	s_add_i32 s75, s94, 0x80
	s_and_b64 s[50:51], s[50:51], exec
	s_cselect_b32 s50, s75, s49
	s_cselect_b32 s75, s95, s93
	s_add_i32 s51, s75, 0x80
	v_add_u32_e32 v144, s94, v183
	s_add_i32 m0, s52, 0xc000
	ds_read_b128 v[204:207], v184
	ds_read_b128 v[214:217], v184 offset:1024
	ds_read_b128 v[218:221], v184 offset:2048
	ds_read_b128 v[222:225], v184 offset:3072
	ds_read_b128 v[226:229], v184 offset:4096
	ds_read_b128 v[230:233], v184 offset:5120
	ds_read_b128 v[234:237], v184 offset:6144
	ds_read_b128 v[238:241], v184 offset:7168
	global_load_lds_dwordx4 v144, s[8:9]
	v_add_u32_e32 v144, s94, v182
	s_add_i32 m0, s52, 0xe000
	s_nop 0
	global_load_lds_dwordx4 v144, s[8:9]
	s_waitcnt vmcnt(8)
	s_waitcnt lgkmcnt(0)
	s_setprio 1
	s_barrier
	s_waitcnt lgkmcnt(0)
	v_mfma_f32_16x16x32_bf16 v[126:129], v[140:143], v[204:207], v[126:129]
	v_mfma_f32_16x16x32_bf16 v[122:125], v[136:139], v[204:207], v[122:125]
	v_mfma_f32_16x16x32_bf16 v[110:113], v[140:143], v[218:221], v[110:113]
	v_mfma_f32_16x16x32_bf16 v[106:109], v[136:139], v[218:221], v[106:109]
	v_mfma_f32_16x16x32_bf16 v[94:97], v[140:143], v[226:229], v[94:97]
	v_mfma_f32_16x16x32_bf16 v[90:93], v[136:139], v[226:229], v[90:93]
	v_mfma_f32_16x16x32_bf16 v[78:81], v[140:143], v[234:237], v[78:81]
	v_mfma_f32_16x16x32_bf16 v[74:77], v[136:139], v[234:237], v[74:77]
	v_mfma_f32_16x16x32_bf16 v[126:129], v[132:135], v[214:217], v[126:129]
	v_mfma_f32_16x16x32_bf16 v[122:125], v[188:191], v[214:217], v[122:125]
	v_mfma_f32_16x16x32_bf16 v[110:113], v[132:135], v[222:225], v[110:113]
	v_mfma_f32_16x16x32_bf16 v[106:109], v[188:191], v[222:225], v[106:109]
	v_mfma_f32_16x16x32_bf16 v[94:97], v[132:135], v[230:233], v[94:97]
	v_mfma_f32_16x16x32_bf16 v[90:93], v[188:191], v[230:233], v[90:93]
	v_mfma_f32_16x16x32_bf16 v[78:81], v[132:135], v[238:241], v[78:81]
	v_mfma_f32_16x16x32_bf16 v[74:77], v[188:191], v[238:241], v[74:77]
	s_setprio 0
	s_setprio 1
	v_mfma_f32_16x16x32_bf16 v[118:121], v[154:157], v[204:207], v[118:121]
	v_mfma_f32_16x16x32_bf16 v[114:117], v[196:199], v[204:207], v[114:117]
	v_mfma_f32_16x16x32_bf16 v[102:105], v[154:157], v[218:221], v[102:105]
	v_mfma_f32_16x16x32_bf16 v[98:101], v[196:199], v[218:221], v[98:101]
	v_mfma_f32_16x16x32_bf16 v[86:89], v[154:157], v[226:229], v[86:89]
	v_mfma_f32_16x16x32_bf16 v[82:85], v[196:199], v[226:229], v[82:85]
	v_mfma_f32_16x16x32_bf16 v[70:73], v[154:157], v[234:237], v[70:73]
	v_mfma_f32_16x16x32_bf16 v[66:69], v[196:199], v[234:237], v[66:69]
	v_mfma_f32_16x16x32_bf16 v[118:121], v[192:195], v[214:217], v[118:121]
	v_mfma_f32_16x16x32_bf16 v[114:117], v[200:203], v[214:217], v[114:117]
	v_mfma_f32_16x16x32_bf16 v[102:105], v[192:195], v[222:225], v[102:105]
	v_mfma_f32_16x16x32_bf16 v[98:101], v[200:203], v[222:225], v[98:101]
	v_mfma_f32_16x16x32_bf16 v[86:89], v[192:195], v[230:233], v[86:89]
	v_mfma_f32_16x16x32_bf16 v[82:85], v[200:203], v[230:233], v[82:85]
	v_mfma_f32_16x16x32_bf16 v[70:73], v[192:195], v[238:241], v[70:73]
	v_mfma_f32_16x16x32_bf16 v[66:69], v[200:203], v[238:241], v[66:69]
	s_setprio 0
	s_barrier
	s_mov_b32 m0, s53
	v_add_u32_e32 v144, s75, v160
	ds_read_b128 v[204:207], v184 offset:16384
	ds_read_b128 v[214:217], v184 offset:17408
	ds_read_b128 v[218:221], v184 offset:18432
	ds_read_b128 v[222:225], v184 offset:19456
	ds_read_b128 v[226:229], v184 offset:20480
	ds_read_b128 v[230:233], v184 offset:21504
	ds_read_b128 v[234:237], v184 offset:22528
	ds_read_b128 v[238:241], v184 offset:23552
	global_load_lds_dwordx4 v144, s[20:21]
	v_add_u32_e32 v144, s45, v144
	s_mov_b32 m0, s54
	s_nop 0
	global_load_lds_dwordx4 v144, s[20:21]
	v_add_u32_e32 v144, s75, v161
	s_mov_b32 m0, s55
	s_nop 0
	global_load_lds_dwordx4 v144, s[20:21]
	v_add_u32_e32 v144, s45, v144
	s_mov_b32 m0, s56
	s_nop 0
	global_load_lds_dwordx4 v144, s[20:21]
	v_add_u32_e32 v144, s50, v1
	s_mov_b32 m0, s52
	s_nop 0
	global_load_lds_dwordx4 v144, s[8:9]
	v_add_u32_e32 v144, s44, v144
	s_mov_b32 m0, s57
	s_nop 0
	global_load_lds_dwordx4 v144, s[8:9]
	s_waitcnt vmcnt(8)
	s_waitcnt lgkmcnt(0)
	s_setprio 1
	s_barrier
	s_waitcnt lgkmcnt(0)
	v_mfma_f32_16x16x32_bf16 v[62:65], v[140:143], v[204:207], v[62:65]
	v_mfma_f32_16x16x32_bf16 v[58:61], v[136:139], v[204:207], v[58:61]
	v_mfma_f32_16x16x32_bf16 v[46:49], v[140:143], v[218:221], v[46:49]
	v_mfma_f32_16x16x32_bf16 v[42:45], v[136:139], v[218:221], v[42:45]
	v_mfma_f32_16x16x32_bf16 v[30:33], v[140:143], v[226:229], v[30:33]
	v_mfma_f32_16x16x32_bf16 v[26:29], v[136:139], v[226:229], v[26:29]
	v_mfma_f32_16x16x32_bf16 v[14:17], v[140:143], v[234:237], v[14:17]
	v_mfma_f32_16x16x32_bf16 v[10:13], v[136:139], v[234:237], v[10:13]
	v_mfma_f32_16x16x32_bf16 v[62:65], v[132:135], v[214:217], v[62:65]
	v_mfma_f32_16x16x32_bf16 v[58:61], v[188:191], v[214:217], v[58:61]
	v_mfma_f32_16x16x32_bf16 v[46:49], v[132:135], v[222:225], v[46:49]
	v_mfma_f32_16x16x32_bf16 v[42:45], v[188:191], v[222:225], v[42:45]
	v_mfma_f32_16x16x32_bf16 v[30:33], v[132:135], v[230:233], v[30:33]
	v_mfma_f32_16x16x32_bf16 v[26:29], v[188:191], v[230:233], v[26:29]
	v_mfma_f32_16x16x32_bf16 v[14:17], v[132:135], v[238:241], v[14:17]
	v_mfma_f32_16x16x32_bf16 v[10:13], v[188:191], v[238:241], v[10:13]
	s_setprio 0
	s_setprio 1
	v_mfma_f32_16x16x32_bf16 v[54:57], v[154:157], v[204:207], v[54:57]
	v_mfma_f32_16x16x32_bf16 v[50:53], v[196:199], v[204:207], v[50:53]
	v_mfma_f32_16x16x32_bf16 v[38:41], v[154:157], v[218:221], v[38:41]
	v_mfma_f32_16x16x32_bf16 v[34:37], v[196:199], v[218:221], v[34:37]
	v_mfma_f32_16x16x32_bf16 v[22:25], v[154:157], v[226:229], v[22:25]
	v_mfma_f32_16x16x32_bf16 v[18:21], v[196:199], v[226:229], v[18:21]
	v_mfma_f32_16x16x32_bf16 v[6:9], v[154:157], v[234:237], v[6:9]
	v_mfma_f32_16x16x32_bf16 v[2:5], v[196:199], v[234:237], v[2:5]
	v_mfma_f32_16x16x32_bf16 v[54:57], v[192:195], v[214:217], v[54:57]
	v_mfma_f32_16x16x32_bf16 v[50:53], v[200:203], v[214:217], v[50:53]
	v_mfma_f32_16x16x32_bf16 v[38:41], v[192:195], v[222:225], v[38:41]
	v_mfma_f32_16x16x32_bf16 v[34:37], v[200:203], v[222:225], v[34:37]
	v_mfma_f32_16x16x32_bf16 v[22:25], v[192:195], v[230:233], v[22:25]
	v_mfma_f32_16x16x32_bf16 v[18:21], v[200:203], v[230:233], v[18:21]
	v_mfma_f32_16x16x32_bf16 v[6:9], v[192:195], v[238:241], v[6:9]
	v_mfma_f32_16x16x32_bf16 v[2:5], v[200:203], v[238:241], v[2:5]
	s_setprio 0
	s_barrier
	ds_read_b128 v[132:135], v176
	ds_read_b128 v[136:139], v177
	ds_read_b128 v[140:143], v168
	ds_read_b128 v[154:157], v169
	ds_read_b128 v[188:191], v178
	ds_read_b128 v[192:195], v179
	ds_read_b128 v[196:199], v180
	ds_read_b128 v[200:203], v181
	s_mov_b32 m0, s58
	v_add_u32_e32 v144, s50, v162
	ds_read_b128 v[204:207], v184 offset:32768
	ds_read_b128 v[214:217], v184 offset:33792
	ds_read_b128 v[218:221], v184 offset:34816
	ds_read_b128 v[222:225], v184 offset:35840
	ds_read_b128 v[226:229], v184 offset:36864
	ds_read_b128 v[230:233], v184 offset:37888
	ds_read_b128 v[234:237], v184 offset:38912
	ds_read_b128 v[238:241], v184 offset:39936
	global_load_lds_dwordx4 v144, s[8:9]
	v_add_u32_e32 v144, s44, v144
	s_mov_b32 m0, s59
	s_nop 0
	global_load_lds_dwordx4 v144, s[8:9]
	s_waitcnt vmcnt(8)
	s_waitcnt lgkmcnt(0)
	s_setprio 1
	s_barrier
	s_waitcnt lgkmcnt(0)
	v_mfma_f32_16x16x32_bf16 v[126:129], v[140:143], v[204:207], v[126:129]
	v_mfma_f32_16x16x32_bf16 v[122:125], v[136:139], v[204:207], v[122:125]
	v_mfma_f32_16x16x32_bf16 v[110:113], v[140:143], v[218:221], v[110:113]
	v_mfma_f32_16x16x32_bf16 v[106:109], v[136:139], v[218:221], v[106:109]
	v_mfma_f32_16x16x32_bf16 v[94:97], v[140:143], v[226:229], v[94:97]
	v_mfma_f32_16x16x32_bf16 v[90:93], v[136:139], v[226:229], v[90:93]
	v_mfma_f32_16x16x32_bf16 v[78:81], v[140:143], v[234:237], v[78:81]
	v_mfma_f32_16x16x32_bf16 v[74:77], v[136:139], v[234:237], v[74:77]
	v_mfma_f32_16x16x32_bf16 v[126:129], v[132:135], v[214:217], v[126:129]
	v_mfma_f32_16x16x32_bf16 v[122:125], v[188:191], v[214:217], v[122:125]
	v_mfma_f32_16x16x32_bf16 v[110:113], v[132:135], v[222:225], v[110:113]
	v_mfma_f32_16x16x32_bf16 v[106:109], v[188:191], v[222:225], v[106:109]
	v_mfma_f32_16x16x32_bf16 v[94:97], v[132:135], v[230:233], v[94:97]
	v_mfma_f32_16x16x32_bf16 v[90:93], v[188:191], v[230:233], v[90:93]
	v_mfma_f32_16x16x32_bf16 v[78:81], v[132:135], v[238:241], v[78:81]
	v_mfma_f32_16x16x32_bf16 v[74:77], v[188:191], v[238:241], v[74:77]
	s_setprio 0
	s_setprio 1
	v_mfma_f32_16x16x32_bf16 v[118:121], v[154:157], v[204:207], v[118:121]
	v_mfma_f32_16x16x32_bf16 v[114:117], v[196:199], v[204:207], v[114:117]
	v_mfma_f32_16x16x32_bf16 v[102:105], v[154:157], v[218:221], v[102:105]
	v_mfma_f32_16x16x32_bf16 v[98:101], v[196:199], v[218:221], v[98:101]
	v_mfma_f32_16x16x32_bf16 v[86:89], v[154:157], v[226:229], v[86:89]
	v_mfma_f32_16x16x32_bf16 v[82:85], v[196:199], v[226:229], v[82:85]
	v_mfma_f32_16x16x32_bf16 v[70:73], v[154:157], v[234:237], v[70:73]
	v_mfma_f32_16x16x32_bf16 v[66:69], v[196:199], v[234:237], v[66:69]
	v_mfma_f32_16x16x32_bf16 v[118:121], v[192:195], v[214:217], v[118:121]
	v_mfma_f32_16x16x32_bf16 v[114:117], v[200:203], v[214:217], v[114:117]
	v_mfma_f32_16x16x32_bf16 v[102:105], v[192:195], v[222:225], v[102:105]
	v_mfma_f32_16x16x32_bf16 v[98:101], v[200:203], v[222:225], v[98:101]
	v_mfma_f32_16x16x32_bf16 v[86:89], v[192:195], v[230:233], v[86:89]
	v_mfma_f32_16x16x32_bf16 v[82:85], v[200:203], v[230:233], v[82:85]
	v_mfma_f32_16x16x32_bf16 v[70:73], v[192:195], v[238:241], v[70:73]
	v_mfma_f32_16x16x32_bf16 v[66:69], v[200:203], v[238:241], v[66:69]
	s_setprio 0
	s_barrier
	s_mov_b32 m0, s64
	v_add_u32_e32 v144, s51, v160
	ds_read_b128 v[204:207], v184 offset:49152
	ds_read_b128 v[214:217], v184 offset:50176
	ds_read_b128 v[218:221], v184 offset:51200
	ds_read_b128 v[222:225], v184 offset:52224
	ds_read_b128 v[226:229], v184 offset:53248
	ds_read_b128 v[230:233], v184 offset:54272
	ds_read_b128 v[234:237], v184 offset:55296
	ds_read_b128 v[238:241], v184 offset:56320
	global_load_lds_dwordx4 v144, s[20:21]
	v_add_u32_e32 v144, s45, v144
	s_mov_b32 m0, s65
	s_nop 0
	global_load_lds_dwordx4 v144, s[20:21]
	v_add_u32_e32 v144, s51, v161
	s_mov_b32 m0, s68
	s_nop 0
	global_load_lds_dwordx4 v144, s[20:21]
	v_add_u32_e32 v144, s45, v144
	s_mov_b32 m0, s69
	s_nop 0
	global_load_lds_dwordx4 v144, s[20:21]
	v_add_u32_e32 v144, s50, v165
	s_mov_b32 m0, s66
	s_nop 0
	global_load_lds_dwordx4 v144, s[8:9]
	v_add_u32_e32 v144, s44, v144
	s_mov_b32 m0, s67
	s_nop 0
	global_load_lds_dwordx4 v144, s[8:9]
	s_waitcnt vmcnt(8)
	s_waitcnt lgkmcnt(0)
	s_setprio 1
	s_barrier
	s_waitcnt lgkmcnt(0)
	v_mfma_f32_16x16x32_bf16 v[62:65], v[140:143], v[204:207], v[62:65]
	v_mfma_f32_16x16x32_bf16 v[58:61], v[136:139], v[204:207], v[58:61]
	v_mfma_f32_16x16x32_bf16 v[46:49], v[140:143], v[218:221], v[46:49]
	v_mfma_f32_16x16x32_bf16 v[42:45], v[136:139], v[218:221], v[42:45]
	v_mfma_f32_16x16x32_bf16 v[30:33], v[140:143], v[226:229], v[30:33]
	v_mfma_f32_16x16x32_bf16 v[26:29], v[136:139], v[226:229], v[26:29]
	v_mfma_f32_16x16x32_bf16 v[14:17], v[140:143], v[234:237], v[14:17]
	v_mfma_f32_16x16x32_bf16 v[10:13], v[136:139], v[234:237], v[10:13]
	v_mfma_f32_16x16x32_bf16 v[62:65], v[132:135], v[214:217], v[62:65]
	v_mfma_f32_16x16x32_bf16 v[58:61], v[188:191], v[214:217], v[58:61]
	v_mfma_f32_16x16x32_bf16 v[46:49], v[132:135], v[222:225], v[46:49]
	v_mfma_f32_16x16x32_bf16 v[42:45], v[188:191], v[222:225], v[42:45]
	v_mfma_f32_16x16x32_bf16 v[30:33], v[132:135], v[230:233], v[30:33]
	v_mfma_f32_16x16x32_bf16 v[26:29], v[188:191], v[230:233], v[26:29]
	v_mfma_f32_16x16x32_bf16 v[14:17], v[132:135], v[238:241], v[14:17]
	v_mfma_f32_16x16x32_bf16 v[10:13], v[188:191], v[238:241], v[10:13]
	s_setprio 0
	s_setprio 1
	v_mfma_f32_16x16x32_bf16 v[54:57], v[154:157], v[204:207], v[54:57]
	v_mfma_f32_16x16x32_bf16 v[50:53], v[196:199], v[204:207], v[50:53]
	v_mfma_f32_16x16x32_bf16 v[38:41], v[154:157], v[218:221], v[38:41]
	v_mfma_f32_16x16x32_bf16 v[34:37], v[196:199], v[218:221], v[34:37]
	v_mfma_f32_16x16x32_bf16 v[22:25], v[154:157], v[226:229], v[22:25]
	v_mfma_f32_16x16x32_bf16 v[18:21], v[196:199], v[226:229], v[18:21]
	v_mfma_f32_16x16x32_bf16 v[6:9], v[154:157], v[234:237], v[6:9]
	v_mfma_f32_16x16x32_bf16 v[2:5], v[196:199], v[234:237], v[2:5]
	v_mfma_f32_16x16x32_bf16 v[54:57], v[192:195], v[214:217], v[54:57]
	v_mfma_f32_16x16x32_bf16 v[50:53], v[200:203], v[214:217], v[50:53]
	v_mfma_f32_16x16x32_bf16 v[38:41], v[192:195], v[222:225], v[38:41]
	v_mfma_f32_16x16x32_bf16 v[34:37], v[200:203], v[222:225], v[34:37]
	v_mfma_f32_16x16x32_bf16 v[22:25], v[192:195], v[230:233], v[22:25]
	v_mfma_f32_16x16x32_bf16 v[18:21], v[200:203], v[230:233], v[18:21]
	v_mfma_f32_16x16x32_bf16 v[6:9], v[192:195], v[238:241], v[6:9]
	v_mfma_f32_16x16x32_bf16 v[2:5], v[200:203], v[238:241], v[2:5]
	s_setprio 0
	s_barrier
	s_add_i32 s96, s96, 2
	s_addk_i32 s94, 0x100
	s_addk_i32 s95, 0x100
	s_cmp_ge_i32 s96, s62
	s_cbranch_scc1 .LBB0_1844

.LBB0_2047:
	ds_read_b128 v[138:141], v156
	ds_read_b128 v[142:145], v157
	ds_read_b128 v[168:171], v152
	ds_read_b128 v[172:175], v153
	ds_read_b128 v[176:179], v158
	ds_read_b128 v[180:183], v159
	ds_read_b128 v[184:187], v160
	ds_read_b128 v[188:191], v161
	s_add_i32 s49, s48, 2
	s_add_i32 s50, s73, s46
	s_cmp_eq_u32 s71, s48
	s_cselect_b32 s48, s47, s50
	s_cselect_b32 s51, s31, s30
	v_add_u32_e32 v133, s46, v132
	s_add_i32 m0, s52, 0xc000
	ds_read_b128 v[192:195], v131
	ds_read_b128 v[196:199], v131 offset:1024
	ds_read_b128 v[200:203], v131 offset:2048
	ds_read_b128 v[204:207], v131 offset:3072
	ds_read_b128 v[214:217], v131 offset:4096
	ds_read_b128 v[218:221], v131 offset:5120
	ds_read_b128 v[222:225], v131 offset:6144
	ds_read_b128 v[226:229], v131 offset:7168
	global_load_lds_dwordx4 v133, s[6:7]
	v_add_u32_e32 v133, s46, v130
	s_add_i32 m0, s52, 0xe000
	s_nop 0
	global_load_lds_dwordx4 v133, s[6:7]
	s_waitcnt vmcnt(8)
	s_waitcnt lgkmcnt(0)
	s_setprio 1
	s_barrier
	s_waitcnt lgkmcnt(0)
	v_mfma_f32_16x16x32_bf16 v[122:125], v[168:171], v[192:195], v[122:125]
	v_mfma_f32_16x16x32_bf16 v[126:129], v[142:145], v[192:195], v[126:129]
	v_mfma_f32_16x16x32_bf16 v[110:113], v[168:171], v[200:203], v[110:113]
	v_mfma_f32_16x16x32_bf16 v[106:109], v[142:145], v[200:203], v[106:109]
	v_mfma_f32_16x16x32_bf16 v[94:97], v[168:171], v[214:217], v[94:97]
	v_mfma_f32_16x16x32_bf16 v[90:93], v[142:145], v[214:217], v[90:93]
	v_mfma_f32_16x16x32_bf16 v[78:81], v[168:171], v[222:225], v[78:81]
	v_mfma_f32_16x16x32_bf16 v[74:77], v[142:145], v[222:225], v[74:77]
	v_mfma_f32_16x16x32_bf16 v[122:125], v[138:141], v[196:199], v[122:125]
	v_mfma_f32_16x16x32_bf16 v[126:129], v[176:179], v[196:199], v[126:129]
	v_mfma_f32_16x16x32_bf16 v[110:113], v[138:141], v[204:207], v[110:113]
	v_mfma_f32_16x16x32_bf16 v[106:109], v[176:179], v[204:207], v[106:109]
	v_mfma_f32_16x16x32_bf16 v[94:97], v[138:141], v[218:221], v[94:97]
	v_mfma_f32_16x16x32_bf16 v[90:93], v[176:179], v[218:221], v[90:93]
	v_mfma_f32_16x16x32_bf16 v[78:81], v[138:141], v[226:229], v[78:81]
	v_mfma_f32_16x16x32_bf16 v[74:77], v[176:179], v[226:229], v[74:77]
	s_setprio 0
	s_setprio 1
	v_mfma_f32_16x16x32_bf16 v[118:121], v[172:175], v[192:195], v[118:121]
	v_mfma_f32_16x16x32_bf16 v[114:117], v[184:187], v[192:195], v[114:117]
	v_mfma_f32_16x16x32_bf16 v[102:105], v[172:175], v[200:203], v[102:105]
	v_mfma_f32_16x16x32_bf16 v[98:101], v[184:187], v[200:203], v[98:101]
	v_mfma_f32_16x16x32_bf16 v[86:89], v[172:175], v[214:217], v[86:89]
	v_mfma_f32_16x16x32_bf16 v[82:85], v[184:187], v[214:217], v[82:85]
	v_mfma_f32_16x16x32_bf16 v[70:73], v[172:175], v[222:225], v[70:73]
	v_mfma_f32_16x16x32_bf16 v[66:69], v[184:187], v[222:225], v[66:69]
	v_mfma_f32_16x16x32_bf16 v[118:121], v[180:183], v[196:199], v[118:121]
	v_mfma_f32_16x16x32_bf16 v[114:117], v[188:191], v[196:199], v[114:117]
	v_mfma_f32_16x16x32_bf16 v[102:105], v[180:183], v[204:207], v[102:105]
	v_mfma_f32_16x16x32_bf16 v[98:101], v[188:191], v[204:207], v[98:101]
	v_mfma_f32_16x16x32_bf16 v[86:89], v[180:183], v[218:221], v[86:89]
	v_mfma_f32_16x16x32_bf16 v[82:85], v[188:191], v[218:221], v[82:85]
	v_mfma_f32_16x16x32_bf16 v[70:73], v[180:183], v[226:229], v[70:73]
	v_mfma_f32_16x16x32_bf16 v[66:69], v[188:191], v[226:229], v[66:69]
	s_setprio 0
	s_barrier
	s_mov_b32 m0, s53
	v_add_u32_e32 v133, s51, v146
	ds_read_b128 v[192:195], v131 offset:16384
	ds_read_b128 v[196:199], v131 offset:17408
	ds_read_b128 v[200:203], v131 offset:18432
	ds_read_b128 v[204:207], v131 offset:19456
	ds_read_b128 v[214:217], v131 offset:20480
	ds_read_b128 v[218:221], v131 offset:21504
	ds_read_b128 v[222:225], v131 offset:22528
	ds_read_b128 v[226:229], v131 offset:23552
	global_load_lds_dwordx4 v133, s[8:9]
	v_add_u32_e32 v133, s45, v133
	s_mov_b32 m0, s54
	s_nop 0
	global_load_lds_dwordx4 v133, s[8:9]
	v_add_u32_e32 v133, s51, v147
	s_mov_b32 m0, s55
	s_nop 0
	global_load_lds_dwordx4 v133, s[8:9]
	v_add_u32_e32 v133, s45, v133
	s_mov_b32 m0, s56
	s_nop 0
	global_load_lds_dwordx4 v133, s[8:9]
	v_add_u32_e32 v133, s48, v1
	s_mov_b32 m0, s52
	s_nop 0
	global_load_lds_dwordx4 v133, s[6:7]
	v_add_u32_e32 v133, s44, v133
	s_mov_b32 m0, s57
	s_nop 0
	global_load_lds_dwordx4 v133, s[6:7]
	s_waitcnt vmcnt(8)
	s_waitcnt lgkmcnt(0)
	s_setprio 1
	s_barrier
	s_waitcnt lgkmcnt(0)
	v_mfma_f32_16x16x32_bf16 v[62:65], v[168:171], v[192:195], v[62:65]
	v_mfma_f32_16x16x32_bf16 v[58:61], v[142:145], v[192:195], v[58:61]
	v_mfma_f32_16x16x32_bf16 v[46:49], v[168:171], v[200:203], v[46:49]
	v_mfma_f32_16x16x32_bf16 v[42:45], v[142:145], v[200:203], v[42:45]
	v_mfma_f32_16x16x32_bf16 v[30:33], v[168:171], v[214:217], v[30:33]
	v_mfma_f32_16x16x32_bf16 v[26:29], v[142:145], v[214:217], v[26:29]
	v_mfma_f32_16x16x32_bf16 v[14:17], v[168:171], v[222:225], v[14:17]
	v_mfma_f32_16x16x32_bf16 v[10:13], v[142:145], v[222:225], v[10:13]
	v_mfma_f32_16x16x32_bf16 v[62:65], v[138:141], v[196:199], v[62:65]
	v_mfma_f32_16x16x32_bf16 v[58:61], v[176:179], v[196:199], v[58:61]
	v_mfma_f32_16x16x32_bf16 v[46:49], v[138:141], v[204:207], v[46:49]
	v_mfma_f32_16x16x32_bf16 v[42:45], v[176:179], v[204:207], v[42:45]
	v_mfma_f32_16x16x32_bf16 v[30:33], v[138:141], v[218:221], v[30:33]
	v_mfma_f32_16x16x32_bf16 v[26:29], v[176:179], v[218:221], v[26:29]
	v_mfma_f32_16x16x32_bf16 v[14:17], v[138:141], v[226:229], v[14:17]
	v_mfma_f32_16x16x32_bf16 v[10:13], v[176:179], v[226:229], v[10:13]
	s_setprio 0
	s_setprio 1
	v_mfma_f32_16x16x32_bf16 v[54:57], v[172:175], v[192:195], v[54:57]
	v_mfma_f32_16x16x32_bf16 v[50:53], v[184:187], v[192:195], v[50:53]
	v_mfma_f32_16x16x32_bf16 v[38:41], v[172:175], v[200:203], v[38:41]
	v_mfma_f32_16x16x32_bf16 v[34:37], v[184:187], v[200:203], v[34:37]
	v_mfma_f32_16x16x32_bf16 v[22:25], v[172:175], v[214:217], v[22:25]
	v_mfma_f32_16x16x32_bf16 v[18:21], v[184:187], v[214:217], v[18:21]
	v_mfma_f32_16x16x32_bf16 v[6:9], v[172:175], v[222:225], v[6:9]
	v_mfma_f32_16x16x32_bf16 v[2:5], v[184:187], v[222:225], v[2:5]
	v_mfma_f32_16x16x32_bf16 v[54:57], v[180:183], v[196:199], v[54:57]
	v_mfma_f32_16x16x32_bf16 v[50:53], v[188:191], v[196:199], v[50:53]
	v_mfma_f32_16x16x32_bf16 v[38:41], v[180:183], v[204:207], v[38:41]
	v_mfma_f32_16x16x32_bf16 v[34:37], v[188:191], v[204:207], v[34:37]
	v_mfma_f32_16x16x32_bf16 v[22:25], v[180:183], v[218:221], v[22:25]
	v_mfma_f32_16x16x32_bf16 v[18:21], v[188:191], v[218:221], v[18:21]
	v_mfma_f32_16x16x32_bf16 v[6:9], v[180:183], v[226:229], v[6:9]
	v_mfma_f32_16x16x32_bf16 v[2:5], v[188:191], v[226:229], v[2:5]
	s_setprio 0
	s_barrier
	ds_read_b128 v[138:141], v162
	ds_read_b128 v[142:145], v163
	ds_read_b128 v[168:171], v154
	ds_read_b128 v[172:175], v155
	ds_read_b128 v[176:179], v164
	ds_read_b128 v[180:183], v165
	ds_read_b128 v[184:187], v166
	ds_read_b128 v[188:191], v167
	s_mov_b32 m0, s58
	v_add_u32_e32 v133, s48, v148
	ds_read_b128 v[192:195], v131 offset:32768
	ds_read_b128 v[196:199], v131 offset:33792
	ds_read_b128 v[200:203], v131 offset:34816
	ds_read_b128 v[204:207], v131 offset:35840
	ds_read_b128 v[214:217], v131 offset:36864
	ds_read_b128 v[218:221], v131 offset:37888
	ds_read_b128 v[222:225], v131 offset:38912
	ds_read_b128 v[226:229], v131 offset:39936
	global_load_lds_dwordx4 v133, s[6:7]
	v_add_u32_e32 v133, s44, v133
	s_mov_b32 m0, s59
	s_nop 0
	global_load_lds_dwordx4 v133, s[6:7]
	s_waitcnt vmcnt(8)
	s_waitcnt lgkmcnt(0)
	s_setprio 1
	s_barrier
	s_waitcnt lgkmcnt(0)
	v_mfma_f32_16x16x32_bf16 v[122:125], v[168:171], v[192:195], v[122:125]
	v_mfma_f32_16x16x32_bf16 v[126:129], v[142:145], v[192:195], v[126:129]
	v_mfma_f32_16x16x32_bf16 v[110:113], v[168:171], v[200:203], v[110:113]
	v_mfma_f32_16x16x32_bf16 v[106:109], v[142:145], v[200:203], v[106:109]
	v_mfma_f32_16x16x32_bf16 v[94:97], v[168:171], v[214:217], v[94:97]
	v_mfma_f32_16x16x32_bf16 v[90:93], v[142:145], v[214:217], v[90:93]
	v_mfma_f32_16x16x32_bf16 v[78:81], v[168:171], v[222:225], v[78:81]
	v_mfma_f32_16x16x32_bf16 v[74:77], v[142:145], v[222:225], v[74:77]
	v_mfma_f32_16x16x32_bf16 v[122:125], v[138:141], v[196:199], v[122:125]
	v_mfma_f32_16x16x32_bf16 v[126:129], v[176:179], v[196:199], v[126:129]
	v_mfma_f32_16x16x32_bf16 v[110:113], v[138:141], v[204:207], v[110:113]
	v_mfma_f32_16x16x32_bf16 v[106:109], v[176:179], v[204:207], v[106:109]
	v_mfma_f32_16x16x32_bf16 v[94:97], v[138:141], v[218:221], v[94:97]
	v_mfma_f32_16x16x32_bf16 v[90:93], v[176:179], v[218:221], v[90:93]
	v_mfma_f32_16x16x32_bf16 v[78:81], v[138:141], v[226:229], v[78:81]
	v_mfma_f32_16x16x32_bf16 v[74:77], v[176:179], v[226:229], v[74:77]
	s_setprio 0
	s_setprio 1
	v_mfma_f32_16x16x32_bf16 v[118:121], v[172:175], v[192:195], v[118:121]
	v_mfma_f32_16x16x32_bf16 v[114:117], v[184:187], v[192:195], v[114:117]
	v_mfma_f32_16x16x32_bf16 v[102:105], v[172:175], v[200:203], v[102:105]
	v_mfma_f32_16x16x32_bf16 v[98:101], v[184:187], v[200:203], v[98:101]
	v_mfma_f32_16x16x32_bf16 v[86:89], v[172:175], v[214:217], v[86:89]
	v_mfma_f32_16x16x32_bf16 v[82:85], v[184:187], v[214:217], v[82:85]
	v_mfma_f32_16x16x32_bf16 v[70:73], v[172:175], v[222:225], v[70:73]
	v_mfma_f32_16x16x32_bf16 v[66:69], v[184:187], v[222:225], v[66:69]
	v_mfma_f32_16x16x32_bf16 v[118:121], v[180:183], v[196:199], v[118:121]
	v_mfma_f32_16x16x32_bf16 v[114:117], v[188:191], v[196:199], v[114:117]
	v_mfma_f32_16x16x32_bf16 v[102:105], v[180:183], v[204:207], v[102:105]
	v_mfma_f32_16x16x32_bf16 v[98:101], v[188:191], v[204:207], v[98:101]
	v_mfma_f32_16x16x32_bf16 v[86:89], v[180:183], v[218:221], v[86:89]
	v_mfma_f32_16x16x32_bf16 v[82:85], v[188:191], v[218:221], v[82:85]
	v_mfma_f32_16x16x32_bf16 v[70:73], v[180:183], v[226:229], v[70:73]
	v_mfma_f32_16x16x32_bf16 v[66:69], v[188:191], v[226:229], v[66:69]
	s_setprio 0
	s_barrier
	s_addk_i32 s51, 0x80
	s_mov_b32 m0, s61
	v_add_u32_e32 v133, s51, v146
	ds_read_b128 v[192:195], v131 offset:49152
	ds_read_b128 v[196:199], v131 offset:50176
	ds_read_b128 v[200:203], v131 offset:51200
	ds_read_b128 v[204:207], v131 offset:52224
	ds_read_b128 v[214:217], v131 offset:53248
	ds_read_b128 v[218:221], v131 offset:54272
	ds_read_b128 v[222:225], v131 offset:55296
	ds_read_b128 v[226:229], v131 offset:56320
	global_load_lds_dwordx4 v133, s[8:9]
	v_add_u32_e32 v133, s45, v133
	s_mov_b32 m0, s62
	s_nop 0
	global_load_lds_dwordx4 v133, s[8:9]
	v_add_u32_e32 v133, s51, v147
	s_mov_b32 m0, s65
	s_nop 0
	global_load_lds_dwordx4 v133, s[8:9]
	v_add_u32_e32 v133, s45, v133
	s_mov_b32 m0, s66
	s_nop 0
	global_load_lds_dwordx4 v133, s[8:9]
	v_add_u32_e32 v133, s48, v149
	s_mov_b32 m0, s63
	s_nop 0
	global_load_lds_dwordx4 v133, s[6:7]
	v_add_u32_e32 v133, s44, v133
	s_mov_b32 m0, s64
	s_nop 0
	global_load_lds_dwordx4 v133, s[6:7]
	s_waitcnt vmcnt(8)
	s_waitcnt lgkmcnt(0)
	s_setprio 1
	s_barrier
	s_waitcnt lgkmcnt(0)
	v_mfma_f32_16x16x32_bf16 v[62:65], v[168:171], v[192:195], v[62:65]
	v_mfma_f32_16x16x32_bf16 v[58:61], v[142:145], v[192:195], v[58:61]
	v_mfma_f32_16x16x32_bf16 v[46:49], v[168:171], v[200:203], v[46:49]
	v_mfma_f32_16x16x32_bf16 v[42:45], v[142:145], v[200:203], v[42:45]
	v_mfma_f32_16x16x32_bf16 v[30:33], v[168:171], v[214:217], v[30:33]
	v_mfma_f32_16x16x32_bf16 v[26:29], v[142:145], v[214:217], v[26:29]
	v_mfma_f32_16x16x32_bf16 v[14:17], v[168:171], v[222:225], v[14:17]
	v_mfma_f32_16x16x32_bf16 v[10:13], v[142:145], v[222:225], v[10:13]
	v_mfma_f32_16x16x32_bf16 v[62:65], v[138:141], v[196:199], v[62:65]
	v_mfma_f32_16x16x32_bf16 v[58:61], v[176:179], v[196:199], v[58:61]
	v_mfma_f32_16x16x32_bf16 v[46:49], v[138:141], v[204:207], v[46:49]
	v_mfma_f32_16x16x32_bf16 v[42:45], v[176:179], v[204:207], v[42:45]
	v_mfma_f32_16x16x32_bf16 v[30:33], v[138:141], v[218:221], v[30:33]
	v_mfma_f32_16x16x32_bf16 v[26:29], v[176:179], v[218:221], v[26:29]
	v_mfma_f32_16x16x32_bf16 v[14:17], v[138:141], v[226:229], v[14:17]
	v_mfma_f32_16x16x32_bf16 v[10:13], v[176:179], v[226:229], v[10:13]
	s_setprio 0
	s_setprio 1
	v_mfma_f32_16x16x32_bf16 v[54:57], v[172:175], v[192:195], v[54:57]
	v_mfma_f32_16x16x32_bf16 v[50:53], v[184:187], v[192:195], v[50:53]
	v_mfma_f32_16x16x32_bf16 v[38:41], v[172:175], v[200:203], v[38:41]
	v_mfma_f32_16x16x32_bf16 v[34:37], v[184:187], v[200:203], v[34:37]
	v_mfma_f32_16x16x32_bf16 v[22:25], v[172:175], v[214:217], v[22:25]
	v_mfma_f32_16x16x32_bf16 v[18:21], v[184:187], v[214:217], v[18:21]
	v_mfma_f32_16x16x32_bf16 v[6:9], v[172:175], v[222:225], v[6:9]
	v_mfma_f32_16x16x32_bf16 v[2:5], v[184:187], v[222:225], v[2:5]
	v_mfma_f32_16x16x32_bf16 v[54:57], v[180:183], v[196:199], v[54:57]
	v_mfma_f32_16x16x32_bf16 v[50:53], v[188:191], v[196:199], v[50:53]
	v_mfma_f32_16x16x32_bf16 v[38:41], v[180:183], v[204:207], v[38:41]
	v_mfma_f32_16x16x32_bf16 v[34:37], v[188:191], v[204:207], v[34:37]
	v_mfma_f32_16x16x32_bf16 v[22:25], v[180:183], v[218:221], v[22:25]
	v_mfma_f32_16x16x32_bf16 v[18:21], v[188:191], v[218:221], v[18:21]
	v_mfma_f32_16x16x32_bf16 v[6:9], v[180:183], v[226:229], v[6:9]
	v_mfma_f32_16x16x32_bf16 v[2:5], v[188:191], v[226:229], v[2:5]
	s_setprio 0
	s_barrier
	s_addk_i32 s30, 0x100
	s_cmp_ge_i32 s49, s67
	s_mov_b32 s46, s50
	s_mov_b32 s48, s49
	s_cbranch_scc0 .LBB0_2047

.LBB0_2337:
	ds_read_b128 v[130:133], v194
	ds_read_b128 v[134:137], v195
	ds_read_b128 v[138:141], v190
	ds_read_b128 v[142:145], v191
	ds_read_b128 v[146:149], v196
	ds_read_b128 v[150:153], v197
	ds_read_b128 v[154:157], v198
	ds_read_b128 v[158:161], v199
	s_add_i32 s75, s50, 0x80
	s_cmp_eq_u32 s70, s88
	s_cselect_b32 s89, s51, s87
	s_cselect_b32 s75, s49, s75
	v_add_u32_e32 v178, s50, v207
	s_add_i32 m0, s53, 0xc000
	ds_read_b128 v[162:165], v208
	ds_read_b128 v[166:169], v208 offset:1024
	ds_read_b128 v[170:173], v208 offset:2048
	ds_read_b128 v[180:183], v208 offset:3072
	ds_read_b128 v[214:217], v208 offset:4096
	ds_read_b128 v[218:221], v208 offset:5120
	ds_read_b128 v[222:225], v208 offset:6144
	ds_read_b128 v[226:229], v208 offset:7168
	global_load_lds_dwordx4 v178, s[4:5]
	v_add_u32_e32 v178, s50, v206
	s_add_i32 m0, s53, 0xe000
	s_nop 0
	global_load_lds_dwordx4 v178, s[4:5]
	s_waitcnt vmcnt(8)
	s_waitcnt lgkmcnt(0)
	s_setprio 1
	s_barrier
	s_waitcnt lgkmcnt(0)
	v_mfma_f32_16x16x32_bf16 v[126:129], v[138:141], v[162:165], v[126:129]
	v_mfma_f32_16x16x32_bf16 v[122:125], v[134:137], v[162:165], v[122:125]
	v_mfma_f32_16x16x32_bf16 v[110:113], v[138:141], v[170:173], v[110:113]
	v_mfma_f32_16x16x32_bf16 v[106:109], v[134:137], v[170:173], v[106:109]
	v_mfma_f32_16x16x32_bf16 v[94:97], v[138:141], v[214:217], v[94:97]
	v_mfma_f32_16x16x32_bf16 v[90:93], v[134:137], v[214:217], v[90:93]
	v_mfma_f32_16x16x32_bf16 v[78:81], v[138:141], v[222:225], v[78:81]
	v_mfma_f32_16x16x32_bf16 v[74:77], v[134:137], v[222:225], v[74:77]
	v_mfma_f32_16x16x32_bf16 v[126:129], v[130:133], v[166:169], v[126:129]
	v_mfma_f32_16x16x32_bf16 v[122:125], v[146:149], v[166:169], v[122:125]
	v_mfma_f32_16x16x32_bf16 v[110:113], v[130:133], v[180:183], v[110:113]
	v_mfma_f32_16x16x32_bf16 v[106:109], v[146:149], v[180:183], v[106:109]
	v_mfma_f32_16x16x32_bf16 v[94:97], v[130:133], v[218:221], v[94:97]
	v_mfma_f32_16x16x32_bf16 v[90:93], v[146:149], v[218:221], v[90:93]
	v_mfma_f32_16x16x32_bf16 v[78:81], v[130:133], v[226:229], v[78:81]
	v_mfma_f32_16x16x32_bf16 v[74:77], v[146:149], v[226:229], v[74:77]
	s_setprio 0
	s_setprio 1
	v_mfma_f32_16x16x32_bf16 v[118:121], v[142:145], v[162:165], v[118:121]
	v_mfma_f32_16x16x32_bf16 v[114:117], v[154:157], v[162:165], v[114:117]
	v_mfma_f32_16x16x32_bf16 v[102:105], v[142:145], v[170:173], v[102:105]
	v_mfma_f32_16x16x32_bf16 v[98:101], v[154:157], v[170:173], v[98:101]
	v_mfma_f32_16x16x32_bf16 v[86:89], v[142:145], v[214:217], v[86:89]
	v_mfma_f32_16x16x32_bf16 v[82:85], v[154:157], v[214:217], v[82:85]
	v_mfma_f32_16x16x32_bf16 v[70:73], v[142:145], v[222:225], v[70:73]
	v_mfma_f32_16x16x32_bf16 v[66:69], v[154:157], v[222:225], v[66:69]
	v_mfma_f32_16x16x32_bf16 v[118:121], v[150:153], v[166:169], v[118:121]
	v_mfma_f32_16x16x32_bf16 v[114:117], v[158:161], v[166:169], v[114:117]
	v_mfma_f32_16x16x32_bf16 v[102:105], v[150:153], v[180:183], v[102:105]
	v_mfma_f32_16x16x32_bf16 v[98:101], v[158:161], v[180:183], v[98:101]
	v_mfma_f32_16x16x32_bf16 v[86:89], v[150:153], v[218:221], v[86:89]
	v_mfma_f32_16x16x32_bf16 v[82:85], v[158:161], v[218:221], v[82:85]
	v_mfma_f32_16x16x32_bf16 v[70:73], v[150:153], v[226:229], v[70:73]
	v_mfma_f32_16x16x32_bf16 v[66:69], v[158:161], v[226:229], v[66:69]
	s_setprio 0
	s_barrier
	s_mov_b32 m0, s54
	v_add_u32_e32 v178, s89, v184
	ds_read_b128 v[162:165], v208 offset:16384
	ds_read_b128 v[166:169], v208 offset:17408
	ds_read_b128 v[170:173], v208 offset:18432
	ds_read_b128 v[180:183], v208 offset:19456
	ds_read_b128 v[214:217], v208 offset:20480
	ds_read_b128 v[218:221], v208 offset:21504
	ds_read_b128 v[222:225], v208 offset:22528
	ds_read_b128 v[226:229], v208 offset:23552
	global_load_lds_dwordx4 v178, s[6:7]
	v_add_u32_e32 v178, s52, v178
	s_mov_b32 m0, s55
	s_nop 0
	global_load_lds_dwordx4 v178, s[6:7]
	v_add_u32_e32 v178, s89, v185
	s_mov_b32 m0, s56
	s_nop 0
	global_load_lds_dwordx4 v178, s[6:7]
	v_add_u32_e32 v178, s52, v178
	s_mov_b32 m0, s57
	s_nop 0
	global_load_lds_dwordx4 v178, s[6:7]
	v_add_u32_e32 v178, s75, v1
	s_mov_b32 m0, s53
	s_nop 0
	global_load_lds_dwordx4 v178, s[4:5]
	v_add_u32_e32 v178, s45, v178
	s_mov_b32 m0, s58
	s_nop 0
	global_load_lds_dwordx4 v178, s[4:5]
	s_waitcnt vmcnt(8)
	s_waitcnt lgkmcnt(0)
	s_setprio 1
	s_barrier
	s_waitcnt lgkmcnt(0)
	v_mfma_f32_16x16x32_bf16 v[62:65], v[138:141], v[162:165], v[62:65]
	v_mfma_f32_16x16x32_bf16 v[58:61], v[134:137], v[162:165], v[58:61]
	v_mfma_f32_16x16x32_bf16 v[46:49], v[138:141], v[170:173], v[46:49]
	v_mfma_f32_16x16x32_bf16 v[42:45], v[134:137], v[170:173], v[42:45]
	v_mfma_f32_16x16x32_bf16 v[30:33], v[138:141], v[214:217], v[30:33]
	v_mfma_f32_16x16x32_bf16 v[26:29], v[134:137], v[214:217], v[26:29]
	v_mfma_f32_16x16x32_bf16 v[14:17], v[138:141], v[222:225], v[14:17]
	v_mfma_f32_16x16x32_bf16 v[10:13], v[134:137], v[222:225], v[10:13]
	v_mfma_f32_16x16x32_bf16 v[62:65], v[130:133], v[166:169], v[62:65]
	v_mfma_f32_16x16x32_bf16 v[58:61], v[146:149], v[166:169], v[58:61]
	v_mfma_f32_16x16x32_bf16 v[46:49], v[130:133], v[180:183], v[46:49]
	v_mfma_f32_16x16x32_bf16 v[42:45], v[146:149], v[180:183], v[42:45]
	v_mfma_f32_16x16x32_bf16 v[30:33], v[130:133], v[218:221], v[30:33]
	v_mfma_f32_16x16x32_bf16 v[26:29], v[146:149], v[218:221], v[26:29]
	v_mfma_f32_16x16x32_bf16 v[14:17], v[130:133], v[226:229], v[14:17]
	v_mfma_f32_16x16x32_bf16 v[10:13], v[146:149], v[226:229], v[10:13]
	s_setprio 0
	s_setprio 1
	v_mfma_f32_16x16x32_bf16 v[54:57], v[142:145], v[162:165], v[54:57]
	v_mfma_f32_16x16x32_bf16 v[50:53], v[154:157], v[162:165], v[50:53]
	v_mfma_f32_16x16x32_bf16 v[38:41], v[142:145], v[170:173], v[38:41]
	v_mfma_f32_16x16x32_bf16 v[34:37], v[154:157], v[170:173], v[34:37]
	v_mfma_f32_16x16x32_bf16 v[22:25], v[142:145], v[214:217], v[22:25]
	v_mfma_f32_16x16x32_bf16 v[18:21], v[154:157], v[214:217], v[18:21]
	v_mfma_f32_16x16x32_bf16 v[6:9], v[142:145], v[222:225], v[6:9]
	v_mfma_f32_16x16x32_bf16 v[2:5], v[154:157], v[222:225], v[2:5]
	v_mfma_f32_16x16x32_bf16 v[54:57], v[150:153], v[166:169], v[54:57]
	v_mfma_f32_16x16x32_bf16 v[50:53], v[158:161], v[166:169], v[50:53]
	v_mfma_f32_16x16x32_bf16 v[38:41], v[150:153], v[180:183], v[38:41]
	v_mfma_f32_16x16x32_bf16 v[34:37], v[158:161], v[180:183], v[34:37]
	v_mfma_f32_16x16x32_bf16 v[22:25], v[150:153], v[218:221], v[22:25]
	v_mfma_f32_16x16x32_bf16 v[18:21], v[158:161], v[218:221], v[18:21]
	v_mfma_f32_16x16x32_bf16 v[6:9], v[150:153], v[226:229], v[6:9]
	v_mfma_f32_16x16x32_bf16 v[2:5], v[158:161], v[226:229], v[2:5]
	s_setprio 0
	s_barrier
	ds_read_b128 v[130:133], v200
	ds_read_b128 v[134:137], v201
	ds_read_b128 v[138:141], v192
	ds_read_b128 v[142:145], v193
	ds_read_b128 v[146:149], v202
	ds_read_b128 v[150:153], v203
	ds_read_b128 v[154:157], v204
	ds_read_b128 v[158:161], v205
	s_mov_b32 m0, s59
	v_add_u32_e32 v178, s75, v186
	ds_read_b128 v[162:165], v208 offset:32768
	ds_read_b128 v[166:169], v208 offset:33792
	ds_read_b128 v[170:173], v208 offset:34816
	ds_read_b128 v[180:183], v208 offset:35840
	ds_read_b128 v[214:217], v208 offset:36864
	ds_read_b128 v[218:221], v208 offset:37888
	ds_read_b128 v[222:225], v208 offset:38912
	ds_read_b128 v[226:229], v208 offset:39936
	global_load_lds_dwordx4 v178, s[4:5]
	v_add_u32_e32 v178, s45, v178
	s_mov_b32 m0, s60
	s_nop 0
	global_load_lds_dwordx4 v178, s[4:5]
	s_waitcnt vmcnt(8)
	s_waitcnt lgkmcnt(0)
	s_setprio 1
	s_barrier
	s_waitcnt lgkmcnt(0)
	v_mfma_f32_16x16x32_bf16 v[126:129], v[138:141], v[162:165], v[126:129]
	v_mfma_f32_16x16x32_bf16 v[122:125], v[134:137], v[162:165], v[122:125]
	v_mfma_f32_16x16x32_bf16 v[110:113], v[138:141], v[170:173], v[110:113]
	v_mfma_f32_16x16x32_bf16 v[106:109], v[134:137], v[170:173], v[106:109]
	v_mfma_f32_16x16x32_bf16 v[94:97], v[138:141], v[214:217], v[94:97]
	v_mfma_f32_16x16x32_bf16 v[90:93], v[134:137], v[214:217], v[90:93]
	v_mfma_f32_16x16x32_bf16 v[78:81], v[138:141], v[222:225], v[78:81]
	v_mfma_f32_16x16x32_bf16 v[74:77], v[134:137], v[222:225], v[74:77]
	v_mfma_f32_16x16x32_bf16 v[126:129], v[130:133], v[166:169], v[126:129]
	v_mfma_f32_16x16x32_bf16 v[122:125], v[146:149], v[166:169], v[122:125]
	v_mfma_f32_16x16x32_bf16 v[110:113], v[130:133], v[180:183], v[110:113]
	v_mfma_f32_16x16x32_bf16 v[106:109], v[146:149], v[180:183], v[106:109]
	v_mfma_f32_16x16x32_bf16 v[94:97], v[130:133], v[218:221], v[94:97]
	v_mfma_f32_16x16x32_bf16 v[90:93], v[146:149], v[218:221], v[90:93]
	v_mfma_f32_16x16x32_bf16 v[78:81], v[130:133], v[226:229], v[78:81]
	v_mfma_f32_16x16x32_bf16 v[74:77], v[146:149], v[226:229], v[74:77]
	s_setprio 0
	s_setprio 1
	v_mfma_f32_16x16x32_bf16 v[118:121], v[142:145], v[162:165], v[118:121]
	v_mfma_f32_16x16x32_bf16 v[114:117], v[154:157], v[162:165], v[114:117]
	v_mfma_f32_16x16x32_bf16 v[102:105], v[142:145], v[170:173], v[102:105]
	v_mfma_f32_16x16x32_bf16 v[98:101], v[154:157], v[170:173], v[98:101]
	v_mfma_f32_16x16x32_bf16 v[86:89], v[142:145], v[214:217], v[86:89]
	v_mfma_f32_16x16x32_bf16 v[82:85], v[154:157], v[214:217], v[82:85]
	v_mfma_f32_16x16x32_bf16 v[70:73], v[142:145], v[222:225], v[70:73]
	v_mfma_f32_16x16x32_bf16 v[66:69], v[154:157], v[222:225], v[66:69]
	v_mfma_f32_16x16x32_bf16 v[118:121], v[150:153], v[166:169], v[118:121]
	v_mfma_f32_16x16x32_bf16 v[114:117], v[158:161], v[166:169], v[114:117]
	v_mfma_f32_16x16x32_bf16 v[102:105], v[150:153], v[180:183], v[102:105]
	v_mfma_f32_16x16x32_bf16 v[98:101], v[158:161], v[180:183], v[98:101]
	v_mfma_f32_16x16x32_bf16 v[86:89], v[150:153], v[218:221], v[86:89]
	v_mfma_f32_16x16x32_bf16 v[82:85], v[158:161], v[218:221], v[82:85]
	v_mfma_f32_16x16x32_bf16 v[70:73], v[150:153], v[226:229], v[70:73]
	v_mfma_f32_16x16x32_bf16 v[66:69], v[158:161], v[226:229], v[66:69]
	s_setprio 0
	s_barrier
	s_addk_i32 s89, 0x80
	s_mov_b32 m0, s63
	v_add_u32_e32 v178, s89, v184
	ds_read_b128 v[162:165], v208 offset:49152
	ds_read_b128 v[166:169], v208 offset:50176
	ds_read_b128 v[170:173], v208 offset:51200
	ds_read_b128 v[180:183], v208 offset:52224
	ds_read_b128 v[214:217], v208 offset:53248
	ds_read_b128 v[218:221], v208 offset:54272
	ds_read_b128 v[222:225], v208 offset:55296
	ds_read_b128 v[226:229], v208 offset:56320
	global_load_lds_dwordx4 v178, s[6:7]
	v_add_u32_e32 v178, s52, v178
	s_mov_b32 m0, s64
	s_nop 0
	global_load_lds_dwordx4 v178, s[6:7]
	v_add_u32_e32 v178, s89, v185
	s_mov_b32 m0, s67
	s_nop 0
	global_load_lds_dwordx4 v178, s[6:7]
	v_add_u32_e32 v178, s52, v178
	s_mov_b32 m0, s68
	s_nop 0
	global_load_lds_dwordx4 v178, s[6:7]
	v_add_u32_e32 v178, s75, v189
	s_mov_b32 m0, s65
	s_nop 0
	global_load_lds_dwordx4 v178, s[4:5]
	v_add_u32_e32 v178, s45, v178
	s_mov_b32 m0, s66
	s_nop 0
	global_load_lds_dwordx4 v178, s[4:5]
	s_waitcnt vmcnt(8)
	s_waitcnt lgkmcnt(0)
	s_setprio 1
	s_barrier
	s_waitcnt lgkmcnt(0)
	v_mfma_f32_16x16x32_bf16 v[62:65], v[138:141], v[162:165], v[62:65]
	v_mfma_f32_16x16x32_bf16 v[58:61], v[134:137], v[162:165], v[58:61]
	v_mfma_f32_16x16x32_bf16 v[46:49], v[138:141], v[170:173], v[46:49]
	v_mfma_f32_16x16x32_bf16 v[42:45], v[134:137], v[170:173], v[42:45]
	v_mfma_f32_16x16x32_bf16 v[30:33], v[138:141], v[214:217], v[30:33]
	v_mfma_f32_16x16x32_bf16 v[26:29], v[134:137], v[214:217], v[26:29]
	v_mfma_f32_16x16x32_bf16 v[14:17], v[138:141], v[222:225], v[14:17]
	v_mfma_f32_16x16x32_bf16 v[10:13], v[134:137], v[222:225], v[10:13]
	v_mfma_f32_16x16x32_bf16 v[62:65], v[130:133], v[166:169], v[62:65]
	v_mfma_f32_16x16x32_bf16 v[58:61], v[146:149], v[166:169], v[58:61]
	v_mfma_f32_16x16x32_bf16 v[46:49], v[130:133], v[180:183], v[46:49]
	v_mfma_f32_16x16x32_bf16 v[42:45], v[146:149], v[180:183], v[42:45]
	v_mfma_f32_16x16x32_bf16 v[30:33], v[130:133], v[218:221], v[30:33]
	v_mfma_f32_16x16x32_bf16 v[26:29], v[146:149], v[218:221], v[26:29]
	v_mfma_f32_16x16x32_bf16 v[14:17], v[130:133], v[226:229], v[14:17]
	v_mfma_f32_16x16x32_bf16 v[10:13], v[146:149], v[226:229], v[10:13]
	s_setprio 0
	s_setprio 1
	v_mfma_f32_16x16x32_bf16 v[54:57], v[142:145], v[162:165], v[54:57]
	v_mfma_f32_16x16x32_bf16 v[50:53], v[154:157], v[162:165], v[50:53]
	v_mfma_f32_16x16x32_bf16 v[38:41], v[142:145], v[170:173], v[38:41]
	v_mfma_f32_16x16x32_bf16 v[34:37], v[154:157], v[170:173], v[34:37]
	v_mfma_f32_16x16x32_bf16 v[22:25], v[142:145], v[214:217], v[22:25]
	v_mfma_f32_16x16x32_bf16 v[18:21], v[154:157], v[214:217], v[18:21]
	v_mfma_f32_16x16x32_bf16 v[6:9], v[142:145], v[222:225], v[6:9]
	v_mfma_f32_16x16x32_bf16 v[2:5], v[154:157], v[222:225], v[2:5]
	v_mfma_f32_16x16x32_bf16 v[54:57], v[150:153], v[166:169], v[54:57]
	v_mfma_f32_16x16x32_bf16 v[50:53], v[158:161], v[166:169], v[50:53]
	v_mfma_f32_16x16x32_bf16 v[38:41], v[150:153], v[180:183], v[38:41]
	v_mfma_f32_16x16x32_bf16 v[34:37], v[158:161], v[180:183], v[34:37]
	v_mfma_f32_16x16x32_bf16 v[22:25], v[150:153], v[218:221], v[22:25]
	v_mfma_f32_16x16x32_bf16 v[18:21], v[158:161], v[218:221], v[18:21]
	v_mfma_f32_16x16x32_bf16 v[6:9], v[150:153], v[226:229], v[6:9]
	v_mfma_f32_16x16x32_bf16 v[2:5], v[158:161], v[226:229], v[2:5]
	s_setprio 0
	s_barrier
	s_add_i32 s88, s88, 2
	s_addk_i32 s50, 0x100
	s_addk_i32 s87, 0x100
	s_cmp_ge_i32 s88, s61
	s_cbranch_scc0 .LBB0_2337

.LBB0_2521:
	ds_read_b128 v[90:93], v160
	ds_read_b128 v[94:97], v161
	ds_read_b128 v[142:145], v156
	ds_read_b128 v[146:149], v157
	ds_read_b128 v[176:179], v162
	ds_read_b128 v[180:183], v163
	ds_read_b128 v[184:187], v164
	ds_read_b128 v[188:191], v165
	s_add_i32 s96, s56, 0x80
	s_cmp_eq_u32 s81, s74
	s_cselect_b32 vcc_lo, s55, s57
	s_cselect_b32 s96, s45, s96
	v_add_u32_e32 v175, s56, v173
	s_add_i32 m0, s60, 0xc000
	ds_read_b128 v[192:195], v174
	ds_read_b128 v[196:199], v174 offset:1024
	ds_read_b128 v[200:203], v174 offset:2048
	ds_read_b128 v[204:207], v174 offset:3072
	ds_read_b128 v[214:217], v174 offset:4096
	ds_read_b128 v[218:221], v174 offset:5120
	ds_read_b128 v[222:225], v174 offset:6144
	ds_read_b128 v[226:229], v174 offset:7168
	global_load_lds_dwordx4 v175, s[4:5]
	v_add_u32_e32 v175, s56, v172
	s_add_i32 m0, s60, 0xe000
	s_nop 0
	global_load_lds_dwordx4 v175, s[4:5]
	s_waitcnt vmcnt(8)
	s_waitcnt lgkmcnt(0)
	s_setprio 1
	s_barrier
	s_waitcnt lgkmcnt(0)
	v_mfma_f32_16x16x32_bf16 v[134:137], v[142:145], v[192:195], v[134:137]
	v_mfma_f32_16x16x32_bf16 v[130:133], v[94:97], v[192:195], v[130:133]
	v_mfma_f32_16x16x32_bf16 v[126:129], v[142:145], v[200:203], v[126:129]
	v_mfma_f32_16x16x32_bf16 v[122:125], v[94:97], v[200:203], v[122:125]
	v_mfma_f32_16x16x32_bf16 v[118:121], v[142:145], v[214:217], v[118:121]
	v_mfma_f32_16x16x32_bf16 v[114:117], v[94:97], v[214:217], v[114:117]
	v_mfma_f32_16x16x32_bf16 v[110:113], v[142:145], v[222:225], v[110:113]
	v_mfma_f32_16x16x32_bf16 v[106:109], v[94:97], v[222:225], v[106:109]
	v_mfma_f32_16x16x32_bf16 v[134:137], v[90:93], v[196:199], v[134:137]
	v_mfma_f32_16x16x32_bf16 v[130:133], v[176:179], v[196:199], v[130:133]
	v_mfma_f32_16x16x32_bf16 v[126:129], v[90:93], v[204:207], v[126:129]
	v_mfma_f32_16x16x32_bf16 v[122:125], v[176:179], v[204:207], v[122:125]
	v_mfma_f32_16x16x32_bf16 v[118:121], v[90:93], v[218:221], v[118:121]
	v_mfma_f32_16x16x32_bf16 v[114:117], v[176:179], v[218:221], v[114:117]
	v_mfma_f32_16x16x32_bf16 v[110:113], v[90:93], v[226:229], v[110:113]
	v_mfma_f32_16x16x32_bf16 v[106:109], v[176:179], v[226:229], v[106:109]
	s_setprio 0
	s_setprio 1
	v_mfma_f32_16x16x32_bf16 v[62:65], v[146:149], v[192:195], v[62:65]
	v_mfma_f32_16x16x32_bf16 v[58:61], v[184:187], v[192:195], v[58:61]
	v_mfma_f32_16x16x32_bf16 v[54:57], v[146:149], v[200:203], v[54:57]
	v_mfma_f32_16x16x32_bf16 v[50:53], v[184:187], v[200:203], v[50:53]
	v_mfma_f32_16x16x32_bf16 v[46:49], v[146:149], v[214:217], v[46:49]
	v_mfma_f32_16x16x32_bf16 v[42:45], v[184:187], v[214:217], v[42:45]
	v_mfma_f32_16x16x32_bf16 v[38:41], v[146:149], v[222:225], v[38:41]
	v_mfma_f32_16x16x32_bf16 v[34:37], v[184:187], v[222:225], v[34:37]
	v_mfma_f32_16x16x32_bf16 v[62:65], v[180:183], v[196:199], v[62:65]
	v_mfma_f32_16x16x32_bf16 v[58:61], v[188:191], v[196:199], v[58:61]
	v_mfma_f32_16x16x32_bf16 v[54:57], v[180:183], v[204:207], v[54:57]
	v_mfma_f32_16x16x32_bf16 v[50:53], v[188:191], v[204:207], v[50:53]
	v_mfma_f32_16x16x32_bf16 v[46:49], v[180:183], v[218:221], v[46:49]
	v_mfma_f32_16x16x32_bf16 v[42:45], v[188:191], v[218:221], v[42:45]
	v_mfma_f32_16x16x32_bf16 v[38:41], v[180:183], v[226:229], v[38:41]
	v_mfma_f32_16x16x32_bf16 v[34:37], v[188:191], v[226:229], v[34:37]
	s_setprio 0
	s_barrier
	s_mov_b32 m0, s61
	v_add_u32_e32 v175, vcc_lo, v150
	ds_read_b128 v[192:195], v174 offset:16384
	ds_read_b128 v[196:199], v174 offset:17408
	ds_read_b128 v[200:203], v174 offset:18432
	ds_read_b128 v[204:207], v174 offset:19456
	ds_read_b128 v[214:217], v174 offset:20480
	ds_read_b128 v[218:221], v174 offset:21504
	ds_read_b128 v[222:225], v174 offset:22528
	ds_read_b128 v[226:229], v174 offset:23552
	global_load_lds_dwordx4 v175, s[6:7]
	v_add_u32_e32 v175, s59, v175
	s_mov_b32 m0, s62
	s_nop 0
	global_load_lds_dwordx4 v175, s[6:7]
	v_add_u32_e32 v175, vcc_lo, v151
	s_mov_b32 m0, s63
	s_nop 0
	global_load_lds_dwordx4 v175, s[6:7]
	v_add_u32_e32 v175, s59, v175
	s_mov_b32 m0, s64
	s_nop 0
	global_load_lds_dwordx4 v175, s[6:7]
	v_add_u32_e32 v175, s96, v1
	s_mov_b32 m0, s60
	s_nop 0
	global_load_lds_dwordx4 v175, s[4:5]
	v_add_u32_e32 v175, s58, v175
	s_mov_b32 m0, s65
	s_nop 0
	global_load_lds_dwordx4 v175, s[4:5]
	s_waitcnt vmcnt(8)
	s_waitcnt lgkmcnt(0)
	s_setprio 1
	s_barrier
	s_waitcnt lgkmcnt(0)
	v_mfma_f32_16x16x32_bf16 v[102:105], v[142:145], v[192:195], v[102:105]
	v_mfma_f32_16x16x32_bf16 v[98:101], v[94:97], v[192:195], v[98:101]
	v_mfma_f32_16x16x32_bf16 v[86:89], v[142:145], v[200:203], v[86:89]
	v_mfma_f32_16x16x32_bf16 v[82:85], v[94:97], v[200:203], v[82:85]
	v_mfma_f32_16x16x32_bf16 v[78:81], v[142:145], v[214:217], v[78:81]
	v_mfma_f32_16x16x32_bf16 v[74:77], v[94:97], v[214:217], v[74:77]
	v_mfma_f32_16x16x32_bf16 v[70:73], v[142:145], v[222:225], v[70:73]
	v_mfma_f32_16x16x32_bf16 v[66:69], v[94:97], v[222:225], v[66:69]
	v_mfma_f32_16x16x32_bf16 v[102:105], v[90:93], v[196:199], v[102:105]
	v_mfma_f32_16x16x32_bf16 v[98:101], v[176:179], v[196:199], v[98:101]
	v_mfma_f32_16x16x32_bf16 v[86:89], v[90:93], v[204:207], v[86:89]
	v_mfma_f32_16x16x32_bf16 v[82:85], v[176:179], v[204:207], v[82:85]
	v_mfma_f32_16x16x32_bf16 v[78:81], v[90:93], v[218:221], v[78:81]
	v_mfma_f32_16x16x32_bf16 v[74:77], v[176:179], v[218:221], v[74:77]
	v_mfma_f32_16x16x32_bf16 v[70:73], v[90:93], v[226:229], v[70:73]
	v_mfma_f32_16x16x32_bf16 v[66:69], v[176:179], v[226:229], v[66:69]
	s_setprio 0
	s_setprio 1
	v_mfma_f32_16x16x32_bf16 v[30:33], v[146:149], v[192:195], v[30:33]
	v_mfma_f32_16x16x32_bf16 v[26:29], v[184:187], v[192:195], v[26:29]
	v_mfma_f32_16x16x32_bf16 v[22:25], v[146:149], v[200:203], v[22:25]
	v_mfma_f32_16x16x32_bf16 v[18:21], v[184:187], v[200:203], v[18:21]
	v_mfma_f32_16x16x32_bf16 v[14:17], v[146:149], v[214:217], v[14:17]
	v_mfma_f32_16x16x32_bf16 v[10:13], v[184:187], v[214:217], v[10:13]
	v_mfma_f32_16x16x32_bf16 v[6:9], v[146:149], v[222:225], v[6:9]
	v_mfma_f32_16x16x32_bf16 v[2:5], v[184:187], v[222:225], v[2:5]
	v_mfma_f32_16x16x32_bf16 v[30:33], v[180:183], v[196:199], v[30:33]
	v_mfma_f32_16x16x32_bf16 v[26:29], v[188:191], v[196:199], v[26:29]
	v_mfma_f32_16x16x32_bf16 v[22:25], v[180:183], v[204:207], v[22:25]
	v_mfma_f32_16x16x32_bf16 v[18:21], v[188:191], v[204:207], v[18:21]
	v_mfma_f32_16x16x32_bf16 v[14:17], v[180:183], v[218:221], v[14:17]
	v_mfma_f32_16x16x32_bf16 v[10:13], v[188:191], v[218:221], v[10:13]
	v_mfma_f32_16x16x32_bf16 v[6:9], v[180:183], v[226:229], v[6:9]
	v_mfma_f32_16x16x32_bf16 v[2:5], v[188:191], v[226:229], v[2:5]
	s_setprio 0
	s_barrier
	ds_read_b128 v[90:93], v166
	ds_read_b128 v[94:97], v167
	ds_read_b128 v[142:145], v158
	ds_read_b128 v[146:149], v159
	ds_read_b128 v[176:179], v168
	ds_read_b128 v[180:183], v169
	ds_read_b128 v[184:187], v170
	ds_read_b128 v[188:191], v171
	s_mov_b32 m0, s66
	v_add_u32_e32 v175, s96, v152
	ds_read_b128 v[192:195], v174 offset:32768
	ds_read_b128 v[196:199], v174 offset:33792
	ds_read_b128 v[200:203], v174 offset:34816
	ds_read_b128 v[204:207], v174 offset:35840
	ds_read_b128 v[214:217], v174 offset:36864
	ds_read_b128 v[218:221], v174 offset:37888
	ds_read_b128 v[222:225], v174 offset:38912
	ds_read_b128 v[226:229], v174 offset:39936
	global_load_lds_dwordx4 v175, s[4:5]
	v_add_u32_e32 v175, s58, v175
	s_mov_b32 m0, s67
	s_nop 0
	global_load_lds_dwordx4 v175, s[4:5]
	s_waitcnt vmcnt(8)
	s_waitcnt lgkmcnt(0)
	s_setprio 1
	s_barrier
	s_waitcnt lgkmcnt(0)
	v_mfma_f32_16x16x32_bf16 v[134:137], v[142:145], v[192:195], v[134:137]
	v_mfma_f32_16x16x32_bf16 v[130:133], v[94:97], v[192:195], v[130:133]
	v_mfma_f32_16x16x32_bf16 v[126:129], v[142:145], v[200:203], v[126:129]
	v_mfma_f32_16x16x32_bf16 v[122:125], v[94:97], v[200:203], v[122:125]
	v_mfma_f32_16x16x32_bf16 v[118:121], v[142:145], v[214:217], v[118:121]
	v_mfma_f32_16x16x32_bf16 v[114:117], v[94:97], v[214:217], v[114:117]
	v_mfma_f32_16x16x32_bf16 v[110:113], v[142:145], v[222:225], v[110:113]
	v_mfma_f32_16x16x32_bf16 v[106:109], v[94:97], v[222:225], v[106:109]
	v_mfma_f32_16x16x32_bf16 v[134:137], v[90:93], v[196:199], v[134:137]
	v_mfma_f32_16x16x32_bf16 v[130:133], v[176:179], v[196:199], v[130:133]
	v_mfma_f32_16x16x32_bf16 v[126:129], v[90:93], v[204:207], v[126:129]
	v_mfma_f32_16x16x32_bf16 v[122:125], v[176:179], v[204:207], v[122:125]
	v_mfma_f32_16x16x32_bf16 v[118:121], v[90:93], v[218:221], v[118:121]
	v_mfma_f32_16x16x32_bf16 v[114:117], v[176:179], v[218:221], v[114:117]
	v_mfma_f32_16x16x32_bf16 v[110:113], v[90:93], v[226:229], v[110:113]
	v_mfma_f32_16x16x32_bf16 v[106:109], v[176:179], v[226:229], v[106:109]
	s_setprio 0
	s_setprio 1
	v_mfma_f32_16x16x32_bf16 v[62:65], v[146:149], v[192:195], v[62:65]
	v_mfma_f32_16x16x32_bf16 v[58:61], v[184:187], v[192:195], v[58:61]
	v_mfma_f32_16x16x32_bf16 v[54:57], v[146:149], v[200:203], v[54:57]
	v_mfma_f32_16x16x32_bf16 v[50:53], v[184:187], v[200:203], v[50:53]
	v_mfma_f32_16x16x32_bf16 v[46:49], v[146:149], v[214:217], v[46:49]
	v_mfma_f32_16x16x32_bf16 v[42:45], v[184:187], v[214:217], v[42:45]
	v_mfma_f32_16x16x32_bf16 v[38:41], v[146:149], v[222:225], v[38:41]
	v_mfma_f32_16x16x32_bf16 v[34:37], v[184:187], v[222:225], v[34:37]
	v_mfma_f32_16x16x32_bf16 v[62:65], v[180:183], v[196:199], v[62:65]
	v_mfma_f32_16x16x32_bf16 v[58:61], v[188:191], v[196:199], v[58:61]
	v_mfma_f32_16x16x32_bf16 v[54:57], v[180:183], v[204:207], v[54:57]
	v_mfma_f32_16x16x32_bf16 v[50:53], v[188:191], v[204:207], v[50:53]
	v_mfma_f32_16x16x32_bf16 v[46:49], v[180:183], v[218:221], v[46:49]
	v_mfma_f32_16x16x32_bf16 v[42:45], v[188:191], v[218:221], v[42:45]
	v_mfma_f32_16x16x32_bf16 v[38:41], v[180:183], v[226:229], v[38:41]
	v_mfma_f32_16x16x32_bf16 v[34:37], v[188:191], v[226:229], v[34:37]
	s_setprio 0
	s_barrier
	s_addk_i32 vcc_lo, 0x80
	s_mov_b32 m0, s71
	v_add_u32_e32 v175, vcc_lo, v150
	ds_read_b128 v[192:195], v174 offset:49152
	ds_read_b128 v[196:199], v174 offset:50176
	ds_read_b128 v[200:203], v174 offset:51200
	ds_read_b128 v[204:207], v174 offset:52224
	ds_read_b128 v[214:217], v174 offset:53248
	ds_read_b128 v[218:221], v174 offset:54272
	ds_read_b128 v[222:225], v174 offset:55296
	ds_read_b128 v[226:229], v174 offset:56320
	global_load_lds_dwordx4 v175, s[6:7]
	v_add_u32_e32 v175, s59, v175
	s_mov_b32 m0, s72
	s_nop 0
	global_load_lds_dwordx4 v175, s[6:7]
	v_add_u32_e32 v175, vcc_lo, v151
	s_mov_b32 m0, s77
	s_nop 0
	global_load_lds_dwordx4 v175, s[6:7]
	v_add_u32_e32 v175, s59, v175
	s_mov_b32 m0, s78
	s_nop 0
	global_load_lds_dwordx4 v175, s[6:7]
	v_add_u32_e32 v175, s96, v155
	s_mov_b32 m0, s73
	s_nop 0
	global_load_lds_dwordx4 v175, s[4:5]
	v_add_u32_e32 v175, s58, v175
	s_mov_b32 m0, s76
	s_nop 0
	global_load_lds_dwordx4 v175, s[4:5]
	s_waitcnt vmcnt(8)
	s_waitcnt lgkmcnt(0)
	s_setprio 1
	s_barrier
	s_waitcnt lgkmcnt(0)
	v_mfma_f32_16x16x32_bf16 v[102:105], v[142:145], v[192:195], v[102:105]
	v_mfma_f32_16x16x32_bf16 v[98:101], v[94:97], v[192:195], v[98:101]
	v_mfma_f32_16x16x32_bf16 v[86:89], v[142:145], v[200:203], v[86:89]
	v_mfma_f32_16x16x32_bf16 v[82:85], v[94:97], v[200:203], v[82:85]
	v_mfma_f32_16x16x32_bf16 v[78:81], v[142:145], v[214:217], v[78:81]
	v_mfma_f32_16x16x32_bf16 v[74:77], v[94:97], v[214:217], v[74:77]
	v_mfma_f32_16x16x32_bf16 v[70:73], v[142:145], v[222:225], v[70:73]
	v_mfma_f32_16x16x32_bf16 v[66:69], v[94:97], v[222:225], v[66:69]
	v_mfma_f32_16x16x32_bf16 v[102:105], v[90:93], v[196:199], v[102:105]
	v_mfma_f32_16x16x32_bf16 v[98:101], v[176:179], v[196:199], v[98:101]
	v_mfma_f32_16x16x32_bf16 v[86:89], v[90:93], v[204:207], v[86:89]
	v_mfma_f32_16x16x32_bf16 v[82:85], v[176:179], v[204:207], v[82:85]
	v_mfma_f32_16x16x32_bf16 v[78:81], v[90:93], v[218:221], v[78:81]
	v_mfma_f32_16x16x32_bf16 v[74:77], v[176:179], v[218:221], v[74:77]
	v_mfma_f32_16x16x32_bf16 v[70:73], v[90:93], v[226:229], v[70:73]
	v_mfma_f32_16x16x32_bf16 v[66:69], v[176:179], v[226:229], v[66:69]
	s_setprio 0
	s_setprio 1
	v_mfma_f32_16x16x32_bf16 v[30:33], v[146:149], v[192:195], v[30:33]
	v_mfma_f32_16x16x32_bf16 v[26:29], v[184:187], v[192:195], v[26:29]
	v_mfma_f32_16x16x32_bf16 v[22:25], v[146:149], v[200:203], v[22:25]
	v_mfma_f32_16x16x32_bf16 v[18:21], v[184:187], v[200:203], v[18:21]
	v_mfma_f32_16x16x32_bf16 v[14:17], v[146:149], v[214:217], v[14:17]
	v_mfma_f32_16x16x32_bf16 v[10:13], v[184:187], v[214:217], v[10:13]
	v_mfma_f32_16x16x32_bf16 v[6:9], v[146:149], v[222:225], v[6:9]
	v_mfma_f32_16x16x32_bf16 v[2:5], v[184:187], v[222:225], v[2:5]
	v_mfma_f32_16x16x32_bf16 v[30:33], v[180:183], v[196:199], v[30:33]
	v_mfma_f32_16x16x32_bf16 v[26:29], v[188:191], v[196:199], v[26:29]
	v_mfma_f32_16x16x32_bf16 v[22:25], v[180:183], v[204:207], v[22:25]
	v_mfma_f32_16x16x32_bf16 v[18:21], v[188:191], v[204:207], v[18:21]
	v_mfma_f32_16x16x32_bf16 v[14:17], v[180:183], v[218:221], v[14:17]
	v_mfma_f32_16x16x32_bf16 v[10:13], v[188:191], v[218:221], v[10:13]
	v_mfma_f32_16x16x32_bf16 v[6:9], v[180:183], v[226:229], v[6:9]
	v_mfma_f32_16x16x32_bf16 v[2:5], v[188:191], v[226:229], v[2:5]
	s_setprio 0
	s_barrier
	s_add_i32 s74, s74, 2
	s_addk_i32 s56, 0x100
	s_addk_i32 s57, 0x100
	s_cmp_ge_i32 s74, s69
	s_cbranch_scc0 .LBB0_2521

.LBB0_2597:
	ds_read_b128 v[130:133], v206
	ds_read_b128 v[134:137], v207
	ds_read_b128 v[138:141], v202
	ds_read_b128 v[142:145], v203
	ds_read_b128 v[146:149], v208
	ds_read_b128 v[150:153], v209
	ds_read_b128 v[154:157], v211
	ds_read_b128 v[158:161], v213
	s_add_i32 s65, s60, 0x80
	s_cmp_eq_u32 s84, s64
	s_cselect_b32 s75, s61, s63
	s_cselect_b32 s65, s5, s65
	v_add_u32_e32 v194, s60, v221
	s_add_i32 m0, s45, 0xc000
	ds_read_b128 v[162:165], v222
	ds_read_b128 v[166:169], v222 offset:1024
	ds_read_b128 v[170:173], v222 offset:2048
	ds_read_b128 v[174:177], v222 offset:3072
	ds_read_b128 v[182:185], v222 offset:4096
	ds_read_b128 v[186:189], v222 offset:5120
	ds_read_b128 v[190:193], v222 offset:6144
	ds_read_b128 v[224:227], v222 offset:7168
	global_load_lds_dwordx4 v194, s[6:7]
	v_add_u32_e32 v194, s60, v220
	s_add_i32 m0, s45, 0xe000
	s_nop 0
	global_load_lds_dwordx4 v194, s[6:7]
	s_waitcnt vmcnt(8)
	s_waitcnt lgkmcnt(0)
	s_setprio 1
	s_barrier
	s_waitcnt lgkmcnt(0)
	v_mfma_f32_16x16x32_bf16 v[126:129], v[138:141], v[162:165], v[126:129]
	v_mfma_f32_16x16x32_bf16 v[122:125], v[134:137], v[162:165], v[122:125]
	v_mfma_f32_16x16x32_bf16 v[110:113], v[138:141], v[170:173], v[110:113]
	v_mfma_f32_16x16x32_bf16 v[106:109], v[134:137], v[170:173], v[106:109]
	v_mfma_f32_16x16x32_bf16 v[94:97], v[138:141], v[182:185], v[94:97]
	v_mfma_f32_16x16x32_bf16 v[90:93], v[134:137], v[182:185], v[90:93]
	v_mfma_f32_16x16x32_bf16 v[78:81], v[138:141], v[190:193], v[78:81]
	v_mfma_f32_16x16x32_bf16 v[74:77], v[134:137], v[190:193], v[74:77]
	v_mfma_f32_16x16x32_bf16 v[126:129], v[130:133], v[166:169], v[126:129]
	v_mfma_f32_16x16x32_bf16 v[122:125], v[146:149], v[166:169], v[122:125]
	v_mfma_f32_16x16x32_bf16 v[110:113], v[130:133], v[174:177], v[110:113]
	v_mfma_f32_16x16x32_bf16 v[106:109], v[146:149], v[174:177], v[106:109]
	v_mfma_f32_16x16x32_bf16 v[94:97], v[130:133], v[186:189], v[94:97]
	v_mfma_f32_16x16x32_bf16 v[90:93], v[146:149], v[186:189], v[90:93]
	v_mfma_f32_16x16x32_bf16 v[78:81], v[130:133], v[224:227], v[78:81]
	v_mfma_f32_16x16x32_bf16 v[74:77], v[146:149], v[224:227], v[74:77]
	s_setprio 0
	s_setprio 1
	v_mfma_f32_16x16x32_bf16 v[118:121], v[142:145], v[162:165], v[118:121]
	v_mfma_f32_16x16x32_bf16 v[114:117], v[154:157], v[162:165], v[114:117]
	v_mfma_f32_16x16x32_bf16 v[102:105], v[142:145], v[170:173], v[102:105]
	v_mfma_f32_16x16x32_bf16 v[98:101], v[154:157], v[170:173], v[98:101]
	v_mfma_f32_16x16x32_bf16 v[86:89], v[142:145], v[182:185], v[86:89]
	v_mfma_f32_16x16x32_bf16 v[82:85], v[154:157], v[182:185], v[82:85]
	v_mfma_f32_16x16x32_bf16 v[70:73], v[142:145], v[190:193], v[70:73]
	v_mfma_f32_16x16x32_bf16 v[66:69], v[154:157], v[190:193], v[66:69]
	v_mfma_f32_16x16x32_bf16 v[118:121], v[150:153], v[166:169], v[118:121]
	v_mfma_f32_16x16x32_bf16 v[114:117], v[158:161], v[166:169], v[114:117]
	v_mfma_f32_16x16x32_bf16 v[102:105], v[150:153], v[174:177], v[102:105]
	v_mfma_f32_16x16x32_bf16 v[98:101], v[158:161], v[174:177], v[98:101]
	v_mfma_f32_16x16x32_bf16 v[86:89], v[150:153], v[186:189], v[86:89]
	v_mfma_f32_16x16x32_bf16 v[82:85], v[158:161], v[186:189], v[82:85]
	v_mfma_f32_16x16x32_bf16 v[70:73], v[150:153], v[224:227], v[70:73]
	v_mfma_f32_16x16x32_bf16 v[66:69], v[158:161], v[224:227], v[66:69]
	s_setprio 0
	s_barrier
	s_mov_b32 m0, s66
	v_add_u32_e32 v194, s75, v196
	ds_read_b128 v[162:165], v222 offset:16384
	ds_read_b128 v[166:169], v222 offset:17408
	ds_read_b128 v[170:173], v222 offset:18432
	ds_read_b128 v[174:177], v222 offset:19456
	ds_read_b128 v[182:185], v222 offset:20480
	ds_read_b128 v[186:189], v222 offset:21504
	ds_read_b128 v[190:193], v222 offset:22528
	ds_read_b128 v[224:227], v222 offset:23552
	global_load_lds_dwordx4 v194, s[8:9]
	v_add_u32_e32 v194, s44, v194
	s_mov_b32 m0, s67
	s_nop 0
	global_load_lds_dwordx4 v194, s[8:9]
	v_add_u32_e32 v194, s75, v197
	s_mov_b32 m0, s68
	s_nop 0
	global_load_lds_dwordx4 v194, s[8:9]
	v_add_u32_e32 v194, s44, v194
	s_mov_b32 m0, s69
	s_nop 0
	global_load_lds_dwordx4 v194, s[8:9]
	v_add_u32_e32 v194, s65, v1
	s_mov_b32 m0, s45
	s_nop 0
	global_load_lds_dwordx4 v194, s[6:7]
	v_add_u32_e32 v194, s35, v194
	s_mov_b32 m0, s70
	s_nop 0
	global_load_lds_dwordx4 v194, s[6:7]
	s_waitcnt vmcnt(8)
	s_waitcnt lgkmcnt(0)
	s_setprio 1
	s_barrier
	s_waitcnt lgkmcnt(0)
	v_mfma_f32_16x16x32_bf16 v[62:65], v[138:141], v[162:165], v[62:65]
	v_mfma_f32_16x16x32_bf16 v[58:61], v[134:137], v[162:165], v[58:61]
	v_mfma_f32_16x16x32_bf16 v[46:49], v[138:141], v[170:173], v[46:49]
	v_mfma_f32_16x16x32_bf16 v[42:45], v[134:137], v[170:173], v[42:45]
	v_mfma_f32_16x16x32_bf16 v[30:33], v[138:141], v[182:185], v[30:33]
	v_mfma_f32_16x16x32_bf16 v[26:29], v[134:137], v[182:185], v[26:29]
	v_mfma_f32_16x16x32_bf16 v[14:17], v[138:141], v[190:193], v[14:17]
	v_mfma_f32_16x16x32_bf16 v[10:13], v[134:137], v[190:193], v[10:13]
	v_mfma_f32_16x16x32_bf16 v[62:65], v[130:133], v[166:169], v[62:65]
	v_mfma_f32_16x16x32_bf16 v[58:61], v[146:149], v[166:169], v[58:61]
	v_mfma_f32_16x16x32_bf16 v[46:49], v[130:133], v[174:177], v[46:49]
	v_mfma_f32_16x16x32_bf16 v[42:45], v[146:149], v[174:177], v[42:45]
	v_mfma_f32_16x16x32_bf16 v[30:33], v[130:133], v[186:189], v[30:33]
	v_mfma_f32_16x16x32_bf16 v[26:29], v[146:149], v[186:189], v[26:29]
	v_mfma_f32_16x16x32_bf16 v[14:17], v[130:133], v[224:227], v[14:17]
	v_mfma_f32_16x16x32_bf16 v[10:13], v[146:149], v[224:227], v[10:13]
	s_setprio 0
	s_setprio 1
	v_mfma_f32_16x16x32_bf16 v[54:57], v[142:145], v[162:165], v[54:57]
	v_mfma_f32_16x16x32_bf16 v[50:53], v[154:157], v[162:165], v[50:53]
	v_mfma_f32_16x16x32_bf16 v[38:41], v[142:145], v[170:173], v[38:41]
	v_mfma_f32_16x16x32_bf16 v[34:37], v[154:157], v[170:173], v[34:37]
	v_mfma_f32_16x16x32_bf16 v[22:25], v[142:145], v[182:185], v[22:25]
	v_mfma_f32_16x16x32_bf16 v[18:21], v[154:157], v[182:185], v[18:21]
	v_mfma_f32_16x16x32_bf16 v[6:9], v[142:145], v[190:193], v[6:9]
	v_mfma_f32_16x16x32_bf16 v[2:5], v[154:157], v[190:193], v[2:5]
	v_mfma_f32_16x16x32_bf16 v[54:57], v[150:153], v[166:169], v[54:57]
	v_mfma_f32_16x16x32_bf16 v[50:53], v[158:161], v[166:169], v[50:53]
	v_mfma_f32_16x16x32_bf16 v[38:41], v[150:153], v[174:177], v[38:41]
	v_mfma_f32_16x16x32_bf16 v[34:37], v[158:161], v[174:177], v[34:37]
	v_mfma_f32_16x16x32_bf16 v[22:25], v[150:153], v[186:189], v[22:25]
	v_mfma_f32_16x16x32_bf16 v[18:21], v[158:161], v[186:189], v[18:21]
	v_mfma_f32_16x16x32_bf16 v[6:9], v[150:153], v[224:227], v[6:9]
	v_mfma_f32_16x16x32_bf16 v[2:5], v[158:161], v[224:227], v[2:5]
	s_setprio 0
	s_barrier
	ds_read_b128 v[130:133], v214
	ds_read_b128 v[134:137], v215
	ds_read_b128 v[138:141], v204
	ds_read_b128 v[142:145], v205
	ds_read_b128 v[146:149], v216
	ds_read_b128 v[150:153], v217
	ds_read_b128 v[154:157], v218
	ds_read_b128 v[158:161], v219
	s_mov_b32 m0, s71
	v_add_u32_e32 v194, s65, v198
	ds_read_b128 v[162:165], v222 offset:32768
	ds_read_b128 v[166:169], v222 offset:33792
	ds_read_b128 v[170:173], v222 offset:34816
	ds_read_b128 v[174:177], v222 offset:35840
	ds_read_b128 v[182:185], v222 offset:36864
	ds_read_b128 v[186:189], v222 offset:37888
	ds_read_b128 v[190:193], v222 offset:38912
	ds_read_b128 v[224:227], v222 offset:39936
	global_load_lds_dwordx4 v194, s[6:7]
	v_add_u32_e32 v194, s35, v194
	s_mov_b32 m0, s72
	s_nop 0
	global_load_lds_dwordx4 v194, s[6:7]
	s_waitcnt vmcnt(8)
	s_waitcnt lgkmcnt(0)
	s_setprio 1
	s_barrier
	s_waitcnt lgkmcnt(0)
	v_mfma_f32_16x16x32_bf16 v[126:129], v[138:141], v[162:165], v[126:129]
	v_mfma_f32_16x16x32_bf16 v[122:125], v[134:137], v[162:165], v[122:125]
	v_mfma_f32_16x16x32_bf16 v[110:113], v[138:141], v[170:173], v[110:113]
	v_mfma_f32_16x16x32_bf16 v[106:109], v[134:137], v[170:173], v[106:109]
	v_mfma_f32_16x16x32_bf16 v[94:97], v[138:141], v[182:185], v[94:97]
	v_mfma_f32_16x16x32_bf16 v[90:93], v[134:137], v[182:185], v[90:93]
	v_mfma_f32_16x16x32_bf16 v[78:81], v[138:141], v[190:193], v[78:81]
	v_mfma_f32_16x16x32_bf16 v[74:77], v[134:137], v[190:193], v[74:77]
	v_mfma_f32_16x16x32_bf16 v[126:129], v[130:133], v[166:169], v[126:129]
	v_mfma_f32_16x16x32_bf16 v[122:125], v[146:149], v[166:169], v[122:125]
	v_mfma_f32_16x16x32_bf16 v[110:113], v[130:133], v[174:177], v[110:113]
	v_mfma_f32_16x16x32_bf16 v[106:109], v[146:149], v[174:177], v[106:109]
	v_mfma_f32_16x16x32_bf16 v[94:97], v[130:133], v[186:189], v[94:97]
	v_mfma_f32_16x16x32_bf16 v[90:93], v[146:149], v[186:189], v[90:93]
	v_mfma_f32_16x16x32_bf16 v[78:81], v[130:133], v[224:227], v[78:81]
	v_mfma_f32_16x16x32_bf16 v[74:77], v[146:149], v[224:227], v[74:77]
	s_setprio 0
	s_setprio 1
	v_mfma_f32_16x16x32_bf16 v[118:121], v[142:145], v[162:165], v[118:121]
	v_mfma_f32_16x16x32_bf16 v[114:117], v[154:157], v[162:165], v[114:117]
	v_mfma_f32_16x16x32_bf16 v[102:105], v[142:145], v[170:173], v[102:105]
	v_mfma_f32_16x16x32_bf16 v[98:101], v[154:157], v[170:173], v[98:101]
	v_mfma_f32_16x16x32_bf16 v[86:89], v[142:145], v[182:185], v[86:89]
	v_mfma_f32_16x16x32_bf16 v[82:85], v[154:157], v[182:185], v[82:85]
	v_mfma_f32_16x16x32_bf16 v[70:73], v[142:145], v[190:193], v[70:73]
	v_mfma_f32_16x16x32_bf16 v[66:69], v[154:157], v[190:193], v[66:69]
	v_mfma_f32_16x16x32_bf16 v[118:121], v[150:153], v[166:169], v[118:121]
	v_mfma_f32_16x16x32_bf16 v[114:117], v[158:161], v[166:169], v[114:117]
	v_mfma_f32_16x16x32_bf16 v[102:105], v[150:153], v[174:177], v[102:105]
	v_mfma_f32_16x16x32_bf16 v[98:101], v[158:161], v[174:177], v[98:101]
	v_mfma_f32_16x16x32_bf16 v[86:89], v[150:153], v[186:189], v[86:89]
	v_mfma_f32_16x16x32_bf16 v[82:85], v[158:161], v[186:189], v[82:85]
	v_mfma_f32_16x16x32_bf16 v[70:73], v[150:153], v[224:227], v[70:73]
	v_mfma_f32_16x16x32_bf16 v[66:69], v[158:161], v[224:227], v[66:69]
	s_setprio 0
	s_barrier
	s_addk_i32 s75, 0x80
	s_mov_b32 m0, s77
	v_add_u32_e32 v194, s75, v196
	ds_read_b128 v[162:165], v222 offset:49152
	ds_read_b128 v[166:169], v222 offset:50176
	ds_read_b128 v[170:173], v222 offset:51200
	ds_read_b128 v[174:177], v222 offset:52224
	ds_read_b128 v[182:185], v222 offset:53248
	ds_read_b128 v[186:189], v222 offset:54272
	ds_read_b128 v[190:193], v222 offset:55296
	ds_read_b128 v[224:227], v222 offset:56320
	global_load_lds_dwordx4 v194, s[8:9]
	v_add_u32_e32 v194, s44, v194
	s_mov_b32 m0, s78
	s_nop 0
	global_load_lds_dwordx4 v194, s[8:9]
	v_add_u32_e32 v194, s75, v197
	s_mov_b32 m0, s81
	s_nop 0
	global_load_lds_dwordx4 v194, s[8:9]
	v_add_u32_e32 v194, s44, v194
	s_mov_b32 m0, s82
	s_nop 0
	global_load_lds_dwordx4 v194, s[8:9]
	v_add_u32_e32 v194, s65, v201
	s_mov_b32 m0, s79
	s_nop 0
	global_load_lds_dwordx4 v194, s[6:7]
	v_add_u32_e32 v194, s35, v194
	s_mov_b32 m0, s80
	s_nop 0
	global_load_lds_dwordx4 v194, s[6:7]
	s_waitcnt vmcnt(8)
	s_waitcnt lgkmcnt(0)
	s_setprio 1
	s_barrier
	s_waitcnt lgkmcnt(0)
	v_mfma_f32_16x16x32_bf16 v[62:65], v[138:141], v[162:165], v[62:65]
	v_mfma_f32_16x16x32_bf16 v[58:61], v[134:137], v[162:165], v[58:61]
	v_mfma_f32_16x16x32_bf16 v[46:49], v[138:141], v[170:173], v[46:49]
	v_mfma_f32_16x16x32_bf16 v[42:45], v[134:137], v[170:173], v[42:45]
	v_mfma_f32_16x16x32_bf16 v[30:33], v[138:141], v[182:185], v[30:33]
	v_mfma_f32_16x16x32_bf16 v[26:29], v[134:137], v[182:185], v[26:29]
	v_mfma_f32_16x16x32_bf16 v[14:17], v[138:141], v[190:193], v[14:17]
	v_mfma_f32_16x16x32_bf16 v[10:13], v[134:137], v[190:193], v[10:13]
	v_mfma_f32_16x16x32_bf16 v[62:65], v[130:133], v[166:169], v[62:65]
	v_mfma_f32_16x16x32_bf16 v[58:61], v[146:149], v[166:169], v[58:61]
	v_mfma_f32_16x16x32_bf16 v[46:49], v[130:133], v[174:177], v[46:49]
	v_mfma_f32_16x16x32_bf16 v[42:45], v[146:149], v[174:177], v[42:45]
	v_mfma_f32_16x16x32_bf16 v[30:33], v[130:133], v[186:189], v[30:33]
	v_mfma_f32_16x16x32_bf16 v[26:29], v[146:149], v[186:189], v[26:29]
	v_mfma_f32_16x16x32_bf16 v[14:17], v[130:133], v[224:227], v[14:17]
	v_mfma_f32_16x16x32_bf16 v[10:13], v[146:149], v[224:227], v[10:13]
	s_setprio 0
	s_setprio 1
	v_mfma_f32_16x16x32_bf16 v[54:57], v[142:145], v[162:165], v[54:57]
	v_mfma_f32_16x16x32_bf16 v[50:53], v[154:157], v[162:165], v[50:53]
	v_mfma_f32_16x16x32_bf16 v[38:41], v[142:145], v[170:173], v[38:41]
	v_mfma_f32_16x16x32_bf16 v[34:37], v[154:157], v[170:173], v[34:37]
	v_mfma_f32_16x16x32_bf16 v[22:25], v[142:145], v[182:185], v[22:25]
	v_mfma_f32_16x16x32_bf16 v[18:21], v[154:157], v[182:185], v[18:21]
	v_mfma_f32_16x16x32_bf16 v[6:9], v[142:145], v[190:193], v[6:9]
	v_mfma_f32_16x16x32_bf16 v[2:5], v[154:157], v[190:193], v[2:5]
	v_mfma_f32_16x16x32_bf16 v[54:57], v[150:153], v[166:169], v[54:57]
	v_mfma_f32_16x16x32_bf16 v[50:53], v[158:161], v[166:169], v[50:53]
	v_mfma_f32_16x16x32_bf16 v[38:41], v[150:153], v[174:177], v[38:41]
	v_mfma_f32_16x16x32_bf16 v[34:37], v[158:161], v[174:177], v[34:37]
	v_mfma_f32_16x16x32_bf16 v[22:25], v[150:153], v[186:189], v[22:25]
	v_mfma_f32_16x16x32_bf16 v[18:21], v[158:161], v[186:189], v[18:21]
	v_mfma_f32_16x16x32_bf16 v[6:9], v[150:153], v[224:227], v[6:9]
	v_mfma_f32_16x16x32_bf16 v[2:5], v[158:161], v[224:227], v[2:5]
	s_setprio 0
	s_barrier
	s_add_i32 s64, s64, 2
	s_addk_i32 s60, 0x100
	s_addk_i32 s63, 0x100
	s_cmp_ge_i32 s64, s74
	s_cbranch_scc0 .LBB0_2597

.LBB0_2600:
	s_min_i32 s64, s4, 0x80
	s_lshr_b32 s64, s64, 5
	s_mulk_i32 s64, 0x3000
	s_ashr_i32 s65, s64, 31
	v_mov_b32_e32 v130, v200
	v_mov_b32_e32 v146, v199
	s_mov_b32 s63, s38
	s_mov_b32 s60, s36
	s_mov_b32 s75, s39
	s_mov_b32 s61, s37
	s_ashr_i32 s5, s4, 31
	s_lshl_b64 s[64:65], s[64:65], 2
	s_add_u32 s64, s63, s64
	s_addc_u32 s65, s75, s65
	s_lshl_b32 s62, s62, 8
	s_or_b32 s62, s62, s83
	v_lshl_add_u32 v182, v130, 3, s62
	v_ashrrev_i32_e32 v183, 31, v182
	v_lshl_add_u64 v[130:131], v[182:183], 2, s[64:65]
	v_lshl_add_u64 v[132:133], v[130:131], 0, s[16:17]
	v_add_co_u32_e32 v130, vcc, s88, v130
	s_add_u32 s62, s63, 0x800000
	s_nop 0
	v_addc_co_u32_e32 v131, vcc, 0, v131, vcc
	flat_load_dwordx4 v[138:141], v[132:133] offset:16
	flat_load_dwordx4 v[134:137], v[132:133] offset:512
	flat_load_dwordx4 v[142:145], v[130:131]
	s_nop 0
	flat_load_dwordx4 v[130:133], v[132:133] offset:528
	s_addc_u32 s63, s75, 0
	s_lshl_b64 s[4:5], s[4:5], 8
	s_add_u32 s4, s4, s76
	v_ashrrev_i32_e32 v147, 31, v146
	s_addc_u32 s5, s5, s85
	v_lshl_add_u64 v[184:185], s[4:5], 0, v[146:147]
	v_lshlrev_b64 v[146:147], 13, v[184:185]
	v_cmp_lt_i64_e64 s[4:5], s[18:19], v[184:185]
	v_lshl_add_u64 v[190:191], s[62:63], 0, v[146:147]
	s_and_saveexec_b64 s[64:65], s[4:5]
	s_xor_b64 s[64:65], exec, s[64:65]
	v_lshl_add_u64 v[146:147], v[190:191], 0, s[20:21]
	s_or_saveexec_b64 s[64:65], s[64:65]
	v_bfe_u32 v226, v184, 7, 6
	v_and_b32_e32 v193, 0x7ffff, v185
	v_and_b32_e32 v227, 0xffffe000, v184
	v_lshlrev_b32_e32 v228, 6, v184
	s_xor_b64 exec, exec, s[64:65]
	v_and_b32_e32 v146, 0x1fc0, v228
	v_or3_b32 v192, v227, v146, v226
	v_lshlrev_b64 v[146:147], 13, v[192:193]
	v_lshl_add_u64 v[146:147], s[60:61], 0, v[146:147]
	s_or_b64 exec, exec, s[64:65]
	v_lshl_add_u64 v[146:147], v[182:183], 2, v[146:147]
	flat_load_dwordx4 v[174:177], v[146:147] nt
	flat_load_dwordx4 v[170:173], v[146:147] offset:16 nt
	flat_load_dwordx4 v[166:169], v[146:147] offset:512 nt
	flat_load_dwordx4 v[162:165], v[146:147] offset:528 nt
	v_lshl_add_u64 v[148:149], v[184:185], 0, 16
	v_lshlrev_b64 v[146:147], 13, v[148:149]
	v_cmp_lt_i64_e32 vcc, s[22:23], v[184:185]
	v_lshl_add_u64 v[188:189], s[62:63], 0, v[146:147]
	s_and_saveexec_b64 s[64:65], vcc
	s_xor_b64 s[64:65], exec, s[64:65]
	v_lshl_add_u64 v[146:147], v[188:189], 0, s[20:21]
	s_or_saveexec_b64 s[64:65], s[64:65]
	v_bfe_u32 v223, v148, 7, 6
	v_and_b32_e32 v187, 0x7ffff, v149
	v_and_b32_e32 v224, 0xffffe000, v148
	v_lshlrev_b32_e32 v225, 6, v148
	s_xor_b64 exec, exec, s[64:65]
	v_and_b32_e32 v146, 0x1fc0, v225
	v_or3_b32 v186, v224, v146, v223
	v_lshlrev_b64 v[146:147], 13, v[186:187]
	v_lshl_add_u64 v[146:147], s[60:61], 0, v[146:147]
	s_or_b64 exec, exec, s[64:65]
	v_lshl_add_u64 v[146:147], v[182:183], 2, v[146:147]
	flat_load_dwordx4 v[158:161], v[146:147] nt
	flat_load_dwordx4 v[154:157], v[146:147] offset:16 nt
	flat_load_dwordx4 v[150:153], v[146:147] offset:512 nt
	s_nop 0
	flat_load_dwordx4 v[146:149], v[146:147] offset:528 nt
	s_and_saveexec_b64 s[64:65], s[4:5]
	s_xor_b64 s[4:5], exec, s[64:65]
	v_lshl_add_u64 v[194:195], v[190:191], 0, s[20:21]
	s_andn2_saveexec_b64 s[4:5], s[4:5]
	v_and_b32_e32 v186, 0x1fc0, v228
	v_or3_b32 v192, v227, v186, v226
	v_lshlrev_b64 v[190:191], 13, v[192:193]
	v_lshl_add_u64 v[194:195], s[60:61], 0, v[190:191]
	s_or_b64 exec, exec, s[4:5]
	s_waitcnt vmcnt(0) lgkmcnt(0)
	v_pk_fma_f32 v[128:129], v[128:129], v[144:145], v[176:177]
	v_pk_fma_f32 v[126:127], v[126:127], v[142:143], v[174:175]
	v_pk_fma_f32 v[122:123], v[122:123], v[138:139], v[170:171]
	v_lshl_add_u64 v[170:171], v[182:183], 2, v[194:195]
	v_pk_fma_f32 v[120:121], v[120:121], v[136:137], v[168:169]
	v_pk_fma_f32 v[118:119], v[118:119], v[134:135], v[166:167]
	v_pk_fma_f32 v[116:117], v[116:117], v[132:133], v[164:165]
	v_pk_fma_f32 v[124:125], v[124:125], v[140:141], v[172:173]
	flat_store_dwordx4 v[170:171], v[126:129] nt
	flat_store_dwordx4 v[170:171], v[122:125] offset:16 nt
	v_pk_fma_f32 v[114:115], v[114:115], v[130:131], v[162:163]
	flat_store_dwordx4 v[170:171], v[118:121] offset:512 nt
	flat_store_dwordx4 v[170:171], v[114:117] offset:528 nt
	v_cmp_lt_i64_e64 s[4:5], s[24:25], v[184:185]
	s_nop 0
	v_lshl_add_u64 v[116:117], v[184:185], 0, 32
	v_lshlrev_b64 v[114:115], 13, v[116:117]
	v_lshl_add_u64 v[164:165], s[62:63], 0, v[114:115]
	s_and_saveexec_b64 s[64:65], s[4:5]
	s_xor_b64 s[64:65], exec, s[64:65]
	v_lshl_add_u64 v[114:115], v[164:165], 0, s[20:21]
	s_or_saveexec_b64 s[64:65], s[64:65]
	v_bfe_u32 v168, v116, 7, 6
	v_and_b32_e32 v163, 0x7ffff, v117
	v_and_b32_e32 v169, 0xffffe000, v116
	v_lshlrev_b32_e32 v170, 6, v116
	s_xor_b64 exec, exec, s[64:65]
	v_and_b32_e32 v114, 0x1fc0, v170
	v_or3_b32 v162, v169, v114, v168
	v_lshlrev_b64 v[114:115], 13, v[162:163]
	v_lshl_add_u64 v[114:115], s[60:61], 0, v[114:115]
	s_or_b64 exec, exec, s[64:65]
	v_lshl_add_u64 v[114:115], v[182:183], 2, v[114:115]
	flat_load_dwordx4 v[126:129], v[114:115] nt
	flat_load_dwordx4 v[122:125], v[114:115] offset:16 nt
	flat_load_dwordx4 v[118:121], v[114:115] offset:512 nt
	s_nop 0
	flat_load_dwordx4 v[114:117], v[114:115] offset:528 nt
	s_and_saveexec_b64 s[64:65], vcc
	s_xor_b64 s[64:65], exec, s[64:65]
	v_lshl_add_u64 v[166:167], v[188:189], 0, s[20:21]
	s_andn2_saveexec_b64 s[64:65], s[64:65]
	v_and_b32_e32 v162, 0x1fc0, v225
	v_or3_b32 v186, v224, v162, v223
	v_lshlrev_b64 v[166:167], 13, v[186:187]
	v_lshl_add_u64 v[166:167], s[60:61], 0, v[166:167]
	s_or_b64 exec, exec, s[64:65]
	v_pk_fma_f32 v[112:113], v[112:113], v[144:145], v[160:161]
	v_pk_fma_f32 v[110:111], v[110:111], v[142:143], v[158:159]
	v_pk_fma_f32 v[106:107], v[106:107], v[138:139], v[154:155]
	v_lshl_add_u64 v[154:155], v[182:183], 2, v[166:167]
	v_pk_fma_f32 v[104:105], v[104:105], v[136:137], v[152:153]
	v_pk_fma_f32 v[102:103], v[102:103], v[134:135], v[150:151]
	v_pk_fma_f32 v[100:101], v[100:101], v[132:133], v[148:149]
	v_pk_fma_f32 v[108:109], v[108:109], v[140:141], v[156:157]
	flat_store_dwordx4 v[154:155], v[110:113] nt
	flat_store_dwordx4 v[154:155], v[106:109] offset:16 nt
	v_pk_fma_f32 v[98:99], v[98:99], v[130:131], v[146:147]
	flat_store_dwordx4 v[154:155], v[102:105] offset:512 nt
	flat_store_dwordx4 v[154:155], v[98:101] offset:528 nt
	v_cmp_lt_i64_e32 vcc, s[28:29], v[184:185]
	s_nop 0
	v_lshl_add_u64 v[100:101], v[184:185], 0, 48
	v_lshlrev_b64 v[98:99], 13, v[100:101]
	v_lshl_add_u64 v[148:149], s[62:63], 0, v[98:99]
	s_and_saveexec_b64 s[64:65], vcc
	s_xor_b64 s[64:65], exec, s[64:65]
	v_lshl_add_u64 v[98:99], v[148:149], 0, s[20:21]
	s_or_saveexec_b64 s[64:65], s[64:65]
	v_bfe_u32 v152, v100, 7, 6
	v_and_b32_e32 v147, 0x7ffff, v101
	v_and_b32_e32 v153, 0xffffe000, v100
	v_lshlrev_b32_e32 v154, 6, v100
	s_xor_b64 exec, exec, s[64:65]
	v_and_b32_e32 v98, 0x1fc0, v154
	v_or3_b32 v146, v153, v98, v152
	v_lshlrev_b64 v[98:99], 13, v[146:147]
	v_lshl_add_u64 v[98:99], s[60:61], 0, v[98:99]
	s_or_b64 exec, exec, s[64:65]
	v_lshl_add_u64 v[98:99], v[182:183], 2, v[98:99]
	flat_load_dwordx4 v[110:113], v[98:99] nt
	flat_load_dwordx4 v[106:109], v[98:99] offset:16 nt
	flat_load_dwordx4 v[102:105], v[98:99] offset:512 nt
	s_nop 0
	flat_load_dwordx4 v[98:101], v[98:99] offset:528 nt
	s_and_saveexec_b64 s[64:65], s[4:5]
	s_xor_b64 s[4:5], exec, s[64:65]
	v_lshl_add_u64 v[150:151], v[164:165], 0, s[20:21]
	s_andn2_saveexec_b64 s[4:5], s[4:5]
	v_and_b32_e32 v146, 0x1fc0, v170
	v_or3_b32 v162, v169, v146, v168
	v_lshlrev_b64 v[150:151], 13, v[162:163]
	v_lshl_add_u64 v[150:151], s[60:61], 0, v[150:151]
	s_or_b64 exec, exec, s[4:5]
	s_waitcnt vmcnt(0) lgkmcnt(0)
	v_pk_fma_f32 v[96:97], v[96:97], v[144:145], v[128:129]
	v_pk_fma_f32 v[94:95], v[94:95], v[142:143], v[126:127]
	v_pk_fma_f32 v[90:91], v[90:91], v[138:139], v[122:123]
	v_lshl_add_u64 v[122:123], v[182:183], 2, v[150:151]
	v_pk_fma_f32 v[88:89], v[88:89], v[136:137], v[120:121]
	v_pk_fma_f32 v[86:87], v[86:87], v[134:135], v[118:119]
	v_pk_fma_f32 v[84:85], v[84:85], v[132:133], v[116:117]
	v_pk_fma_f32 v[92:93], v[92:93], v[140:141], v[124:125]
	flat_store_dwordx4 v[122:123], v[94:97] nt
	flat_store_dwordx4 v[122:123], v[90:93] offset:16 nt
	v_pk_fma_f32 v[82:83], v[82:83], v[130:131], v[114:115]
	flat_store_dwordx4 v[122:123], v[86:89] offset:512 nt
	flat_store_dwordx4 v[122:123], v[82:85] offset:528 nt
	v_cmp_lt_i64_e64 s[4:5], s[46:47], v[184:185]
	s_nop 0
	v_lshl_add_u64 v[84:85], v[184:185], 0, s[30:31]
	v_lshlrev_b64 v[82:83], 13, v[84:85]
	v_lshl_add_u64 v[116:117], s[62:63], 0, v[82:83]
	s_and_saveexec_b64 s[64:65], s[4:5]
	s_xor_b64 s[64:65], exec, s[64:65]
	v_lshl_add_u64 v[82:83], v[116:117], 0, s[20:21]
	s_or_saveexec_b64 s[64:65], s[64:65]
	v_bfe_u32 v120, v84, 7, 6
	v_and_b32_e32 v115, 0x7ffff, v85
	v_and_b32_e32 v121, 0xffffe000, v84
	v_lshlrev_b32_e32 v122, 6, v84
	s_xor_b64 exec, exec, s[64:65]
	v_and_b32_e32 v82, 0x1fc0, v122
	v_or3_b32 v114, v121, v82, v120
	v_lshlrev_b64 v[82:83], 13, v[114:115]
	v_lshl_add_u64 v[82:83], s[60:61], 0, v[82:83]
	s_or_b64 exec, exec, s[64:65]
	v_lshl_add_u64 v[82:83], v[182:183], 2, v[82:83]
	flat_load_dwordx4 v[94:97], v[82:83] nt
	flat_load_dwordx4 v[90:93], v[82:83] offset:16 nt
	flat_load_dwordx4 v[86:89], v[82:83] offset:512 nt
	s_nop 0
	flat_load_dwordx4 v[82:85], v[82:83] offset:528 nt
	s_and_saveexec_b64 s[64:65], vcc
	s_xor_b64 s[64:65], exec, s[64:65]
	v_lshl_add_u64 v[118:119], v[148:149], 0, s[20:21]
	s_andn2_saveexec_b64 s[64:65], s[64:65]
	v_and_b32_e32 v114, 0x1fc0, v154
	v_or3_b32 v146, v153, v114, v152
	v_lshlrev_b64 v[118:119], 13, v[146:147]
	v_lshl_add_u64 v[118:119], s[60:61], 0, v[118:119]
	s_or_b64 exec, exec, s[64:65]
	v_pk_fma_f32 v[80:81], v[80:81], v[144:145], v[112:113]
	v_pk_fma_f32 v[78:79], v[78:79], v[142:143], v[110:111]
	v_pk_fma_f32 v[74:75], v[74:75], v[138:139], v[106:107]
	v_lshl_add_u64 v[106:107], v[182:183], 2, v[118:119]
	v_pk_fma_f32 v[72:73], v[72:73], v[136:137], v[104:105]
	v_pk_fma_f32 v[70:71], v[70:71], v[134:135], v[102:103]
	v_pk_fma_f32 v[68:69], v[68:69], v[132:133], v[100:101]
	v_pk_fma_f32 v[76:77], v[76:77], v[140:141], v[108:109]
	flat_store_dwordx4 v[106:107], v[78:81] nt
	flat_store_dwordx4 v[106:107], v[74:77] offset:16 nt
	v_pk_fma_f32 v[66:67], v[66:67], v[130:131], v[98:99]
	flat_store_dwordx4 v[106:107], v[70:73] offset:512 nt
	flat_store_dwordx4 v[106:107], v[66:69] offset:528 nt
	v_cmp_lt_i64_e32 vcc, s[50:51], v[184:185]
	s_nop 0
	v_lshl_add_u64 v[68:69], v[184:185], 0, s[48:49]
	v_lshlrev_b64 v[66:67], 13, v[68:69]
	v_lshl_add_u64 v[100:101], s[62:63], 0, v[66:67]
	s_and_saveexec_b64 s[64:65], vcc
	s_xor_b64 s[64:65], exec, s[64:65]
	v_lshl_add_u64 v[66:67], v[100:101], 0, s[20:21]
	s_or_saveexec_b64 s[64:65], s[64:65]
	v_bfe_u32 v104, v68, 7, 6
	v_and_b32_e32 v99, 0x7ffff, v69
	v_and_b32_e32 v105, 0xffffe000, v68
	v_lshlrev_b32_e32 v106, 6, v68
	s_xor_b64 exec, exec, s[64:65]
	v_and_b32_e32 v66, 0x1fc0, v106
	v_or3_b32 v98, v105, v66, v104
	v_lshlrev_b64 v[66:67], 13, v[98:99]
	v_lshl_add_u64 v[66:67], s[60:61], 0, v[66:67]
	s_or_b64 exec, exec, s[64:65]
	v_lshl_add_u64 v[66:67], v[182:183], 2, v[66:67]
	flat_load_dwordx4 v[78:81], v[66:67] nt
	flat_load_dwordx4 v[74:77], v[66:67] offset:16 nt
	flat_load_dwordx4 v[70:73], v[66:67] offset:512 nt
	s_nop 0
	flat_load_dwordx4 v[66:69], v[66:67] offset:528 nt
	s_and_saveexec_b64 s[64:65], s[4:5]
	s_xor_b64 s[4:5], exec, s[64:65]
	v_lshl_add_u64 v[102:103], v[116:117], 0, s[20:21]
	s_andn2_saveexec_b64 s[4:5], s[4:5]
	v_and_b32_e32 v98, 0x1fc0, v122
	v_or3_b32 v114, v121, v98, v120
	v_lshlrev_b64 v[102:103], 13, v[114:115]
	v_lshl_add_u64 v[102:103], s[60:61], 0, v[102:103]
	s_or_b64 exec, exec, s[4:5]
	s_waitcnt vmcnt(0) lgkmcnt(0)
	v_pk_fma_f32 v[64:65], v[64:65], v[144:145], v[96:97]
	v_pk_fma_f32 v[62:63], v[62:63], v[142:143], v[94:95]
	v_pk_fma_f32 v[58:59], v[58:59], v[138:139], v[90:91]
	v_lshl_add_u64 v[90:91], v[182:183], 2, v[102:103]
	v_pk_fma_f32 v[56:57], v[56:57], v[136:137], v[88:89]
	v_pk_fma_f32 v[54:55], v[54:55], v[134:135], v[86:87]
	v_pk_fma_f32 v[52:53], v[52:53], v[132:133], v[84:85]
	v_pk_fma_f32 v[60:61], v[60:61], v[140:141], v[92:93]
	flat_store_dwordx4 v[90:91], v[62:65] nt
	flat_store_dwordx4 v[90:91], v[58:61] offset:16 nt
	v_pk_fma_f32 v[50:51], v[50:51], v[130:131], v[82:83]
	flat_store_dwordx4 v[90:91], v[54:57] offset:512 nt
	flat_store_dwordx4 v[90:91], v[50:53] offset:528 nt
	v_cmp_lt_i64_e64 s[4:5], s[54:55], v[184:185]
	s_nop 0
	v_lshl_add_u64 v[52:53], v[184:185], 0, s[52:53]
	v_lshlrev_b64 v[50:51], 13, v[52:53]
	v_lshl_add_u64 v[84:85], s[62:63], 0, v[50:51]
	s_and_saveexec_b64 s[64:65], s[4:5]
	s_xor_b64 s[64:65], exec, s[64:65]
	v_lshl_add_u64 v[50:51], v[84:85], 0, s[20:21]
	s_or_saveexec_b64 s[64:65], s[64:65]
	v_bfe_u32 v88, v52, 7, 6
	v_and_b32_e32 v83, 0x7ffff, v53
	v_and_b32_e32 v89, 0xffffe000, v52
	v_lshlrev_b32_e32 v90, 6, v52
	s_xor_b64 exec, exec, s[64:65]
	v_and_b32_e32 v50, 0x1fc0, v90
	v_or3_b32 v82, v89, v50, v88
	v_lshlrev_b64 v[50:51], 13, v[82:83]
	v_lshl_add_u64 v[50:51], s[60:61], 0, v[50:51]
	s_or_b64 exec, exec, s[64:65]
	v_lshl_add_u64 v[50:51], v[182:183], 2, v[50:51]
	flat_load_dwordx4 v[62:65], v[50:51] nt
	flat_load_dwordx4 v[58:61], v[50:51] offset:16 nt
	flat_load_dwordx4 v[54:57], v[50:51] offset:512 nt
	s_nop 0
	flat_load_dwordx4 v[50:53], v[50:51] offset:528 nt
	s_and_saveexec_b64 s[64:65], vcc
	s_xor_b64 s[64:65], exec, s[64:65]
	v_lshl_add_u64 v[86:87], v[100:101], 0, s[20:21]
	s_andn2_saveexec_b64 s[64:65], s[64:65]
	v_and_b32_e32 v82, 0x1fc0, v106
	v_or3_b32 v98, v105, v82, v104
	v_lshlrev_b64 v[86:87], 13, v[98:99]
	v_lshl_add_u64 v[86:87], s[60:61], 0, v[86:87]
	s_or_b64 exec, exec, s[64:65]
	v_pk_fma_f32 v[48:49], v[48:49], v[144:145], v[80:81]
	v_pk_fma_f32 v[46:47], v[46:47], v[142:143], v[78:79]
	v_pk_fma_f32 v[42:43], v[42:43], v[138:139], v[74:75]
	v_lshl_add_u64 v[74:75], v[182:183], 2, v[86:87]
	v_pk_fma_f32 v[40:41], v[40:41], v[136:137], v[72:73]
	v_pk_fma_f32 v[38:39], v[38:39], v[134:135], v[70:71]
	v_pk_fma_f32 v[36:37], v[36:37], v[132:133], v[68:69]
	v_pk_fma_f32 v[44:45], v[44:45], v[140:141], v[76:77]
	flat_store_dwordx4 v[74:75], v[46:49] nt
	flat_store_dwordx4 v[74:75], v[42:45] offset:16 nt
	v_pk_fma_f32 v[34:35], v[34:35], v[130:131], v[66:67]
	flat_store_dwordx4 v[74:75], v[38:41] offset:512 nt
	flat_store_dwordx4 v[74:75], v[34:37] offset:528 nt
	v_cmp_lt_i64_e32 vcc, s[58:59], v[184:185]
	s_nop 0
	v_lshl_add_u64 v[36:37], v[184:185], 0, s[56:57]
	v_lshlrev_b64 v[34:35], 13, v[36:37]
	v_lshl_add_u64 v[68:69], s[62:63], 0, v[34:35]
	s_and_saveexec_b64 s[62:63], vcc
	s_xor_b64 s[62:63], exec, s[62:63]
	v_lshl_add_u64 v[34:35], v[68:69], 0, s[20:21]
	s_or_saveexec_b64 s[62:63], s[62:63]
	v_bfe_u32 v72, v36, 7, 6
	v_and_b32_e32 v67, 0x7ffff, v37
	v_and_b32_e32 v73, 0xffffe000, v36
	v_lshlrev_b32_e32 v74, 6, v36
	s_xor_b64 exec, exec, s[62:63]
	v_and_b32_e32 v34, 0x1fc0, v74
	v_or3_b32 v66, v73, v34, v72
	v_lshlrev_b64 v[34:35], 13, v[66:67]
	v_lshl_add_u64 v[34:35], s[60:61], 0, v[34:35]
	s_or_b64 exec, exec, s[62:63]
	v_lshl_add_u64 v[34:35], v[182:183], 2, v[34:35]
	flat_load_dwordx4 v[46:49], v[34:35] nt
	flat_load_dwordx4 v[42:45], v[34:35] offset:16 nt
	flat_load_dwordx4 v[38:41], v[34:35] offset:512 nt
	s_nop 0
	flat_load_dwordx4 v[34:37], v[34:35] offset:528 nt
	s_and_saveexec_b64 s[62:63], s[4:5]
	s_xor_b64 s[4:5], exec, s[62:63]
	v_lshl_add_u64 v[70:71], v[84:85], 0, s[20:21]
	s_andn2_saveexec_b64 s[4:5], s[4:5]
	v_and_b32_e32 v66, 0x1fc0, v90
	v_or3_b32 v82, v89, v66, v88
	v_lshlrev_b64 v[70:71], 13, v[82:83]
	v_lshl_add_u64 v[70:71], s[60:61], 0, v[70:71]
	s_or_b64 exec, exec, s[4:5]
	s_waitcnt vmcnt(0) lgkmcnt(0)
	v_pk_fma_f32 v[32:33], v[32:33], v[144:145], v[64:65]
	v_pk_fma_f32 v[30:31], v[30:31], v[142:143], v[62:63]
	v_pk_fma_f32 v[26:27], v[26:27], v[138:139], v[58:59]
	v_lshl_add_u64 v[58:59], v[182:183], 2, v[70:71]
	v_pk_fma_f32 v[24:25], v[24:25], v[136:137], v[56:57]
	v_pk_fma_f32 v[22:23], v[22:23], v[134:135], v[54:55]
	v_pk_fma_f32 v[18:19], v[18:19], v[130:131], v[50:51]
	v_pk_fma_f32 v[28:29], v[28:29], v[140:141], v[60:61]
	flat_store_dwordx4 v[58:59], v[30:33] nt
	flat_store_dwordx4 v[58:59], v[26:29] offset:16 nt
	v_pk_fma_f32 v[20:21], v[20:21], v[132:133], v[52:53]
	flat_store_dwordx4 v[58:59], v[22:25] offset:512 nt
	flat_store_dwordx4 v[58:59], v[18:21] offset:528 nt
	s_and_saveexec_b64 s[4:5], vcc
	s_xor_b64 s[4:5], exec, s[4:5]
	v_lshl_add_u64 v[18:19], v[68:69], 0, s[20:21]
	s_andn2_saveexec_b64 s[4:5], s[4:5]
	v_and_b32_e32 v18, 0x1fc0, v74
	v_or3_b32 v66, v73, v18, v72
	v_lshlrev_b64 v[18:19], 13, v[66:67]
	v_lshl_add_u64 v[18:19], s[60:61], 0, v[18:19]
	s_or_b64 exec, exec, s[4:5]
	v_pk_fma_f32 v[16:17], v[16:17], v[144:145], v[48:49]
	v_pk_fma_f32 v[14:15], v[14:15], v[142:143], v[46:47]
	v_lshl_add_u64 v[18:19], v[182:183], 2, v[18:19]
	v_pk_fma_f32 v[8:9], v[8:9], v[136:137], v[40:41]
	v_pk_fma_f32 v[6:7], v[6:7], v[134:135], v[38:39]
	s_andn2_b64 vcc, exec, s[2:3]
	s_mov_b64 s[2:3], -1
	v_pk_fma_f32 v[12:13], v[12:13], v[140:141], v[44:45]
	v_pk_fma_f32 v[10:11], v[10:11], v[138:139], v[42:43]
	flat_store_dwordx4 v[18:19], v[14:17] nt
	flat_store_dwordx4 v[18:19], v[10:13] offset:16 nt
	v_pk_fma_f32 v[4:5], v[4:5], v[132:133], v[36:37]
	v_pk_fma_f32 v[2:3], v[2:3], v[130:131], v[34:35]
	flat_store_dwordx4 v[18:19], v[6:9] offset:512 nt
	flat_store_dwordx4 v[18:19], v[2:5] offset:528 nt
	s_cbranch_vccnz .LBB0_2588
	s_andn2_b64 vcc, exec, s[10:11]
	s_cbranch_vccnz .LBB0_2587
	s_barrier
	s_branch .LBB0_2587

.LBB0_2937:
	ds_read_b128 v[18:21], v180
	ds_read_b128 v[22:25], v181
	ds_read_b128 v[26:29], v188
	ds_read_b128 v[30:33], v189
	ds_read_b128 v[2:5], v182
	ds_read_b128 v[6:9], v183
	ds_read_b128 v[10:13], v190
	ds_read_b128 v[14:17], v191
	s_add_i32 s84, s28, 0x80
	s_cmp_eq_u32 s67, s83
	s_cselect_b32 s86, s25, s84
	s_cselect_b32 s87, s29, s82
	s_add_i32 s84, s86, 0x80
	s_add_i32 s85, s87, 0x80
	v_mov_b32_e32 v172, v176
	ds_read_b128 v[164:167], v196
	ds_read_b128 v[168:171], v196 offset:1024
	ds_read_b128 v[198:201], v196 offset:2048
	ds_read_b128 v[202:205], v196 offset:3072
	ds_read_b128 v[214:217], v196 offset:4096
	ds_read_b128 v[218:221], v196 offset:5120
	ds_read_b128 v[222:225], v196 offset:6144
	ds_read_b128 v[226:229], v196 offset:7168
	s_add_i32 s88, s28, s65
	v_add_u32_e32 v172, s88, v172
	s_add_i32 m0, s49, 0xc000
	s_add_i32 s88, s28, s70
	global_load_lds_dwordx4 v172, s[4:5]
	v_mov_b32_e32 v172, v176
	s_add_i32 m0, s49, 0xe000
	v_add_u32_e32 v172, s88, v172
	global_load_lds_dwordx4 v172, s[4:5]
	s_waitcnt vmcnt(8)
	s_waitcnt lgkmcnt(0)
	s_setprio 1
	s_barrier
	s_waitcnt lgkmcnt(0)
	v_mfma_f32_16x16x128_f8f6f4 v[158:161], v[18:25], v[164:171], v[158:161]
	v_mfma_f32_16x16x128_f8f6f4 v[154:157], v[26:33], v[164:171], v[154:157]
	v_mfma_f32_16x16x128_f8f6f4 v[150:153], v[18:25], v[198:205], v[150:153]
	v_mfma_f32_16x16x128_f8f6f4 v[146:149], v[26:33], v[198:205], v[146:149]
	v_mfma_f32_16x16x128_f8f6f4 v[138:141], v[18:25], v[214:221], v[138:141]
	v_mfma_f32_16x16x128_f8f6f4 v[130:133], v[26:33], v[214:221], v[130:133]
	v_mfma_f32_16x16x128_f8f6f4 v[122:125], v[18:25], v[222:229], v[122:125]
	v_mfma_f32_16x16x128_f8f6f4 v[114:117], v[26:33], v[222:229], v[114:117]
	s_setprio 0
	s_setprio 1
	v_mfma_f32_16x16x128_f8f6f4 v[142:145], v[2:9], v[164:171], v[142:145]
	v_mfma_f32_16x16x128_f8f6f4 v[134:137], v[10:17], v[164:171], v[134:137]
	v_mfma_f32_16x16x128_f8f6f4 v[126:129], v[2:9], v[198:205], v[126:129]
	v_mfma_f32_16x16x128_f8f6f4 v[118:121], v[10:17], v[198:205], v[118:121]
	v_mfma_f32_16x16x128_f8f6f4 v[110:113], v[2:9], v[214:221], v[110:113]
	v_mfma_f32_16x16x128_f8f6f4 v[106:109], v[10:17], v[214:221], v[106:109]
	v_mfma_f32_16x16x128_f8f6f4 v[102:105], v[2:9], v[222:229], v[102:105]
	v_mfma_f32_16x16x128_f8f6f4 v[98:101], v[10:17], v[222:229], v[98:101]
	s_setprio 0
	s_barrier
	v_mov_b32_e32 v172, v177
	ds_read_b128 v[164:167], v196 offset:16384
	ds_read_b128 v[168:171], v196 offset:17408
	ds_read_b128 v[198:201], v196 offset:18432
	ds_read_b128 v[202:205], v196 offset:19456
	ds_read_b128 v[214:217], v196 offset:20480
	ds_read_b128 v[218:221], v196 offset:21504
	ds_read_b128 v[222:225], v196 offset:22528
	ds_read_b128 v[226:229], v196 offset:23552
	s_mov_b32 m0, s50
	v_add_u32_e32 v172, s87, v172
	global_load_lds_dwordx4 v172, s[6:7]
	v_mov_b32_e32 v172, v177
	s_add_i32 s87, s87, s48
	v_add_u32_e32 v172, s87, v172
	s_mov_b32 m0, s51
	s_add_i32 s87, s87, s48
	global_load_lds_dwordx4 v172, s[6:7]
	v_mov_b32_e32 v172, v177
	s_mov_b32 m0, s52
	v_add_u32_e32 v172, s87, v172
	global_load_lds_dwordx4 v172, s[6:7]
	v_mov_b32_e32 v172, v177
	s_add_i32 s87, s87, s48
	v_add_u32_e32 v172, s87, v172
	s_mov_b32 m0, s53
	s_nop 0
	global_load_lds_dwordx4 v172, s[6:7]
	v_mov_b32_e32 v172, v176
	s_mov_b32 m0, s49
	v_add_u32_e32 v172, s86, v172
	global_load_lds_dwordx4 v172, s[4:5]
	v_mov_b32_e32 v172, v176
	s_add_i32 s86, s86, s47
	v_add_u32_e32 v172, s86, v172
	s_mov_b32 m0, s54
	s_nop 0
	global_load_lds_dwordx4 v172, s[4:5]
	s_waitcnt vmcnt(8)
	s_waitcnt lgkmcnt(0)
	s_setprio 1
	s_barrier
	s_waitcnt lgkmcnt(0)
	v_mfma_f32_16x16x128_f8f6f4 v[94:97], v[18:25], v[164:171], v[94:97]
	v_mfma_f32_16x16x128_f8f6f4 v[90:93], v[26:33], v[164:171], v[90:93]
	v_mfma_f32_16x16x128_f8f6f4 v[86:89], v[18:25], v[198:205], v[86:89]
	v_mfma_f32_16x16x128_f8f6f4 v[82:85], v[26:33], v[198:205], v[82:85]
	v_mfma_f32_16x16x128_f8f6f4 v[74:77], v[18:25], v[214:221], v[74:77]
	v_mfma_f32_16x16x128_f8f6f4 v[66:69], v[26:33], v[214:221], v[66:69]
	v_mfma_f32_16x16x128_f8f6f4 v[58:61], v[18:25], v[222:229], v[58:61]
	v_mfma_f32_16x16x128_f8f6f4 v[50:53], v[26:33], v[222:229], v[50:53]
	s_setprio 0
	s_setprio 1
	v_mfma_f32_16x16x128_f8f6f4 v[78:81], v[2:9], v[164:171], v[78:81]
	v_mfma_f32_16x16x128_f8f6f4 v[70:73], v[10:17], v[164:171], v[70:73]
	v_mfma_f32_16x16x128_f8f6f4 v[62:65], v[2:9], v[198:205], v[62:65]
	v_mfma_f32_16x16x128_f8f6f4 v[54:57], v[10:17], v[198:205], v[54:57]
	v_mfma_f32_16x16x128_f8f6f4 v[46:49], v[2:9], v[214:221], v[46:49]
	v_mfma_f32_16x16x128_f8f6f4 v[42:45], v[10:17], v[214:221], v[42:45]
	v_mfma_f32_16x16x128_f8f6f4 v[38:41], v[2:9], v[222:229], v[38:41]
	v_mfma_f32_16x16x128_f8f6f4 v[34:37], v[10:17], v[222:229], v[34:37]
	s_setprio 0
	s_barrier
	ds_read_b128 v[2:5], v184
	ds_read_b128 v[6:9], v185
	ds_read_b128 v[10:13], v192
	ds_read_b128 v[14:17], v193
	ds_read_b128 v[18:21], v186
	ds_read_b128 v[22:25], v187
	ds_read_b128 v[26:29], v194
	ds_read_b128 v[30:33], v195
	v_mov_b32_e32 v172, v176
	ds_read_b128 v[164:167], v196 offset:32768
	ds_read_b128 v[168:171], v196 offset:33792
	ds_read_b128 v[198:201], v196 offset:34816
	ds_read_b128 v[202:205], v196 offset:35840
	ds_read_b128 v[214:217], v196 offset:36864
	ds_read_b128 v[218:221], v196 offset:37888
	ds_read_b128 v[222:225], v196 offset:38912
	ds_read_b128 v[226:229], v196 offset:39936
	s_add_i32 s86, s86, s47
	s_mov_b32 m0, s55
	v_add_u32_e32 v172, s86, v172
	global_load_lds_dwordx4 v172, s[4:5]
	v_mov_b32_e32 v172, v176
	s_add_i32 s86, s86, s47
	v_add_u32_e32 v172, s86, v172
	s_mov_b32 m0, s56
	s_nop 0
	global_load_lds_dwordx4 v172, s[4:5]
	s_waitcnt vmcnt(8)
	s_waitcnt lgkmcnt(0)
	s_setprio 1
	s_barrier
	s_waitcnt lgkmcnt(0)
	v_mfma_f32_16x16x128_f8f6f4 v[158:161], v[2:9], v[164:171], v[158:161]
	v_mfma_f32_16x16x128_f8f6f4 v[154:157], v[10:17], v[164:171], v[154:157]
	v_mfma_f32_16x16x128_f8f6f4 v[150:153], v[2:9], v[198:205], v[150:153]
	v_mfma_f32_16x16x128_f8f6f4 v[146:149], v[10:17], v[198:205], v[146:149]
	v_mfma_f32_16x16x128_f8f6f4 v[138:141], v[2:9], v[214:221], v[138:141]
	v_mfma_f32_16x16x128_f8f6f4 v[130:133], v[10:17], v[214:221], v[130:133]
	v_mfma_f32_16x16x128_f8f6f4 v[122:125], v[2:9], v[222:229], v[122:125]
	v_mfma_f32_16x16x128_f8f6f4 v[114:117], v[10:17], v[222:229], v[114:117]
	s_setprio 0
	s_setprio 1
	v_mfma_f32_16x16x128_f8f6f4 v[142:145], v[18:25], v[164:171], v[142:145]
	v_mfma_f32_16x16x128_f8f6f4 v[134:137], v[26:33], v[164:171], v[134:137]
	v_mfma_f32_16x16x128_f8f6f4 v[126:129], v[18:25], v[198:205], v[126:129]
	v_mfma_f32_16x16x128_f8f6f4 v[118:121], v[26:33], v[198:205], v[118:121]
	v_mfma_f32_16x16x128_f8f6f4 v[110:113], v[18:25], v[214:221], v[110:113]
	v_mfma_f32_16x16x128_f8f6f4 v[106:109], v[26:33], v[214:221], v[106:109]
	v_mfma_f32_16x16x128_f8f6f4 v[102:105], v[18:25], v[222:229], v[102:105]
	v_mfma_f32_16x16x128_f8f6f4 v[98:101], v[26:33], v[222:229], v[98:101]
	s_setprio 0
	s_barrier
	v_mov_b32_e32 v172, v177
	ds_read_b128 v[164:167], v196 offset:49152
	ds_read_b128 v[168:171], v196 offset:50176
	ds_read_b128 v[198:201], v196 offset:51200
	ds_read_b128 v[202:205], v196 offset:52224
	ds_read_b128 v[214:217], v196 offset:53248
	ds_read_b128 v[218:221], v196 offset:54272
	ds_read_b128 v[222:225], v196 offset:55296
	ds_read_b128 v[226:229], v196 offset:56320
	s_mov_b32 m0, s58
	v_add_u32_e32 v172, s85, v172
	global_load_lds_dwordx4 v172, s[6:7]
	v_mov_b32_e32 v172, v177
	s_add_i32 s85, s85, s48
	v_add_u32_e32 v172, s85, v172
	s_mov_b32 m0, s59
	s_add_i32 s85, s85, s48
	global_load_lds_dwordx4 v172, s[6:7]
	v_mov_b32_e32 v172, v177
	s_mov_b32 m0, s62
	v_add_u32_e32 v172, s85, v172
	global_load_lds_dwordx4 v172, s[6:7]
	v_mov_b32_e32 v172, v177
	s_add_i32 s85, s85, s48
	v_add_u32_e32 v172, s85, v172
	s_mov_b32 m0, s63
	s_nop 0
	global_load_lds_dwordx4 v172, s[6:7]
	v_mov_b32_e32 v172, v176
	s_mov_b32 m0, s60
	v_add_u32_e32 v172, s84, v172
	global_load_lds_dwordx4 v172, s[4:5]
	v_mov_b32_e32 v172, v176
	s_add_i32 s84, s84, s47
	v_add_u32_e32 v172, s84, v172
	s_mov_b32 m0, s61
	s_nop 0
	global_load_lds_dwordx4 v172, s[4:5]
	s_waitcnt vmcnt(8)
	s_waitcnt lgkmcnt(0)
	s_setprio 1
	s_barrier
	s_waitcnt lgkmcnt(0)
	v_mfma_f32_16x16x128_f8f6f4 v[94:97], v[2:9], v[164:171], v[94:97]
	v_mfma_f32_16x16x128_f8f6f4 v[90:93], v[10:17], v[164:171], v[90:93]
	v_mfma_f32_16x16x128_f8f6f4 v[86:89], v[2:9], v[198:205], v[86:89]
	v_mfma_f32_16x16x128_f8f6f4 v[82:85], v[10:17], v[198:205], v[82:85]
	v_mfma_f32_16x16x128_f8f6f4 v[74:77], v[2:9], v[214:221], v[74:77]
	v_mfma_f32_16x16x128_f8f6f4 v[66:69], v[10:17], v[214:221], v[66:69]
	v_mfma_f32_16x16x128_f8f6f4 v[58:61], v[2:9], v[222:229], v[58:61]
	v_mfma_f32_16x16x128_f8f6f4 v[50:53], v[10:17], v[222:229], v[50:53]
	s_setprio 0
	s_setprio 1
	v_mfma_f32_16x16x128_f8f6f4 v[78:81], v[18:25], v[164:171], v[78:81]
	v_mfma_f32_16x16x128_f8f6f4 v[70:73], v[26:33], v[164:171], v[70:73]
	v_mfma_f32_16x16x128_f8f6f4 v[62:65], v[18:25], v[198:205], v[62:65]
	v_mfma_f32_16x16x128_f8f6f4 v[54:57], v[26:33], v[198:205], v[54:57]
	v_mfma_f32_16x16x128_f8f6f4 v[46:49], v[18:25], v[214:221], v[46:49]
	v_mfma_f32_16x16x128_f8f6f4 v[42:45], v[26:33], v[214:221], v[42:45]
	v_mfma_f32_16x16x128_f8f6f4 v[38:41], v[18:25], v[222:229], v[38:41]
	v_mfma_f32_16x16x128_f8f6f4 v[34:37], v[26:33], v[222:229], v[34:37]
	s_setprio 0
	s_barrier
	s_add_i32 s83, s83, 2
	s_addk_i32 s28, 0x100
	s_addk_i32 s82, 0x100
	s_cmp_ge_i32 s83, s64
	s_cbranch_scc0 .LBB0_2937
	v_pk_fma_f32 v[164:165], v[160:161], s[18:19], 0 op_sel_hi:[1,0,0]
	v_pk_fma_f32 v[168:169], v[158:159], s[18:19], 0 op_sel_hi:[1,0,0]
	v_pk_fma_f32 v[172:173], v[144:145], s[20:21], 0 op_sel_hi:[1,0,0]
	v_pk_fma_f32 v[174:175], v[142:143], s[20:21], 0 op_sel_hi:[1,0,0]
	v_pk_fma_f32 v[156:157], v[156:157], s[18:19], 0 op_sel_hi:[1,0,0]
	v_pk_fma_f32 v[160:161], v[154:155], s[18:19], 0 op_sel_hi:[1,0,0]
	v_pk_fma_f32 v[166:167], v[136:137], s[20:21], 0 op_sel_hi:[1,0,0]
	v_pk_fma_f32 v[170:171], v[134:135], s[20:21], 0 op_sel_hi:[1,0,0]
	v_pk_fma_f32 v[152:153], v[152:153], s[18:19], 0 op_sel_hi:[1,0,0]
	v_pk_fma_f32 v[150:151], v[150:151], s[18:19], 0 op_sel_hi:[1,0,0]
	v_pk_fma_f32 v[154:155], v[128:129], s[20:21], 0 op_sel_hi:[1,0,0]
	v_pk_fma_f32 v[158:159], v[126:127], s[20:21], 0 op_sel_hi:[1,0,0]
	v_pk_fma_f32 v[142:143], v[148:149], s[18:19], 0 op_sel_hi:[1,0,0]
	v_pk_fma_f32 v[144:145], v[146:147], s[18:19], 0 op_sel_hi:[1,0,0]
	v_pk_fma_f32 v[146:147], v[120:121], s[20:21], 0 op_sel_hi:[1,0,0]
	v_pk_fma_f32 v[148:149], v[118:119], s[20:21], 0 op_sel_hi:[1,0,0]
	v_pk_fma_f32 v[134:135], v[140:141], s[18:19], 0 op_sel_hi:[1,0,0]
	v_pk_fma_f32 v[136:137], v[138:139], s[18:19], 0 op_sel_hi:[1,0,0]
	v_pk_fma_f32 v[138:139], v[112:113], s[20:21], 0 op_sel_hi:[1,0,0]
	v_pk_fma_f32 v[140:141], v[110:111], s[20:21], 0 op_sel_hi:[1,0,0]
	v_pk_fma_f32 v[126:127], v[132:133], s[18:19], 0 op_sel_hi:[1,0,0]
	v_pk_fma_f32 v[128:129], v[130:131], s[18:19], 0 op_sel_hi:[1,0,0]
	v_pk_fma_f32 v[130:131], v[108:109], s[20:21], 0 op_sel_hi:[1,0,0]
	v_pk_fma_f32 v[132:133], v[106:107], s[20:21], 0 op_sel_hi:[1,0,0]
	v_pk_fma_f32 v[108:109], v[124:125], s[18:19], 0 op_sel_hi:[1,0,0]
	v_pk_fma_f32 v[118:119], v[122:123], s[18:19], 0 op_sel_hi:[1,0,0]
	v_pk_fma_f32 v[120:121], v[104:105], s[20:21], 0 op_sel_hi:[1,0,0]
	v_pk_fma_f32 v[122:123], v[102:103], s[20:21], 0 op_sel_hi:[1,0,0]
	v_pk_fma_f32 v[102:103], v[116:117], s[18:19], 0 op_sel_hi:[1,0,0]
	v_pk_fma_f32 v[104:105], v[114:115], s[18:19], 0 op_sel_hi:[1,0,0]
	v_pk_fma_f32 v[106:107], v[100:101], s[20:21], 0 op_sel_hi:[1,0,0]
	v_pk_fma_f32 v[112:113], v[98:99], s[20:21], 0 op_sel_hi:[1,0,0]
	v_pk_fma_f32 v[96:97], v[96:97], s[18:19], 0 op_sel_hi:[1,0,0]
	v_pk_fma_f32 v[98:99], v[94:95], s[18:19], 0 op_sel_hi:[1,0,0]
	v_pk_fma_f32 v[100:101], v[80:81], s[20:21], 0 op_sel_hi:[1,0,0]
	v_pk_fma_f32 v[110:111], v[78:79], s[20:21], 0 op_sel_hi:[1,0,0]
	v_pk_fma_f32 v[78:79], v[92:93], s[18:19], 0 op_sel_hi:[1,0,0]
	v_pk_fma_f32 v[90:91], v[90:91], s[18:19], 0 op_sel_hi:[1,0,0]
	v_pk_fma_f32 v[92:93], v[72:73], s[20:21], 0 op_sel_hi:[1,0,0]
	v_pk_fma_f32 v[94:95], v[70:71], s[20:21], 0 op_sel_hi:[1,0,0]
	v_pk_fma_f32 v[70:71], v[88:89], s[18:19], 0 op_sel_hi:[1,0,0]
	v_pk_fma_f32 v[72:73], v[86:87], s[18:19], 0 op_sel_hi:[1,0,0]
	v_pk_fma_f32 v[64:65], v[64:65], s[20:21], 0 op_sel_hi:[1,0,0]
	v_pk_fma_f32 v[80:81], v[62:63], s[20:21], 0 op_sel_hi:[1,0,0]
	v_pk_fma_f32 v[32:33], v[84:85], s[18:19], 0 op_sel_hi:[1,0,0]
	v_pk_fma_f32 v[62:63], v[82:83], s[18:19], 0 op_sel_hi:[1,0,0]
	v_pk_fma_f32 v[56:57], v[56:57], s[20:21], 0 op_sel_hi:[1,0,0]
	v_pk_fma_f32 v[54:55], v[54:55], s[20:21], 0 op_sel_hi:[1,0,0]
	v_pk_fma_f32 v[24:25], v[76:77], s[18:19], 0 op_sel_hi:[1,0,0]
	v_pk_fma_f32 v[28:29], v[74:75], s[18:19], 0 op_sel_hi:[1,0,0]
	v_pk_fma_f32 v[30:31], v[48:49], s[20:21], 0 op_sel_hi:[1,0,0]
	v_pk_fma_f32 v[46:47], v[46:47], s[20:21], 0 op_sel_hi:[1,0,0]
	v_pk_fma_f32 v[16:17], v[68:69], s[18:19], 0 op_sel_hi:[1,0,0]
	v_pk_fma_f32 v[20:21], v[66:67], s[18:19], 0 op_sel_hi:[1,0,0]
	v_pk_fma_f32 v[22:23], v[44:45], s[20:21], 0 op_sel_hi:[1,0,0]
	v_pk_fma_f32 v[26:27], v[42:43], s[20:21], 0 op_sel_hi:[1,0,0]
	v_pk_fma_f32 v[8:9], v[60:61], s[18:19], 0 op_sel_hi:[1,0,0]
	v_pk_fma_f32 v[12:13], v[58:59], s[18:19], 0 op_sel_hi:[1,0,0]
	v_pk_fma_f32 v[14:15], v[40:41], s[20:21], 0 op_sel_hi:[1,0,0]
	v_pk_fma_f32 v[18:19], v[38:39], s[20:21], 0 op_sel_hi:[1,0,0]
	v_pk_fma_f32 v[2:3], v[52:53], s[18:19], 0 op_sel_hi:[1,0,0]
	v_pk_fma_f32 v[4:5], v[50:51], s[18:19], 0 op_sel_hi:[1,0,0]
	v_pk_fma_f32 v[6:7], v[36:37], s[20:21], 0 op_sel_hi:[1,0,0]
	v_pk_fma_f32 v[10:11], v[34:35], s[20:21], 0 op_sel_hi:[1,0,0]

.LBB0_3007:
	ds_read_b128 v[18:21], v168
	ds_read_b128 v[22:25], v169
	ds_read_b128 v[26:29], v176
	ds_read_b128 v[30:33], v177
	ds_read_b128 v[2:5], v170
	ds_read_b128 v[6:9], v171
	ds_read_b128 v[10:13], v178
	ds_read_b128 v[14:17], v179
	s_add_i32 s76, s20, 0x80
	s_cmp_eq_u32 s61, s75
	s_cselect_b32 s78, s11, s76
	s_cselect_b32 s77, s21, s74
	s_add_i32 s76, s78, 0x80
	v_mov_b32_e32 v185, v164
	ds_read_b128 v[186:189], v184
	ds_read_b128 v[190:193], v184 offset:1024
	ds_read_b128 v[194:197], v184 offset:2048
	ds_read_b128 v[198:201], v184 offset:3072
	ds_read_b128 v[202:205], v184 offset:4096
	ds_read_b128 v[206:209], v184 offset:5120
	ds_read_b128 v[214:217], v184 offset:6144
	ds_read_b128 v[218:221], v184 offset:7168
	s_add_i32 s79, s20, s59
	v_add_u32_e32 v185, s79, v185
	s_add_i32 m0, s30, 0xc000
	s_add_i32 s79, s20, s66
	global_load_lds_dwordx4 v185, s[4:5]
	v_mov_b32_e32 v185, v164
	s_add_i32 m0, s30, 0xe000
	v_add_u32_e32 v185, s79, v185
	global_load_lds_dwordx4 v185, s[4:5]
	s_waitcnt vmcnt(8)
	s_waitcnt lgkmcnt(0)
	s_setprio 1
	s_barrier
	s_waitcnt lgkmcnt(0)
	v_mfma_f32_16x16x128_f8f6f4 v[158:161], v[18:25], v[186:193], v[158:161]
	v_mfma_f32_16x16x128_f8f6f4 v[154:157], v[26:33], v[186:193], v[154:157]
	v_mfma_f32_16x16x128_f8f6f4 v[150:153], v[18:25], v[194:201], v[150:153]
	v_mfma_f32_16x16x128_f8f6f4 v[146:149], v[26:33], v[194:201], v[146:149]
	v_mfma_f32_16x16x128_f8f6f4 v[138:141], v[18:25], v[202:209], v[138:141]
	v_mfma_f32_16x16x128_f8f6f4 v[130:133], v[26:33], v[202:209], v[130:133]
	v_mfma_f32_16x16x128_f8f6f4 v[122:125], v[18:25], v[214:221], v[122:125]
	v_mfma_f32_16x16x128_f8f6f4 v[114:117], v[26:33], v[214:221], v[114:117]
	s_setprio 0
	s_setprio 1
	v_mfma_f32_16x16x128_f8f6f4 v[142:145], v[2:9], v[186:193], v[142:145]
	v_mfma_f32_16x16x128_f8f6f4 v[134:137], v[10:17], v[186:193], v[134:137]
	v_mfma_f32_16x16x128_f8f6f4 v[126:129], v[2:9], v[194:201], v[126:129]
	v_mfma_f32_16x16x128_f8f6f4 v[118:121], v[10:17], v[194:201], v[118:121]
	v_mfma_f32_16x16x128_f8f6f4 v[110:113], v[2:9], v[202:209], v[110:113]
	v_mfma_f32_16x16x128_f8f6f4 v[106:109], v[10:17], v[202:209], v[106:109]
	v_mfma_f32_16x16x128_f8f6f4 v[102:105], v[2:9], v[214:221], v[102:105]
	v_mfma_f32_16x16x128_f8f6f4 v[98:101], v[10:17], v[214:221], v[98:101]
	s_setprio 0
	s_barrier
	v_mov_b32_e32 v185, v165
	ds_read_b128 v[186:189], v184 offset:16384
	ds_read_b128 v[190:193], v184 offset:17408
	ds_read_b128 v[194:197], v184 offset:18432
	ds_read_b128 v[198:201], v184 offset:19456
	ds_read_b128 v[202:205], v184 offset:20480
	ds_read_b128 v[206:209], v184 offset:21504
	ds_read_b128 v[214:217], v184 offset:22528
	ds_read_b128 v[218:221], v184 offset:23552
	s_mov_b32 m0, s31
	v_add_u32_e32 v185, s77, v185
	global_load_lds_dwordx4 v185, s[6:7]
	v_mov_b32_e32 v185, v165
	s_add_i32 s79, s77, s25
	v_add_u32_e32 v185, s79, v185
	s_mov_b32 m0, s35
	s_add_i32 s79, s79, s25
	global_load_lds_dwordx4 v185, s[6:7]
	v_mov_b32_e32 v185, v165
	s_mov_b32 m0, s44
	v_add_u32_e32 v185, s79, v185
	global_load_lds_dwordx4 v185, s[6:7]
	v_mov_b32_e32 v185, v165
	s_add_i32 s79, s79, s25
	v_add_u32_e32 v185, s79, v185
	s_mov_b32 m0, s45
	s_nop 0
	global_load_lds_dwordx4 v185, s[6:7]
	v_mov_b32_e32 v185, v164
	s_mov_b32 m0, s30
	v_add_u32_e32 v185, s78, v185
	global_load_lds_dwordx4 v185, s[4:5]
	v_mov_b32_e32 v185, v164
	s_add_i32 s78, s78, s24
	v_add_u32_e32 v185, s78, v185
	s_mov_b32 m0, s46
	s_nop 0
	global_load_lds_dwordx4 v185, s[4:5]
	s_waitcnt vmcnt(8)
	s_waitcnt lgkmcnt(0)
	s_setprio 1
	s_barrier
	s_waitcnt lgkmcnt(0)
	v_mfma_f32_16x16x128_f8f6f4 v[94:97], v[18:25], v[186:193], v[94:97]
	v_mfma_f32_16x16x128_f8f6f4 v[90:93], v[26:33], v[186:193], v[90:93]
	v_mfma_f32_16x16x128_f8f6f4 v[86:89], v[18:25], v[194:201], v[86:89]
	v_mfma_f32_16x16x128_f8f6f4 v[82:85], v[26:33], v[194:201], v[82:85]
	v_mfma_f32_16x16x128_f8f6f4 v[74:77], v[18:25], v[202:209], v[74:77]
	v_mfma_f32_16x16x128_f8f6f4 v[66:69], v[26:33], v[202:209], v[66:69]
	v_mfma_f32_16x16x128_f8f6f4 v[58:61], v[18:25], v[214:221], v[58:61]
	v_mfma_f32_16x16x128_f8f6f4 v[50:53], v[26:33], v[214:221], v[50:53]
	s_setprio 0
	s_setprio 1
	v_mfma_f32_16x16x128_f8f6f4 v[78:81], v[2:9], v[186:193], v[78:81]
	v_mfma_f32_16x16x128_f8f6f4 v[70:73], v[10:17], v[186:193], v[70:73]
	v_mfma_f32_16x16x128_f8f6f4 v[62:65], v[2:9], v[194:201], v[62:65]
	v_mfma_f32_16x16x128_f8f6f4 v[54:57], v[10:17], v[194:201], v[54:57]
	v_mfma_f32_16x16x128_f8f6f4 v[46:49], v[2:9], v[202:209], v[46:49]
	v_mfma_f32_16x16x128_f8f6f4 v[42:45], v[10:17], v[202:209], v[42:45]
	v_mfma_f32_16x16x128_f8f6f4 v[38:41], v[2:9], v[214:221], v[38:41]
	v_mfma_f32_16x16x128_f8f6f4 v[34:37], v[10:17], v[214:221], v[34:37]
	s_setprio 0
	s_barrier
	ds_read_b128 v[2:5], v172
	ds_read_b128 v[6:9], v173
	ds_read_b128 v[10:13], v180
	ds_read_b128 v[14:17], v181
	ds_read_b128 v[18:21], v174
	ds_read_b128 v[22:25], v175
	ds_read_b128 v[26:29], v182
	ds_read_b128 v[30:33], v183
	v_mov_b32_e32 v185, v164
	ds_read_b128 v[186:189], v184 offset:32768
	ds_read_b128 v[190:193], v184 offset:33792
	ds_read_b128 v[194:197], v184 offset:34816
	ds_read_b128 v[198:201], v184 offset:35840
	ds_read_b128 v[202:205], v184 offset:36864
	ds_read_b128 v[206:209], v184 offset:37888
	ds_read_b128 v[214:217], v184 offset:38912
	ds_read_b128 v[218:221], v184 offset:39936
	s_add_i32 s78, s78, s24
	s_mov_b32 m0, s47
	v_add_u32_e32 v185, s78, v185
	global_load_lds_dwordx4 v185, s[4:5]
	v_mov_b32_e32 v185, v164
	s_add_i32 s78, s78, s24
	v_add_u32_e32 v185, s78, v185
	s_mov_b32 m0, s48
	s_nop 0
	global_load_lds_dwordx4 v185, s[4:5]
	s_waitcnt vmcnt(8)
	s_waitcnt lgkmcnt(0)
	s_setprio 1
	s_barrier
	s_waitcnt lgkmcnt(0)
	v_mfma_f32_16x16x128_f8f6f4 v[158:161], v[2:9], v[186:193], v[158:161]
	v_mfma_f32_16x16x128_f8f6f4 v[154:157], v[10:17], v[186:193], v[154:157]
	v_mfma_f32_16x16x128_f8f6f4 v[150:153], v[2:9], v[194:201], v[150:153]
	v_mfma_f32_16x16x128_f8f6f4 v[146:149], v[10:17], v[194:201], v[146:149]
	v_mfma_f32_16x16x128_f8f6f4 v[138:141], v[2:9], v[202:209], v[138:141]
	v_mfma_f32_16x16x128_f8f6f4 v[130:133], v[10:17], v[202:209], v[130:133]
	v_mfma_f32_16x16x128_f8f6f4 v[122:125], v[2:9], v[214:221], v[122:125]
	v_mfma_f32_16x16x128_f8f6f4 v[114:117], v[10:17], v[214:221], v[114:117]
	s_setprio 0
	s_setprio 1
	v_mfma_f32_16x16x128_f8f6f4 v[142:145], v[18:25], v[186:193], v[142:145]
	v_mfma_f32_16x16x128_f8f6f4 v[134:137], v[26:33], v[186:193], v[134:137]
	v_mfma_f32_16x16x128_f8f6f4 v[126:129], v[18:25], v[194:201], v[126:129]
	v_mfma_f32_16x16x128_f8f6f4 v[118:121], v[26:33], v[194:201], v[118:121]
	v_mfma_f32_16x16x128_f8f6f4 v[110:113], v[18:25], v[202:209], v[110:113]
	v_mfma_f32_16x16x128_f8f6f4 v[106:109], v[26:33], v[202:209], v[106:109]
	v_mfma_f32_16x16x128_f8f6f4 v[102:105], v[18:25], v[214:221], v[102:105]
	v_mfma_f32_16x16x128_f8f6f4 v[98:101], v[26:33], v[214:221], v[98:101]
	s_setprio 0
	s_barrier
	v_mov_b32_e32 v185, v165
	ds_read_b128 v[186:189], v184 offset:49152
	ds_read_b128 v[190:193], v184 offset:50176
	ds_read_b128 v[194:197], v184 offset:51200
	ds_read_b128 v[198:201], v184 offset:52224
	ds_read_b128 v[202:205], v184 offset:53248
	ds_read_b128 v[206:209], v184 offset:54272
	ds_read_b128 v[214:217], v184 offset:55296
	ds_read_b128 v[218:221], v184 offset:56320
	s_addk_i32 s77, 0x80
	s_mov_b32 m0, s51
	v_add_u32_e32 v185, s77, v185
	global_load_lds_dwordx4 v185, s[6:7]
	v_mov_b32_e32 v185, v165
	s_add_i32 s77, s77, s25
	v_add_u32_e32 v185, s77, v185
	s_mov_b32 m0, s52
	s_add_i32 s77, s77, s25
	global_load_lds_dwordx4 v185, s[6:7]
	v_mov_b32_e32 v185, v165
	s_mov_b32 m0, s55
	v_add_u32_e32 v185, s77, v185
	global_load_lds_dwordx4 v185, s[6:7]
	v_mov_b32_e32 v185, v165
	s_add_i32 s77, s77, s25
	v_add_u32_e32 v185, s77, v185
	s_mov_b32 m0, s57
	s_nop 0
	global_load_lds_dwordx4 v185, s[6:7]
	v_mov_b32_e32 v185, v164
	s_mov_b32 m0, s53
	v_add_u32_e32 v185, s76, v185
	global_load_lds_dwordx4 v185, s[4:5]
	v_mov_b32_e32 v185, v164
	s_add_i32 s76, s76, s24
	v_add_u32_e32 v185, s76, v185
	s_mov_b32 m0, s54
	s_nop 0
	global_load_lds_dwordx4 v185, s[4:5]
	s_waitcnt vmcnt(8)
	s_waitcnt lgkmcnt(0)
	s_setprio 1
	s_barrier
	s_waitcnt lgkmcnt(0)
	v_mfma_f32_16x16x128_f8f6f4 v[94:97], v[2:9], v[186:193], v[94:97]
	v_mfma_f32_16x16x128_f8f6f4 v[90:93], v[10:17], v[186:193], v[90:93]
	v_mfma_f32_16x16x128_f8f6f4 v[86:89], v[2:9], v[194:201], v[86:89]
	v_mfma_f32_16x16x128_f8f6f4 v[82:85], v[10:17], v[194:201], v[82:85]
	v_mfma_f32_16x16x128_f8f6f4 v[74:77], v[2:9], v[202:209], v[74:77]
	v_mfma_f32_16x16x128_f8f6f4 v[66:69], v[10:17], v[202:209], v[66:69]
	v_mfma_f32_16x16x128_f8f6f4 v[58:61], v[2:9], v[214:221], v[58:61]
	v_mfma_f32_16x16x128_f8f6f4 v[50:53], v[10:17], v[214:221], v[50:53]
	s_setprio 0
	s_setprio 1
	v_mfma_f32_16x16x128_f8f6f4 v[78:81], v[18:25], v[186:193], v[78:81]
	v_mfma_f32_16x16x128_f8f6f4 v[70:73], v[26:33], v[186:193], v[70:73]
	v_mfma_f32_16x16x128_f8f6f4 v[62:65], v[18:25], v[194:201], v[62:65]
	v_mfma_f32_16x16x128_f8f6f4 v[54:57], v[26:33], v[194:201], v[54:57]
	v_mfma_f32_16x16x128_f8f6f4 v[46:49], v[18:25], v[202:209], v[46:49]
	v_mfma_f32_16x16x128_f8f6f4 v[42:45], v[26:33], v[202:209], v[42:45]
	v_mfma_f32_16x16x128_f8f6f4 v[38:41], v[18:25], v[214:221], v[38:41]
	v_mfma_f32_16x16x128_f8f6f4 v[34:37], v[26:33], v[214:221], v[34:37]
	s_setprio 0
	s_barrier
	s_add_i32 s75, s75, 2
	s_addk_i32 s20, 0x100
	s_addk_i32 s74, 0x100
	s_cmp_ge_i32 s75, s58
	s_cbranch_scc0 .LBB0_3007
	v_pk_mul_f32 v[2:3], v[160:161], s[16:17] op_sel_hi:[1,0]
	v_pk_mul_f32 v[4:5], v[158:159], s[16:17] op_sel_hi:[1,0]
	v_pk_mul_f32 v[6:7], v[156:157], s[16:17] op_sel_hi:[1,0]
	v_pk_mul_f32 v[12:13], v[154:155], s[16:17] op_sel_hi:[1,0]
	v_pk_mul_f32 v[144:145], v[144:145], s[16:17] op_sel_hi:[1,0]
	v_pk_mul_f32 v[142:143], v[142:143], s[16:17] op_sel_hi:[1,0]
	v_pk_mul_f32 v[136:137], v[136:137], s[16:17] op_sel_hi:[1,0]
	v_pk_mul_f32 v[134:135], v[134:135], s[16:17] op_sel_hi:[1,0]
	v_pk_mul_f32 v[8:9], v[152:153], s[16:17] op_sel_hi:[1,0]
	v_pk_mul_f32 v[14:15], v[150:151], s[16:17] op_sel_hi:[1,0]
	v_pk_mul_f32 v[18:19], v[148:149], s[16:17] op_sel_hi:[1,0]
	v_pk_mul_f32 v[26:27], v[146:147], s[16:17] op_sel_hi:[1,0]
	v_pk_mul_f32 v[128:129], v[128:129], s[16:17] op_sel_hi:[1,0]
	v_pk_mul_f32 v[126:127], v[126:127], s[16:17] op_sel_hi:[1,0]
	v_pk_mul_f32 v[120:121], v[120:121], s[16:17] op_sel_hi:[1,0]
	v_pk_mul_f32 v[118:119], v[118:119], s[16:17] op_sel_hi:[1,0]
	v_pk_mul_f32 v[10:11], v[140:141], s[16:17] op_sel_hi:[1,0]
	v_pk_mul_f32 v[20:21], v[138:139], s[16:17] op_sel_hi:[1,0]
	v_pk_mul_f32 v[22:23], v[132:133], s[16:17] op_sel_hi:[1,0]
	v_pk_mul_f32 v[30:31], v[130:131], s[16:17] op_sel_hi:[1,0]
	v_pk_mul_f32 v[112:113], v[112:113], s[16:17] op_sel_hi:[1,0]
	v_pk_mul_f32 v[110:111], v[110:111], s[16:17] op_sel_hi:[1,0]
	v_pk_mul_f32 v[108:109], v[108:109], s[16:17] op_sel_hi:[1,0]
	v_pk_mul_f32 v[106:107], v[106:107], s[16:17] op_sel_hi:[1,0]
	v_pk_mul_f32 v[16:17], v[124:125], s[16:17] op_sel_hi:[1,0]
	v_pk_mul_f32 v[24:25], v[122:123], s[16:17] op_sel_hi:[1,0]
	v_pk_mul_f32 v[28:29], v[116:117], s[16:17] op_sel_hi:[1,0]
	v_pk_mul_f32 v[32:33], v[114:115], s[16:17] op_sel_hi:[1,0]
	v_pk_mul_f32 v[104:105], v[104:105], s[16:17] op_sel_hi:[1,0]
	v_pk_mul_f32 v[102:103], v[102:103], s[16:17] op_sel_hi:[1,0]
	v_pk_mul_f32 v[100:101], v[100:101], s[16:17] op_sel_hi:[1,0]
	v_pk_mul_f32 v[98:99], v[98:99], s[16:17] op_sel_hi:[1,0]
	v_pk_mul_f32 v[96:97], v[96:97], s[16:17] op_sel_hi:[1,0]
	v_pk_mul_f32 v[94:95], v[94:95], s[16:17] op_sel_hi:[1,0]
	v_pk_mul_f32 v[92:93], v[92:93], s[16:17] op_sel_hi:[1,0]
	v_pk_mul_f32 v[90:91], v[90:91], s[16:17] op_sel_hi:[1,0]
	v_pk_mul_f32 v[114:115], v[80:81], s[16:17] op_sel_hi:[1,0]
	v_pk_mul_f32 v[116:117], v[78:79], s[16:17] op_sel_hi:[1,0]
	v_pk_mul_f32 v[122:123], v[72:73], s[16:17] op_sel_hi:[1,0]
	v_pk_mul_f32 v[124:125], v[70:71], s[16:17] op_sel_hi:[1,0]
	v_pk_mul_f32 v[70:71], v[88:89], s[16:17] op_sel_hi:[1,0]
	v_pk_mul_f32 v[72:73], v[86:87], s[16:17] op_sel_hi:[1,0]
	v_pk_mul_f32 v[78:79], v[84:85], s[16:17] op_sel_hi:[1,0]
	v_pk_mul_f32 v[80:81], v[82:83], s[16:17] op_sel_hi:[1,0]
	v_pk_mul_f32 v[82:83], v[64:65], s[16:17] op_sel_hi:[1,0]
	v_pk_mul_f32 v[84:85], v[62:63], s[16:17] op_sel_hi:[1,0]
	v_pk_mul_f32 v[86:87], v[56:57], s[16:17] op_sel_hi:[1,0]
	v_pk_mul_f32 v[88:89], v[54:55], s[16:17] op_sel_hi:[1,0]
	v_pk_mul_f32 v[54:55], v[76:77], s[16:17] op_sel_hi:[1,0]
	v_pk_mul_f32 v[56:57], v[74:75], s[16:17] op_sel_hi:[1,0]
	v_pk_mul_f32 v[62:63], v[68:69], s[16:17] op_sel_hi:[1,0]
	v_pk_mul_f32 v[64:65], v[66:67], s[16:17] op_sel_hi:[1,0]
	v_pk_mul_f32 v[66:67], v[48:49], s[16:17] op_sel_hi:[1,0]
	v_pk_mul_f32 v[68:69], v[46:47], s[16:17] op_sel_hi:[1,0]
	v_pk_mul_f32 v[74:75], v[44:45], s[16:17] op_sel_hi:[1,0]
	v_pk_mul_f32 v[76:77], v[42:43], s[16:17] op_sel_hi:[1,0]
	v_pk_mul_f32 v[42:43], v[60:61], s[16:17] op_sel_hi:[1,0]
	v_pk_mul_f32 v[44:45], v[58:59], s[16:17] op_sel_hi:[1,0]
	v_pk_mul_f32 v[46:47], v[52:53], s[16:17] op_sel_hi:[1,0]
	v_pk_mul_f32 v[48:49], v[50:51], s[16:17] op_sel_hi:[1,0]
	v_pk_mul_f32 v[40:41], v[40:41], s[16:17] op_sel_hi:[1,0]
	v_pk_mul_f32 v[38:39], v[38:39], s[16:17] op_sel_hi:[1,0]
	v_pk_mul_f32 v[36:37], v[36:37], s[16:17] op_sel_hi:[1,0]
	v_pk_mul_f32 v[34:35], v[34:35], s[16:17] op_sel_hi:[1,0]

	.amdhsa_kernel _Z4mega6Params
		.amdhsa_group_segment_fixed_size 0
		.amdhsa_private_segment_fixed_size 0
		.amdhsa_kernarg_size 696
		.amdhsa_user_sgpr_count 2
		.amdhsa_user_sgpr_dispatch_ptr 0
		.amdhsa_user_sgpr_queue_ptr 0
		.amdhsa_user_sgpr_kernarg_segment_ptr 1
		.amdhsa_user_sgpr_dispatch_id 0
		.amdhsa_user_sgpr_kernarg_preload_length 0
		.amdhsa_user_sgpr_kernarg_preload_offset 0
		.amdhsa_user_sgpr_private_segment_size 0
		.amdhsa_uses_dynamic_stack 0
		.amdhsa_enable_private_segment 0
		.amdhsa_system_sgpr_workgroup_id_x 1
		.amdhsa_system_sgpr_workgroup_id_y 0
		.amdhsa_system_sgpr_workgroup_id_z 0
		.amdhsa_system_sgpr_workgroup_info 0
		.amdhsa_system_vgpr_workitem_id 0
		.amdhsa_next_free_vgpr 255
		.amdhsa_next_free_sgpr 98
		.amdhsa_accum_offset 256
		.amdhsa_reserve_vcc 1
		.amdhsa_float_round_mode_32 0
		.amdhsa_float_round_mode_16_64 0
		.amdhsa_float_denorm_mode_32 3
		.amdhsa_float_denorm_mode_16_64 3
		.amdhsa_dx10_clamp 1
		.amdhsa_ieee_mode 1
		.amdhsa_fp16_overflow 0
		.amdhsa_tg_split 0
		.amdhsa_exception_fp_ieee_invalid_op 0
		.amdhsa_exception_fp_denorm_src 0
		.amdhsa_exception_fp_ieee_div_zero 0
		.amdhsa_exception_fp_ieee_overflow 0
		.amdhsa_exception_fp_ieee_underflow 0
		.amdhsa_exception_fp_ieee_inexact 0
		.amdhsa_exception_int_div_zero 0
	.end_amdhsa_kernel

amdhsa.kernels:
  - .agpr_count:     0
    .args:
      - .offset:         0
        .size:           440
        .value_kind:     by_value
      - .offset:         440
        .size:           4
        .value_kind:     hidden_block_count_x
      - .offset:         444
        .size:           4
        .value_kind:     hidden_block_count_y
      - .offset:         448
        .size:           4
        .value_kind:     hidden_block_count_z
      - .offset:         452
        .size:           2
        .value_kind:     hidden_group_size_x
      - .offset:         454
        .size:           2
        .value_kind:     hidden_group_size_y
      - .offset:         456
        .size:           2
        .value_kind:     hidden_group_size_z
      - .offset:         458
        .size:           2
        .value_kind:     hidden_remainder_x
      - .offset:         460
        .size:           2
        .value_kind:     hidden_remainder_y
      - .offset:         462
        .size:           2
        .value_kind:     hidden_remainder_z
      - .offset:         480
        .size:           8
        .value_kind:     hidden_global_offset_x
      - .offset:         488
        .size:           8
        .value_kind:     hidden_global_offset_y
      - .offset:         496
        .size:           8
        .value_kind:     hidden_global_offset_z
      - .offset:         504
        .size:           2
        .value_kind:     hidden_grid_dims
      - .offset:         560
        .size:           4
        .value_kind:     hidden_dynamic_lds_size
    .group_segment_fixed_size: 0
    .kernarg_segment_align: 8
    .kernarg_segment_size: 696
    .language:       OpenCL C
    .language_version:
      - 2
      - 0
    .max_flat_workgroup_size: 512
    .name:           _Z4mega6Params
    .private_segment_fixed_size: 0
    .sgpr_count:     104
    .sgpr_spill_count: 4
    .symbol:         _Z4mega6Params.kd
    .uniform_work_group_size: 1
    .uses_dynamic_stack: false
    .vgpr_count:     255
    .vgpr_spill_count: 0
    .wavefront_size: 64
